# one static s_setprio 1 for waves 4-7 per GEMM unit (reset after the K-loop), hipcc's per-segment flips deleted
# speedup vs baseline: 1.0070x; 1.0003x over previous
; #define PG8_STAGE(bufoff, gbase, o0, o1) do { \
;         __builtin_amdgcn_global_load_lds((const unsigned*)((const char*)(gbase) + (o0)), (LAS unsigned*)(lds + (bufoff) + ldsw), 16, 0, 0); \
;         __builtin_amdgcn_global_load_lds((const unsigned*)((const char*)(gbase) + (o1)), (LAS unsigned*)(lds + (bufoff) + ldsw + 8192), 16, 0, 0); } while (0)
; #define PG8_LDA(dst, b, h) do { _Pragma("unroll") for (int m = 0; m < 4; ++m) _Pragma("unroll") for (int k = 0; k < 2; ++k) dst[m][k] = *(const LAS bf16x8*)(lds + PG8_SA(b, h) + aoff + m * 2048 + k * 1024); } while (0)
; #define PG8_LDB(dst, b, h) do { _Pragma("unroll") for (int n = 0; n < 2; ++n) _Pragma("unroll") for (int k = 0; k < 2; ++k) dst[n][k] = *(const LAS bf16x8*)(lds + PG8_SB(b, h) + boff + n * 2048 + k * 1024); } while (0)
; #define PG8_WAIT_V(n) asm volatile("s_waitcnt vmcnt(" #n ")" ::: "memory")
; #define PG8_WAIT_L(n) asm volatile("s_waitcnt lgkmcnt(" #n ")" ::: "memory")
; #define PG8_BAR __builtin_amdgcn_s_barrier()
; #define PG8_SCHED __builtin_amdgcn_sched_barrier(0)
; template <class Epi, class Sched, class Prob>
; __device__ __forceinline__ void gemm_phase(LAS unsigned char* lds, LAS unsigned char* lds_epi, const Prob g, const Sched& S, const Epi& E, int wid) {
;     ...
;         const bool has_next = S.next(ui + 1, nxt);
;         const char* nA = has_next ? g.a_base(nxt) : cA; const char* nB = has_next ? g.b_base(nxt) : cB;
; _Pragma("clang loop unroll(disable)")
;         for (int t = 0; t < nt; t += 2) {
;             const bool last = (t == nt - 2);
;             const char* a1 = cA + (size_t)(t + 1) * kstep;
;             const char* a2 = last ? nA : cA + (size_t)(t + 2) * kstep; const char* b2 = last ? nB : cB + (size_t)(t + 2) * kstep;
;             const char* a3 = a2 + kstep; const char* b3 = b2 + kstep;
;             PG8_LDB(B0, 0, 0); PG8_LDB(B1, 0, 1); PG8_SCHED; PG8_LDA(At, 0, 0); PG8_STAGE(PG8_SA(1, 1), a1, cA10, cA11);
;             PG8_WAIT_V(8); PG8_WAIT_L(0); PG8_BAR; PG8_MMA(0, 0, At, B0); PG8_MMA(0, 1, At, B1); PG8_BAR; PG8_SCHED;
;             PG8_LDA(At, 0, 1); PG8_STAGE(PG8_SB(0, 0), b2, vB0, vB1); PG8_STAGE(PG8_SB(0, 1), b2 + hstepB, vB0, vB1); PG8_STAGE(PG8_SA(0, 0), a2, cA00, cA01);
;             PG8_WAIT_V(8); PG8_WAIT_L(0); PG8_BAR; PG8_MMA(1, 0, At, B0); PG8_MMA(1, 1, At, B1); PG8_BAR; PG8_SCHED;
.LBB0_261:
	s_ashr_i32 s3, s2, 31
	s_lshl_b64 s[48:49], s[2:3], 20
	s_add_u32 s48, s33, s48
	s_addc_u32 s49, s39, s49
	s_and_b64 s[50:51], s[46:47], exec
	s_cselect_b32 s3, s49, s15
	s_cselect_b32 s77, s48, s14
	s_ashr_i32 s45, s44, 31
	s_lshl_b64 s[50:51], s[44:45], 20
	s_add_u32 s50, s56, s50
	s_addc_u32 s51, s57, s51
	s_and_b64 s[54:55], s[46:47], exec
	s_cselect_b32 s45, s51, s53
	s_cselect_b32 s78, s50, s52
	s_add_u32 s14, s14, 0x80
	s_addc_u32 s15, s15, 0
	s_add_u32 s79, s52, 0x100
	v_mov_b32_e32 v44, 0
	s_addc_u32 s80, s53, 0
	s_mov_b32 s81, -2
	s_cmp_lt_u32 s91, 0x100
	s_cbranch_scc1 .Lyoung_0
	s_setprio 1
.Lyoung_0:
	v_add_u32_e32 v140, s72, v194
	v_add_u32_e32 v156, s73, v194
	ds_read_b128 v[128:131], v140
	ds_read_b128 v[132:135], v140 offset:1024
	ds_read_b128 v[136:139], v140 offset:2048
	ds_read_b128 v[140:143], v140 offset:3072
	ds_read_b128 v[174:177], v156
	ds_read_b128 v[178:181], v156 offset:1024
	ds_read_b128 v[182:185], v156 offset:2048
	ds_read_b128 v[186:189], v156 offset:3072
	s_add_u32 s52, s14, 0x80
	s_addc_u32 s53, s15, 0
	s_cmp_eq_u32 s81, 28
	s_cselect_b32 s55, s3, s53
	s_cselect_b32 s54, s77, s52
	s_cselect_b32 s53, s45, s80
	s_cselect_b32 s52, s78, s79
	v_lshl_add_u64 v[190:191], s[14:15], 0, v[170:171]
	s_add_i32 m0, s25, 0xc000
	ds_read_b128 v[208:211], v204
	ds_read_b128 v[212:215], v204 offset:1024
	ds_read_b128 v[216:219], v204 offset:2048
	ds_read_b128 v[220:223], v204 offset:3072
	ds_read_b128 v[224:227], v204 offset:4096
	ds_read_b128 v[228:231], v204 offset:5120
	ds_read_b128 v[232:235], v204 offset:6144
	ds_read_b128 v[238:241], v204 offset:7168
	global_load_lds_dwordx4 v[190:191], off
	v_lshl_add_u64 v[190:191], s[14:15], 0, v[168:169]
	s_add_i32 m0, s25, 0xe000
	s_nop 0
	global_load_lds_dwordx4 v[190:191], off
	s_waitcnt vmcnt(8)
	s_waitcnt lgkmcnt(0)
	s_barrier
	s_waitcnt lgkmcnt(0)
	v_mfma_f32_16x16x32_bf16 v[80:83], v[128:131], v[208:211], 0
	v_mfma_f32_16x16x32_bf16 v[92:95], v[136:139], v[208:211], 0
	v_mfma_f32_16x16x32_bf16 v[52:55], v[128:131], v[216:219], 0
	v_mfma_f32_16x16x32_bf16 v[68:71], v[136:139], v[216:219], 0
	v_mfma_f32_16x16x32_bf16 v[28:31], v[128:131], v[224:227], 0
	v_mfma_f32_16x16x32_bf16 v[36:39], v[136:139], v[224:227], 0
	v_mfma_f32_16x16x32_bf16 v[8:11], v[128:131], v[232:235], 0
	v_mfma_f32_16x16x32_bf16 v[16:19], v[136:139], v[232:235], 0
	v_mfma_f32_16x16x32_bf16 v[80:83], v[132:135], v[212:215], v[80:83]
	v_mfma_f32_16x16x32_bf16 v[92:95], v[140:143], v[212:215], v[92:95]
	v_mfma_f32_16x16x32_bf16 v[52:55], v[132:135], v[220:223], v[52:55]
	v_mfma_f32_16x16x32_bf16 v[68:71], v[140:143], v[220:223], v[68:71]
	v_mfma_f32_16x16x32_bf16 v[28:31], v[132:135], v[228:231], v[28:31]
	v_mfma_f32_16x16x32_bf16 v[36:39], v[140:143], v[228:231], v[36:39]
	v_mfma_f32_16x16x32_bf16 v[8:11], v[132:135], v[238:241], v[8:11]
	v_mfma_f32_16x16x32_bf16 v[16:19], v[140:143], v[238:241], v[16:19]
	v_mfma_f32_16x16x32_bf16 v[120:123], v[174:177], v[208:211], 0
	v_mfma_f32_16x16x32_bf16 v[124:127], v[182:185], v[208:211], 0
	v_mfma_f32_16x16x32_bf16 v[104:107], v[174:177], v[216:219], 0
	v_mfma_f32_16x16x32_bf16 v[112:115], v[182:185], v[216:219], 0
	v_mfma_f32_16x16x32_bf16 v[84:87], v[174:177], v[224:227], 0
	v_mfma_f32_16x16x32_bf16 v[96:99], v[182:185], v[224:227], 0
	v_mfma_f32_16x16x32_bf16 v[48:51], v[174:177], v[232:235], 0
	v_mfma_f32_16x16x32_bf16 v[64:67], v[182:185], v[232:235], 0
	v_mfma_f32_16x16x32_bf16 v[120:123], v[178:181], v[212:215], v[120:123]
	v_mfma_f32_16x16x32_bf16 v[124:127], v[186:189], v[212:215], v[124:127]
	v_mfma_f32_16x16x32_bf16 v[104:107], v[178:181], v[220:223], v[104:107]
	v_mfma_f32_16x16x32_bf16 v[112:115], v[186:189], v[220:223], v[112:115]
	v_mfma_f32_16x16x32_bf16 v[84:87], v[178:181], v[228:231], v[84:87]
	v_mfma_f32_16x16x32_bf16 v[96:99], v[186:189], v[228:231], v[96:99]
	v_mfma_f32_16x16x32_bf16 v[48:51], v[178:181], v[238:241], v[48:51]
	v_mfma_f32_16x16x32_bf16 v[64:67], v[186:189], v[238:241], v[64:67]
	s_barrier
	s_add_i32 s82, s72, s97
	v_lshl_add_u64 v[190:191], s[52:53], 0, v[144:145]
	s_mov_b32 m0, s82
	ds_read_b128 v[208:211], v204 offset:16384
	ds_read_b128 v[212:215], v204 offset:17408
	ds_read_b128 v[216:219], v204 offset:18432
	ds_read_b128 v[220:223], v204 offset:19456
	ds_read_b128 v[224:227], v204 offset:20480
	ds_read_b128 v[228:231], v204 offset:21504
	ds_read_b128 v[232:235], v204 offset:22528
	ds_read_b128 v[238:241], v204 offset:23552
	global_load_lds_dwordx4 v[190:191], off
	s_add_i32 m0, s82, 0x2000
	s_add_u32 s82, s52, 0x80000
	v_lshl_add_u64 v[236:237], s[52:53], 0, v[146:147]
	s_addc_u32 s83, s53, 0
	s_add_i32 s84, s73, s97
	global_load_lds_dwordx4 v[236:237], off
	v_lshl_add_u64 v[242:243], s[82:83], 0, v[144:145]
	s_mov_b32 m0, s84
	v_lshl_add_u64 v[244:245], s[54:55], 0, v[152:153]
	global_load_lds_dwordx4 v[242:243], off
	v_lshl_add_u64 v[242:243], s[82:83], 0, v[146:147]
	s_add_i32 m0, s84, 0x2000
	s_nop 0
	global_load_lds_dwordx4 v[242:243], off
	v_lshl_add_u64 v[242:243], s[54:55], 0, v[148:149]
	s_mov_b32 m0, s25
	s_nop 0
	global_load_lds_dwordx4 v[242:243], off
	s_mov_b32 m0, s58
	s_nop 0
	global_load_lds_dwordx4 v[244:245], off
	s_waitcnt vmcnt(8)
	s_waitcnt lgkmcnt(0)
	s_barrier
; #define PG8_STAGE(bufoff, gbase, o0, o1) do { \
;         __builtin_amdgcn_global_load_lds((const unsigned*)((const char*)(gbase) + (o0)), (LAS unsigned*)(lds + (bufoff) + ldsw), 16, 0, 0); \
;         __builtin_amdgcn_global_load_lds((const unsigned*)((const char*)(gbase) + (o1)), (LAS unsigned*)(lds + (bufoff) + ldsw + 8192), 16, 0, 0); } while (0)
; #define PG8_LDA(dst, b, h) do { _Pragma("unroll") for (int m = 0; m < 4; ++m) _Pragma("unroll") for (int k = 0; k < 2; ++k) dst[m][k] = *(const LAS bf16x8*)(lds + PG8_SA(b, h) + aoff + m * 2048 + k * 1024); } while (0)
; #define PG8_LDB(dst, b, h) do { _Pragma("unroll") for (int n = 0; n < 2; ++n) _Pragma("unroll") for (int k = 0; k < 2; ++k) dst[n][k] = *(const LAS bf16x8*)(lds + PG8_SB(b, h) + boff + n * 2048 + k * 1024); } while (0)
; #define PG8_WAIT_V(n) asm volatile("s_waitcnt vmcnt(" #n ")" ::: "memory")
; #define PG8_WAIT_L(n) asm volatile("s_waitcnt lgkmcnt(" #n ")" ::: "memory")
; #define PG8_BAR __builtin_amdgcn_s_barrier()
; #define PG8_SCHED __builtin_amdgcn_sched_barrier(0)
; template <class Epi, class Sched, class Prob>
; __device__ __forceinline__ void gemm_phase(LAS unsigned char* lds, LAS unsigned char* lds_epi, const Prob g, const Sched& S, const Epi& E, int wid) {
;     ...
;             PG8_WAIT_V(8); PG8_WAIT_L(0); PG8_BAR; PG8_MMA(1, 0, At, B0); PG8_MMA(1, 1, At, B1); PG8_BAR; PG8_SCHED;
;             PG8_LDB(B0, 1, 0); PG8_LDB(B1, 1, 1); PG8_SCHED; PG8_LDA(At, 1, 0); PG8_STAGE(PG8_SA(0, 1), a2, cA10, cA11);
;             PG8_WAIT_V(8); PG8_WAIT_L(0); PG8_BAR; PG8_MMA(0, 0, At, B0); PG8_MMA(0, 1, At, B1); PG8_BAR; PG8_SCHED;
	s_waitcnt lgkmcnt(0)
	v_mfma_f32_16x16x32_bf16 v[56:59], v[128:131], v[208:211], 0
	v_mfma_f32_16x16x32_bf16 v[72:75], v[136:139], v[208:211], 0
	v_mfma_f32_16x16x32_bf16 v[32:35], v[128:131], v[216:219], 0
	v_mfma_f32_16x16x32_bf16 v[40:43], v[136:139], v[216:219], 0
	v_mfma_f32_16x16x32_bf16 v[12:15], v[128:131], v[224:227], 0
	v_mfma_f32_16x16x32_bf16 v[20:23], v[136:139], v[224:227], 0
	v_mfma_f32_16x16x32_bf16 v[0:3], v[128:131], v[232:235], 0
	v_mfma_f32_16x16x32_bf16 v[4:7], v[136:139], v[232:235], 0
	v_mfma_f32_16x16x32_bf16 v[56:59], v[132:135], v[212:215], v[56:59]
	v_mfma_f32_16x16x32_bf16 v[72:75], v[140:143], v[212:215], v[72:75]
	v_mfma_f32_16x16x32_bf16 v[32:35], v[132:135], v[220:223], v[32:35]
	v_mfma_f32_16x16x32_bf16 v[40:43], v[140:143], v[220:223], v[40:43]
	v_mfma_f32_16x16x32_bf16 v[12:15], v[132:135], v[228:231], v[12:15]
	v_mfma_f32_16x16x32_bf16 v[20:23], v[140:143], v[228:231], v[20:23]
	v_mfma_f32_16x16x32_bf16 v[0:3], v[132:135], v[238:241], v[0:3]
	v_mfma_f32_16x16x32_bf16 v[4:7], v[140:143], v[238:241], v[4:7]
	v_mfma_f32_16x16x32_bf16 v[108:111], v[174:177], v[208:211], 0
	v_mfma_f32_16x16x32_bf16 v[116:119], v[182:185], v[208:211], 0
	v_mfma_f32_16x16x32_bf16 v[88:91], v[174:177], v[216:219], 0
	v_mfma_f32_16x16x32_bf16 v[100:103], v[182:185], v[216:219], 0
	v_mfma_f32_16x16x32_bf16 v[60:63], v[174:177], v[224:227], 0
	v_mfma_f32_16x16x32_bf16 v[76:79], v[182:185], v[224:227], 0
	v_mfma_f32_16x16x32_bf16 v[24:27], v[174:177], v[232:235], 0
	v_mfma_f32_16x16x32_bf16 v[44:47], v[182:185], v[232:235], 0
	v_mfma_f32_16x16x32_bf16 v[108:111], v[178:181], v[212:215], v[108:111]
	v_mfma_f32_16x16x32_bf16 v[116:119], v[186:189], v[212:215], v[116:119]
	v_mfma_f32_16x16x32_bf16 v[88:91], v[178:181], v[220:223], v[88:91]
	v_mfma_f32_16x16x32_bf16 v[100:103], v[186:189], v[220:223], v[100:103]
	v_mfma_f32_16x16x32_bf16 v[60:63], v[178:181], v[228:231], v[60:63]
	v_mfma_f32_16x16x32_bf16 v[76:79], v[186:189], v[228:231], v[76:79]
	v_mfma_f32_16x16x32_bf16 v[24:27], v[178:181], v[238:241], v[24:27]
	v_mfma_f32_16x16x32_bf16 v[44:47], v[186:189], v[238:241], v[44:47]
	s_barrier
	s_add_i32 s82, 0, 0x18000
	s_add_i32 s83, 0, 0x1c000
	v_add_u32_e32 v140, s82, v194
	v_add_u32_e32 v156, s83, v194
	ds_read_b128 v[128:131], v140
	ds_read_b128 v[132:135], v140 offset:1024
	ds_read_b128 v[136:139], v140 offset:2048
	ds_read_b128 v[140:143], v140 offset:3072
	ds_read_b128 v[174:177], v156
	ds_read_b128 v[178:181], v156 offset:1024
	ds_read_b128 v[182:185], v156 offset:2048
	ds_read_b128 v[186:189], v156 offset:3072
	s_mov_b32 m0, s59
	v_lshl_add_u64 v[246:247], s[54:55], 0, v[150:151]
	ds_read_b128 v[208:211], v204 offset:32768
	ds_read_b128 v[212:215], v204 offset:33792
	ds_read_b128 v[216:219], v204 offset:34816
	ds_read_b128 v[220:223], v204 offset:35840
	ds_read_b128 v[224:227], v204 offset:36864
	ds_read_b128 v[228:231], v204 offset:37888
	ds_read_b128 v[232:235], v204 offset:38912
	ds_read_b128 v[238:241], v204 offset:39936
	global_load_lds_dwordx4 v[246:247], off
	v_lshl_add_u64 v[246:247], s[54:55], 0, v[154:155]
	s_mov_b32 m0, s60
	s_nop 0
	global_load_lds_dwordx4 v[246:247], off
	s_waitcnt vmcnt(8)
	s_waitcnt lgkmcnt(0)
	s_barrier
	s_waitcnt lgkmcnt(0)
	v_mfma_f32_16x16x32_bf16 v[80:83], v[128:131], v[208:211], v[80:83]
	v_mfma_f32_16x16x32_bf16 v[92:95], v[136:139], v[208:211], v[92:95]
	v_mfma_f32_16x16x32_bf16 v[52:55], v[128:131], v[216:219], v[52:55]
	v_mfma_f32_16x16x32_bf16 v[68:71], v[136:139], v[216:219], v[68:71]
	v_mfma_f32_16x16x32_bf16 v[28:31], v[128:131], v[224:227], v[28:31]
	v_mfma_f32_16x16x32_bf16 v[36:39], v[136:139], v[224:227], v[36:39]
	v_mfma_f32_16x16x32_bf16 v[8:11], v[128:131], v[232:235], v[8:11]
	v_mfma_f32_16x16x32_bf16 v[16:19], v[136:139], v[232:235], v[16:19]
	v_mfma_f32_16x16x32_bf16 v[80:83], v[132:135], v[212:215], v[80:83]
	v_mfma_f32_16x16x32_bf16 v[92:95], v[140:143], v[212:215], v[92:95]
	v_mfma_f32_16x16x32_bf16 v[52:55], v[132:135], v[220:223], v[52:55]
	v_mfma_f32_16x16x32_bf16 v[68:71], v[140:143], v[220:223], v[68:71]
	v_mfma_f32_16x16x32_bf16 v[28:31], v[132:135], v[228:231], v[28:31]
	v_mfma_f32_16x16x32_bf16 v[36:39], v[140:143], v[228:231], v[36:39]
	v_mfma_f32_16x16x32_bf16 v[8:11], v[132:135], v[238:241], v[8:11]
	v_mfma_f32_16x16x32_bf16 v[16:19], v[140:143], v[238:241], v[16:19]
	v_mfma_f32_16x16x32_bf16 v[120:123], v[174:177], v[208:211], v[120:123]
	v_mfma_f32_16x16x32_bf16 v[124:127], v[182:185], v[208:211], v[124:127]
	v_mfma_f32_16x16x32_bf16 v[104:107], v[174:177], v[216:219], v[104:107]
	v_mfma_f32_16x16x32_bf16 v[112:115], v[182:185], v[216:219], v[112:115]
	v_mfma_f32_16x16x32_bf16 v[84:87], v[174:177], v[224:227], v[84:87]
	v_mfma_f32_16x16x32_bf16 v[96:99], v[182:185], v[224:227], v[96:99]
	v_mfma_f32_16x16x32_bf16 v[48:51], v[174:177], v[232:235], v[48:51]
	v_mfma_f32_16x16x32_bf16 v[64:67], v[182:185], v[232:235], v[64:67]
	v_mfma_f32_16x16x32_bf16 v[120:123], v[178:181], v[212:215], v[120:123]
	v_mfma_f32_16x16x32_bf16 v[124:127], v[186:189], v[212:215], v[124:127]
	v_mfma_f32_16x16x32_bf16 v[104:107], v[178:181], v[220:223], v[104:107]
	v_mfma_f32_16x16x32_bf16 v[112:115], v[186:189], v[220:223], v[112:115]
	v_mfma_f32_16x16x32_bf16 v[84:87], v[178:181], v[228:231], v[84:87]
	v_mfma_f32_16x16x32_bf16 v[96:99], v[186:189], v[228:231], v[96:99]
	v_mfma_f32_16x16x32_bf16 v[48:51], v[178:181], v[238:241], v[48:51]
	v_mfma_f32_16x16x32_bf16 v[64:67], v[186:189], v[238:241], v[64:67]
	s_barrier
; #define PG8_STAGE(bufoff, gbase, o0, o1) do { \
;         __builtin_amdgcn_global_load_lds((const unsigned*)((const char*)(gbase) + (o0)), (LAS unsigned*)(lds + (bufoff) + ldsw), 16, 0, 0); \
;         __builtin_amdgcn_global_load_lds((const unsigned*)((const char*)(gbase) + (o1)), (LAS unsigned*)(lds + (bufoff) + ldsw + 8192), 16, 0, 0); } while (0)
; #define PG8_LDA(dst, b, h) do { _Pragma("unroll") for (int m = 0; m < 4; ++m) _Pragma("unroll") for (int k = 0; k < 2; ++k) dst[m][k] = *(const LAS bf16x8*)(lds + PG8_SA(b, h) + aoff + m * 2048 + k * 1024); } while (0)
; #define PG8_LDB(dst, b, h) do { _Pragma("unroll") for (int n = 0; n < 2; ++n) _Pragma("unroll") for (int k = 0; k < 2; ++k) dst[n][k] = *(const LAS bf16x8*)(lds + PG8_SB(b, h) + boff + n * 2048 + k * 1024); } while (0)
; #define PG8_WAIT_V(n) asm volatile("s_waitcnt vmcnt(" #n ")" ::: "memory")
; #define PG8_WAIT_L(n) asm volatile("s_waitcnt lgkmcnt(" #n ")" ::: "memory")
; #define PG8_BAR __builtin_amdgcn_s_barrier()
; #define PG8_SCHED __builtin_amdgcn_sched_barrier(0)
; template <class Epi, class Sched, class Prob>
; __device__ __forceinline__ void gemm_phase(LAS unsigned char* lds, LAS unsigned char* lds_epi, const Prob g, const Sched& S, const Epi& E, int wid) {
;     ...
;         for (int t = 0; t < nt; t += 2) {
;             const bool last = (t == nt - 2);
;             const char* a1 = cA + (size_t)(t + 1) * kstep;
;             const char* a2 = last ? nA : cA + (size_t)(t + 2) * kstep; const char* b2 = last ? nB : cB + (size_t)(t + 2) * kstep;
;             const char* a3 = a2 + kstep; const char* b3 = b2 + kstep;
;             PG8_LDB(B0, 0, 0); PG8_LDB(B1, 0, 1); PG8_SCHED; PG8_LDA(At, 0, 0); PG8_STAGE(PG8_SA(1, 1), a1, cA10, cA11);
;             PG8_WAIT_V(8); PG8_WAIT_L(0); PG8_BAR; PG8_MMA(0, 0, At, B0); PG8_MMA(0, 1, At, B1); PG8_BAR; PG8_SCHED;
;     ...
;             PG8_LDA(At, 1, 1); PG8_STAGE(PG8_SB(1, 0), b3, vB0, vB1); PG8_STAGE(PG8_SB(1, 1), b3 + hstepB, vB0, vB1); PG8_STAGE(PG8_SA(1, 0), a3, cA00, cA01);
;             PG8_WAIT_V(8); PG8_WAIT_L(0); PG8_BAR; PG8_MMA(1, 0, At, B0); PG8_MMA(1, 1, At, B1); PG8_BAR; PG8_SCHED;
	s_add_i32 s54, s82, s97
	v_lshl_add_u64 v[190:191], v[190:191], 0, s[20:21]
	s_mov_b32 m0, s54
	ds_read_b128 v[208:211], v204 offset:49152
	ds_read_b128 v[212:215], v204 offset:50176
	ds_read_b128 v[216:219], v204 offset:51200
	ds_read_b128 v[220:223], v204 offset:52224
	ds_read_b128 v[224:227], v204 offset:53248
	ds_read_b128 v[228:231], v204 offset:54272
	ds_read_b128 v[232:235], v204 offset:55296
	ds_read_b128 v[238:241], v204 offset:56320
	global_load_lds_dwordx4 v[190:191], off
	s_add_i32 m0, s54, 0x2000
	s_add_u32 s52, s52, 0x80080
	v_lshl_add_u64 v[190:191], v[236:237], 0, s[20:21]
	s_addc_u32 s53, s53, 0
	s_add_i32 s54, s83, s97
	global_load_lds_dwordx4 v[190:191], off
	v_lshl_add_u64 v[190:191], s[52:53], 0, v[144:145]
	s_mov_b32 m0, s54
	s_nop 0
	global_load_lds_dwordx4 v[190:191], off
	v_lshl_add_u64 v[190:191], s[52:53], 0, v[146:147]
	s_add_i32 m0, s54, 0x2000
	s_nop 0
	global_load_lds_dwordx4 v[190:191], off
	v_lshl_add_u64 v[190:191], v[242:243], 0, s[20:21]
	s_mov_b32 m0, s70
	s_nop 0
	global_load_lds_dwordx4 v[190:191], off
	v_lshl_add_u64 v[190:191], v[244:245], 0, s[20:21]
	s_mov_b32 m0, s71
	s_nop 0
	global_load_lds_dwordx4 v[190:191], off
	s_waitcnt vmcnt(8)
	s_waitcnt lgkmcnt(0)
	s_barrier
	s_waitcnt lgkmcnt(0)
	v_mfma_f32_16x16x32_bf16 v[56:59], v[128:131], v[208:211], v[56:59]
	v_mfma_f32_16x16x32_bf16 v[72:75], v[136:139], v[208:211], v[72:75]
	v_mfma_f32_16x16x32_bf16 v[32:35], v[128:131], v[216:219], v[32:35]
	v_mfma_f32_16x16x32_bf16 v[40:43], v[136:139], v[216:219], v[40:43]
	v_mfma_f32_16x16x32_bf16 v[12:15], v[128:131], v[224:227], v[12:15]
	v_mfma_f32_16x16x32_bf16 v[20:23], v[136:139], v[224:227], v[20:23]
	v_mfma_f32_16x16x32_bf16 v[0:3], v[128:131], v[232:235], v[0:3]
	v_mfma_f32_16x16x32_bf16 v[4:7], v[136:139], v[232:235], v[4:7]
	v_mfma_f32_16x16x32_bf16 v[56:59], v[132:135], v[212:215], v[56:59]
	v_mfma_f32_16x16x32_bf16 v[72:75], v[140:143], v[212:215], v[72:75]
	v_mfma_f32_16x16x32_bf16 v[32:35], v[132:135], v[220:223], v[32:35]
	v_mfma_f32_16x16x32_bf16 v[40:43], v[140:143], v[220:223], v[40:43]
	v_mfma_f32_16x16x32_bf16 v[12:15], v[132:135], v[228:231], v[12:15]
	v_mfma_f32_16x16x32_bf16 v[20:23], v[140:143], v[228:231], v[20:23]
	v_mfma_f32_16x16x32_bf16 v[0:3], v[132:135], v[238:241], v[0:3]
	v_mfma_f32_16x16x32_bf16 v[4:7], v[140:143], v[238:241], v[4:7]
	v_mfma_f32_16x16x32_bf16 v[108:111], v[174:177], v[208:211], v[108:111]
	v_mfma_f32_16x16x32_bf16 v[116:119], v[182:185], v[208:211], v[116:119]
	v_mfma_f32_16x16x32_bf16 v[88:91], v[174:177], v[216:219], v[88:91]
	v_mfma_f32_16x16x32_bf16 v[100:103], v[182:185], v[216:219], v[100:103]
	v_mfma_f32_16x16x32_bf16 v[60:63], v[174:177], v[224:227], v[60:63]
	v_mfma_f32_16x16x32_bf16 v[76:79], v[182:185], v[224:227], v[76:79]
	v_mfma_f32_16x16x32_bf16 v[24:27], v[174:177], v[232:235], v[24:27]
	v_mfma_f32_16x16x32_bf16 v[44:47], v[182:185], v[232:235], v[44:47]
	v_mfma_f32_16x16x32_bf16 v[108:111], v[178:181], v[212:215], v[108:111]
	v_mfma_f32_16x16x32_bf16 v[116:119], v[186:189], v[212:215], v[116:119]
	v_mfma_f32_16x16x32_bf16 v[88:91], v[178:181], v[220:223], v[88:91]
	v_mfma_f32_16x16x32_bf16 v[100:103], v[186:189], v[220:223], v[100:103]
	v_mfma_f32_16x16x32_bf16 v[60:63], v[178:181], v[228:231], v[60:63]
	v_mfma_f32_16x16x32_bf16 v[76:79], v[186:189], v[228:231], v[76:79]
	v_mfma_f32_16x16x32_bf16 v[24:27], v[178:181], v[238:241], v[24:27]
	v_mfma_f32_16x16x32_bf16 v[44:47], v[186:189], v[238:241], v[44:47]
	s_barrier
	s_add_i32 s81, s81, 2
	s_add_u32 s14, s14, 0x100
	s_addc_u32 s15, s15, 0
	s_add_u32 s79, s79, 0x100
	s_addc_u32 s80, s80, 0
	s_cmp_gt_u32 s81, 29
.LBB0_262:
	v_add_u32_e32 v140, s72, v194
	v_add_u32_e32 v156, s73, v194
	ds_read_b128 v[128:131], v140
	ds_read_b128 v[132:135], v140 offset:1024
	ds_read_b128 v[136:139], v140 offset:2048
	ds_read_b128 v[140:143], v140 offset:3072
	ds_read_b128 v[174:177], v156
	ds_read_b128 v[178:181], v156 offset:1024
	ds_read_b128 v[182:185], v156 offset:2048
	ds_read_b128 v[186:189], v156 offset:3072
	s_add_u32 s52, s14, 0x80
	s_addc_u32 s53, s15, 0
	s_cmp_eq_u32 s81, 28
	s_cselect_b32 s55, s3, s53
	s_cselect_b32 s54, s77, s52
	s_cselect_b32 s53, s45, s80
	s_cselect_b32 s52, s78, s79
	v_lshl_add_u64 v[190:191], s[14:15], 0, v[170:171]
	s_add_i32 m0, s25, 0xc000
	ds_read_b128 v[208:211], v204
	ds_read_b128 v[212:215], v204 offset:1024
	ds_read_b128 v[216:219], v204 offset:2048
	ds_read_b128 v[220:223], v204 offset:3072
	ds_read_b128 v[224:227], v204 offset:4096
	ds_read_b128 v[228:231], v204 offset:5120
	ds_read_b128 v[232:235], v204 offset:6144
	ds_read_b128 v[238:241], v204 offset:7168
	global_load_lds_dwordx4 v[190:191], off
	v_lshl_add_u64 v[190:191], s[14:15], 0, v[168:169]
	s_add_i32 m0, s25, 0xe000
	s_nop 0
	global_load_lds_dwordx4 v[190:191], off
	s_waitcnt vmcnt(8)
	s_waitcnt lgkmcnt(0)
	s_barrier
; #define PG8_STAGE(bufoff, gbase, o0, o1) do { \
;         __builtin_amdgcn_global_load_lds((const unsigned*)((const char*)(gbase) + (o0)), (LAS unsigned*)(lds + (bufoff) + ldsw), 16, 0, 0); \
;         __builtin_amdgcn_global_load_lds((const unsigned*)((const char*)(gbase) + (o1)), (LAS unsigned*)(lds + (bufoff) + ldsw + 8192), 16, 0, 0); } while (0)
; #define PG8_LDA(dst, b, h) do { _Pragma("unroll") for (int m = 0; m < 4; ++m) _Pragma("unroll") for (int k = 0; k < 2; ++k) dst[m][k] = *(const LAS bf16x8*)(lds + PG8_SA(b, h) + aoff + m * 2048 + k * 1024); } while (0)
; #define PG8_WAIT_V(n) asm volatile("s_waitcnt vmcnt(" #n ")" ::: "memory")
; #define PG8_WAIT_L(n) asm volatile("s_waitcnt lgkmcnt(" #n ")" ::: "memory")
; #define PG8_BAR __builtin_amdgcn_s_barrier()
; #define PG8_SCHED __builtin_amdgcn_sched_barrier(0)
; template <class Epi, class Sched, class Prob>
; __device__ __forceinline__ void gemm_phase(LAS unsigned char* lds, LAS unsigned char* lds_epi, const Prob g, const Sched& S, const Epi& E, int wid) {
;     ...
;             PG8_WAIT_V(8); PG8_WAIT_L(0); PG8_BAR; PG8_MMA(0, 0, At, B0); PG8_MMA(0, 1, At, B1); PG8_BAR; PG8_SCHED;
;             PG8_LDA(At, 0, 1); PG8_STAGE(PG8_SB(0, 0), b2, vB0, vB1); PG8_STAGE(PG8_SB(0, 1), b2 + hstepB, vB0, vB1); PG8_STAGE(PG8_SA(0, 0), a2, cA00, cA01);
;             PG8_WAIT_V(8); PG8_WAIT_L(0); PG8_BAR; PG8_MMA(1, 0, At, B0); PG8_MMA(1, 1, At, B1); PG8_BAR; PG8_SCHED;
	s_waitcnt lgkmcnt(0)
	v_mfma_f32_16x16x32_bf16 v[80:83], v[128:131], v[208:211], v[80:83]
	v_mfma_f32_16x16x32_bf16 v[92:95], v[136:139], v[208:211], v[92:95]
	v_mfma_f32_16x16x32_bf16 v[52:55], v[128:131], v[216:219], v[52:55]
	v_mfma_f32_16x16x32_bf16 v[68:71], v[136:139], v[216:219], v[68:71]
	v_mfma_f32_16x16x32_bf16 v[28:31], v[128:131], v[224:227], v[28:31]
	v_mfma_f32_16x16x32_bf16 v[36:39], v[136:139], v[224:227], v[36:39]
	v_mfma_f32_16x16x32_bf16 v[8:11], v[128:131], v[232:235], v[8:11]
	v_mfma_f32_16x16x32_bf16 v[16:19], v[136:139], v[232:235], v[16:19]
	v_mfma_f32_16x16x32_bf16 v[80:83], v[132:135], v[212:215], v[80:83]
	v_mfma_f32_16x16x32_bf16 v[92:95], v[140:143], v[212:215], v[92:95]
	v_mfma_f32_16x16x32_bf16 v[52:55], v[132:135], v[220:223], v[52:55]
	v_mfma_f32_16x16x32_bf16 v[68:71], v[140:143], v[220:223], v[68:71]
	v_mfma_f32_16x16x32_bf16 v[28:31], v[132:135], v[228:231], v[28:31]
	v_mfma_f32_16x16x32_bf16 v[36:39], v[140:143], v[228:231], v[36:39]
	v_mfma_f32_16x16x32_bf16 v[8:11], v[132:135], v[238:241], v[8:11]
	v_mfma_f32_16x16x32_bf16 v[16:19], v[140:143], v[238:241], v[16:19]
	v_mfma_f32_16x16x32_bf16 v[120:123], v[174:177], v[208:211], v[120:123]
	v_mfma_f32_16x16x32_bf16 v[124:127], v[182:185], v[208:211], v[124:127]
	v_mfma_f32_16x16x32_bf16 v[104:107], v[174:177], v[216:219], v[104:107]
	v_mfma_f32_16x16x32_bf16 v[112:115], v[182:185], v[216:219], v[112:115]
	v_mfma_f32_16x16x32_bf16 v[84:87], v[174:177], v[224:227], v[84:87]
	v_mfma_f32_16x16x32_bf16 v[96:99], v[182:185], v[224:227], v[96:99]
	v_mfma_f32_16x16x32_bf16 v[48:51], v[174:177], v[232:235], v[48:51]
	v_mfma_f32_16x16x32_bf16 v[64:67], v[182:185], v[232:235], v[64:67]
	v_mfma_f32_16x16x32_bf16 v[120:123], v[178:181], v[212:215], v[120:123]
	v_mfma_f32_16x16x32_bf16 v[124:127], v[186:189], v[212:215], v[124:127]
	v_mfma_f32_16x16x32_bf16 v[104:107], v[178:181], v[220:223], v[104:107]
	v_mfma_f32_16x16x32_bf16 v[112:115], v[186:189], v[220:223], v[112:115]
	v_mfma_f32_16x16x32_bf16 v[84:87], v[178:181], v[228:231], v[84:87]
	v_mfma_f32_16x16x32_bf16 v[96:99], v[186:189], v[228:231], v[96:99]
	v_mfma_f32_16x16x32_bf16 v[48:51], v[178:181], v[238:241], v[48:51]
	v_mfma_f32_16x16x32_bf16 v[64:67], v[186:189], v[238:241], v[64:67]
	s_barrier
	s_add_i32 s82, s72, s97
	v_lshl_add_u64 v[190:191], s[52:53], 0, v[144:145]
	s_mov_b32 m0, s82
	ds_read_b128 v[208:211], v204 offset:16384
	ds_read_b128 v[212:215], v204 offset:17408
	ds_read_b128 v[216:219], v204 offset:18432
	ds_read_b128 v[220:223], v204 offset:19456
	ds_read_b128 v[224:227], v204 offset:20480
	ds_read_b128 v[228:231], v204 offset:21504
	ds_read_b128 v[232:235], v204 offset:22528
	ds_read_b128 v[238:241], v204 offset:23552
	global_load_lds_dwordx4 v[190:191], off
	s_add_i32 m0, s82, 0x2000
	s_add_u32 s82, s52, 0x80000
	v_lshl_add_u64 v[236:237], s[52:53], 0, v[146:147]
	s_addc_u32 s83, s53, 0
	s_add_i32 s84, s73, s97
	global_load_lds_dwordx4 v[236:237], off
	v_lshl_add_u64 v[242:243], s[82:83], 0, v[144:145]
	s_mov_b32 m0, s84
	v_lshl_add_u64 v[244:245], s[54:55], 0, v[152:153]
	global_load_lds_dwordx4 v[242:243], off
	v_lshl_add_u64 v[242:243], s[82:83], 0, v[146:147]
	s_add_i32 m0, s84, 0x2000
	s_nop 0
	global_load_lds_dwordx4 v[242:243], off
	v_lshl_add_u64 v[242:243], s[54:55], 0, v[148:149]
	s_mov_b32 m0, s25
	s_nop 0
	global_load_lds_dwordx4 v[242:243], off
	s_mov_b32 m0, s58
	s_nop 0
	global_load_lds_dwordx4 v[244:245], off
	s_waitcnt vmcnt(8)
	s_waitcnt lgkmcnt(0)
	s_barrier
	s_waitcnt lgkmcnt(0)
	v_mfma_f32_16x16x32_bf16 v[56:59], v[128:131], v[208:211], v[56:59]
	v_mfma_f32_16x16x32_bf16 v[72:75], v[136:139], v[208:211], v[72:75]
	v_mfma_f32_16x16x32_bf16 v[32:35], v[128:131], v[216:219], v[32:35]
	v_mfma_f32_16x16x32_bf16 v[40:43], v[136:139], v[216:219], v[40:43]
	v_mfma_f32_16x16x32_bf16 v[12:15], v[128:131], v[224:227], v[12:15]
	v_mfma_f32_16x16x32_bf16 v[20:23], v[136:139], v[224:227], v[20:23]
	v_mfma_f32_16x16x32_bf16 v[0:3], v[128:131], v[232:235], v[0:3]
	v_mfma_f32_16x16x32_bf16 v[4:7], v[136:139], v[232:235], v[4:7]
	v_mfma_f32_16x16x32_bf16 v[56:59], v[132:135], v[212:215], v[56:59]
	v_mfma_f32_16x16x32_bf16 v[72:75], v[140:143], v[212:215], v[72:75]
	v_mfma_f32_16x16x32_bf16 v[32:35], v[132:135], v[220:223], v[32:35]
	v_mfma_f32_16x16x32_bf16 v[40:43], v[140:143], v[220:223], v[40:43]
	v_mfma_f32_16x16x32_bf16 v[12:15], v[132:135], v[228:231], v[12:15]
	v_mfma_f32_16x16x32_bf16 v[20:23], v[140:143], v[228:231], v[20:23]
	v_mfma_f32_16x16x32_bf16 v[0:3], v[132:135], v[238:241], v[0:3]
	v_mfma_f32_16x16x32_bf16 v[4:7], v[140:143], v[238:241], v[4:7]
	v_mfma_f32_16x16x32_bf16 v[108:111], v[174:177], v[208:211], v[108:111]
	v_mfma_f32_16x16x32_bf16 v[116:119], v[182:185], v[208:211], v[116:119]
	v_mfma_f32_16x16x32_bf16 v[88:91], v[174:177], v[216:219], v[88:91]
	v_mfma_f32_16x16x32_bf16 v[100:103], v[182:185], v[216:219], v[100:103]
	v_mfma_f32_16x16x32_bf16 v[60:63], v[174:177], v[224:227], v[60:63]
	v_mfma_f32_16x16x32_bf16 v[76:79], v[182:185], v[224:227], v[76:79]
	v_mfma_f32_16x16x32_bf16 v[24:27], v[174:177], v[232:235], v[24:27]
	v_mfma_f32_16x16x32_bf16 v[44:47], v[182:185], v[232:235], v[44:47]
	v_mfma_f32_16x16x32_bf16 v[108:111], v[178:181], v[212:215], v[108:111]
	v_mfma_f32_16x16x32_bf16 v[116:119], v[186:189], v[212:215], v[116:119]
	v_mfma_f32_16x16x32_bf16 v[88:91], v[178:181], v[220:223], v[88:91]
	v_mfma_f32_16x16x32_bf16 v[100:103], v[186:189], v[220:223], v[100:103]
	v_mfma_f32_16x16x32_bf16 v[60:63], v[178:181], v[228:231], v[60:63]
	v_mfma_f32_16x16x32_bf16 v[76:79], v[186:189], v[228:231], v[76:79]
	v_mfma_f32_16x16x32_bf16 v[24:27], v[178:181], v[238:241], v[24:27]
	v_mfma_f32_16x16x32_bf16 v[44:47], v[186:189], v[238:241], v[44:47]
	s_barrier
; #define PG8_STAGE(bufoff, gbase, o0, o1) do { \
;         __builtin_amdgcn_global_load_lds((const unsigned*)((const char*)(gbase) + (o0)), (LAS unsigned*)(lds + (bufoff) + ldsw), 16, 0, 0); \
;         __builtin_amdgcn_global_load_lds((const unsigned*)((const char*)(gbase) + (o1)), (LAS unsigned*)(lds + (bufoff) + ldsw + 8192), 16, 0, 0); } while (0)
; #define PG8_LDA(dst, b, h) do { _Pragma("unroll") for (int m = 0; m < 4; ++m) _Pragma("unroll") for (int k = 0; k < 2; ++k) dst[m][k] = *(const LAS bf16x8*)(lds + PG8_SA(b, h) + aoff + m * 2048 + k * 1024); } while (0)
; #define PG8_LDB(dst, b, h) do { _Pragma("unroll") for (int n = 0; n < 2; ++n) _Pragma("unroll") for (int k = 0; k < 2; ++k) dst[n][k] = *(const LAS bf16x8*)(lds + PG8_SB(b, h) + boff + n * 2048 + k * 1024); } while (0)
; #define PG8_WAIT_V(n) asm volatile("s_waitcnt vmcnt(" #n ")" ::: "memory")
; #define PG8_WAIT_L(n) asm volatile("s_waitcnt lgkmcnt(" #n ")" ::: "memory")
; #define PG8_BAR __builtin_amdgcn_s_barrier()
; #define PG8_SCHED __builtin_amdgcn_sched_barrier(0)
; template <class Epi, class Sched, class Prob>
; __device__ __forceinline__ void gemm_phase(LAS unsigned char* lds, LAS unsigned char* lds_epi, const Prob g, const Sched& S, const Epi& E, int wid) {
;     ...
;             PG8_LDB(B0, 1, 0); PG8_LDB(B1, 1, 1); PG8_SCHED; PG8_LDA(At, 1, 0); PG8_STAGE(PG8_SA(0, 1), a2, cA10, cA11);
;             PG8_WAIT_V(8); PG8_WAIT_L(0); PG8_BAR; PG8_MMA(0, 0, At, B0); PG8_MMA(0, 1, At, B1); PG8_BAR; PG8_SCHED;
	s_add_i32 s82, 0, 0x18000
	s_add_i32 s83, 0, 0x1c000
	v_add_u32_e32 v140, s82, v194
	v_add_u32_e32 v156, s83, v194
	ds_read_b128 v[128:131], v140
	ds_read_b128 v[132:135], v140 offset:1024
	ds_read_b128 v[136:139], v140 offset:2048
	ds_read_b128 v[140:143], v140 offset:3072
	ds_read_b128 v[174:177], v156
	ds_read_b128 v[178:181], v156 offset:1024
	ds_read_b128 v[182:185], v156 offset:2048
	ds_read_b128 v[186:189], v156 offset:3072
	s_mov_b32 m0, s59
	v_lshl_add_u64 v[246:247], s[54:55], 0, v[150:151]
	ds_read_b128 v[208:211], v204 offset:32768
	ds_read_b128 v[212:215], v204 offset:33792
	ds_read_b128 v[216:219], v204 offset:34816
	ds_read_b128 v[220:223], v204 offset:35840
	ds_read_b128 v[224:227], v204 offset:36864
	ds_read_b128 v[228:231], v204 offset:37888
	ds_read_b128 v[232:235], v204 offset:38912
	ds_read_b128 v[238:241], v204 offset:39936
	global_load_lds_dwordx4 v[246:247], off
	v_lshl_add_u64 v[246:247], s[54:55], 0, v[154:155]
	s_mov_b32 m0, s60
	s_nop 0
	global_load_lds_dwordx4 v[246:247], off
	s_waitcnt vmcnt(8)
	s_waitcnt lgkmcnt(0)
	s_barrier
	s_waitcnt lgkmcnt(0)
	v_mfma_f32_16x16x32_bf16 v[80:83], v[128:131], v[208:211], v[80:83]
	v_mfma_f32_16x16x32_bf16 v[92:95], v[136:139], v[208:211], v[92:95]
	v_mfma_f32_16x16x32_bf16 v[52:55], v[128:131], v[216:219], v[52:55]
	v_mfma_f32_16x16x32_bf16 v[68:71], v[136:139], v[216:219], v[68:71]
	v_mfma_f32_16x16x32_bf16 v[28:31], v[128:131], v[224:227], v[28:31]
	v_mfma_f32_16x16x32_bf16 v[36:39], v[136:139], v[224:227], v[36:39]
	v_mfma_f32_16x16x32_bf16 v[8:11], v[128:131], v[232:235], v[8:11]
	v_mfma_f32_16x16x32_bf16 v[16:19], v[136:139], v[232:235], v[16:19]
	v_mfma_f32_16x16x32_bf16 v[80:83], v[132:135], v[212:215], v[80:83]
	v_mfma_f32_16x16x32_bf16 v[92:95], v[140:143], v[212:215], v[92:95]
	v_mfma_f32_16x16x32_bf16 v[52:55], v[132:135], v[220:223], v[52:55]
	v_mfma_f32_16x16x32_bf16 v[68:71], v[140:143], v[220:223], v[68:71]
	v_mfma_f32_16x16x32_bf16 v[28:31], v[132:135], v[228:231], v[28:31]
	v_mfma_f32_16x16x32_bf16 v[36:39], v[140:143], v[228:231], v[36:39]
	v_mfma_f32_16x16x32_bf16 v[8:11], v[132:135], v[238:241], v[8:11]
	v_mfma_f32_16x16x32_bf16 v[16:19], v[140:143], v[238:241], v[16:19]
	v_mfma_f32_16x16x32_bf16 v[120:123], v[174:177], v[208:211], v[120:123]
	v_mfma_f32_16x16x32_bf16 v[124:127], v[182:185], v[208:211], v[124:127]
	v_mfma_f32_16x16x32_bf16 v[104:107], v[174:177], v[216:219], v[104:107]
	v_mfma_f32_16x16x32_bf16 v[112:115], v[182:185], v[216:219], v[112:115]
	v_mfma_f32_16x16x32_bf16 v[84:87], v[174:177], v[224:227], v[84:87]
	v_mfma_f32_16x16x32_bf16 v[96:99], v[182:185], v[224:227], v[96:99]
	v_mfma_f32_16x16x32_bf16 v[48:51], v[174:177], v[232:235], v[48:51]
	v_mfma_f32_16x16x32_bf16 v[64:67], v[182:185], v[232:235], v[64:67]
	v_mfma_f32_16x16x32_bf16 v[120:123], v[178:181], v[212:215], v[120:123]
	v_mfma_f32_16x16x32_bf16 v[124:127], v[186:189], v[212:215], v[124:127]
	v_mfma_f32_16x16x32_bf16 v[104:107], v[178:181], v[220:223], v[104:107]
	v_mfma_f32_16x16x32_bf16 v[112:115], v[186:189], v[220:223], v[112:115]
	v_mfma_f32_16x16x32_bf16 v[84:87], v[178:181], v[228:231], v[84:87]
	v_mfma_f32_16x16x32_bf16 v[96:99], v[186:189], v[228:231], v[96:99]
	v_mfma_f32_16x16x32_bf16 v[48:51], v[178:181], v[238:241], v[48:51]
	v_mfma_f32_16x16x32_bf16 v[64:67], v[186:189], v[238:241], v[64:67]
	s_barrier
; #define PG8_STAGE(bufoff, gbase, o0, o1) do { \
;         __builtin_amdgcn_global_load_lds((const unsigned*)((const char*)(gbase) + (o0)), (LAS unsigned*)(lds + (bufoff) + ldsw), 16, 0, 0); \
;         __builtin_amdgcn_global_load_lds((const unsigned*)((const char*)(gbase) + (o1)), (LAS unsigned*)(lds + (bufoff) + ldsw + 8192), 16, 0, 0); } while (0)
; #define PG8_LDA(dst, b, h) do { _Pragma("unroll") for (int m = 0; m < 4; ++m) _Pragma("unroll") for (int k = 0; k < 2; ++k) dst[m][k] = *(const LAS bf16x8*)(lds + PG8_SA(b, h) + aoff + m * 2048 + k * 1024); } while (0)
; #define PG8_WAIT_V(n) asm volatile("s_waitcnt vmcnt(" #n ")" ::: "memory")
; #define PG8_WAIT_L(n) asm volatile("s_waitcnt lgkmcnt(" #n ")" ::: "memory")
; #define PG8_BAR __builtin_amdgcn_s_barrier()
; #define PG8_SCHED __builtin_amdgcn_sched_barrier(0)
; template <class Epi, class Sched, class Prob>
; __device__ __forceinline__ void gemm_phase(LAS unsigned char* lds, LAS unsigned char* lds_epi, const Prob g, const Sched& S, const Epi& E, int wid) {
;     ...
;             PG8_LDA(At, 1, 1); PG8_STAGE(PG8_SB(1, 0), b3, vB0, vB1); PG8_STAGE(PG8_SB(1, 1), b3 + hstepB, vB0, vB1); PG8_STAGE(PG8_SA(1, 0), a3, cA00, cA01);
;             PG8_WAIT_V(8); PG8_WAIT_L(0); PG8_BAR; PG8_MMA(1, 0, At, B0); PG8_MMA(1, 1, At, B1); PG8_BAR; PG8_SCHED;
;         }
;         if constexpr (Prob::FP8) asm volatile("s_nop 7\n\ts_nop 7\n\ts_nop 7" ::: "memory");
;         if (wr == 0) PG8_BAR;
	s_add_i32 s54, s82, s97
	v_lshl_add_u64 v[190:191], v[190:191], 0, s[20:21]
	s_mov_b32 m0, s54
	ds_read_b128 v[208:211], v204 offset:49152
	ds_read_b128 v[212:215], v204 offset:50176
	ds_read_b128 v[216:219], v204 offset:51200
	ds_read_b128 v[220:223], v204 offset:52224
	ds_read_b128 v[224:227], v204 offset:53248
	ds_read_b128 v[228:231], v204 offset:54272
	ds_read_b128 v[232:235], v204 offset:55296
	ds_read_b128 v[238:241], v204 offset:56320
	global_load_lds_dwordx4 v[190:191], off
	s_add_i32 m0, s54, 0x2000
	s_add_u32 s52, s52, 0x80080
	v_lshl_add_u64 v[190:191], v[236:237], 0, s[20:21]
	s_addc_u32 s53, s53, 0
	s_add_i32 s54, s83, s97
	global_load_lds_dwordx4 v[190:191], off
	v_lshl_add_u64 v[190:191], s[52:53], 0, v[144:145]
	s_mov_b32 m0, s54
	s_nop 0
	global_load_lds_dwordx4 v[190:191], off
	v_lshl_add_u64 v[190:191], s[52:53], 0, v[146:147]
	s_add_i32 m0, s54, 0x2000
	s_nop 0
	global_load_lds_dwordx4 v[190:191], off
	v_lshl_add_u64 v[190:191], v[242:243], 0, s[20:21]
	s_mov_b32 m0, s70
	s_nop 0
	global_load_lds_dwordx4 v[190:191], off
	v_lshl_add_u64 v[190:191], v[244:245], 0, s[20:21]
	s_mov_b32 m0, s71
	s_nop 0
	global_load_lds_dwordx4 v[190:191], off
	s_waitcnt vmcnt(8)
	s_waitcnt lgkmcnt(0)
	s_barrier
	s_waitcnt lgkmcnt(0)
	v_mfma_f32_16x16x32_bf16 v[56:59], v[128:131], v[208:211], v[56:59]
	v_mfma_f32_16x16x32_bf16 v[72:75], v[136:139], v[208:211], v[72:75]
	v_mfma_f32_16x16x32_bf16 v[32:35], v[128:131], v[216:219], v[32:35]
	v_mfma_f32_16x16x32_bf16 v[40:43], v[136:139], v[216:219], v[40:43]
	v_mfma_f32_16x16x32_bf16 v[12:15], v[128:131], v[224:227], v[12:15]
	v_mfma_f32_16x16x32_bf16 v[20:23], v[136:139], v[224:227], v[20:23]
	v_mfma_f32_16x16x32_bf16 v[0:3], v[128:131], v[232:235], v[0:3]
	v_mfma_f32_16x16x32_bf16 v[4:7], v[136:139], v[232:235], v[4:7]
	v_mfma_f32_16x16x32_bf16 v[56:59], v[132:135], v[212:215], v[56:59]
	v_mfma_f32_16x16x32_bf16 v[72:75], v[140:143], v[212:215], v[72:75]
	v_mfma_f32_16x16x32_bf16 v[32:35], v[132:135], v[220:223], v[32:35]
	v_mfma_f32_16x16x32_bf16 v[40:43], v[140:143], v[220:223], v[40:43]
	v_mfma_f32_16x16x32_bf16 v[12:15], v[132:135], v[228:231], v[12:15]
	v_mfma_f32_16x16x32_bf16 v[20:23], v[140:143], v[228:231], v[20:23]
	v_mfma_f32_16x16x32_bf16 v[0:3], v[132:135], v[238:241], v[0:3]
	v_mfma_f32_16x16x32_bf16 v[4:7], v[140:143], v[238:241], v[4:7]
	v_mfma_f32_16x16x32_bf16 v[108:111], v[174:177], v[208:211], v[108:111]
	v_mfma_f32_16x16x32_bf16 v[116:119], v[182:185], v[208:211], v[116:119]
	v_mfma_f32_16x16x32_bf16 v[88:91], v[174:177], v[216:219], v[88:91]
	v_mfma_f32_16x16x32_bf16 v[100:103], v[182:185], v[216:219], v[100:103]
	v_mfma_f32_16x16x32_bf16 v[60:63], v[174:177], v[224:227], v[60:63]
	v_mfma_f32_16x16x32_bf16 v[76:79], v[182:185], v[224:227], v[76:79]
	v_mfma_f32_16x16x32_bf16 v[24:27], v[174:177], v[232:235], v[24:27]
	v_mfma_f32_16x16x32_bf16 v[44:47], v[182:185], v[232:235], v[44:47]
	v_mfma_f32_16x16x32_bf16 v[108:111], v[178:181], v[212:215], v[108:111]
	v_mfma_f32_16x16x32_bf16 v[116:119], v[186:189], v[212:215], v[116:119]
	v_mfma_f32_16x16x32_bf16 v[88:91], v[178:181], v[220:223], v[88:91]
	v_mfma_f32_16x16x32_bf16 v[100:103], v[186:189], v[220:223], v[100:103]
	v_mfma_f32_16x16x32_bf16 v[60:63], v[178:181], v[228:231], v[60:63]
	v_mfma_f32_16x16x32_bf16 v[76:79], v[186:189], v[228:231], v[76:79]
	v_mfma_f32_16x16x32_bf16 v[24:27], v[178:181], v[238:241], v[24:27]
	v_mfma_f32_16x16x32_bf16 v[44:47], v[186:189], v[238:241], v[44:47]
	s_barrier
	s_add_i32 s81, s81, 2
	s_add_u32 s14, s14, 0x100
	s_addc_u32 s15, s15, 0
	s_add_u32 s79, s79, 0x100
	s_addc_u32 s80, s80, 0
	s_cmp_gt_u32 s81, 29
	s_cbranch_scc0 .LBB0_262
	s_setprio 0
	v_readlane_b32 s14, v254, 27
	v_readlane_b32 s15, v254, 28
	s_and_b64 vcc, exec, s[14:15]
	s_cbranch_vccz .LBB0_265
	s_barrier

; #define PG8_STAGE(bufoff, gbase, o0, o1) do { \
;         __builtin_amdgcn_global_load_lds((const unsigned*)((const char*)(gbase) + (o0)), (LAS unsigned*)(lds + (bufoff) + ldsw), 16, 0, 0); \
;         __builtin_amdgcn_global_load_lds((const unsigned*)((const char*)(gbase) + (o1)), (LAS unsigned*)(lds + (bufoff) + ldsw + 8192), 16, 0, 0); } while (0)
; #define PG8_LDA(dst, b, h) do { _Pragma("unroll") for (int m = 0; m < 4; ++m) _Pragma("unroll") for (int k = 0; k < 2; ++k) dst[m][k] = *(const LAS bf16x8*)(lds + PG8_SA(b, h) + aoff + m * 2048 + k * 1024); } while (0)
; #define PG8_LDB(dst, b, h) do { _Pragma("unroll") for (int n = 0; n < 2; ++n) _Pragma("unroll") for (int k = 0; k < 2; ++k) dst[n][k] = *(const LAS bf16x8*)(lds + PG8_SB(b, h) + boff + n * 2048 + k * 1024); } while (0)
; #define PG8_WAIT_V(n) asm volatile("s_waitcnt vmcnt(" #n ")" ::: "memory")
; #define PG8_WAIT_L(n) asm volatile("s_waitcnt lgkmcnt(" #n ")" ::: "memory")
; #define PG8_BAR __builtin_amdgcn_s_barrier()
; #define PG8_SCHED __builtin_amdgcn_sched_barrier(0)
; template <class Epi, class Sched, class Prob>
; __device__ __forceinline__ void gemm_phase(LAS unsigned char* lds, LAS unsigned char* lds_epi, const Prob g, const Sched& S, const Epi& E, int wid) {
;     ...
;         const bool has_next = S.next(ui + 1, nxt);
;         const char* nA = has_next ? g.a_base(nxt) : cA; const char* nB = has_next ? g.b_base(nxt) : cB;
; _Pragma("clang loop unroll(disable)")
;         for (int t = 0; t < nt; t += 2) {
;             const bool last = (t == nt - 2);
;             const char* a1 = cA + (size_t)(t + 1) * kstep;
;             const char* a2 = last ? nA : cA + (size_t)(t + 2) * kstep; const char* b2 = last ? nB : cB + (size_t)(t + 2) * kstep;
;             const char* a3 = a2 + kstep; const char* b3 = b2 + kstep;
;             PG8_LDB(B0, 0, 0); PG8_LDB(B1, 0, 1); PG8_SCHED; PG8_LDA(At, 0, 0); PG8_STAGE(PG8_SA(1, 1), a1, cA10, cA11);
;             PG8_WAIT_V(8); PG8_WAIT_L(0); PG8_BAR; PG8_MMA(0, 0, At, B0); PG8_MMA(0, 1, At, B1); PG8_BAR; PG8_SCHED;
.LBB0_1155:
	s_ashr_i32 s25, s24, 31
	s_lshl_b64 s[28:29], s[24:25], 20
	s_add_u32 s28, s44, s28
	s_addc_u32 s29, s45, s29
	s_and_b64 s[30:31], s[34:35], exec
	s_cselect_b32 s25, s29, s39
	s_cselect_b32 s27, s28, s38
	s_ashr_i32 s23, s22, 31
	s_lshl_b64 s[30:31], s[22:23], 20
	s_add_u32 s30, s46, s30
	s_addc_u32 s31, s47, s31
	s_and_b64 s[42:43], s[34:35], exec
	s_cselect_b32 s23, s31, s41
	s_cselect_b32 s37, s30, s40
	s_add_u32 s38, s38, 0x80
	s_addc_u32 s39, s39, 0
	s_add_u32 s66, s40, 0x100
	s_addc_u32 s67, s41, 0
	s_mov_b32 s68, -2
	s_cmp_lt_u32 s91, 0x100
	s_cbranch_scc1 .Lyoung_1
	s_setprio 1
.Lyoung_1:
.LBB0_1156:
	v_add_u32_e32 v146, s62, v149
	ds_read_b128 v[158:161], v146
	ds_read_b128 v[162:165], v146 offset:1024
	ds_read_b128 v[166:169], v146 offset:2048
	ds_read_b128 v[170:173], v146 offset:3072
	v_add_u32_e32 v146, s63, v149
	ds_read_b128 v[174:177], v146
	ds_read_b128 v[178:181], v146 offset:1024
	ds_read_b128 v[182:185], v146 offset:2048
	ds_read_b128 v[186:189], v146 offset:3072
	s_add_u32 s40, s38, 0x80
	s_addc_u32 s41, s39, 0
	s_cmp_eq_u32 s68, 28
	s_cselect_b32 s43, s25, s41
	s_cselect_b32 s42, s27, s40
	s_cselect_b32 s41, s23, s67
	s_cselect_b32 s40, s37, s66
	v_lshl_add_u64 v[146:147], s[38:39], 0, v[140:141]
	s_add_i32 m0, s53, 0xc000
	ds_read_b128 v[190:193], v153
	ds_read_b128 v[194:197], v153 offset:1024
	ds_read_b128 v[198:201], v153 offset:2048
	ds_read_b128 v[202:205], v153 offset:3072
	ds_read_b128 v[206:209], v153 offset:4096
	ds_read_b128 v[210:213], v153 offset:5120
	ds_read_b128 v[214:217], v153 offset:6144
	ds_read_b128 v[218:221], v153 offset:7168
	global_load_lds_dwordx4 v[146:147], off
	v_lshl_add_u64 v[146:147], s[38:39], 0, v[142:143]
	s_add_i32 m0, s53, 0xe000
	s_nop 0
	global_load_lds_dwordx4 v[146:147], off
	s_waitcnt vmcnt(8)
	s_waitcnt lgkmcnt(0)
	s_barrier
	s_waitcnt lgkmcnt(0)
	v_mfma_f32_16x16x32_bf16 v[124:127], v[158:161], v[190:193], v[124:127]
	v_mfma_f32_16x16x32_bf16 v[120:123], v[166:169], v[190:193], v[120:123]
	v_mfma_f32_16x16x32_bf16 v[108:111], v[158:161], v[198:201], v[108:111]
	v_mfma_f32_16x16x32_bf16 v[104:107], v[166:169], v[198:201], v[104:107]
	v_mfma_f32_16x16x32_bf16 v[92:95], v[158:161], v[206:209], v[92:95]
	v_mfma_f32_16x16x32_bf16 v[88:91], v[166:169], v[206:209], v[88:91]
	v_mfma_f32_16x16x32_bf16 v[76:79], v[158:161], v[214:217], v[76:79]
	v_mfma_f32_16x16x32_bf16 v[72:75], v[166:169], v[214:217], v[72:75]
	v_mfma_f32_16x16x32_bf16 v[124:127], v[162:165], v[194:197], v[124:127]
	v_mfma_f32_16x16x32_bf16 v[120:123], v[170:173], v[194:197], v[120:123]
	v_mfma_f32_16x16x32_bf16 v[108:111], v[162:165], v[202:205], v[108:111]
	v_mfma_f32_16x16x32_bf16 v[104:107], v[170:173], v[202:205], v[104:107]
	v_mfma_f32_16x16x32_bf16 v[92:95], v[162:165], v[210:213], v[92:95]
	v_mfma_f32_16x16x32_bf16 v[88:91], v[170:173], v[210:213], v[88:91]
	v_mfma_f32_16x16x32_bf16 v[76:79], v[162:165], v[218:221], v[76:79]
	v_mfma_f32_16x16x32_bf16 v[72:75], v[170:173], v[218:221], v[72:75]
	v_mfma_f32_16x16x32_bf16 v[116:119], v[174:177], v[190:193], v[116:119]
	v_mfma_f32_16x16x32_bf16 v[112:115], v[182:185], v[190:193], v[112:115]
	v_mfma_f32_16x16x32_bf16 v[100:103], v[174:177], v[198:201], v[100:103]
	v_mfma_f32_16x16x32_bf16 v[96:99], v[182:185], v[198:201], v[96:99]
	v_mfma_f32_16x16x32_bf16 v[84:87], v[174:177], v[206:209], v[84:87]
	v_mfma_f32_16x16x32_bf16 v[80:83], v[182:185], v[206:209], v[80:83]
	v_mfma_f32_16x16x32_bf16 v[68:71], v[174:177], v[214:217], v[68:71]
	v_mfma_f32_16x16x32_bf16 v[64:67], v[182:185], v[214:217], v[64:67]
	v_mfma_f32_16x16x32_bf16 v[116:119], v[178:181], v[194:197], v[116:119]
	v_mfma_f32_16x16x32_bf16 v[112:115], v[186:189], v[194:197], v[112:115]
	v_mfma_f32_16x16x32_bf16 v[100:103], v[178:181], v[202:205], v[100:103]
	v_mfma_f32_16x16x32_bf16 v[96:99], v[186:189], v[202:205], v[96:99]
	v_mfma_f32_16x16x32_bf16 v[84:87], v[178:181], v[210:213], v[84:87]
	v_mfma_f32_16x16x32_bf16 v[80:83], v[186:189], v[210:213], v[80:83]
	v_mfma_f32_16x16x32_bf16 v[68:71], v[178:181], v[218:221], v[68:71]
	v_mfma_f32_16x16x32_bf16 v[64:67], v[186:189], v[218:221], v[64:67]
	s_barrier
	s_add_i32 s69, s62, s97
	v_lshl_add_u64 v[146:147], s[40:41], 0, v[130:131]
	s_mov_b32 m0, s69
	ds_read_b128 v[190:193], v153 offset:16384
	ds_read_b128 v[194:197], v153 offset:17408
	ds_read_b128 v[198:201], v153 offset:18432
	ds_read_b128 v[202:205], v153 offset:19456
	ds_read_b128 v[206:209], v153 offset:20480
	ds_read_b128 v[210:213], v153 offset:21504
	ds_read_b128 v[214:217], v153 offset:22528
	ds_read_b128 v[218:221], v153 offset:23552
	global_load_lds_dwordx4 v[146:147], off
	s_add_i32 m0, s69, 0x2000
	s_add_u32 s70, s40, 0x80000
	v_lshl_add_u64 v[222:223], s[40:41], 0, v[128:129]
	s_addc_u32 s71, s41, 0
	s_add_i32 s69, s63, s97
	global_load_lds_dwordx4 v[222:223], off
	v_lshl_add_u64 v[224:225], s[70:71], 0, v[130:131]
	s_mov_b32 m0, s69
	v_lshl_add_u64 v[226:227], s[42:43], 0, v[128:129]
	global_load_lds_dwordx4 v[224:225], off
	v_lshl_add_u64 v[224:225], s[70:71], 0, v[128:129]
	s_add_i32 m0, s69, 0x2000
	s_nop 0
	global_load_lds_dwordx4 v[224:225], off
	v_lshl_add_u64 v[224:225], s[42:43], 0, v[130:131]
	s_mov_b32 m0, s53
	s_nop 0
	global_load_lds_dwordx4 v[224:225], off
	s_mov_b32 m0, s54
	s_nop 0
	global_load_lds_dwordx4 v[226:227], off
	s_waitcnt vmcnt(8)
	s_waitcnt lgkmcnt(0)
	s_barrier
; #define PG8_STAGE(bufoff, gbase, o0, o1) do { \
;         __builtin_amdgcn_global_load_lds((const unsigned*)((const char*)(gbase) + (o0)), (LAS unsigned*)(lds + (bufoff) + ldsw), 16, 0, 0); \
;         __builtin_amdgcn_global_load_lds((const unsigned*)((const char*)(gbase) + (o1)), (LAS unsigned*)(lds + (bufoff) + ldsw + 8192), 16, 0, 0); } while (0)
; #define PG8_LDA(dst, b, h) do { _Pragma("unroll") for (int m = 0; m < 4; ++m) _Pragma("unroll") for (int k = 0; k < 2; ++k) dst[m][k] = *(const LAS bf16x8*)(lds + PG8_SA(b, h) + aoff + m * 2048 + k * 1024); } while (0)
; #define PG8_LDB(dst, b, h) do { _Pragma("unroll") for (int n = 0; n < 2; ++n) _Pragma("unroll") for (int k = 0; k < 2; ++k) dst[n][k] = *(const LAS bf16x8*)(lds + PG8_SB(b, h) + boff + n * 2048 + k * 1024); } while (0)
; #define PG8_WAIT_V(n) asm volatile("s_waitcnt vmcnt(" #n ")" ::: "memory")
; #define PG8_WAIT_L(n) asm volatile("s_waitcnt lgkmcnt(" #n ")" ::: "memory")
; #define PG8_BAR __builtin_amdgcn_s_barrier()
; #define PG8_SCHED __builtin_amdgcn_sched_barrier(0)
; template <class Epi, class Sched, class Prob>
; __device__ __forceinline__ void gemm_phase(LAS unsigned char* lds, LAS unsigned char* lds_epi, const Prob g, const Sched& S, const Epi& E, int wid) {
;     ...
;             PG8_WAIT_V(8); PG8_WAIT_L(0); PG8_BAR; PG8_MMA(1, 0, At, B0); PG8_MMA(1, 1, At, B1); PG8_BAR; PG8_SCHED;
;             PG8_LDB(B0, 1, 0); PG8_LDB(B1, 1, 1); PG8_SCHED; PG8_LDA(At, 1, 0); PG8_STAGE(PG8_SA(0, 1), a2, cA10, cA11);
;             PG8_WAIT_V(8); PG8_WAIT_L(0); PG8_BAR; PG8_MMA(0, 0, At, B0); PG8_MMA(0, 1, At, B1); PG8_BAR; PG8_SCHED;
	s_waitcnt lgkmcnt(0)
	v_mfma_f32_16x16x32_bf16 v[60:63], v[158:161], v[190:193], v[60:63]
	v_mfma_f32_16x16x32_bf16 v[56:59], v[166:169], v[190:193], v[56:59]
	v_mfma_f32_16x16x32_bf16 v[44:47], v[158:161], v[198:201], v[44:47]
	v_mfma_f32_16x16x32_bf16 v[40:43], v[166:169], v[198:201], v[40:43]
	v_mfma_f32_16x16x32_bf16 v[28:31], v[158:161], v[206:209], v[28:31]
	v_mfma_f32_16x16x32_bf16 v[24:27], v[166:169], v[206:209], v[24:27]
	v_mfma_f32_16x16x32_bf16 v[0:3], v[158:161], v[214:217], v[0:3]
	v_mfma_f32_16x16x32_bf16 v[12:15], v[166:169], v[214:217], v[12:15]
	v_mfma_f32_16x16x32_bf16 v[60:63], v[162:165], v[194:197], v[60:63]
	v_mfma_f32_16x16x32_bf16 v[56:59], v[170:173], v[194:197], v[56:59]
	v_mfma_f32_16x16x32_bf16 v[44:47], v[162:165], v[202:205], v[44:47]
	v_mfma_f32_16x16x32_bf16 v[40:43], v[170:173], v[202:205], v[40:43]
	v_mfma_f32_16x16x32_bf16 v[28:31], v[162:165], v[210:213], v[28:31]
	v_mfma_f32_16x16x32_bf16 v[24:27], v[170:173], v[210:213], v[24:27]
	v_mfma_f32_16x16x32_bf16 v[0:3], v[162:165], v[218:221], v[0:3]
	v_mfma_f32_16x16x32_bf16 v[12:15], v[170:173], v[218:221], v[12:15]
	v_mfma_f32_16x16x32_bf16 v[52:55], v[174:177], v[190:193], v[52:55]
	v_mfma_f32_16x16x32_bf16 v[48:51], v[182:185], v[190:193], v[48:51]
	v_mfma_f32_16x16x32_bf16 v[36:39], v[174:177], v[198:201], v[36:39]
	v_mfma_f32_16x16x32_bf16 v[32:35], v[182:185], v[198:201], v[32:35]
	v_mfma_f32_16x16x32_bf16 v[20:23], v[174:177], v[206:209], v[20:23]
	v_mfma_f32_16x16x32_bf16 v[16:19], v[182:185], v[206:209], v[16:19]
	v_mfma_f32_16x16x32_bf16 v[8:11], v[174:177], v[214:217], v[8:11]
	v_mfma_f32_16x16x32_bf16 v[4:7], v[182:185], v[214:217], v[4:7]
	v_mfma_f32_16x16x32_bf16 v[52:55], v[178:181], v[194:197], v[52:55]
	v_mfma_f32_16x16x32_bf16 v[48:51], v[186:189], v[194:197], v[48:51]
	v_mfma_f32_16x16x32_bf16 v[36:39], v[178:181], v[202:205], v[36:39]
	v_mfma_f32_16x16x32_bf16 v[32:35], v[186:189], v[202:205], v[32:35]
	v_mfma_f32_16x16x32_bf16 v[20:23], v[178:181], v[210:213], v[20:23]
	v_mfma_f32_16x16x32_bf16 v[16:19], v[186:189], v[210:213], v[16:19]
	v_mfma_f32_16x16x32_bf16 v[8:11], v[178:181], v[218:221], v[8:11]
	v_mfma_f32_16x16x32_bf16 v[4:7], v[186:189], v[218:221], v[4:7]
	s_barrier
	s_add_i32 s69, 0, 0x18000
	v_add_u32_e32 v157, s69, v149
	s_add_i32 s70, 0, 0x1c000
	ds_read_b128 v[158:161], v157
	ds_read_b128 v[162:165], v157 offset:1024
	ds_read_b128 v[166:169], v157 offset:2048
	ds_read_b128 v[170:173], v157 offset:3072
	v_add_u32_e32 v157, s70, v149
	ds_read_b128 v[174:177], v157
	ds_read_b128 v[178:181], v157 offset:1024
	ds_read_b128 v[182:185], v157 offset:2048
	ds_read_b128 v[186:189], v157 offset:3072
	s_mov_b32 m0, s55
	v_lshl_add_u64 v[228:229], s[42:43], 0, v[132:133]
	ds_read_b128 v[190:193], v153 offset:32768
	ds_read_b128 v[194:197], v153 offset:33792
	ds_read_b128 v[198:201], v153 offset:34816
	ds_read_b128 v[202:205], v153 offset:35840
	ds_read_b128 v[206:209], v153 offset:36864
	ds_read_b128 v[210:213], v153 offset:37888
	ds_read_b128 v[214:217], v153 offset:38912
	ds_read_b128 v[218:221], v153 offset:39936
	global_load_lds_dwordx4 v[228:229], off
	v_lshl_add_u64 v[228:229], s[42:43], 0, v[134:135]
	s_mov_b32 m0, s56
	s_nop 0
	global_load_lds_dwordx4 v[228:229], off
	s_waitcnt vmcnt(8)
	s_waitcnt lgkmcnt(0)
	s_barrier
	s_waitcnt lgkmcnt(0)
	v_mfma_f32_16x16x32_bf16 v[124:127], v[158:161], v[190:193], v[124:127]
	v_mfma_f32_16x16x32_bf16 v[120:123], v[166:169], v[190:193], v[120:123]
	v_mfma_f32_16x16x32_bf16 v[108:111], v[158:161], v[198:201], v[108:111]
	v_mfma_f32_16x16x32_bf16 v[104:107], v[166:169], v[198:201], v[104:107]
	v_mfma_f32_16x16x32_bf16 v[92:95], v[158:161], v[206:209], v[92:95]
	v_mfma_f32_16x16x32_bf16 v[88:91], v[166:169], v[206:209], v[88:91]
	v_mfma_f32_16x16x32_bf16 v[76:79], v[158:161], v[214:217], v[76:79]
	v_mfma_f32_16x16x32_bf16 v[72:75], v[166:169], v[214:217], v[72:75]
	v_mfma_f32_16x16x32_bf16 v[124:127], v[162:165], v[194:197], v[124:127]
	v_mfma_f32_16x16x32_bf16 v[120:123], v[170:173], v[194:197], v[120:123]
	v_mfma_f32_16x16x32_bf16 v[108:111], v[162:165], v[202:205], v[108:111]
	v_mfma_f32_16x16x32_bf16 v[104:107], v[170:173], v[202:205], v[104:107]
	v_mfma_f32_16x16x32_bf16 v[92:95], v[162:165], v[210:213], v[92:95]
	v_mfma_f32_16x16x32_bf16 v[88:91], v[170:173], v[210:213], v[88:91]
	v_mfma_f32_16x16x32_bf16 v[76:79], v[162:165], v[218:221], v[76:79]
	v_mfma_f32_16x16x32_bf16 v[72:75], v[170:173], v[218:221], v[72:75]
	v_mfma_f32_16x16x32_bf16 v[116:119], v[174:177], v[190:193], v[116:119]
	v_mfma_f32_16x16x32_bf16 v[112:115], v[182:185], v[190:193], v[112:115]
	v_mfma_f32_16x16x32_bf16 v[100:103], v[174:177], v[198:201], v[100:103]
	v_mfma_f32_16x16x32_bf16 v[96:99], v[182:185], v[198:201], v[96:99]
	v_mfma_f32_16x16x32_bf16 v[84:87], v[174:177], v[206:209], v[84:87]
	v_mfma_f32_16x16x32_bf16 v[80:83], v[182:185], v[206:209], v[80:83]
	v_mfma_f32_16x16x32_bf16 v[68:71], v[174:177], v[214:217], v[68:71]
	v_mfma_f32_16x16x32_bf16 v[64:67], v[182:185], v[214:217], v[64:67]
	v_mfma_f32_16x16x32_bf16 v[116:119], v[178:181], v[194:197], v[116:119]
	v_mfma_f32_16x16x32_bf16 v[112:115], v[186:189], v[194:197], v[112:115]
	v_mfma_f32_16x16x32_bf16 v[100:103], v[178:181], v[202:205], v[100:103]
	v_mfma_f32_16x16x32_bf16 v[96:99], v[186:189], v[202:205], v[96:99]
	v_mfma_f32_16x16x32_bf16 v[84:87], v[178:181], v[210:213], v[84:87]
	v_mfma_f32_16x16x32_bf16 v[80:83], v[186:189], v[210:213], v[80:83]
	v_mfma_f32_16x16x32_bf16 v[68:71], v[178:181], v[218:221], v[68:71]
	v_mfma_f32_16x16x32_bf16 v[64:67], v[186:189], v[218:221], v[64:67]
	s_barrier
; #define PG8_STAGE(bufoff, gbase, o0, o1) do { \
;         __builtin_amdgcn_global_load_lds((const unsigned*)((const char*)(gbase) + (o0)), (LAS unsigned*)(lds + (bufoff) + ldsw), 16, 0, 0); \
;         __builtin_amdgcn_global_load_lds((const unsigned*)((const char*)(gbase) + (o1)), (LAS unsigned*)(lds + (bufoff) + ldsw + 8192), 16, 0, 0); } while (0)
; #define PG8_LDA(dst, b, h) do { _Pragma("unroll") for (int m = 0; m < 4; ++m) _Pragma("unroll") for (int k = 0; k < 2; ++k) dst[m][k] = *(const LAS bf16x8*)(lds + PG8_SA(b, h) + aoff + m * 2048 + k * 1024); } while (0)
; #define PG8_WAIT_V(n) asm volatile("s_waitcnt vmcnt(" #n ")" ::: "memory")
; #define PG8_WAIT_L(n) asm volatile("s_waitcnt lgkmcnt(" #n ")" ::: "memory")
; #define PG8_BAR __builtin_amdgcn_s_barrier()
; #define PG8_SCHED __builtin_amdgcn_sched_barrier(0)
; template <class Epi, class Sched, class Prob>
; __device__ __forceinline__ void gemm_phase(LAS unsigned char* lds, LAS unsigned char* lds_epi, const Prob g, const Sched& S, const Epi& E, int wid) {
;     ...
;             PG8_LDA(At, 1, 1); PG8_STAGE(PG8_SB(1, 0), b3, vB0, vB1); PG8_STAGE(PG8_SB(1, 1), b3 + hstepB, vB0, vB1); PG8_STAGE(PG8_SA(1, 0), a3, cA00, cA01);
;             PG8_WAIT_V(8); PG8_WAIT_L(0); PG8_BAR; PG8_MMA(1, 0, At, B0); PG8_MMA(1, 1, At, B1); PG8_BAR; PG8_SCHED;
;         }
;         if constexpr (Prob::FP8) asm volatile("s_nop 7\n\ts_nop 7\n\ts_nop 7" ::: "memory");
;         if (wr == 0) PG8_BAR;
	s_add_i32 s42, s69, s97
	v_lshl_add_u64 v[146:147], v[146:147], 0, s[16:17]
	s_mov_b32 m0, s42
	ds_read_b128 v[190:193], v153 offset:49152
	ds_read_b128 v[194:197], v153 offset:50176
	ds_read_b128 v[198:201], v153 offset:51200
	ds_read_b128 v[202:205], v153 offset:52224
	ds_read_b128 v[206:209], v153 offset:53248
	ds_read_b128 v[210:213], v153 offset:54272
	ds_read_b128 v[214:217], v153 offset:55296
	ds_read_b128 v[218:221], v153 offset:56320
	global_load_lds_dwordx4 v[146:147], off
	s_add_i32 m0, s42, 0x2000
	s_add_u32 s40, s40, 0x80080
	v_lshl_add_u64 v[146:147], v[222:223], 0, s[16:17]
	s_addc_u32 s41, s41, 0
	s_add_i32 s42, s70, s97
	global_load_lds_dwordx4 v[146:147], off
	v_lshl_add_u64 v[146:147], s[40:41], 0, v[130:131]
	s_mov_b32 m0, s42
	s_nop 0
	global_load_lds_dwordx4 v[146:147], off
	v_lshl_add_u64 v[146:147], s[40:41], 0, v[128:129]
	s_add_i32 m0, s42, 0x2000
	s_nop 0
	global_load_lds_dwordx4 v[146:147], off
	v_lshl_add_u64 v[146:147], v[224:225], 0, s[16:17]
	s_mov_b32 m0, s60
	s_nop 0
	global_load_lds_dwordx4 v[146:147], off
	v_lshl_add_u64 v[146:147], v[226:227], 0, s[16:17]
	s_mov_b32 m0, s61
	s_nop 0
	global_load_lds_dwordx4 v[146:147], off
	s_waitcnt vmcnt(8)
	s_waitcnt lgkmcnt(0)
	s_barrier
	s_waitcnt lgkmcnt(0)
	v_mfma_f32_16x16x32_bf16 v[60:63], v[158:161], v[190:193], v[60:63]
	v_mfma_f32_16x16x32_bf16 v[56:59], v[166:169], v[190:193], v[56:59]
	v_mfma_f32_16x16x32_bf16 v[44:47], v[158:161], v[198:201], v[44:47]
	v_mfma_f32_16x16x32_bf16 v[40:43], v[166:169], v[198:201], v[40:43]
	v_mfma_f32_16x16x32_bf16 v[28:31], v[158:161], v[206:209], v[28:31]
	v_mfma_f32_16x16x32_bf16 v[24:27], v[166:169], v[206:209], v[24:27]
	v_mfma_f32_16x16x32_bf16 v[0:3], v[158:161], v[214:217], v[0:3]
	v_mfma_f32_16x16x32_bf16 v[12:15], v[166:169], v[214:217], v[12:15]
	v_mfma_f32_16x16x32_bf16 v[60:63], v[162:165], v[194:197], v[60:63]
	v_mfma_f32_16x16x32_bf16 v[56:59], v[170:173], v[194:197], v[56:59]
	v_mfma_f32_16x16x32_bf16 v[44:47], v[162:165], v[202:205], v[44:47]
	v_mfma_f32_16x16x32_bf16 v[40:43], v[170:173], v[202:205], v[40:43]
	v_mfma_f32_16x16x32_bf16 v[28:31], v[162:165], v[210:213], v[28:31]
	v_mfma_f32_16x16x32_bf16 v[24:27], v[170:173], v[210:213], v[24:27]
	v_mfma_f32_16x16x32_bf16 v[0:3], v[162:165], v[218:221], v[0:3]
	v_mfma_f32_16x16x32_bf16 v[12:15], v[170:173], v[218:221], v[12:15]
	v_mfma_f32_16x16x32_bf16 v[52:55], v[174:177], v[190:193], v[52:55]
	v_mfma_f32_16x16x32_bf16 v[48:51], v[182:185], v[190:193], v[48:51]
	v_mfma_f32_16x16x32_bf16 v[36:39], v[174:177], v[198:201], v[36:39]
	v_mfma_f32_16x16x32_bf16 v[32:35], v[182:185], v[198:201], v[32:35]
	v_mfma_f32_16x16x32_bf16 v[20:23], v[174:177], v[206:209], v[20:23]
	v_mfma_f32_16x16x32_bf16 v[16:19], v[182:185], v[206:209], v[16:19]
	v_mfma_f32_16x16x32_bf16 v[8:11], v[174:177], v[214:217], v[8:11]
	v_mfma_f32_16x16x32_bf16 v[4:7], v[182:185], v[214:217], v[4:7]
	v_mfma_f32_16x16x32_bf16 v[52:55], v[178:181], v[194:197], v[52:55]
	v_mfma_f32_16x16x32_bf16 v[48:51], v[186:189], v[194:197], v[48:51]
	v_mfma_f32_16x16x32_bf16 v[36:39], v[178:181], v[202:205], v[36:39]
	v_mfma_f32_16x16x32_bf16 v[32:35], v[186:189], v[202:205], v[32:35]
	v_mfma_f32_16x16x32_bf16 v[20:23], v[178:181], v[210:213], v[20:23]
	v_mfma_f32_16x16x32_bf16 v[16:19], v[186:189], v[210:213], v[16:19]
	v_mfma_f32_16x16x32_bf16 v[8:11], v[178:181], v[218:221], v[8:11]
	v_mfma_f32_16x16x32_bf16 v[4:7], v[186:189], v[218:221], v[4:7]
	s_barrier
	s_add_i32 s68, s68, 2
	s_add_u32 s38, s38, 0x100
	s_addc_u32 s39, s39, 0
	s_add_u32 s66, s66, 0x100
	s_addc_u32 s67, s67, 0
	s_cmp_gt_u32 s68, 29
	s_cbranch_scc0 .LBB0_1156
	s_setprio 0
	v_readlane_b32 s38, v254, 27
	v_readlane_b32 s39, v254, 28
	s_and_b64 vcc, exec, s[38:39]
	s_cbranch_vccz .LBB0_1159
	s_barrier

; #define PG8_STAGE(bufoff, gbase, o0, o1) do { \
;         __builtin_amdgcn_global_load_lds((const unsigned*)((const char*)(gbase) + (o0)), (LAS unsigned*)(lds + (bufoff) + ldsw), 16, 0, 0); \
;         __builtin_amdgcn_global_load_lds((const unsigned*)((const char*)(gbase) + (o1)), (LAS unsigned*)(lds + (bufoff) + ldsw + 8192), 16, 0, 0); } while (0)
; #define PG8_LDA(dst, b, h) do { _Pragma("unroll") for (int m = 0; m < 4; ++m) _Pragma("unroll") for (int k = 0; k < 2; ++k) dst[m][k] = *(const LAS bf16x8*)(lds + PG8_SA(b, h) + aoff + m * 2048 + k * 1024); } while (0)
; #define PG8_LDB(dst, b, h) do { _Pragma("unroll") for (int n = 0; n < 2; ++n) _Pragma("unroll") for (int k = 0; k < 2; ++k) dst[n][k] = *(const LAS bf16x8*)(lds + PG8_SB(b, h) + boff + n * 2048 + k * 1024); } while (0)
; #define PG8_WAIT_V(n) asm volatile("s_waitcnt vmcnt(" #n ")" ::: "memory")
; #define PG8_WAIT_L(n) asm volatile("s_waitcnt lgkmcnt(" #n ")" ::: "memory")
; #define PG8_BAR __builtin_amdgcn_s_barrier()
; #define PG8_SCHED __builtin_amdgcn_sched_barrier(0)
; template <class Epi, class Sched, class Prob>
; __device__ __forceinline__ void gemm_phase(LAS unsigned char* lds, LAS unsigned char* lds_epi, const Prob g, const Sched& S, const Epi& E, int wid) {
;     ...
;         const bool has_next = S.next(ui + 1, nxt);
;         const char* nA = has_next ? g.a_base(nxt) : cA; const char* nB = has_next ? g.b_base(nxt) : cB;
; _Pragma("clang loop unroll(disable)")
;         for (int t = 0; t < nt; t += 2) {
;             const bool last = (t == nt - 2);
;             const char* a1 = cA + (size_t)(t + 1) * kstep;
;             const char* a2 = last ? nA : cA + (size_t)(t + 2) * kstep; const char* b2 = last ? nB : cB + (size_t)(t + 2) * kstep;
;             const char* a3 = a2 + kstep; const char* b3 = b2 + kstep;
;             PG8_LDB(B0, 0, 0); PG8_LDB(B1, 0, 1); PG8_SCHED; PG8_LDA(At, 0, 0); PG8_STAGE(PG8_SA(1, 1), a1, cA10, cA11);
;             PG8_WAIT_V(8); PG8_WAIT_L(0); PG8_BAR; PG8_MMA(0, 0, At, B0); PG8_MMA(0, 1, At, B1); PG8_BAR; PG8_SCHED;
;             PG8_LDA(At, 0, 1); PG8_STAGE(PG8_SB(0, 0), b2, vB0, vB1); PG8_STAGE(PG8_SB(0, 1), b2 + hstepB, vB0, vB1); PG8_STAGE(PG8_SA(0, 0), a2, cA00, cA01);
;             PG8_WAIT_V(8); PG8_WAIT_L(0); PG8_BAR; PG8_MMA(1, 0, At, B0); PG8_MMA(1, 1, At, B1); PG8_BAR; PG8_SCHED;
.LBB0_1247:
	s_ashr_i32 s3, s2, 31
	s_lshl_b64 s[24:25], s[2:3], 19
	s_add_u32 s24, s36, s24
	s_addc_u32 s25, s37, s25
	s_and_b64 s[26:27], s[22:23], exec
	s_cselect_b32 s3, s25, s11
	s_cselect_b32 s54, s24, s10
	s_ashr_i32 s21, s20, 31
	s_lshl_b64 s[26:27], s[20:21], 19
	s_add_u32 s26, s40, s26
	s_addc_u32 s27, s41, s27
	s_and_b64 s[34:35], s[22:23], exec
	s_cselect_b32 s21, s27, s31
	s_cselect_b32 s55, s26, s30
	s_add_u32 s10, s10, 0x80
	s_addc_u32 s11, s11, 0
	s_add_u32 s56, s30, 0x100
	v_mov_b32_e32 v32, 0
	s_addc_u32 s58, s31, 0
	s_mov_b32 s59, -2
	s_cmp_lt_u32 s91, 0x100
	s_cbranch_scc1 .Lyoung_2
	s_setprio 1
.Lyoung_2:
	ds_read_b128 v[24:27], v194
	ds_read_b128 v[28:31], v194 offset:1024
	ds_read_b128 v[16:19], v194 offset:2048
	ds_read_b128 v[20:23], v194 offset:3072
	ds_read_b128 v[8:11], v195
	ds_read_b128 v[12:15], v195 offset:1024
	ds_read_b128 v[0:3], v195 offset:2048
	ds_read_b128 v[4:7], v195 offset:3072
	s_add_u32 s30, s10, 0x80
	s_addc_u32 s31, s11, 0
	s_cmp_eq_u32 s59, 12
	s_cselect_b32 s35, s3, s31
	s_cselect_b32 s34, s54, s30
	s_cselect_b32 s31, s21, s58
	s_cselect_b32 s30, s55, s56
	v_lshl_add_u64 v[224:225], s[10:11], 0, v[178:179]
	s_add_i32 m0, s29, 0xc000
	ds_read_b128 v[182:185], v196
	ds_read_b128 v[186:189], v196 offset:1024
	ds_read_b128 v[200:203], v196 offset:2048
	ds_read_b128 v[204:207], v196 offset:3072
	ds_read_b128 v[208:211], v196 offset:4096
	ds_read_b128 v[212:215], v196 offset:5120
	ds_read_b128 v[216:219], v196 offset:6144
	ds_read_b128 v[220:223], v196 offset:7168
	global_load_lds_dwordx4 v[224:225], off
	v_lshl_add_u64 v[224:225], s[10:11], 0, v[176:177]
	s_add_i32 m0, s29, 0xe000
	s_nop 0
	global_load_lds_dwordx4 v[224:225], off
	s_waitcnt vmcnt(8)
	s_waitcnt lgkmcnt(0)
	s_barrier
	s_waitcnt lgkmcnt(0)
	v_mfma_f32_16x16x128_f8f6f4 v[156:159], v[24:31], v[182:189], 0
	v_mfma_f32_16x16x128_f8f6f4 v[144:147], v[16:23], v[182:189], 0
	v_mfma_f32_16x16x128_f8f6f4 v[140:143], v[24:31], v[200:207], 0
	v_mfma_f32_16x16x128_f8f6f4 v[132:135], v[16:23], v[200:207], 0
	v_mfma_f32_16x16x128_f8f6f4 v[124:127], v[24:31], v[208:215], 0
	v_mfma_f32_16x16x128_f8f6f4 v[116:119], v[16:23], v[208:215], 0
	v_mfma_f32_16x16x128_f8f6f4 v[108:111], v[24:31], v[216:223], 0
	v_mfma_f32_16x16x128_f8f6f4 v[100:103], v[16:23], v[216:223], 0
	v_mfma_f32_16x16x128_f8f6f4 v[152:155], v[8:15], v[182:189], 0
	v_mfma_f32_16x16x128_f8f6f4 v[148:151], v[0:7], v[182:189], 0
	v_mfma_f32_16x16x128_f8f6f4 v[136:139], v[8:15], v[200:207], 0
	v_mfma_f32_16x16x128_f8f6f4 v[128:131], v[0:7], v[200:207], 0
	v_mfma_f32_16x16x128_f8f6f4 v[120:123], v[8:15], v[208:215], 0
	v_mfma_f32_16x16x128_f8f6f4 v[112:115], v[0:7], v[208:215], 0
	v_mfma_f32_16x16x128_f8f6f4 v[104:107], v[8:15], v[216:223], 0
	v_mfma_f32_16x16x128_f8f6f4 v[96:99], v[0:7], v[216:223], 0
	s_barrier
	s_add_i32 s60, s50, s97
	v_lshl_add_u64 v[182:183], s[30:31], 0, v[162:163]
	s_mov_b32 m0, s60
	ds_read_b128 v[200:203], v196 offset:16384
	ds_read_b128 v[204:207], v196 offset:17408
	ds_read_b128 v[208:211], v196 offset:18432
	ds_read_b128 v[212:215], v196 offset:19456
	ds_read_b128 v[216:219], v196 offset:20480
	ds_read_b128 v[220:223], v196 offset:21504
	ds_read_b128 v[224:227], v196 offset:22528
	ds_read_b128 v[228:231], v196 offset:23552
	global_load_lds_dwordx4 v[182:183], off
	s_add_i32 m0, s60, 0x2000
	s_add_u32 s60, s30, 0x40000
	v_lshl_add_u64 v[184:185], s[30:31], 0, v[160:161]
	s_addc_u32 s61, s31, 0
	s_add_i32 s62, s51, s97
	global_load_lds_dwordx4 v[184:185], off
	v_lshl_add_u64 v[186:187], s[60:61], 0, v[162:163]
	s_mov_b32 m0, s62
	v_lshl_add_u64 v[188:189], s[34:35], 0, v[168:169]
	global_load_lds_dwordx4 v[186:187], off
	v_lshl_add_u64 v[186:187], s[60:61], 0, v[160:161]
	s_add_i32 m0, s62, 0x2000
	s_nop 0
	global_load_lds_dwordx4 v[186:187], off
	v_lshl_add_u64 v[186:187], s[34:35], 0, v[164:165]
	s_mov_b32 m0, s29
	s_nop 0
	global_load_lds_dwordx4 v[186:187], off
	s_mov_b32 m0, s43
	s_nop 0
	global_load_lds_dwordx4 v[188:189], off
	s_waitcnt vmcnt(8)
	s_waitcnt lgkmcnt(0)
	s_barrier
	s_waitcnt lgkmcnt(0)
	v_mfma_f32_16x16x128_f8f6f4 v[92:95], v[24:31], v[200:207], 0
	v_mfma_f32_16x16x128_f8f6f4 v[84:87], v[16:23], v[200:207], 0
	v_mfma_f32_16x16x128_f8f6f4 v[76:79], v[24:31], v[208:215], 0
	v_mfma_f32_16x16x128_f8f6f4 v[68:71], v[16:23], v[208:215], 0
	v_mfma_f32_16x16x128_f8f6f4 v[60:63], v[24:31], v[216:223], 0
	v_mfma_f32_16x16x128_f8f6f4 v[52:55], v[16:23], v[216:223], 0
	v_mfma_f32_16x16x128_f8f6f4 v[44:47], v[24:31], v[224:231], 0
	v_mfma_f32_16x16x128_f8f6f4 v[36:39], v[16:23], v[224:231], 0
	v_mfma_f32_16x16x128_f8f6f4 v[88:91], v[8:15], v[200:207], 0
	v_mfma_f32_16x16x128_f8f6f4 v[80:83], v[0:7], v[200:207], 0
	v_mfma_f32_16x16x128_f8f6f4 v[72:75], v[8:15], v[208:215], 0
	v_mfma_f32_16x16x128_f8f6f4 v[64:67], v[0:7], v[208:215], 0
	v_mfma_f32_16x16x128_f8f6f4 v[56:59], v[8:15], v[216:223], 0
	v_mfma_f32_16x16x128_f8f6f4 v[48:51], v[0:7], v[216:223], 0
	v_mfma_f32_16x16x128_f8f6f4 v[40:43], v[8:15], v[224:231], 0
	v_mfma_f32_16x16x128_f8f6f4 v[32:35], v[0:7], v[224:231], 0
	s_barrier
	s_add_i32 s60, 0, 0x18000
	s_add_i32 s61, 0, 0x1c000
	v_add_u32_e32 v12, s60, v191
	v_add_u32_e32 v28, s61, v191
	ds_read_b128 v[0:3], v12
	ds_read_b128 v[4:7], v12 offset:1024
	ds_read_b128 v[8:11], v12 offset:2048
	ds_read_b128 v[12:15], v12 offset:3072
	ds_read_b128 v[16:19], v28
	ds_read_b128 v[20:23], v28 offset:1024
	ds_read_b128 v[24:27], v28 offset:2048
	ds_read_b128 v[28:31], v28 offset:3072
	s_mov_b32 m0, s44
	v_lshl_add_u64 v[232:233], s[34:35], 0, v[166:167]
	ds_read_b128 v[200:203], v196 offset:32768
	ds_read_b128 v[204:207], v196 offset:33792
	ds_read_b128 v[208:211], v196 offset:34816
	ds_read_b128 v[212:215], v196 offset:35840
	ds_read_b128 v[216:219], v196 offset:36864
	ds_read_b128 v[220:223], v196 offset:37888
	ds_read_b128 v[224:227], v196 offset:38912
	ds_read_b128 v[228:231], v196 offset:39936
	global_load_lds_dwordx4 v[232:233], off
	v_lshl_add_u64 v[232:233], s[34:35], 0, v[170:171]
	s_mov_b32 m0, s45
	s_nop 0
	global_load_lds_dwordx4 v[232:233], off
	s_waitcnt vmcnt(8)
	s_waitcnt lgkmcnt(0)
	s_barrier
; #define PG8_STAGE(bufoff, gbase, o0, o1) do { \
;         __builtin_amdgcn_global_load_lds((const unsigned*)((const char*)(gbase) + (o0)), (LAS unsigned*)(lds + (bufoff) + ldsw), 16, 0, 0); \
;         __builtin_amdgcn_global_load_lds((const unsigned*)((const char*)(gbase) + (o1)), (LAS unsigned*)(lds + (bufoff) + ldsw + 8192), 16, 0, 0); } while (0)
; #define PG8_LDA(dst, b, h) do { _Pragma("unroll") for (int m = 0; m < 4; ++m) _Pragma("unroll") for (int k = 0; k < 2; ++k) dst[m][k] = *(const LAS bf16x8*)(lds + PG8_SA(b, h) + aoff + m * 2048 + k * 1024); } while (0)
; #define PG8_LDB(dst, b, h) do { _Pragma("unroll") for (int n = 0; n < 2; ++n) _Pragma("unroll") for (int k = 0; k < 2; ++k) dst[n][k] = *(const LAS bf16x8*)(lds + PG8_SB(b, h) + boff + n * 2048 + k * 1024); } while (0)
; #define PG8_WAIT_V(n) asm volatile("s_waitcnt vmcnt(" #n ")" ::: "memory")
; #define PG8_WAIT_L(n) asm volatile("s_waitcnt lgkmcnt(" #n ")" ::: "memory")
; #define PG8_BAR __builtin_amdgcn_s_barrier()
; #define PG8_SCHED __builtin_amdgcn_sched_barrier(0)
; template <class Epi, class Sched, class Prob>
; __device__ __forceinline__ void gemm_phase(LAS unsigned char* lds, LAS unsigned char* lds_epi, const Prob g, const Sched& S, const Epi& E, int wid) {
;     ...
;         for (int t = 0; t < nt; t += 2) {
;             const bool last = (t == nt - 2);
;             const char* a1 = cA + (size_t)(t + 1) * kstep;
;             const char* a2 = last ? nA : cA + (size_t)(t + 2) * kstep; const char* b2 = last ? nB : cB + (size_t)(t + 2) * kstep;
;             const char* a3 = a2 + kstep; const char* b3 = b2 + kstep;
;             PG8_LDB(B0, 0, 0); PG8_LDB(B1, 0, 1); PG8_SCHED; PG8_LDA(At, 0, 0); PG8_STAGE(PG8_SA(1, 1), a1, cA10, cA11);
;             PG8_WAIT_V(8); PG8_WAIT_L(0); PG8_BAR; PG8_MMA(0, 0, At, B0); PG8_MMA(0, 1, At, B1); PG8_BAR; PG8_SCHED;
;     ...
;             PG8_WAIT_V(8); PG8_WAIT_L(0); PG8_BAR; PG8_MMA(0, 0, At, B0); PG8_MMA(0, 1, At, B1); PG8_BAR; PG8_SCHED;
;             PG8_LDA(At, 1, 1); PG8_STAGE(PG8_SB(1, 0), b3, vB0, vB1); PG8_STAGE(PG8_SB(1, 1), b3 + hstepB, vB0, vB1); PG8_STAGE(PG8_SA(1, 0), a3, cA00, cA01);
;             PG8_WAIT_V(8); PG8_WAIT_L(0); PG8_BAR; PG8_MMA(1, 0, At, B0); PG8_MMA(1, 1, At, B1); PG8_BAR; PG8_SCHED;
	s_waitcnt lgkmcnt(0)
	v_mfma_f32_16x16x128_f8f6f4 v[156:159], v[0:7], v[200:207], v[156:159]
	v_mfma_f32_16x16x128_f8f6f4 v[144:147], v[8:15], v[200:207], v[144:147]
	v_mfma_f32_16x16x128_f8f6f4 v[140:143], v[0:7], v[208:215], v[140:143]
	v_mfma_f32_16x16x128_f8f6f4 v[132:135], v[8:15], v[208:215], v[132:135]
	v_mfma_f32_16x16x128_f8f6f4 v[124:127], v[0:7], v[216:223], v[124:127]
	v_mfma_f32_16x16x128_f8f6f4 v[116:119], v[8:15], v[216:223], v[116:119]
	v_mfma_f32_16x16x128_f8f6f4 v[108:111], v[0:7], v[224:231], v[108:111]
	v_mfma_f32_16x16x128_f8f6f4 v[100:103], v[8:15], v[224:231], v[100:103]
	v_mfma_f32_16x16x128_f8f6f4 v[152:155], v[16:23], v[200:207], v[152:155]
	v_mfma_f32_16x16x128_f8f6f4 v[148:151], v[24:31], v[200:207], v[148:151]
	v_mfma_f32_16x16x128_f8f6f4 v[136:139], v[16:23], v[208:215], v[136:139]
	v_mfma_f32_16x16x128_f8f6f4 v[128:131], v[24:31], v[208:215], v[128:131]
	v_mfma_f32_16x16x128_f8f6f4 v[120:123], v[16:23], v[216:223], v[120:123]
	v_mfma_f32_16x16x128_f8f6f4 v[112:115], v[24:31], v[216:223], v[112:115]
	v_mfma_f32_16x16x128_f8f6f4 v[104:107], v[16:23], v[224:231], v[104:107]
	v_mfma_f32_16x16x128_f8f6f4 v[96:99], v[24:31], v[224:231], v[96:99]
	s_barrier
	s_add_i32 s34, s60, s97
	v_lshl_add_u64 v[182:183], v[182:183], 0, s[14:15]
	s_mov_b32 m0, s34
	ds_read_b128 v[200:203], v196 offset:49152
	ds_read_b128 v[204:207], v196 offset:50176
	ds_read_b128 v[208:211], v196 offset:51200
	ds_read_b128 v[212:215], v196 offset:52224
	ds_read_b128 v[216:219], v196 offset:53248
	ds_read_b128 v[220:223], v196 offset:54272
	ds_read_b128 v[224:227], v196 offset:55296
	ds_read_b128 v[228:231], v196 offset:56320
	global_load_lds_dwordx4 v[182:183], off
	s_add_i32 m0, s34, 0x2000
	s_add_u32 s30, s30, 0x40080
	v_lshl_add_u64 v[182:183], v[184:185], 0, s[14:15]
	s_addc_u32 s31, s31, 0
	s_add_i32 s34, s61, s97
	global_load_lds_dwordx4 v[182:183], off
	v_lshl_add_u64 v[182:183], s[30:31], 0, v[162:163]
	s_mov_b32 m0, s34
	s_nop 0
	global_load_lds_dwordx4 v[182:183], off
	v_lshl_add_u64 v[182:183], s[30:31], 0, v[160:161]
	s_add_i32 m0, s34, 0x2000
	s_nop 0
	global_load_lds_dwordx4 v[182:183], off
	v_lshl_add_u64 v[182:183], v[186:187], 0, s[14:15]
	s_mov_b32 m0, s48
	s_nop 0
	global_load_lds_dwordx4 v[182:183], off
	v_lshl_add_u64 v[182:183], v[188:189], 0, s[14:15]
	s_mov_b32 m0, s49
	s_nop 0
	global_load_lds_dwordx4 v[182:183], off
	s_waitcnt vmcnt(8)
	s_waitcnt lgkmcnt(0)
	s_barrier
	s_waitcnt lgkmcnt(0)
	v_mfma_f32_16x16x128_f8f6f4 v[92:95], v[0:7], v[200:207], v[92:95]
	v_mfma_f32_16x16x128_f8f6f4 v[84:87], v[8:15], v[200:207], v[84:87]
	v_mfma_f32_16x16x128_f8f6f4 v[76:79], v[0:7], v[208:215], v[76:79]
	v_mfma_f32_16x16x128_f8f6f4 v[68:71], v[8:15], v[208:215], v[68:71]
	v_mfma_f32_16x16x128_f8f6f4 v[60:63], v[0:7], v[216:223], v[60:63]
	v_mfma_f32_16x16x128_f8f6f4 v[52:55], v[8:15], v[216:223], v[52:55]
	v_mfma_f32_16x16x128_f8f6f4 v[44:47], v[0:7], v[224:231], v[44:47]
	v_mfma_f32_16x16x128_f8f6f4 v[36:39], v[8:15], v[224:231], v[36:39]
	v_mfma_f32_16x16x128_f8f6f4 v[88:91], v[16:23], v[200:207], v[88:91]
	v_mfma_f32_16x16x128_f8f6f4 v[80:83], v[24:31], v[200:207], v[80:83]
	v_mfma_f32_16x16x128_f8f6f4 v[72:75], v[16:23], v[208:215], v[72:75]
	v_mfma_f32_16x16x128_f8f6f4 v[64:67], v[24:31], v[208:215], v[64:67]
	v_mfma_f32_16x16x128_f8f6f4 v[56:59], v[16:23], v[216:223], v[56:59]
	v_mfma_f32_16x16x128_f8f6f4 v[48:51], v[24:31], v[216:223], v[48:51]
	v_mfma_f32_16x16x128_f8f6f4 v[40:43], v[16:23], v[224:231], v[40:43]
	v_mfma_f32_16x16x128_f8f6f4 v[32:35], v[24:31], v[224:231], v[32:35]
	s_barrier
	s_add_i32 s59, s59, 2
	s_add_u32 s10, s10, 0x100
	s_addc_u32 s11, s11, 0
	s_add_u32 s56, s56, 0x100
	s_addc_u32 s58, s58, 0
	s_cmp_gt_u32 s59, 13
.LBB0_1248:
	ds_read_b128 v[24:27], v194
	ds_read_b128 v[28:31], v194 offset:1024
	ds_read_b128 v[16:19], v194 offset:2048
	ds_read_b128 v[20:23], v194 offset:3072
	ds_read_b128 v[8:11], v195
	ds_read_b128 v[12:15], v195 offset:1024
	ds_read_b128 v[0:3], v195 offset:2048
	ds_read_b128 v[4:7], v195 offset:3072
	s_add_u32 s30, s10, 0x80
	s_addc_u32 s31, s11, 0
	s_cmp_eq_u32 s59, 12
	s_cselect_b32 s35, s3, s31
	s_cselect_b32 s34, s54, s30
	s_cselect_b32 s31, s21, s58
	s_cselect_b32 s30, s55, s56
	v_lshl_add_u64 v[224:225], s[10:11], 0, v[178:179]
	s_add_i32 m0, s29, 0xc000
	ds_read_b128 v[182:185], v196
	ds_read_b128 v[186:189], v196 offset:1024
	ds_read_b128 v[200:203], v196 offset:2048
	ds_read_b128 v[204:207], v196 offset:3072
	ds_read_b128 v[208:211], v196 offset:4096
	ds_read_b128 v[212:215], v196 offset:5120
	ds_read_b128 v[216:219], v196 offset:6144
	ds_read_b128 v[220:223], v196 offset:7168
	global_load_lds_dwordx4 v[224:225], off
	v_lshl_add_u64 v[224:225], s[10:11], 0, v[176:177]
	s_add_i32 m0, s29, 0xe000
	s_nop 0
	global_load_lds_dwordx4 v[224:225], off
	s_waitcnt vmcnt(8)
	s_waitcnt lgkmcnt(0)
	s_barrier
	s_waitcnt lgkmcnt(0)
	v_mfma_f32_16x16x128_f8f6f4 v[156:159], v[24:31], v[182:189], v[156:159]
	v_mfma_f32_16x16x128_f8f6f4 v[144:147], v[16:23], v[182:189], v[144:147]
	v_mfma_f32_16x16x128_f8f6f4 v[140:143], v[24:31], v[200:207], v[140:143]
	v_mfma_f32_16x16x128_f8f6f4 v[132:135], v[16:23], v[200:207], v[132:135]
	v_mfma_f32_16x16x128_f8f6f4 v[124:127], v[24:31], v[208:215], v[124:127]
	v_mfma_f32_16x16x128_f8f6f4 v[116:119], v[16:23], v[208:215], v[116:119]
	v_mfma_f32_16x16x128_f8f6f4 v[108:111], v[24:31], v[216:223], v[108:111]
	v_mfma_f32_16x16x128_f8f6f4 v[100:103], v[16:23], v[216:223], v[100:103]
	v_mfma_f32_16x16x128_f8f6f4 v[152:155], v[8:15], v[182:189], v[152:155]
	v_mfma_f32_16x16x128_f8f6f4 v[148:151], v[0:7], v[182:189], v[148:151]
	v_mfma_f32_16x16x128_f8f6f4 v[136:139], v[8:15], v[200:207], v[136:139]
	v_mfma_f32_16x16x128_f8f6f4 v[128:131], v[0:7], v[200:207], v[128:131]
	v_mfma_f32_16x16x128_f8f6f4 v[120:123], v[8:15], v[208:215], v[120:123]
	v_mfma_f32_16x16x128_f8f6f4 v[112:115], v[0:7], v[208:215], v[112:115]
	v_mfma_f32_16x16x128_f8f6f4 v[104:107], v[8:15], v[216:223], v[104:107]
	v_mfma_f32_16x16x128_f8f6f4 v[96:99], v[0:7], v[216:223], v[96:99]
	s_barrier
; #define PG8_STAGE(bufoff, gbase, o0, o1) do { \
;         __builtin_amdgcn_global_load_lds((const unsigned*)((const char*)(gbase) + (o0)), (LAS unsigned*)(lds + (bufoff) + ldsw), 16, 0, 0); \
;         __builtin_amdgcn_global_load_lds((const unsigned*)((const char*)(gbase) + (o1)), (LAS unsigned*)(lds + (bufoff) + ldsw + 8192), 16, 0, 0); } while (0)
; #define PG8_LDA(dst, b, h) do { _Pragma("unroll") for (int m = 0; m < 4; ++m) _Pragma("unroll") for (int k = 0; k < 2; ++k) dst[m][k] = *(const LAS bf16x8*)(lds + PG8_SA(b, h) + aoff + m * 2048 + k * 1024); } while (0)
; #define PG8_LDB(dst, b, h) do { _Pragma("unroll") for (int n = 0; n < 2; ++n) _Pragma("unroll") for (int k = 0; k < 2; ++k) dst[n][k] = *(const LAS bf16x8*)(lds + PG8_SB(b, h) + boff + n * 2048 + k * 1024); } while (0)
; #define PG8_WAIT_V(n) asm volatile("s_waitcnt vmcnt(" #n ")" ::: "memory")
; #define PG8_WAIT_L(n) asm volatile("s_waitcnt lgkmcnt(" #n ")" ::: "memory")
; #define PG8_BAR __builtin_amdgcn_s_barrier()
; #define PG8_SCHED __builtin_amdgcn_sched_barrier(0)
; template <class Epi, class Sched, class Prob>
; __device__ __forceinline__ void gemm_phase(LAS unsigned char* lds, LAS unsigned char* lds_epi, const Prob g, const Sched& S, const Epi& E, int wid) {
;     ...
;             PG8_LDA(At, 0, 1); PG8_STAGE(PG8_SB(0, 0), b2, vB0, vB1); PG8_STAGE(PG8_SB(0, 1), b2 + hstepB, vB0, vB1); PG8_STAGE(PG8_SA(0, 0), a2, cA00, cA01);
;             PG8_WAIT_V(8); PG8_WAIT_L(0); PG8_BAR; PG8_MMA(1, 0, At, B0); PG8_MMA(1, 1, At, B1); PG8_BAR; PG8_SCHED;
;             PG8_LDB(B0, 1, 0); PG8_LDB(B1, 1, 1); PG8_SCHED; PG8_LDA(At, 1, 0); PG8_STAGE(PG8_SA(0, 1), a2, cA10, cA11);
;             PG8_WAIT_V(8); PG8_WAIT_L(0); PG8_BAR; PG8_MMA(0, 0, At, B0); PG8_MMA(0, 1, At, B1); PG8_BAR; PG8_SCHED;
	s_add_i32 s60, s50, s97
	v_lshl_add_u64 v[182:183], s[30:31], 0, v[162:163]
	s_mov_b32 m0, s60
	ds_read_b128 v[200:203], v196 offset:16384
	ds_read_b128 v[204:207], v196 offset:17408
	ds_read_b128 v[208:211], v196 offset:18432
	ds_read_b128 v[212:215], v196 offset:19456
	ds_read_b128 v[216:219], v196 offset:20480
	ds_read_b128 v[220:223], v196 offset:21504
	ds_read_b128 v[224:227], v196 offset:22528
	ds_read_b128 v[228:231], v196 offset:23552
	global_load_lds_dwordx4 v[182:183], off
	s_add_i32 m0, s60, 0x2000
	s_add_u32 s60, s30, 0x40000
	v_lshl_add_u64 v[184:185], s[30:31], 0, v[160:161]
	s_addc_u32 s61, s31, 0
	s_add_i32 s62, s51, s97
	global_load_lds_dwordx4 v[184:185], off
	v_lshl_add_u64 v[186:187], s[60:61], 0, v[162:163]
	s_mov_b32 m0, s62
	v_lshl_add_u64 v[188:189], s[34:35], 0, v[168:169]
	global_load_lds_dwordx4 v[186:187], off
	v_lshl_add_u64 v[186:187], s[60:61], 0, v[160:161]
	s_add_i32 m0, s62, 0x2000
	s_nop 0
	global_load_lds_dwordx4 v[186:187], off
	v_lshl_add_u64 v[186:187], s[34:35], 0, v[164:165]
	s_mov_b32 m0, s29
	s_nop 0
	global_load_lds_dwordx4 v[186:187], off
	s_mov_b32 m0, s43
	s_nop 0
	global_load_lds_dwordx4 v[188:189], off
	s_waitcnt vmcnt(8)
	s_waitcnt lgkmcnt(0)
	s_barrier
	s_waitcnt lgkmcnt(0)
	v_mfma_f32_16x16x128_f8f6f4 v[92:95], v[24:31], v[200:207], v[92:95]
	v_mfma_f32_16x16x128_f8f6f4 v[84:87], v[16:23], v[200:207], v[84:87]
	v_mfma_f32_16x16x128_f8f6f4 v[76:79], v[24:31], v[208:215], v[76:79]
	v_mfma_f32_16x16x128_f8f6f4 v[68:71], v[16:23], v[208:215], v[68:71]
	v_mfma_f32_16x16x128_f8f6f4 v[60:63], v[24:31], v[216:223], v[60:63]
	v_mfma_f32_16x16x128_f8f6f4 v[52:55], v[16:23], v[216:223], v[52:55]
	v_mfma_f32_16x16x128_f8f6f4 v[44:47], v[24:31], v[224:231], v[44:47]
	v_mfma_f32_16x16x128_f8f6f4 v[36:39], v[16:23], v[224:231], v[36:39]
	v_mfma_f32_16x16x128_f8f6f4 v[88:91], v[8:15], v[200:207], v[88:91]
	v_mfma_f32_16x16x128_f8f6f4 v[80:83], v[0:7], v[200:207], v[80:83]
	v_mfma_f32_16x16x128_f8f6f4 v[72:75], v[8:15], v[208:215], v[72:75]
	v_mfma_f32_16x16x128_f8f6f4 v[64:67], v[0:7], v[208:215], v[64:67]
	v_mfma_f32_16x16x128_f8f6f4 v[56:59], v[8:15], v[216:223], v[56:59]
	v_mfma_f32_16x16x128_f8f6f4 v[48:51], v[0:7], v[216:223], v[48:51]
	v_mfma_f32_16x16x128_f8f6f4 v[40:43], v[8:15], v[224:231], v[40:43]
	v_mfma_f32_16x16x128_f8f6f4 v[32:35], v[0:7], v[224:231], v[32:35]
	s_barrier
	s_add_i32 s60, 0, 0x18000
	s_add_i32 s61, 0, 0x1c000
	v_add_u32_e32 v12, s60, v191
	v_add_u32_e32 v28, s61, v191
	ds_read_b128 v[0:3], v12
	ds_read_b128 v[4:7], v12 offset:1024
	ds_read_b128 v[8:11], v12 offset:2048
	ds_read_b128 v[12:15], v12 offset:3072
	ds_read_b128 v[16:19], v28
	ds_read_b128 v[20:23], v28 offset:1024
	ds_read_b128 v[24:27], v28 offset:2048
	ds_read_b128 v[28:31], v28 offset:3072
	s_mov_b32 m0, s44
	v_lshl_add_u64 v[232:233], s[34:35], 0, v[166:167]
	ds_read_b128 v[200:203], v196 offset:32768
	ds_read_b128 v[204:207], v196 offset:33792
	ds_read_b128 v[208:211], v196 offset:34816
	ds_read_b128 v[212:215], v196 offset:35840
	ds_read_b128 v[216:219], v196 offset:36864
	ds_read_b128 v[220:223], v196 offset:37888
	ds_read_b128 v[224:227], v196 offset:38912
	ds_read_b128 v[228:231], v196 offset:39936
	global_load_lds_dwordx4 v[232:233], off
	v_lshl_add_u64 v[232:233], s[34:35], 0, v[170:171]
	s_mov_b32 m0, s45
	s_nop 0
	global_load_lds_dwordx4 v[232:233], off
	s_waitcnt vmcnt(8)
	s_waitcnt lgkmcnt(0)
	s_barrier
; #define PG8_STAGE(bufoff, gbase, o0, o1) do { \
;         __builtin_amdgcn_global_load_lds((const unsigned*)((const char*)(gbase) + (o0)), (LAS unsigned*)(lds + (bufoff) + ldsw), 16, 0, 0); \
;         __builtin_amdgcn_global_load_lds((const unsigned*)((const char*)(gbase) + (o1)), (LAS unsigned*)(lds + (bufoff) + ldsw + 8192), 16, 0, 0); } while (0)
; #define PG8_LDA(dst, b, h) do { _Pragma("unroll") for (int m = 0; m < 4; ++m) _Pragma("unroll") for (int k = 0; k < 2; ++k) dst[m][k] = *(const LAS bf16x8*)(lds + PG8_SA(b, h) + aoff + m * 2048 + k * 1024); } while (0)
; #define PG8_WAIT_V(n) asm volatile("s_waitcnt vmcnt(" #n ")" ::: "memory")
; #define PG8_WAIT_L(n) asm volatile("s_waitcnt lgkmcnt(" #n ")" ::: "memory")
; #define PG8_BAR __builtin_amdgcn_s_barrier()
; #define PG8_SCHED __builtin_amdgcn_sched_barrier(0)
; template <class Epi, class Sched, class Prob>
; __device__ __forceinline__ void gemm_phase(LAS unsigned char* lds, LAS unsigned char* lds_epi, const Prob g, const Sched& S, const Epi& E, int wid) {
;     ...
;             PG8_WAIT_V(8); PG8_WAIT_L(0); PG8_BAR; PG8_MMA(0, 0, At, B0); PG8_MMA(0, 1, At, B1); PG8_BAR; PG8_SCHED;
;             PG8_LDA(At, 1, 1); PG8_STAGE(PG8_SB(1, 0), b3, vB0, vB1); PG8_STAGE(PG8_SB(1, 1), b3 + hstepB, vB0, vB1); PG8_STAGE(PG8_SA(1, 0), a3, cA00, cA01);
;             PG8_WAIT_V(8); PG8_WAIT_L(0); PG8_BAR; PG8_MMA(1, 0, At, B0); PG8_MMA(1, 1, At, B1); PG8_BAR; PG8_SCHED;
;         }
;         if constexpr (Prob::FP8) asm volatile("s_nop 7\n\ts_nop 7\n\ts_nop 7" ::: "memory");
;         if (wr == 0) PG8_BAR;
	s_waitcnt lgkmcnt(0)
	v_mfma_f32_16x16x128_f8f6f4 v[156:159], v[0:7], v[200:207], v[156:159]
	v_mfma_f32_16x16x128_f8f6f4 v[144:147], v[8:15], v[200:207], v[144:147]
	v_mfma_f32_16x16x128_f8f6f4 v[140:143], v[0:7], v[208:215], v[140:143]
	v_mfma_f32_16x16x128_f8f6f4 v[132:135], v[8:15], v[208:215], v[132:135]
	v_mfma_f32_16x16x128_f8f6f4 v[124:127], v[0:7], v[216:223], v[124:127]
	v_mfma_f32_16x16x128_f8f6f4 v[116:119], v[8:15], v[216:223], v[116:119]
	v_mfma_f32_16x16x128_f8f6f4 v[108:111], v[0:7], v[224:231], v[108:111]
	v_mfma_f32_16x16x128_f8f6f4 v[100:103], v[8:15], v[224:231], v[100:103]
	v_mfma_f32_16x16x128_f8f6f4 v[152:155], v[16:23], v[200:207], v[152:155]
	v_mfma_f32_16x16x128_f8f6f4 v[148:151], v[24:31], v[200:207], v[148:151]
	v_mfma_f32_16x16x128_f8f6f4 v[136:139], v[16:23], v[208:215], v[136:139]
	v_mfma_f32_16x16x128_f8f6f4 v[128:131], v[24:31], v[208:215], v[128:131]
	v_mfma_f32_16x16x128_f8f6f4 v[120:123], v[16:23], v[216:223], v[120:123]
	v_mfma_f32_16x16x128_f8f6f4 v[112:115], v[24:31], v[216:223], v[112:115]
	v_mfma_f32_16x16x128_f8f6f4 v[104:107], v[16:23], v[224:231], v[104:107]
	v_mfma_f32_16x16x128_f8f6f4 v[96:99], v[24:31], v[224:231], v[96:99]
	s_barrier
	s_add_i32 s34, s60, s97
	v_lshl_add_u64 v[182:183], v[182:183], 0, s[14:15]
	s_mov_b32 m0, s34
	ds_read_b128 v[200:203], v196 offset:49152
	ds_read_b128 v[204:207], v196 offset:50176
	ds_read_b128 v[208:211], v196 offset:51200
	ds_read_b128 v[212:215], v196 offset:52224
	ds_read_b128 v[216:219], v196 offset:53248
	ds_read_b128 v[220:223], v196 offset:54272
	ds_read_b128 v[224:227], v196 offset:55296
	ds_read_b128 v[228:231], v196 offset:56320
	global_load_lds_dwordx4 v[182:183], off
	s_add_i32 m0, s34, 0x2000
	s_add_u32 s30, s30, 0x40080
	v_lshl_add_u64 v[182:183], v[184:185], 0, s[14:15]
	s_addc_u32 s31, s31, 0
	s_add_i32 s34, s61, s97
	global_load_lds_dwordx4 v[182:183], off
	v_lshl_add_u64 v[182:183], s[30:31], 0, v[162:163]
	s_mov_b32 m0, s34
	s_nop 0
	global_load_lds_dwordx4 v[182:183], off
	v_lshl_add_u64 v[182:183], s[30:31], 0, v[160:161]
	s_add_i32 m0, s34, 0x2000
	s_nop 0
	global_load_lds_dwordx4 v[182:183], off
	v_lshl_add_u64 v[182:183], v[186:187], 0, s[14:15]
	s_mov_b32 m0, s48
	s_nop 0
	global_load_lds_dwordx4 v[182:183], off
	v_lshl_add_u64 v[182:183], v[188:189], 0, s[14:15]
	s_mov_b32 m0, s49
	s_nop 0
	global_load_lds_dwordx4 v[182:183], off
	s_waitcnt vmcnt(8)
	s_waitcnt lgkmcnt(0)
	s_barrier
	s_waitcnt lgkmcnt(0)
	v_mfma_f32_16x16x128_f8f6f4 v[92:95], v[0:7], v[200:207], v[92:95]
	v_mfma_f32_16x16x128_f8f6f4 v[84:87], v[8:15], v[200:207], v[84:87]
	v_mfma_f32_16x16x128_f8f6f4 v[76:79], v[0:7], v[208:215], v[76:79]
	v_mfma_f32_16x16x128_f8f6f4 v[68:71], v[8:15], v[208:215], v[68:71]
	v_mfma_f32_16x16x128_f8f6f4 v[60:63], v[0:7], v[216:223], v[60:63]
	v_mfma_f32_16x16x128_f8f6f4 v[52:55], v[8:15], v[216:223], v[52:55]
	v_mfma_f32_16x16x128_f8f6f4 v[44:47], v[0:7], v[224:231], v[44:47]
	v_mfma_f32_16x16x128_f8f6f4 v[36:39], v[8:15], v[224:231], v[36:39]
	v_mfma_f32_16x16x128_f8f6f4 v[88:91], v[16:23], v[200:207], v[88:91]
	v_mfma_f32_16x16x128_f8f6f4 v[80:83], v[24:31], v[200:207], v[80:83]
	v_mfma_f32_16x16x128_f8f6f4 v[72:75], v[16:23], v[208:215], v[72:75]
	v_mfma_f32_16x16x128_f8f6f4 v[64:67], v[24:31], v[208:215], v[64:67]
	v_mfma_f32_16x16x128_f8f6f4 v[56:59], v[16:23], v[216:223], v[56:59]
	v_mfma_f32_16x16x128_f8f6f4 v[48:51], v[24:31], v[216:223], v[48:51]
	v_mfma_f32_16x16x128_f8f6f4 v[40:43], v[16:23], v[224:231], v[40:43]
	v_mfma_f32_16x16x128_f8f6f4 v[32:35], v[24:31], v[224:231], v[32:35]
	s_barrier
	s_add_i32 s59, s59, 2
	s_add_u32 s10, s10, 0x100
	s_addc_u32 s11, s11, 0
	s_add_u32 s56, s56, 0x100
	s_addc_u32 s58, s58, 0
	s_cmp_gt_u32 s59, 13
	s_cbranch_scc0 .LBB0_1248
	s_setprio 0
	v_readlane_b32 s10, v254, 27
	v_readlane_b32 s11, v254, 28
	s_and_b64 vcc, exec, s[10:11]
	s_cbranch_vccz .LBB0_1251
	s_barrier

; #define PG8_STAGE(bufoff, gbase, o0, o1) do { \
;         __builtin_amdgcn_global_load_lds((const unsigned*)((const char*)(gbase) + (o0)), (LAS unsigned*)(lds + (bufoff) + ldsw), 16, 0, 0); \
;         __builtin_amdgcn_global_load_lds((const unsigned*)((const char*)(gbase) + (o1)), (LAS unsigned*)(lds + (bufoff) + ldsw + 8192), 16, 0, 0); } while (0)
; #define PG8_LDA(dst, b, h) do { _Pragma("unroll") for (int m = 0; m < 4; ++m) _Pragma("unroll") for (int k = 0; k < 2; ++k) dst[m][k] = *(const LAS bf16x8*)(lds + PG8_SA(b, h) + aoff + m * 2048 + k * 1024); } while (0)
; #define PG8_LDB(dst, b, h) do { _Pragma("unroll") for (int n = 0; n < 2; ++n) _Pragma("unroll") for (int k = 0; k < 2; ++k) dst[n][k] = *(const LAS bf16x8*)(lds + PG8_SB(b, h) + boff + n * 2048 + k * 1024); } while (0)
; #define PG8_WAIT_V(n) asm volatile("s_waitcnt vmcnt(" #n ")" ::: "memory")
; #define PG8_WAIT_L(n) asm volatile("s_waitcnt lgkmcnt(" #n ")" ::: "memory")
; #define PG8_BAR __builtin_amdgcn_s_barrier()
; #define PG8_SCHED __builtin_amdgcn_sched_barrier(0)
; template <class Epi, class Sched, class Prob>
; __device__ __forceinline__ void gemm_phase(LAS unsigned char* lds, LAS unsigned char* lds_epi, const Prob g, const Sched& S, const Epi& E, int wid) {
;     ...
;         const bool has_next = S.next(ui + 1, nxt);
;         const char* nA = has_next ? g.a_base(nxt) : cA; const char* nB = has_next ? g.b_base(nxt) : cB;
; _Pragma("clang loop unroll(disable)")
;         for (int t = 0; t < nt; t += 2) {
;             const bool last = (t == nt - 2);
;             const char* a1 = cA + (size_t)(t + 1) * kstep;
;             const char* a2 = last ? nA : cA + (size_t)(t + 2) * kstep; const char* b2 = last ? nB : cB + (size_t)(t + 2) * kstep;
;             const char* a3 = a2 + kstep; const char* b3 = b2 + kstep;
;             PG8_LDB(B0, 0, 0); PG8_LDB(B1, 0, 1); PG8_SCHED; PG8_LDA(At, 0, 0); PG8_STAGE(PG8_SA(1, 1), a1, cA10, cA11);
;             PG8_WAIT_V(8); PG8_WAIT_L(0); PG8_BAR; PG8_MMA(0, 0, At, B0); PG8_MMA(0, 1, At, B1); PG8_BAR; PG8_SCHED;
;             PG8_LDA(At, 0, 1); PG8_STAGE(PG8_SB(0, 0), b2, vB0, vB1); PG8_STAGE(PG8_SB(0, 1), b2 + hstepB, vB0, vB1); PG8_STAGE(PG8_SA(0, 0), a2, cA00, cA01);
;             PG8_WAIT_V(8); PG8_WAIT_L(0); PG8_BAR; PG8_MMA(1, 0, At, B0); PG8_MMA(1, 1, At, B1); PG8_BAR; PG8_SCHED;
.LBB0_1335:
	s_add_u32 s28, s28, 0x80
	s_addc_u32 s29, s29, 0
	s_add_u32 s60, s30, 0x100
	s_addc_u32 s61, s31, 0
	s_mov_b32 s62, -2
	s_cmp_lt_u32 s91, 0x100
	s_cbranch_scc1 .Lyoung_3
	s_setprio 1
.Lyoung_3:
.LBB0_1336:
	v_add_u32_e32 v146, s55, v149
	ds_read_b128 v[156:159], v146
	ds_read_b128 v[160:163], v146 offset:1024
	ds_read_b128 v[164:167], v146 offset:2048
	ds_read_b128 v[168:171], v146 offset:3072
	v_add_u32_e32 v146, s56, v149
	ds_read_b128 v[172:175], v146
	ds_read_b128 v[176:179], v146 offset:1024
	ds_read_b128 v[180:183], v146 offset:2048
	ds_read_b128 v[184:187], v146 offset:3072
	s_add_u32 s30, s28, 0x80
	s_addc_u32 s31, s29, 0
	s_cmpk_eq_i32 s62, 0x6c
	s_cselect_b32 s35, s25, s31
	s_cselect_b32 s34, s24, s30
	s_cselect_b32 s31, s27, s61
	s_cselect_b32 s30, s26, s60
	v_lshl_add_u64 v[146:147], s[28:29], 0, v[140:141]
	s_add_i32 m0, s47, 0xc000
	ds_read_b128 v[188:191], v153
	ds_read_b128 v[192:195], v153 offset:1024
	ds_read_b128 v[196:199], v153 offset:2048
	ds_read_b128 v[200:203], v153 offset:3072
	ds_read_b128 v[204:207], v153 offset:4096
	ds_read_b128 v[208:211], v153 offset:5120
	ds_read_b128 v[212:215], v153 offset:6144
	ds_read_b128 v[216:219], v153 offset:7168
	global_load_lds_dwordx4 v[146:147], off
	v_lshl_add_u64 v[146:147], s[28:29], 0, v[142:143]
	s_add_i32 m0, s47, 0xe000
	s_nop 0
	global_load_lds_dwordx4 v[146:147], off
	s_waitcnt vmcnt(8)
	s_waitcnt lgkmcnt(0)
	s_barrier
	s_waitcnt lgkmcnt(0)
	v_mfma_f32_16x16x32_bf16 v[120:123], v[156:159], v[188:191], v[120:123]
	v_mfma_f32_16x16x32_bf16 v[112:115], v[164:167], v[188:191], v[112:115]
	v_mfma_f32_16x16x32_bf16 v[104:107], v[156:159], v[196:199], v[104:107]
	v_mfma_f32_16x16x32_bf16 v[96:99], v[164:167], v[196:199], v[96:99]
	v_mfma_f32_16x16x32_bf16 v[88:91], v[156:159], v[204:207], v[88:91]
	v_mfma_f32_16x16x32_bf16 v[80:83], v[164:167], v[204:207], v[80:83]
	v_mfma_f32_16x16x32_bf16 v[72:75], v[156:159], v[212:215], v[72:75]
	v_mfma_f32_16x16x32_bf16 v[64:67], v[164:167], v[212:215], v[64:67]
	v_mfma_f32_16x16x32_bf16 v[120:123], v[160:163], v[192:195], v[120:123]
	v_mfma_f32_16x16x32_bf16 v[112:115], v[168:171], v[192:195], v[112:115]
	v_mfma_f32_16x16x32_bf16 v[104:107], v[160:163], v[200:203], v[104:107]
	v_mfma_f32_16x16x32_bf16 v[96:99], v[168:171], v[200:203], v[96:99]
	v_mfma_f32_16x16x32_bf16 v[88:91], v[160:163], v[208:211], v[88:91]
	v_mfma_f32_16x16x32_bf16 v[80:83], v[168:171], v[208:211], v[80:83]
	v_mfma_f32_16x16x32_bf16 v[72:75], v[160:163], v[216:219], v[72:75]
	v_mfma_f32_16x16x32_bf16 v[64:67], v[168:171], v[216:219], v[64:67]
	v_mfma_f32_16x16x32_bf16 v[124:127], v[172:175], v[188:191], v[124:127]
	v_mfma_f32_16x16x32_bf16 v[116:119], v[180:183], v[188:191], v[116:119]
	v_mfma_f32_16x16x32_bf16 v[108:111], v[172:175], v[196:199], v[108:111]
	v_mfma_f32_16x16x32_bf16 v[100:103], v[180:183], v[196:199], v[100:103]
	v_mfma_f32_16x16x32_bf16 v[92:95], v[172:175], v[204:207], v[92:95]
	v_mfma_f32_16x16x32_bf16 v[84:87], v[180:183], v[204:207], v[84:87]
	v_mfma_f32_16x16x32_bf16 v[76:79], v[172:175], v[212:215], v[76:79]
	v_mfma_f32_16x16x32_bf16 v[68:71], v[180:183], v[212:215], v[68:71]
	v_mfma_f32_16x16x32_bf16 v[124:127], v[176:179], v[192:195], v[124:127]
	v_mfma_f32_16x16x32_bf16 v[116:119], v[184:187], v[192:195], v[116:119]
	v_mfma_f32_16x16x32_bf16 v[108:111], v[176:179], v[200:203], v[108:111]
	v_mfma_f32_16x16x32_bf16 v[100:103], v[184:187], v[200:203], v[100:103]
	v_mfma_f32_16x16x32_bf16 v[92:95], v[176:179], v[208:211], v[92:95]
	v_mfma_f32_16x16x32_bf16 v[84:87], v[184:187], v[208:211], v[84:87]
	v_mfma_f32_16x16x32_bf16 v[76:79], v[176:179], v[216:219], v[76:79]
	v_mfma_f32_16x16x32_bf16 v[68:71], v[184:187], v[216:219], v[68:71]
	s_barrier
	s_add_i32 s63, s55, s97
	v_lshl_add_u64 v[146:147], s[30:31], 0, v[130:131]
	s_mov_b32 m0, s63
	ds_read_b128 v[188:191], v153 offset:16384
	ds_read_b128 v[192:195], v153 offset:17408
	ds_read_b128 v[196:199], v153 offset:18432
	ds_read_b128 v[200:203], v153 offset:19456
	ds_read_b128 v[204:207], v153 offset:20480
	ds_read_b128 v[208:211], v153 offset:21504
	ds_read_b128 v[212:215], v153 offset:22528
	ds_read_b128 v[216:219], v153 offset:23552
	global_load_lds_dwordx4 v[146:147], off
	s_add_i32 m0, s63, 0x2000
	s_add_u32 s64, s30, 0x1c0000
	v_lshl_add_u64 v[220:221], s[30:31], 0, v[128:129]
	s_addc_u32 s65, s31, 0
	s_add_i32 s63, s56, s97
	global_load_lds_dwordx4 v[220:221], off
	v_lshl_add_u64 v[222:223], s[64:65], 0, v[130:131]
	s_mov_b32 m0, s63
	v_lshl_add_u64 v[224:225], s[34:35], 0, v[128:129]
	global_load_lds_dwordx4 v[222:223], off
	v_lshl_add_u64 v[222:223], s[64:65], 0, v[128:129]
	s_add_i32 m0, s63, 0x2000
	s_nop 0
	global_load_lds_dwordx4 v[222:223], off
	v_lshl_add_u64 v[222:223], s[34:35], 0, v[130:131]
	s_mov_b32 m0, s47
	s_nop 0
	global_load_lds_dwordx4 v[222:223], off
	s_mov_b32 m0, s48
	s_nop 0
	global_load_lds_dwordx4 v[224:225], off
	s_waitcnt vmcnt(8)
	s_waitcnt lgkmcnt(0)
	s_barrier
; #define PG8_STAGE(bufoff, gbase, o0, o1) do { \
;         __builtin_amdgcn_global_load_lds((const unsigned*)((const char*)(gbase) + (o0)), (LAS unsigned*)(lds + (bufoff) + ldsw), 16, 0, 0); \
;         __builtin_amdgcn_global_load_lds((const unsigned*)((const char*)(gbase) + (o1)), (LAS unsigned*)(lds + (bufoff) + ldsw + 8192), 16, 0, 0); } while (0)
; #define PG8_LDA(dst, b, h) do { _Pragma("unroll") for (int m = 0; m < 4; ++m) _Pragma("unroll") for (int k = 0; k < 2; ++k) dst[m][k] = *(const LAS bf16x8*)(lds + PG8_SA(b, h) + aoff + m * 2048 + k * 1024); } while (0)
; #define PG8_LDB(dst, b, h) do { _Pragma("unroll") for (int n = 0; n < 2; ++n) _Pragma("unroll") for (int k = 0; k < 2; ++k) dst[n][k] = *(const LAS bf16x8*)(lds + PG8_SB(b, h) + boff + n * 2048 + k * 1024); } while (0)
; #define PG8_WAIT_V(n) asm volatile("s_waitcnt vmcnt(" #n ")" ::: "memory")
; #define PG8_WAIT_L(n) asm volatile("s_waitcnt lgkmcnt(" #n ")" ::: "memory")
; #define PG8_BAR __builtin_amdgcn_s_barrier()
; #define PG8_SCHED __builtin_amdgcn_sched_barrier(0)
; template <class Epi, class Sched, class Prob>
; __device__ __forceinline__ void gemm_phase(LAS unsigned char* lds, LAS unsigned char* lds_epi, const Prob g, const Sched& S, const Epi& E, int wid) {
;     ...
;             PG8_WAIT_V(8); PG8_WAIT_L(0); PG8_BAR; PG8_MMA(1, 0, At, B0); PG8_MMA(1, 1, At, B1); PG8_BAR; PG8_SCHED;
;             PG8_LDB(B0, 1, 0); PG8_LDB(B1, 1, 1); PG8_SCHED; PG8_LDA(At, 1, 0); PG8_STAGE(PG8_SA(0, 1), a2, cA10, cA11);
;             PG8_WAIT_V(8); PG8_WAIT_L(0); PG8_BAR; PG8_MMA(0, 0, At, B0); PG8_MMA(0, 1, At, B1); PG8_BAR; PG8_SCHED;
	s_waitcnt lgkmcnt(0)
	v_mfma_f32_16x16x32_bf16 v[56:59], v[156:159], v[188:191], v[56:59]
	v_mfma_f32_16x16x32_bf16 v[48:51], v[164:167], v[188:191], v[48:51]
	v_mfma_f32_16x16x32_bf16 v[40:43], v[156:159], v[196:199], v[40:43]
	v_mfma_f32_16x16x32_bf16 v[32:35], v[164:167], v[196:199], v[32:35]
	v_mfma_f32_16x16x32_bf16 v[20:23], v[156:159], v[204:207], v[20:23]
	v_mfma_f32_16x16x32_bf16 v[8:11], v[164:167], v[204:207], v[8:11]
	v_mfma_f32_16x16x32_bf16 v[4:7], v[156:159], v[212:215], v[4:7]
	v_mfma_f32_16x16x32_bf16 v[0:3], v[164:167], v[212:215], v[0:3]
	v_mfma_f32_16x16x32_bf16 v[56:59], v[160:163], v[192:195], v[56:59]
	v_mfma_f32_16x16x32_bf16 v[48:51], v[168:171], v[192:195], v[48:51]
	v_mfma_f32_16x16x32_bf16 v[40:43], v[160:163], v[200:203], v[40:43]
	v_mfma_f32_16x16x32_bf16 v[32:35], v[168:171], v[200:203], v[32:35]
	v_mfma_f32_16x16x32_bf16 v[20:23], v[160:163], v[208:211], v[20:23]
	v_mfma_f32_16x16x32_bf16 v[8:11], v[168:171], v[208:211], v[8:11]
	v_mfma_f32_16x16x32_bf16 v[4:7], v[160:163], v[216:219], v[4:7]
	v_mfma_f32_16x16x32_bf16 v[0:3], v[168:171], v[216:219], v[0:3]
	v_mfma_f32_16x16x32_bf16 v[60:63], v[172:175], v[188:191], v[60:63]
	v_mfma_f32_16x16x32_bf16 v[52:55], v[180:183], v[188:191], v[52:55]
	v_mfma_f32_16x16x32_bf16 v[44:47], v[172:175], v[196:199], v[44:47]
	v_mfma_f32_16x16x32_bf16 v[36:39], v[180:183], v[196:199], v[36:39]
	v_mfma_f32_16x16x32_bf16 v[28:31], v[172:175], v[204:207], v[28:31]
	v_mfma_f32_16x16x32_bf16 v[16:19], v[180:183], v[204:207], v[16:19]
	v_mfma_f32_16x16x32_bf16 v[24:27], v[172:175], v[212:215], v[24:27]
	v_mfma_f32_16x16x32_bf16 v[12:15], v[180:183], v[212:215], v[12:15]
	v_mfma_f32_16x16x32_bf16 v[60:63], v[176:179], v[192:195], v[60:63]
	v_mfma_f32_16x16x32_bf16 v[52:55], v[184:187], v[192:195], v[52:55]
	v_mfma_f32_16x16x32_bf16 v[44:47], v[176:179], v[200:203], v[44:47]
	v_mfma_f32_16x16x32_bf16 v[36:39], v[184:187], v[200:203], v[36:39]
	v_mfma_f32_16x16x32_bf16 v[28:31], v[176:179], v[208:211], v[28:31]
	v_mfma_f32_16x16x32_bf16 v[16:19], v[184:187], v[208:211], v[16:19]
	v_mfma_f32_16x16x32_bf16 v[24:27], v[176:179], v[216:219], v[24:27]
	v_mfma_f32_16x16x32_bf16 v[12:15], v[184:187], v[216:219], v[12:15]
	s_barrier
	s_add_i32 s63, 0, 0x18000
	s_add_i32 s64, 0, 0x1c000
	v_add_u32_e32 v168, s63, v149
	v_add_u32_e32 v184, s64, v149
	ds_read_b128 v[156:159], v168
	ds_read_b128 v[160:163], v168 offset:1024
	ds_read_b128 v[164:167], v168 offset:2048
	ds_read_b128 v[168:171], v168 offset:3072
	ds_read_b128 v[172:175], v184
	ds_read_b128 v[176:179], v184 offset:1024
	ds_read_b128 v[180:183], v184 offset:2048
	ds_read_b128 v[184:187], v184 offset:3072
	s_mov_b32 m0, s49
	v_lshl_add_u64 v[226:227], s[34:35], 0, v[132:133]
	ds_read_b128 v[188:191], v153 offset:32768
	ds_read_b128 v[192:195], v153 offset:33792
	ds_read_b128 v[196:199], v153 offset:34816
	ds_read_b128 v[200:203], v153 offset:35840
	ds_read_b128 v[204:207], v153 offset:36864
	ds_read_b128 v[208:211], v153 offset:37888
	ds_read_b128 v[212:215], v153 offset:38912
	ds_read_b128 v[216:219], v153 offset:39936
	global_load_lds_dwordx4 v[226:227], off
	v_lshl_add_u64 v[226:227], s[34:35], 0, v[134:135]
	s_mov_b32 m0, s50
	s_nop 0
	global_load_lds_dwordx4 v[226:227], off
	s_waitcnt vmcnt(8)
	s_waitcnt lgkmcnt(0)
	s_barrier
	s_waitcnt lgkmcnt(0)
	v_mfma_f32_16x16x32_bf16 v[120:123], v[156:159], v[188:191], v[120:123]
	v_mfma_f32_16x16x32_bf16 v[112:115], v[164:167], v[188:191], v[112:115]
	v_mfma_f32_16x16x32_bf16 v[104:107], v[156:159], v[196:199], v[104:107]
	v_mfma_f32_16x16x32_bf16 v[96:99], v[164:167], v[196:199], v[96:99]
	v_mfma_f32_16x16x32_bf16 v[88:91], v[156:159], v[204:207], v[88:91]
	v_mfma_f32_16x16x32_bf16 v[80:83], v[164:167], v[204:207], v[80:83]
	v_mfma_f32_16x16x32_bf16 v[72:75], v[156:159], v[212:215], v[72:75]
	v_mfma_f32_16x16x32_bf16 v[64:67], v[164:167], v[212:215], v[64:67]
	v_mfma_f32_16x16x32_bf16 v[120:123], v[160:163], v[192:195], v[120:123]
	v_mfma_f32_16x16x32_bf16 v[112:115], v[168:171], v[192:195], v[112:115]
	v_mfma_f32_16x16x32_bf16 v[104:107], v[160:163], v[200:203], v[104:107]
	v_mfma_f32_16x16x32_bf16 v[96:99], v[168:171], v[200:203], v[96:99]
	v_mfma_f32_16x16x32_bf16 v[88:91], v[160:163], v[208:211], v[88:91]
	v_mfma_f32_16x16x32_bf16 v[80:83], v[168:171], v[208:211], v[80:83]
	v_mfma_f32_16x16x32_bf16 v[72:75], v[160:163], v[216:219], v[72:75]
	v_mfma_f32_16x16x32_bf16 v[64:67], v[168:171], v[216:219], v[64:67]
	v_mfma_f32_16x16x32_bf16 v[124:127], v[172:175], v[188:191], v[124:127]
	v_mfma_f32_16x16x32_bf16 v[116:119], v[180:183], v[188:191], v[116:119]
	v_mfma_f32_16x16x32_bf16 v[108:111], v[172:175], v[196:199], v[108:111]
	v_mfma_f32_16x16x32_bf16 v[100:103], v[180:183], v[196:199], v[100:103]
	v_mfma_f32_16x16x32_bf16 v[92:95], v[172:175], v[204:207], v[92:95]
	v_mfma_f32_16x16x32_bf16 v[84:87], v[180:183], v[204:207], v[84:87]
	v_mfma_f32_16x16x32_bf16 v[76:79], v[172:175], v[212:215], v[76:79]
	v_mfma_f32_16x16x32_bf16 v[68:71], v[180:183], v[212:215], v[68:71]
	v_mfma_f32_16x16x32_bf16 v[124:127], v[176:179], v[192:195], v[124:127]
	v_mfma_f32_16x16x32_bf16 v[116:119], v[184:187], v[192:195], v[116:119]
	v_mfma_f32_16x16x32_bf16 v[108:111], v[176:179], v[200:203], v[108:111]
	v_mfma_f32_16x16x32_bf16 v[100:103], v[184:187], v[200:203], v[100:103]
	v_mfma_f32_16x16x32_bf16 v[92:95], v[176:179], v[208:211], v[92:95]
	v_mfma_f32_16x16x32_bf16 v[84:87], v[184:187], v[208:211], v[84:87]
	v_mfma_f32_16x16x32_bf16 v[76:79], v[176:179], v[216:219], v[76:79]
	v_mfma_f32_16x16x32_bf16 v[68:71], v[184:187], v[216:219], v[68:71]
	s_barrier
; #define PG8_STAGE(bufoff, gbase, o0, o1) do { \
;         __builtin_amdgcn_global_load_lds((const unsigned*)((const char*)(gbase) + (o0)), (LAS unsigned*)(lds + (bufoff) + ldsw), 16, 0, 0); \
;         __builtin_amdgcn_global_load_lds((const unsigned*)((const char*)(gbase) + (o1)), (LAS unsigned*)(lds + (bufoff) + ldsw + 8192), 16, 0, 0); } while (0)
; #define PG8_LDA(dst, b, h) do { _Pragma("unroll") for (int m = 0; m < 4; ++m) _Pragma("unroll") for (int k = 0; k < 2; ++k) dst[m][k] = *(const LAS bf16x8*)(lds + PG8_SA(b, h) + aoff + m * 2048 + k * 1024); } while (0)
; #define PG8_WAIT_V(n) asm volatile("s_waitcnt vmcnt(" #n ")" ::: "memory")
; #define PG8_WAIT_L(n) asm volatile("s_waitcnt lgkmcnt(" #n ")" ::: "memory")
; #define PG8_BAR __builtin_amdgcn_s_barrier()
; #define PG8_SCHED __builtin_amdgcn_sched_barrier(0)
; template <class Epi, class Sched, class Prob>
; __device__ __forceinline__ void gemm_phase(LAS unsigned char* lds, LAS unsigned char* lds_epi, const Prob g, const Sched& S, const Epi& E, int wid) {
;     ...
;             PG8_LDA(At, 1, 1); PG8_STAGE(PG8_SB(1, 0), b3, vB0, vB1); PG8_STAGE(PG8_SB(1, 1), b3 + hstepB, vB0, vB1); PG8_STAGE(PG8_SA(1, 0), a3, cA00, cA01);
;             PG8_WAIT_V(8); PG8_WAIT_L(0); PG8_BAR; PG8_MMA(1, 0, At, B0); PG8_MMA(1, 1, At, B1); PG8_BAR; PG8_SCHED;
;         }
;         if constexpr (Prob::FP8) asm volatile("s_nop 7\n\ts_nop 7\n\ts_nop 7" ::: "memory");
;         if (wr == 0) PG8_BAR;
	s_add_i32 s34, s63, s97
	v_lshl_add_u64 v[146:147], v[146:147], 0, s[16:17]
	s_mov_b32 m0, s34
	ds_read_b128 v[188:191], v153 offset:49152
	ds_read_b128 v[192:195], v153 offset:50176
	ds_read_b128 v[196:199], v153 offset:51200
	ds_read_b128 v[200:203], v153 offset:52224
	ds_read_b128 v[204:207], v153 offset:53248
	ds_read_b128 v[208:211], v153 offset:54272
	ds_read_b128 v[212:215], v153 offset:55296
	ds_read_b128 v[216:219], v153 offset:56320
	global_load_lds_dwordx4 v[146:147], off
	s_add_i32 m0, s34, 0x2000
	s_add_u32 s30, s30, 0x1c0080
	v_lshl_add_u64 v[146:147], v[220:221], 0, s[16:17]
	s_addc_u32 s31, s31, 0
	s_add_i32 s34, s64, s97
	global_load_lds_dwordx4 v[146:147], off
	v_lshl_add_u64 v[146:147], s[30:31], 0, v[130:131]
	s_mov_b32 m0, s34
	s_nop 0
	global_load_lds_dwordx4 v[146:147], off
	v_lshl_add_u64 v[146:147], s[30:31], 0, v[128:129]
	s_add_i32 m0, s34, 0x2000
	s_nop 0
	global_load_lds_dwordx4 v[146:147], off
	v_lshl_add_u64 v[146:147], v[222:223], 0, s[16:17]
	s_mov_b32 m0, s53
	s_nop 0
	global_load_lds_dwordx4 v[146:147], off
	v_lshl_add_u64 v[146:147], v[224:225], 0, s[16:17]
	s_mov_b32 m0, s54
	s_nop 0
	global_load_lds_dwordx4 v[146:147], off
	s_waitcnt vmcnt(8)
	s_waitcnt lgkmcnt(0)
	s_barrier
	s_waitcnt lgkmcnt(0)
	v_mfma_f32_16x16x32_bf16 v[56:59], v[156:159], v[188:191], v[56:59]
	v_mfma_f32_16x16x32_bf16 v[48:51], v[164:167], v[188:191], v[48:51]
	v_mfma_f32_16x16x32_bf16 v[40:43], v[156:159], v[196:199], v[40:43]
	v_mfma_f32_16x16x32_bf16 v[32:35], v[164:167], v[196:199], v[32:35]
	v_mfma_f32_16x16x32_bf16 v[20:23], v[156:159], v[204:207], v[20:23]
	v_mfma_f32_16x16x32_bf16 v[8:11], v[164:167], v[204:207], v[8:11]
	v_mfma_f32_16x16x32_bf16 v[4:7], v[156:159], v[212:215], v[4:7]
	v_mfma_f32_16x16x32_bf16 v[0:3], v[164:167], v[212:215], v[0:3]
	v_mfma_f32_16x16x32_bf16 v[56:59], v[160:163], v[192:195], v[56:59]
	v_mfma_f32_16x16x32_bf16 v[48:51], v[168:171], v[192:195], v[48:51]
	v_mfma_f32_16x16x32_bf16 v[40:43], v[160:163], v[200:203], v[40:43]
	v_mfma_f32_16x16x32_bf16 v[32:35], v[168:171], v[200:203], v[32:35]
	v_mfma_f32_16x16x32_bf16 v[20:23], v[160:163], v[208:211], v[20:23]
	v_mfma_f32_16x16x32_bf16 v[8:11], v[168:171], v[208:211], v[8:11]
	v_mfma_f32_16x16x32_bf16 v[4:7], v[160:163], v[216:219], v[4:7]
	v_mfma_f32_16x16x32_bf16 v[0:3], v[168:171], v[216:219], v[0:3]
	v_mfma_f32_16x16x32_bf16 v[60:63], v[172:175], v[188:191], v[60:63]
	v_mfma_f32_16x16x32_bf16 v[52:55], v[180:183], v[188:191], v[52:55]
	v_mfma_f32_16x16x32_bf16 v[44:47], v[172:175], v[196:199], v[44:47]
	v_mfma_f32_16x16x32_bf16 v[36:39], v[180:183], v[196:199], v[36:39]
	v_mfma_f32_16x16x32_bf16 v[28:31], v[172:175], v[204:207], v[28:31]
	v_mfma_f32_16x16x32_bf16 v[16:19], v[180:183], v[204:207], v[16:19]
	v_mfma_f32_16x16x32_bf16 v[24:27], v[172:175], v[212:215], v[24:27]
	v_mfma_f32_16x16x32_bf16 v[12:15], v[180:183], v[212:215], v[12:15]
	v_mfma_f32_16x16x32_bf16 v[60:63], v[176:179], v[192:195], v[60:63]
	v_mfma_f32_16x16x32_bf16 v[52:55], v[184:187], v[192:195], v[52:55]
	v_mfma_f32_16x16x32_bf16 v[44:47], v[176:179], v[200:203], v[44:47]
	v_mfma_f32_16x16x32_bf16 v[36:39], v[184:187], v[200:203], v[36:39]
	v_mfma_f32_16x16x32_bf16 v[28:31], v[176:179], v[208:211], v[28:31]
	v_mfma_f32_16x16x32_bf16 v[16:19], v[184:187], v[208:211], v[16:19]
	v_mfma_f32_16x16x32_bf16 v[24:27], v[176:179], v[216:219], v[24:27]
	v_mfma_f32_16x16x32_bf16 v[12:15], v[184:187], v[216:219], v[12:15]
	s_barrier
	s_add_i32 s62, s62, 2
	s_add_u32 s28, s28, 0x100
	s_addc_u32 s29, s29, 0
	s_add_u32 s60, s60, 0x100
	s_addc_u32 s61, s61, 0
	s_cmpk_gt_u32 s62, 0x6d
	s_cbranch_scc0 .LBB0_1336
	s_setprio 0
	v_readlane_b32 s28, v254, 27
	v_readlane_b32 s29, v254, 28
	s_and_b64 vcc, exec, s[28:29]
	s_cbranch_vccz .LBB0_1339
	s_barrier

; #define PG8_STAGE(bufoff, gbase, o0, o1) do { \
;         __builtin_amdgcn_global_load_lds((const unsigned*)((const char*)(gbase) + (o0)), (LAS unsigned*)(lds + (bufoff) + ldsw), 16, 0, 0); \
;         __builtin_amdgcn_global_load_lds((const unsigned*)((const char*)(gbase) + (o1)), (LAS unsigned*)(lds + (bufoff) + ldsw + 8192), 16, 0, 0); } while (0)
; #define PG8_LDA(dst, b, h) do { _Pragma("unroll") for (int m = 0; m < 4; ++m) _Pragma("unroll") for (int k = 0; k < 2; ++k) dst[m][k] = *(const LAS bf16x8*)(lds + PG8_SA(b, h) + aoff + m * 2048 + k * 1024); } while (0)
; #define PG8_LDB(dst, b, h) do { _Pragma("unroll") for (int n = 0; n < 2; ++n) _Pragma("unroll") for (int k = 0; k < 2; ++k) dst[n][k] = *(const LAS bf16x8*)(lds + PG8_SB(b, h) + boff + n * 2048 + k * 1024); } while (0)
; #define PG8_WAIT_V(n) asm volatile("s_waitcnt vmcnt(" #n ")" ::: "memory")
; #define PG8_WAIT_L(n) asm volatile("s_waitcnt lgkmcnt(" #n ")" ::: "memory")
; #define PG8_BAR __builtin_amdgcn_s_barrier()
; #define PG8_SCHED __builtin_amdgcn_sched_barrier(0)
; template <class Epi, class Sched, class Prob>
; __device__ __forceinline__ void gemm_phase(LAS unsigned char* lds, LAS unsigned char* lds_epi, const Prob g, const Sched& S, const Epi& E, int wid) {
;     ...
;         const bool has_next = S.next(ui + 1, nxt);
;         const char* nA = has_next ? g.a_base(nxt) : cA; const char* nB = has_next ? g.b_base(nxt) : cB;
; _Pragma("clang loop unroll(disable)")
;         for (int t = 0; t < nt; t += 2) {
;             const bool last = (t == nt - 2);
;             const char* a1 = cA + (size_t)(t + 1) * kstep;
;             const char* a2 = last ? nA : cA + (size_t)(t + 2) * kstep; const char* b2 = last ? nB : cB + (size_t)(t + 2) * kstep;
;             const char* a3 = a2 + kstep; const char* b3 = b2 + kstep;
;             PG8_LDB(B0, 0, 0); PG8_LDB(B1, 0, 1); PG8_SCHED; PG8_LDA(At, 0, 0); PG8_STAGE(PG8_SA(1, 1), a1, cA10, cA11);
;             PG8_WAIT_V(8); PG8_WAIT_L(0); PG8_BAR; PG8_MMA(0, 0, At, B0); PG8_MMA(0, 1, At, B1); PG8_BAR; PG8_SCHED;
;             PG8_LDA(At, 0, 1); PG8_STAGE(PG8_SB(0, 0), b2, vB0, vB1); PG8_STAGE(PG8_SB(0, 1), b2 + hstepB, vB0, vB1); PG8_STAGE(PG8_SA(0, 0), a2, cA00, cA01);
;             PG8_WAIT_V(8); PG8_WAIT_L(0); PG8_BAR; PG8_MMA(1, 0, At, B0); PG8_MMA(1, 1, At, B1); PG8_BAR; PG8_SCHED;
.LBB0_1433:
	s_ashr_i32 s17, s16, 31
	s_lshl_b64 s[40:41], s[16:17], 20
	s_add_u32 s40, s58, s40
	s_addc_u32 s41, s59, s41
	s_and_b64 s[42:43], s[36:37], exec
	s_cselect_b32 s17, s41, s11
	s_cselect_b32 s52, s40, s10
	s_ashr_i32 s35, s34, 31
	s_lshl_b64 s[42:43], s[34:35], 20
	s_add_u32 s42, s60, s42
	s_addc_u32 s43, s61, s43
	s_and_b64 s[48:49], s[36:37], exec
	s_cselect_b32 s35, s43, s47
	s_cselect_b32 s53, s42, s46
	s_add_u32 s54, s46, 0x100
	v_mov_b32_e32 v0, 0
	s_addc_u32 s55, s47, 0
	s_mov_b32 s87, -2
	s_cmp_lt_u32 s91, 0x100
	s_cbranch_scc1 .Lyoung_4
	s_setprio 1
.Lyoung_4:
	ds_read_b128 v[146:149], v240
	ds_read_b128 v[150:153], v240 offset:1024
	ds_read_b128 v[154:157], v240 offset:2048
	ds_read_b128 v[158:161], v240 offset:3072
	ds_read_b128 v[162:165], v241
	ds_read_b128 v[166:169], v241 offset:1024
	ds_read_b128 v[170:173], v241 offset:2048
	ds_read_b128 v[174:177], v241 offset:3072
	s_add_u32 s46, s10, 0x100
	s_addc_u32 s47, s11, 0
	s_cmp_eq_u32 s87, 28
	s_cselect_b32 s51, s17, s47
	s_cselect_b32 s50, s52, s46
	s_cselect_b32 s49, s35, s55
	s_cselect_b32 s48, s53, s54
	v_lshl_add_u64 v[210:211], s[10:11], 0, v[142:143]
	s_add_i32 m0, s62, 0xc000
	ds_read_b128 v[178:181], v242
	ds_read_b128 v[182:185], v242 offset:1024
	ds_read_b128 v[186:189], v242 offset:2048
	ds_read_b128 v[190:193], v242 offset:3072
	ds_read_b128 v[194:197], v242 offset:4096
	ds_read_b128 v[198:201], v242 offset:5120
	ds_read_b128 v[202:205], v242 offset:6144
	ds_read_b128 v[206:209], v242 offset:7168
	global_load_lds_dwordx4 v[210:211], off
	v_lshl_add_u64 v[210:211], s[10:11], 0, v[140:141]
	s_add_i32 m0, s62, 0xe000
	s_nop 0
	global_load_lds_dwordx4 v[210:211], off
	s_waitcnt vmcnt(8)
	s_waitcnt lgkmcnt(0)
	s_barrier
	s_waitcnt lgkmcnt(0)
	v_mfma_f32_16x16x32_bf16 v[124:127], v[146:149], v[178:181], 0
	v_mfma_f32_16x16x32_bf16 v[120:123], v[154:157], v[178:181], 0
	v_mfma_f32_16x16x32_bf16 v[116:119], v[146:149], v[186:189], 0
	v_mfma_f32_16x16x32_bf16 v[112:115], v[154:157], v[186:189], 0
	v_mfma_f32_16x16x32_bf16 v[108:111], v[146:149], v[194:197], 0
	v_mfma_f32_16x16x32_bf16 v[100:103], v[154:157], v[194:197], 0
	v_mfma_f32_16x16x32_bf16 v[92:95], v[146:149], v[202:205], 0
	v_mfma_f32_16x16x32_bf16 v[84:87], v[154:157], v[202:205], 0
	v_mfma_f32_16x16x32_bf16 v[124:127], v[150:153], v[182:185], v[124:127]
	v_mfma_f32_16x16x32_bf16 v[120:123], v[158:161], v[182:185], v[120:123]
	v_mfma_f32_16x16x32_bf16 v[116:119], v[150:153], v[190:193], v[116:119]
	v_mfma_f32_16x16x32_bf16 v[112:115], v[158:161], v[190:193], v[112:115]
	v_mfma_f32_16x16x32_bf16 v[108:111], v[150:153], v[198:201], v[108:111]
	v_mfma_f32_16x16x32_bf16 v[100:103], v[158:161], v[198:201], v[100:103]
	v_mfma_f32_16x16x32_bf16 v[92:95], v[150:153], v[206:209], v[92:95]
	v_mfma_f32_16x16x32_bf16 v[84:87], v[158:161], v[206:209], v[84:87]
	v_mfma_f32_16x16x32_bf16 v[104:107], v[162:165], v[178:181], 0
	v_mfma_f32_16x16x32_bf16 v[96:99], v[170:173], v[178:181], 0
	v_mfma_f32_16x16x32_bf16 v[88:91], v[162:165], v[186:189], 0
	v_mfma_f32_16x16x32_bf16 v[80:83], v[170:173], v[186:189], 0
	v_mfma_f32_16x16x32_bf16 v[76:79], v[162:165], v[194:197], 0
	v_mfma_f32_16x16x32_bf16 v[72:75], v[170:173], v[194:197], 0
	v_mfma_f32_16x16x32_bf16 v[68:71], v[162:165], v[202:205], 0
	v_mfma_f32_16x16x32_bf16 v[64:67], v[170:173], v[202:205], 0
	v_mfma_f32_16x16x32_bf16 v[104:107], v[166:169], v[182:185], v[104:107]
	v_mfma_f32_16x16x32_bf16 v[96:99], v[174:177], v[182:185], v[96:99]
	v_mfma_f32_16x16x32_bf16 v[88:91], v[166:169], v[190:193], v[88:91]
	v_mfma_f32_16x16x32_bf16 v[80:83], v[174:177], v[190:193], v[80:83]
	v_mfma_f32_16x16x32_bf16 v[76:79], v[166:169], v[198:201], v[76:79]
	v_mfma_f32_16x16x32_bf16 v[72:75], v[174:177], v[198:201], v[72:75]
	v_mfma_f32_16x16x32_bf16 v[68:71], v[166:169], v[206:209], v[68:71]
	v_mfma_f32_16x16x32_bf16 v[64:67], v[174:177], v[206:209], v[64:67]
	s_barrier
	s_add_i32 s10, s80, s97
	v_lshl_add_u64 v[210:211], s[48:49], 0, v[128:129]
	s_mov_b32 m0, s10
	ds_read_b128 v[178:181], v242 offset:16384
	ds_read_b128 v[182:185], v242 offset:17408
	ds_read_b128 v[186:189], v242 offset:18432
	ds_read_b128 v[190:193], v242 offset:19456
	ds_read_b128 v[194:197], v242 offset:20480
	ds_read_b128 v[198:201], v242 offset:21504
	ds_read_b128 v[202:205], v242 offset:22528
	ds_read_b128 v[206:209], v242 offset:23552
	global_load_lds_dwordx4 v[210:211], off
	s_add_i32 m0, s10, 0x2000
	s_add_u32 s10, s48, 0x80000
	v_lshl_add_u64 v[212:213], s[48:49], 0, v[130:131]
	s_addc_u32 s11, s49, 0
	s_add_i32 s88, s81, s97
	global_load_lds_dwordx4 v[212:213], off
	v_lshl_add_u64 v[214:215], s[10:11], 0, v[128:129]
	s_mov_b32 m0, s88
	v_lshl_add_u64 v[216:217], s[50:51], 0, v[136:137]
	global_load_lds_dwordx4 v[214:215], off
	v_lshl_add_u64 v[214:215], s[10:11], 0, v[130:131]
	s_add_i32 m0, s88, 0x2000
	s_nop 0
	global_load_lds_dwordx4 v[214:215], off
	v_lshl_add_u64 v[214:215], s[50:51], 0, v[132:133]
	s_mov_b32 m0, s62
	s_nop 0
	global_load_lds_dwordx4 v[214:215], off
	s_mov_b32 m0, s63
	s_nop 0
	global_load_lds_dwordx4 v[216:217], off
	s_waitcnt vmcnt(8)
	s_waitcnt lgkmcnt(0)
	s_barrier
; #define PG8_STAGE(bufoff, gbase, o0, o1) do { \
;         __builtin_amdgcn_global_load_lds((const unsigned*)((const char*)(gbase) + (o0)), (LAS unsigned*)(lds + (bufoff) + ldsw), 16, 0, 0); \
;         __builtin_amdgcn_global_load_lds((const unsigned*)((const char*)(gbase) + (o1)), (LAS unsigned*)(lds + (bufoff) + ldsw + 8192), 16, 0, 0); } while (0)
; #define PG8_LDA(dst, b, h) do { _Pragma("unroll") for (int m = 0; m < 4; ++m) _Pragma("unroll") for (int k = 0; k < 2; ++k) dst[m][k] = *(const LAS bf16x8*)(lds + PG8_SA(b, h) + aoff + m * 2048 + k * 1024); } while (0)
; #define PG8_LDB(dst, b, h) do { _Pragma("unroll") for (int n = 0; n < 2; ++n) _Pragma("unroll") for (int k = 0; k < 2; ++k) dst[n][k] = *(const LAS bf16x8*)(lds + PG8_SB(b, h) + boff + n * 2048 + k * 1024); } while (0)
; #define PG8_WAIT_V(n) asm volatile("s_waitcnt vmcnt(" #n ")" ::: "memory")
; #define PG8_WAIT_L(n) asm volatile("s_waitcnt lgkmcnt(" #n ")" ::: "memory")
; #define PG8_BAR __builtin_amdgcn_s_barrier()
; #define PG8_SCHED __builtin_amdgcn_sched_barrier(0)
; template <class Epi, class Sched, class Prob>
; __device__ __forceinline__ void gemm_phase(LAS unsigned char* lds, LAS unsigned char* lds_epi, const Prob g, const Sched& S, const Epi& E, int wid) {
;     ...
;             PG8_WAIT_V(8); PG8_WAIT_L(0); PG8_BAR; PG8_MMA(1, 0, At, B0); PG8_MMA(1, 1, At, B1); PG8_BAR; PG8_SCHED;
;             PG8_LDB(B0, 1, 0); PG8_LDB(B1, 1, 1); PG8_SCHED; PG8_LDA(At, 1, 0); PG8_STAGE(PG8_SA(0, 1), a2, cA10, cA11);
;             PG8_WAIT_V(8); PG8_WAIT_L(0); PG8_BAR; PG8_MMA(0, 0, At, B0); PG8_MMA(0, 1, At, B1); PG8_BAR; PG8_SCHED;
	s_waitcnt lgkmcnt(0)
	v_mfma_f32_16x16x32_bf16 v[60:63], v[146:149], v[178:181], 0
	v_mfma_f32_16x16x32_bf16 v[56:59], v[154:157], v[178:181], 0
	v_mfma_f32_16x16x32_bf16 v[52:55], v[146:149], v[186:189], 0
	v_mfma_f32_16x16x32_bf16 v[48:51], v[154:157], v[186:189], 0
	v_mfma_f32_16x16x32_bf16 v[36:39], v[146:149], v[194:197], 0
	v_mfma_f32_16x16x32_bf16 v[32:35], v[154:157], v[194:197], 0
	v_mfma_f32_16x16x32_bf16 v[20:23], v[146:149], v[202:205], 0
	v_mfma_f32_16x16x32_bf16 v[16:19], v[154:157], v[202:205], 0
	v_mfma_f32_16x16x32_bf16 v[60:63], v[150:153], v[182:185], v[60:63]
	v_mfma_f32_16x16x32_bf16 v[56:59], v[158:161], v[182:185], v[56:59]
	v_mfma_f32_16x16x32_bf16 v[52:55], v[150:153], v[190:193], v[52:55]
	v_mfma_f32_16x16x32_bf16 v[48:51], v[158:161], v[190:193], v[48:51]
	v_mfma_f32_16x16x32_bf16 v[36:39], v[150:153], v[198:201], v[36:39]
	v_mfma_f32_16x16x32_bf16 v[32:35], v[158:161], v[198:201], v[32:35]
	v_mfma_f32_16x16x32_bf16 v[20:23], v[150:153], v[206:209], v[20:23]
	v_mfma_f32_16x16x32_bf16 v[16:19], v[158:161], v[206:209], v[16:19]
	v_mfma_f32_16x16x32_bf16 v[44:47], v[162:165], v[178:181], 0
	v_mfma_f32_16x16x32_bf16 v[40:43], v[170:173], v[178:181], 0
	v_mfma_f32_16x16x32_bf16 v[28:31], v[162:165], v[186:189], 0
	v_mfma_f32_16x16x32_bf16 v[24:27], v[170:173], v[186:189], 0
	v_mfma_f32_16x16x32_bf16 v[12:15], v[162:165], v[194:197], 0
	v_mfma_f32_16x16x32_bf16 v[8:11], v[170:173], v[194:197], 0
	v_mfma_f32_16x16x32_bf16 v[4:7], v[162:165], v[202:205], 0
	v_mfma_f32_16x16x32_bf16 v[0:3], v[170:173], v[202:205], 0
	v_mfma_f32_16x16x32_bf16 v[44:47], v[166:169], v[182:185], v[44:47]
	v_mfma_f32_16x16x32_bf16 v[40:43], v[174:177], v[182:185], v[40:43]
	v_mfma_f32_16x16x32_bf16 v[28:31], v[166:169], v[190:193], v[28:31]
	v_mfma_f32_16x16x32_bf16 v[24:27], v[174:177], v[190:193], v[24:27]
	v_mfma_f32_16x16x32_bf16 v[12:15], v[166:169], v[198:201], v[12:15]
	v_mfma_f32_16x16x32_bf16 v[8:11], v[174:177], v[198:201], v[8:11]
	v_mfma_f32_16x16x32_bf16 v[4:7], v[166:169], v[206:209], v[4:7]
	v_mfma_f32_16x16x32_bf16 v[0:3], v[174:177], v[206:209], v[0:3]
	s_barrier
	s_add_i32 s10, 0, 0x18000
	s_add_i32 s88, 0, 0x1c000
	v_add_u32_e32 v158, s10, v239
	v_add_u32_e32 v174, s88, v239
	ds_read_b128 v[146:149], v158
	ds_read_b128 v[150:153], v158 offset:1024
	ds_read_b128 v[154:157], v158 offset:2048
	ds_read_b128 v[158:161], v158 offset:3072
	ds_read_b128 v[162:165], v174
	ds_read_b128 v[166:169], v174 offset:1024
	ds_read_b128 v[170:173], v174 offset:2048
	ds_read_b128 v[174:177], v174 offset:3072
	s_mov_b32 m0, s64
	v_lshl_add_u64 v[218:219], s[50:51], 0, v[134:135]
	ds_read_b128 v[178:181], v242 offset:32768
	ds_read_b128 v[182:185], v242 offset:33792
	ds_read_b128 v[186:189], v242 offset:34816
	ds_read_b128 v[190:193], v242 offset:35840
	ds_read_b128 v[194:197], v242 offset:36864
	ds_read_b128 v[198:201], v242 offset:37888
	ds_read_b128 v[202:205], v242 offset:38912
	ds_read_b128 v[206:209], v242 offset:39936
	global_load_lds_dwordx4 v[218:219], off
	v_lshl_add_u64 v[218:219], s[50:51], 0, v[138:139]
	s_mov_b32 m0, s65
	s_nop 0
	global_load_lds_dwordx4 v[218:219], off
	s_waitcnt vmcnt(8)
	s_waitcnt lgkmcnt(0)
	s_barrier
	s_waitcnt lgkmcnt(0)
	v_mfma_f32_16x16x32_bf16 v[124:127], v[146:149], v[178:181], v[124:127]
	v_mfma_f32_16x16x32_bf16 v[120:123], v[154:157], v[178:181], v[120:123]
	v_mfma_f32_16x16x32_bf16 v[116:119], v[146:149], v[186:189], v[116:119]
	v_mfma_f32_16x16x32_bf16 v[112:115], v[154:157], v[186:189], v[112:115]
	v_mfma_f32_16x16x32_bf16 v[108:111], v[146:149], v[194:197], v[108:111]
	v_mfma_f32_16x16x32_bf16 v[100:103], v[154:157], v[194:197], v[100:103]
	v_mfma_f32_16x16x32_bf16 v[92:95], v[146:149], v[202:205], v[92:95]
	v_mfma_f32_16x16x32_bf16 v[84:87], v[154:157], v[202:205], v[84:87]
	v_mfma_f32_16x16x32_bf16 v[124:127], v[150:153], v[182:185], v[124:127]
	v_mfma_f32_16x16x32_bf16 v[120:123], v[158:161], v[182:185], v[120:123]
	v_mfma_f32_16x16x32_bf16 v[116:119], v[150:153], v[190:193], v[116:119]
	v_mfma_f32_16x16x32_bf16 v[112:115], v[158:161], v[190:193], v[112:115]
	v_mfma_f32_16x16x32_bf16 v[108:111], v[150:153], v[198:201], v[108:111]
	v_mfma_f32_16x16x32_bf16 v[100:103], v[158:161], v[198:201], v[100:103]
	v_mfma_f32_16x16x32_bf16 v[92:95], v[150:153], v[206:209], v[92:95]
	v_mfma_f32_16x16x32_bf16 v[84:87], v[158:161], v[206:209], v[84:87]
	v_mfma_f32_16x16x32_bf16 v[104:107], v[162:165], v[178:181], v[104:107]
	v_mfma_f32_16x16x32_bf16 v[96:99], v[170:173], v[178:181], v[96:99]
	v_mfma_f32_16x16x32_bf16 v[88:91], v[162:165], v[186:189], v[88:91]
	v_mfma_f32_16x16x32_bf16 v[80:83], v[170:173], v[186:189], v[80:83]
	v_mfma_f32_16x16x32_bf16 v[76:79], v[162:165], v[194:197], v[76:79]
	v_mfma_f32_16x16x32_bf16 v[72:75], v[170:173], v[194:197], v[72:75]
	v_mfma_f32_16x16x32_bf16 v[68:71], v[162:165], v[202:205], v[68:71]
	v_mfma_f32_16x16x32_bf16 v[64:67], v[170:173], v[202:205], v[64:67]
	v_mfma_f32_16x16x32_bf16 v[104:107], v[166:169], v[182:185], v[104:107]
	v_mfma_f32_16x16x32_bf16 v[96:99], v[174:177], v[182:185], v[96:99]
	v_mfma_f32_16x16x32_bf16 v[88:91], v[166:169], v[190:193], v[88:91]
	v_mfma_f32_16x16x32_bf16 v[80:83], v[174:177], v[190:193], v[80:83]
	v_mfma_f32_16x16x32_bf16 v[76:79], v[166:169], v[198:201], v[76:79]
	v_mfma_f32_16x16x32_bf16 v[72:75], v[174:177], v[198:201], v[72:75]
	v_mfma_f32_16x16x32_bf16 v[68:71], v[166:169], v[206:209], v[68:71]
	v_mfma_f32_16x16x32_bf16 v[64:67], v[174:177], v[206:209], v[64:67]
	s_barrier
; #define PG8_STAGE(bufoff, gbase, o0, o1) do { \
;         __builtin_amdgcn_global_load_lds((const unsigned*)((const char*)(gbase) + (o0)), (LAS unsigned*)(lds + (bufoff) + ldsw), 16, 0, 0); \
;         __builtin_amdgcn_global_load_lds((const unsigned*)((const char*)(gbase) + (o1)), (LAS unsigned*)(lds + (bufoff) + ldsw + 8192), 16, 0, 0); } while (0)
; #define PG8_LDA(dst, b, h) do { _Pragma("unroll") for (int m = 0; m < 4; ++m) _Pragma("unroll") for (int k = 0; k < 2; ++k) dst[m][k] = *(const LAS bf16x8*)(lds + PG8_SA(b, h) + aoff + m * 2048 + k * 1024); } while (0)
; #define PG8_LDB(dst, b, h) do { _Pragma("unroll") for (int n = 0; n < 2; ++n) _Pragma("unroll") for (int k = 0; k < 2; ++k) dst[n][k] = *(const LAS bf16x8*)(lds + PG8_SB(b, h) + boff + n * 2048 + k * 1024); } while (0)
; #define PG8_WAIT_V(n) asm volatile("s_waitcnt vmcnt(" #n ")" ::: "memory")
; #define PG8_WAIT_L(n) asm volatile("s_waitcnt lgkmcnt(" #n ")" ::: "memory")
; #define PG8_BAR __builtin_amdgcn_s_barrier()
; #define PG8_SCHED __builtin_amdgcn_sched_barrier(0)
; template <class Epi, class Sched, class Prob>
; __device__ __forceinline__ void gemm_phase(LAS unsigned char* lds, LAS unsigned char* lds_epi, const Prob g, const Sched& S, const Epi& E, int wid) {
;     ...
;         for (int t = 0; t < nt; t += 2) {
;             const bool last = (t == nt - 2);
;             const char* a1 = cA + (size_t)(t + 1) * kstep;
;             const char* a2 = last ? nA : cA + (size_t)(t + 2) * kstep; const char* b2 = last ? nB : cB + (size_t)(t + 2) * kstep;
;             const char* a3 = a2 + kstep; const char* b3 = b2 + kstep;
;             PG8_LDB(B0, 0, 0); PG8_LDB(B1, 0, 1); PG8_SCHED; PG8_LDA(At, 0, 0); PG8_STAGE(PG8_SA(1, 1), a1, cA10, cA11);
;             PG8_WAIT_V(8); PG8_WAIT_L(0); PG8_BAR; PG8_MMA(0, 0, At, B0); PG8_MMA(0, 1, At, B1); PG8_BAR; PG8_SCHED;
;     ...
;             PG8_LDA(At, 1, 1); PG8_STAGE(PG8_SB(1, 0), b3, vB0, vB1); PG8_STAGE(PG8_SB(1, 1), b3 + hstepB, vB0, vB1); PG8_STAGE(PG8_SA(1, 0), a3, cA00, cA01);
;             PG8_WAIT_V(8); PG8_WAIT_L(0); PG8_BAR; PG8_MMA(1, 0, At, B0); PG8_MMA(1, 1, At, B1); PG8_BAR; PG8_SCHED;
	s_add_i32 s10, s10, s97
	v_lshl_add_u64 v[210:211], v[210:211], 0, s[24:25]
	s_mov_b32 m0, s10
	ds_read_b128 v[178:181], v242 offset:49152
	ds_read_b128 v[182:185], v242 offset:50176
	ds_read_b128 v[186:189], v242 offset:51200
	ds_read_b128 v[190:193], v242 offset:52224
	ds_read_b128 v[194:197], v242 offset:53248
	ds_read_b128 v[198:201], v242 offset:54272
	ds_read_b128 v[202:205], v242 offset:55296
	ds_read_b128 v[206:209], v242 offset:56320
	global_load_lds_dwordx4 v[210:211], off
	s_add_i32 m0, s10, 0x2000
	s_add_u32 s10, s48, 0x80080
	v_lshl_add_u64 v[210:211], v[212:213], 0, s[24:25]
	s_addc_u32 s11, s49, 0
	s_add_i32 s48, s88, s97
	global_load_lds_dwordx4 v[210:211], off
	v_lshl_add_u64 v[210:211], s[10:11], 0, v[128:129]
	s_mov_b32 m0, s48
	s_nop 0
	global_load_lds_dwordx4 v[210:211], off
	v_lshl_add_u64 v[210:211], s[10:11], 0, v[130:131]
	s_add_i32 m0, s48, 0x2000
	s_nop 0
	global_load_lds_dwordx4 v[210:211], off
	v_lshl_add_u64 v[210:211], v[214:215], 0, s[24:25]
	s_mov_b32 m0, s78
	s_nop 0
	global_load_lds_dwordx4 v[210:211], off
	v_lshl_add_u64 v[210:211], v[216:217], 0, s[24:25]
	s_mov_b32 m0, s79
	s_nop 0
	global_load_lds_dwordx4 v[210:211], off
	s_waitcnt vmcnt(8)
	s_waitcnt lgkmcnt(0)
	s_barrier
	s_waitcnt lgkmcnt(0)
	v_mfma_f32_16x16x32_bf16 v[60:63], v[146:149], v[178:181], v[60:63]
	v_mfma_f32_16x16x32_bf16 v[56:59], v[154:157], v[178:181], v[56:59]
	v_mfma_f32_16x16x32_bf16 v[52:55], v[146:149], v[186:189], v[52:55]
	v_mfma_f32_16x16x32_bf16 v[48:51], v[154:157], v[186:189], v[48:51]
	v_mfma_f32_16x16x32_bf16 v[36:39], v[146:149], v[194:197], v[36:39]
	v_mfma_f32_16x16x32_bf16 v[32:35], v[154:157], v[194:197], v[32:35]
	v_mfma_f32_16x16x32_bf16 v[20:23], v[146:149], v[202:205], v[20:23]
	v_mfma_f32_16x16x32_bf16 v[16:19], v[154:157], v[202:205], v[16:19]
	v_mfma_f32_16x16x32_bf16 v[60:63], v[150:153], v[182:185], v[60:63]
	v_mfma_f32_16x16x32_bf16 v[56:59], v[158:161], v[182:185], v[56:59]
	v_mfma_f32_16x16x32_bf16 v[52:55], v[150:153], v[190:193], v[52:55]
	v_mfma_f32_16x16x32_bf16 v[48:51], v[158:161], v[190:193], v[48:51]
	v_mfma_f32_16x16x32_bf16 v[36:39], v[150:153], v[198:201], v[36:39]
	v_mfma_f32_16x16x32_bf16 v[32:35], v[158:161], v[198:201], v[32:35]
	v_mfma_f32_16x16x32_bf16 v[20:23], v[150:153], v[206:209], v[20:23]
	v_mfma_f32_16x16x32_bf16 v[16:19], v[158:161], v[206:209], v[16:19]
	v_mfma_f32_16x16x32_bf16 v[44:47], v[162:165], v[178:181], v[44:47]
	v_mfma_f32_16x16x32_bf16 v[40:43], v[170:173], v[178:181], v[40:43]
	v_mfma_f32_16x16x32_bf16 v[28:31], v[162:165], v[186:189], v[28:31]
	v_mfma_f32_16x16x32_bf16 v[24:27], v[170:173], v[186:189], v[24:27]
	v_mfma_f32_16x16x32_bf16 v[12:15], v[162:165], v[194:197], v[12:15]
	v_mfma_f32_16x16x32_bf16 v[8:11], v[170:173], v[194:197], v[8:11]
	v_mfma_f32_16x16x32_bf16 v[4:7], v[162:165], v[202:205], v[4:7]
	v_mfma_f32_16x16x32_bf16 v[0:3], v[170:173], v[202:205], v[0:3]
	v_mfma_f32_16x16x32_bf16 v[44:47], v[166:169], v[182:185], v[44:47]
	v_mfma_f32_16x16x32_bf16 v[40:43], v[174:177], v[182:185], v[40:43]
	v_mfma_f32_16x16x32_bf16 v[28:31], v[166:169], v[190:193], v[28:31]
	v_mfma_f32_16x16x32_bf16 v[24:27], v[174:177], v[190:193], v[24:27]
	v_mfma_f32_16x16x32_bf16 v[12:15], v[166:169], v[198:201], v[12:15]
	v_mfma_f32_16x16x32_bf16 v[8:11], v[174:177], v[198:201], v[8:11]
	v_mfma_f32_16x16x32_bf16 v[4:7], v[166:169], v[206:209], v[4:7]
	v_mfma_f32_16x16x32_bf16 v[0:3], v[174:177], v[206:209], v[0:3]
	s_barrier
	s_add_i32 s87, s87, 2
	s_add_u32 s54, s54, 0x100
	s_addc_u32 s55, s55, 0
	s_cmp_gt_u32 s87, 29
	s_mov_b64 s[10:11], s[46:47]
.LBB0_1434:
	ds_read_b128 v[146:149], v240
	ds_read_b128 v[150:153], v240 offset:1024
	ds_read_b128 v[154:157], v240 offset:2048
	ds_read_b128 v[158:161], v240 offset:3072
	ds_read_b128 v[162:165], v241
	ds_read_b128 v[166:169], v241 offset:1024
	ds_read_b128 v[170:173], v241 offset:2048
	ds_read_b128 v[174:177], v241 offset:3072
	s_add_u32 s46, s10, 0x100
	s_addc_u32 s47, s11, 0
	s_cmp_eq_u32 s87, 28
	s_cselect_b32 s51, s17, s47
	s_cselect_b32 s50, s52, s46
	s_cselect_b32 s49, s35, s55
	s_cselect_b32 s48, s53, s54
	v_lshl_add_u64 v[210:211], s[10:11], 0, v[142:143]
	s_add_i32 m0, s62, 0xc000
	ds_read_b128 v[178:181], v242
	ds_read_b128 v[182:185], v242 offset:1024
	ds_read_b128 v[186:189], v242 offset:2048
	ds_read_b128 v[190:193], v242 offset:3072
	ds_read_b128 v[194:197], v242 offset:4096
	ds_read_b128 v[198:201], v242 offset:5120
	ds_read_b128 v[202:205], v242 offset:6144
	ds_read_b128 v[206:209], v242 offset:7168
	global_load_lds_dwordx4 v[210:211], off
	v_lshl_add_u64 v[210:211], s[10:11], 0, v[140:141]
	s_add_i32 m0, s62, 0xe000
	s_nop 0
	global_load_lds_dwordx4 v[210:211], off
	s_waitcnt vmcnt(8)
	s_waitcnt lgkmcnt(0)
	s_barrier
; #define PG8_STAGE(bufoff, gbase, o0, o1) do { \
;         __builtin_amdgcn_global_load_lds((const unsigned*)((const char*)(gbase) + (o0)), (LAS unsigned*)(lds + (bufoff) + ldsw), 16, 0, 0); \
;         __builtin_amdgcn_global_load_lds((const unsigned*)((const char*)(gbase) + (o1)), (LAS unsigned*)(lds + (bufoff) + ldsw + 8192), 16, 0, 0); } while (0)
; #define PG8_LDA(dst, b, h) do { _Pragma("unroll") for (int m = 0; m < 4; ++m) _Pragma("unroll") for (int k = 0; k < 2; ++k) dst[m][k] = *(const LAS bf16x8*)(lds + PG8_SA(b, h) + aoff + m * 2048 + k * 1024); } while (0)
; #define PG8_WAIT_V(n) asm volatile("s_waitcnt vmcnt(" #n ")" ::: "memory")
; #define PG8_WAIT_L(n) asm volatile("s_waitcnt lgkmcnt(" #n ")" ::: "memory")
; #define PG8_BAR __builtin_amdgcn_s_barrier()
; #define PG8_SCHED __builtin_amdgcn_sched_barrier(0)
; template <class Epi, class Sched, class Prob>
; __device__ __forceinline__ void gemm_phase(LAS unsigned char* lds, LAS unsigned char* lds_epi, const Prob g, const Sched& S, const Epi& E, int wid) {
;     ...
;             PG8_WAIT_V(8); PG8_WAIT_L(0); PG8_BAR; PG8_MMA(0, 0, At, B0); PG8_MMA(0, 1, At, B1); PG8_BAR; PG8_SCHED;
;             PG8_LDA(At, 0, 1); PG8_STAGE(PG8_SB(0, 0), b2, vB0, vB1); PG8_STAGE(PG8_SB(0, 1), b2 + hstepB, vB0, vB1); PG8_STAGE(PG8_SA(0, 0), a2, cA00, cA01);
;             PG8_WAIT_V(8); PG8_WAIT_L(0); PG8_BAR; PG8_MMA(1, 0, At, B0); PG8_MMA(1, 1, At, B1); PG8_BAR; PG8_SCHED;
	s_waitcnt lgkmcnt(0)
	v_mfma_f32_16x16x32_bf16 v[124:127], v[146:149], v[178:181], v[124:127]
	v_mfma_f32_16x16x32_bf16 v[120:123], v[154:157], v[178:181], v[120:123]
	v_mfma_f32_16x16x32_bf16 v[116:119], v[146:149], v[186:189], v[116:119]
	v_mfma_f32_16x16x32_bf16 v[112:115], v[154:157], v[186:189], v[112:115]
	v_mfma_f32_16x16x32_bf16 v[108:111], v[146:149], v[194:197], v[108:111]
	v_mfma_f32_16x16x32_bf16 v[100:103], v[154:157], v[194:197], v[100:103]
	v_mfma_f32_16x16x32_bf16 v[92:95], v[146:149], v[202:205], v[92:95]
	v_mfma_f32_16x16x32_bf16 v[84:87], v[154:157], v[202:205], v[84:87]
	v_mfma_f32_16x16x32_bf16 v[124:127], v[150:153], v[182:185], v[124:127]
	v_mfma_f32_16x16x32_bf16 v[120:123], v[158:161], v[182:185], v[120:123]
	v_mfma_f32_16x16x32_bf16 v[116:119], v[150:153], v[190:193], v[116:119]
	v_mfma_f32_16x16x32_bf16 v[112:115], v[158:161], v[190:193], v[112:115]
	v_mfma_f32_16x16x32_bf16 v[108:111], v[150:153], v[198:201], v[108:111]
	v_mfma_f32_16x16x32_bf16 v[100:103], v[158:161], v[198:201], v[100:103]
	v_mfma_f32_16x16x32_bf16 v[92:95], v[150:153], v[206:209], v[92:95]
	v_mfma_f32_16x16x32_bf16 v[84:87], v[158:161], v[206:209], v[84:87]
	v_mfma_f32_16x16x32_bf16 v[104:107], v[162:165], v[178:181], v[104:107]
	v_mfma_f32_16x16x32_bf16 v[96:99], v[170:173], v[178:181], v[96:99]
	v_mfma_f32_16x16x32_bf16 v[88:91], v[162:165], v[186:189], v[88:91]
	v_mfma_f32_16x16x32_bf16 v[80:83], v[170:173], v[186:189], v[80:83]
	v_mfma_f32_16x16x32_bf16 v[76:79], v[162:165], v[194:197], v[76:79]
	v_mfma_f32_16x16x32_bf16 v[72:75], v[170:173], v[194:197], v[72:75]
	v_mfma_f32_16x16x32_bf16 v[68:71], v[162:165], v[202:205], v[68:71]
	v_mfma_f32_16x16x32_bf16 v[64:67], v[170:173], v[202:205], v[64:67]
	v_mfma_f32_16x16x32_bf16 v[104:107], v[166:169], v[182:185], v[104:107]
	v_mfma_f32_16x16x32_bf16 v[96:99], v[174:177], v[182:185], v[96:99]
	v_mfma_f32_16x16x32_bf16 v[88:91], v[166:169], v[190:193], v[88:91]
	v_mfma_f32_16x16x32_bf16 v[80:83], v[174:177], v[190:193], v[80:83]
	v_mfma_f32_16x16x32_bf16 v[76:79], v[166:169], v[198:201], v[76:79]
	v_mfma_f32_16x16x32_bf16 v[72:75], v[174:177], v[198:201], v[72:75]
	v_mfma_f32_16x16x32_bf16 v[68:71], v[166:169], v[206:209], v[68:71]
	v_mfma_f32_16x16x32_bf16 v[64:67], v[174:177], v[206:209], v[64:67]
	s_barrier
	s_add_i32 s10, s80, s97
	v_lshl_add_u64 v[210:211], s[48:49], 0, v[128:129]
	s_mov_b32 m0, s10
	ds_read_b128 v[178:181], v242 offset:16384
	ds_read_b128 v[182:185], v242 offset:17408
	ds_read_b128 v[186:189], v242 offset:18432
	ds_read_b128 v[190:193], v242 offset:19456
	ds_read_b128 v[194:197], v242 offset:20480
	ds_read_b128 v[198:201], v242 offset:21504
	ds_read_b128 v[202:205], v242 offset:22528
	ds_read_b128 v[206:209], v242 offset:23552
	global_load_lds_dwordx4 v[210:211], off
	s_add_i32 m0, s10, 0x2000
	s_add_u32 s10, s48, 0x80000
	v_lshl_add_u64 v[212:213], s[48:49], 0, v[130:131]
	s_addc_u32 s11, s49, 0
	s_add_i32 s88, s81, s97
	global_load_lds_dwordx4 v[212:213], off
	v_lshl_add_u64 v[214:215], s[10:11], 0, v[128:129]
	s_mov_b32 m0, s88
	v_lshl_add_u64 v[216:217], s[50:51], 0, v[136:137]
	global_load_lds_dwordx4 v[214:215], off
	v_lshl_add_u64 v[214:215], s[10:11], 0, v[130:131]
	s_add_i32 m0, s88, 0x2000
	s_nop 0
	global_load_lds_dwordx4 v[214:215], off
	v_lshl_add_u64 v[214:215], s[50:51], 0, v[132:133]
	s_mov_b32 m0, s62
	s_nop 0
	global_load_lds_dwordx4 v[214:215], off
	s_mov_b32 m0, s63
	s_nop 0
	global_load_lds_dwordx4 v[216:217], off
	s_waitcnt vmcnt(8)
	s_waitcnt lgkmcnt(0)
	s_barrier
	s_waitcnt lgkmcnt(0)
	v_mfma_f32_16x16x32_bf16 v[60:63], v[146:149], v[178:181], v[60:63]
	v_mfma_f32_16x16x32_bf16 v[56:59], v[154:157], v[178:181], v[56:59]
	v_mfma_f32_16x16x32_bf16 v[52:55], v[146:149], v[186:189], v[52:55]
	v_mfma_f32_16x16x32_bf16 v[48:51], v[154:157], v[186:189], v[48:51]
	v_mfma_f32_16x16x32_bf16 v[36:39], v[146:149], v[194:197], v[36:39]
	v_mfma_f32_16x16x32_bf16 v[32:35], v[154:157], v[194:197], v[32:35]
	v_mfma_f32_16x16x32_bf16 v[20:23], v[146:149], v[202:205], v[20:23]
	v_mfma_f32_16x16x32_bf16 v[16:19], v[154:157], v[202:205], v[16:19]
	v_mfma_f32_16x16x32_bf16 v[60:63], v[150:153], v[182:185], v[60:63]
	v_mfma_f32_16x16x32_bf16 v[56:59], v[158:161], v[182:185], v[56:59]
	v_mfma_f32_16x16x32_bf16 v[52:55], v[150:153], v[190:193], v[52:55]
	v_mfma_f32_16x16x32_bf16 v[48:51], v[158:161], v[190:193], v[48:51]
	v_mfma_f32_16x16x32_bf16 v[36:39], v[150:153], v[198:201], v[36:39]
	v_mfma_f32_16x16x32_bf16 v[32:35], v[158:161], v[198:201], v[32:35]
	v_mfma_f32_16x16x32_bf16 v[20:23], v[150:153], v[206:209], v[20:23]
	v_mfma_f32_16x16x32_bf16 v[16:19], v[158:161], v[206:209], v[16:19]
	v_mfma_f32_16x16x32_bf16 v[44:47], v[162:165], v[178:181], v[44:47]
	v_mfma_f32_16x16x32_bf16 v[40:43], v[170:173], v[178:181], v[40:43]
	v_mfma_f32_16x16x32_bf16 v[28:31], v[162:165], v[186:189], v[28:31]
	v_mfma_f32_16x16x32_bf16 v[24:27], v[170:173], v[186:189], v[24:27]
	v_mfma_f32_16x16x32_bf16 v[12:15], v[162:165], v[194:197], v[12:15]
	v_mfma_f32_16x16x32_bf16 v[8:11], v[170:173], v[194:197], v[8:11]
	v_mfma_f32_16x16x32_bf16 v[4:7], v[162:165], v[202:205], v[4:7]
	v_mfma_f32_16x16x32_bf16 v[0:3], v[170:173], v[202:205], v[0:3]
	v_mfma_f32_16x16x32_bf16 v[44:47], v[166:169], v[182:185], v[44:47]
	v_mfma_f32_16x16x32_bf16 v[40:43], v[174:177], v[182:185], v[40:43]
	v_mfma_f32_16x16x32_bf16 v[28:31], v[166:169], v[190:193], v[28:31]
	v_mfma_f32_16x16x32_bf16 v[24:27], v[174:177], v[190:193], v[24:27]
	v_mfma_f32_16x16x32_bf16 v[12:15], v[166:169], v[198:201], v[12:15]
	v_mfma_f32_16x16x32_bf16 v[8:11], v[174:177], v[198:201], v[8:11]
	v_mfma_f32_16x16x32_bf16 v[4:7], v[166:169], v[206:209], v[4:7]
	v_mfma_f32_16x16x32_bf16 v[0:3], v[174:177], v[206:209], v[0:3]
	s_barrier
; #define PG8_STAGE(bufoff, gbase, o0, o1) do { \
;         __builtin_amdgcn_global_load_lds((const unsigned*)((const char*)(gbase) + (o0)), (LAS unsigned*)(lds + (bufoff) + ldsw), 16, 0, 0); \
;         __builtin_amdgcn_global_load_lds((const unsigned*)((const char*)(gbase) + (o1)), (LAS unsigned*)(lds + (bufoff) + ldsw + 8192), 16, 0, 0); } while (0)
; #define PG8_LDA(dst, b, h) do { _Pragma("unroll") for (int m = 0; m < 4; ++m) _Pragma("unroll") for (int k = 0; k < 2; ++k) dst[m][k] = *(const LAS bf16x8*)(lds + PG8_SA(b, h) + aoff + m * 2048 + k * 1024); } while (0)
; #define PG8_LDB(dst, b, h) do { _Pragma("unroll") for (int n = 0; n < 2; ++n) _Pragma("unroll") for (int k = 0; k < 2; ++k) dst[n][k] = *(const LAS bf16x8*)(lds + PG8_SB(b, h) + boff + n * 2048 + k * 1024); } while (0)
; #define PG8_WAIT_V(n) asm volatile("s_waitcnt vmcnt(" #n ")" ::: "memory")
; #define PG8_WAIT_L(n) asm volatile("s_waitcnt lgkmcnt(" #n ")" ::: "memory")
; #define PG8_BAR __builtin_amdgcn_s_barrier()
; #define PG8_SCHED __builtin_amdgcn_sched_barrier(0)
; template <class Epi, class Sched, class Prob>
; __device__ __forceinline__ void gemm_phase(LAS unsigned char* lds, LAS unsigned char* lds_epi, const Prob g, const Sched& S, const Epi& E, int wid) {
;     ...
;             PG8_LDB(B0, 1, 0); PG8_LDB(B1, 1, 1); PG8_SCHED; PG8_LDA(At, 1, 0); PG8_STAGE(PG8_SA(0, 1), a2, cA10, cA11);
;             PG8_WAIT_V(8); PG8_WAIT_L(0); PG8_BAR; PG8_MMA(0, 0, At, B0); PG8_MMA(0, 1, At, B1); PG8_BAR; PG8_SCHED;
	s_add_i32 s10, 0, 0x18000
	s_add_i32 s88, 0, 0x1c000
	v_add_u32_e32 v158, s10, v239
	v_add_u32_e32 v174, s88, v239
	ds_read_b128 v[146:149], v158
	ds_read_b128 v[150:153], v158 offset:1024
	ds_read_b128 v[154:157], v158 offset:2048
	ds_read_b128 v[158:161], v158 offset:3072
	ds_read_b128 v[162:165], v174
	ds_read_b128 v[166:169], v174 offset:1024
	ds_read_b128 v[170:173], v174 offset:2048
	ds_read_b128 v[174:177], v174 offset:3072
	s_mov_b32 m0, s64
	v_lshl_add_u64 v[218:219], s[50:51], 0, v[134:135]
	ds_read_b128 v[178:181], v242 offset:32768
	ds_read_b128 v[182:185], v242 offset:33792
	ds_read_b128 v[186:189], v242 offset:34816
	ds_read_b128 v[190:193], v242 offset:35840
	ds_read_b128 v[194:197], v242 offset:36864
	ds_read_b128 v[198:201], v242 offset:37888
	ds_read_b128 v[202:205], v242 offset:38912
	ds_read_b128 v[206:209], v242 offset:39936
	global_load_lds_dwordx4 v[218:219], off
	v_lshl_add_u64 v[218:219], s[50:51], 0, v[138:139]
	s_mov_b32 m0, s65
	s_nop 0
	global_load_lds_dwordx4 v[218:219], off
	s_waitcnt vmcnt(8)
	s_waitcnt lgkmcnt(0)
	s_barrier
	s_waitcnt lgkmcnt(0)
	v_mfma_f32_16x16x32_bf16 v[124:127], v[146:149], v[178:181], v[124:127]
	v_mfma_f32_16x16x32_bf16 v[120:123], v[154:157], v[178:181], v[120:123]
	v_mfma_f32_16x16x32_bf16 v[116:119], v[146:149], v[186:189], v[116:119]
	v_mfma_f32_16x16x32_bf16 v[112:115], v[154:157], v[186:189], v[112:115]
	v_mfma_f32_16x16x32_bf16 v[108:111], v[146:149], v[194:197], v[108:111]
	v_mfma_f32_16x16x32_bf16 v[100:103], v[154:157], v[194:197], v[100:103]
	v_mfma_f32_16x16x32_bf16 v[92:95], v[146:149], v[202:205], v[92:95]
	v_mfma_f32_16x16x32_bf16 v[84:87], v[154:157], v[202:205], v[84:87]
	v_mfma_f32_16x16x32_bf16 v[124:127], v[150:153], v[182:185], v[124:127]
	v_mfma_f32_16x16x32_bf16 v[120:123], v[158:161], v[182:185], v[120:123]
	v_mfma_f32_16x16x32_bf16 v[116:119], v[150:153], v[190:193], v[116:119]
	v_mfma_f32_16x16x32_bf16 v[112:115], v[158:161], v[190:193], v[112:115]
	v_mfma_f32_16x16x32_bf16 v[108:111], v[150:153], v[198:201], v[108:111]
	v_mfma_f32_16x16x32_bf16 v[100:103], v[158:161], v[198:201], v[100:103]
	v_mfma_f32_16x16x32_bf16 v[92:95], v[150:153], v[206:209], v[92:95]
	v_mfma_f32_16x16x32_bf16 v[84:87], v[158:161], v[206:209], v[84:87]
	v_mfma_f32_16x16x32_bf16 v[104:107], v[162:165], v[178:181], v[104:107]
	v_mfma_f32_16x16x32_bf16 v[96:99], v[170:173], v[178:181], v[96:99]
	v_mfma_f32_16x16x32_bf16 v[88:91], v[162:165], v[186:189], v[88:91]
	v_mfma_f32_16x16x32_bf16 v[80:83], v[170:173], v[186:189], v[80:83]
	v_mfma_f32_16x16x32_bf16 v[76:79], v[162:165], v[194:197], v[76:79]
	v_mfma_f32_16x16x32_bf16 v[72:75], v[170:173], v[194:197], v[72:75]
	v_mfma_f32_16x16x32_bf16 v[68:71], v[162:165], v[202:205], v[68:71]
	v_mfma_f32_16x16x32_bf16 v[64:67], v[170:173], v[202:205], v[64:67]
	v_mfma_f32_16x16x32_bf16 v[104:107], v[166:169], v[182:185], v[104:107]
	v_mfma_f32_16x16x32_bf16 v[96:99], v[174:177], v[182:185], v[96:99]
	v_mfma_f32_16x16x32_bf16 v[88:91], v[166:169], v[190:193], v[88:91]
	v_mfma_f32_16x16x32_bf16 v[80:83], v[174:177], v[190:193], v[80:83]
	v_mfma_f32_16x16x32_bf16 v[76:79], v[166:169], v[198:201], v[76:79]
	v_mfma_f32_16x16x32_bf16 v[72:75], v[174:177], v[198:201], v[72:75]
	v_mfma_f32_16x16x32_bf16 v[68:71], v[166:169], v[206:209], v[68:71]
	v_mfma_f32_16x16x32_bf16 v[64:67], v[174:177], v[206:209], v[64:67]
	s_barrier
; #define PG8_STAGE(bufoff, gbase, o0, o1) do { \
;         __builtin_amdgcn_global_load_lds((const unsigned*)((const char*)(gbase) + (o0)), (LAS unsigned*)(lds + (bufoff) + ldsw), 16, 0, 0); \
;         __builtin_amdgcn_global_load_lds((const unsigned*)((const char*)(gbase) + (o1)), (LAS unsigned*)(lds + (bufoff) + ldsw + 8192), 16, 0, 0); } while (0)
; #define PG8_LDA(dst, b, h) do { _Pragma("unroll") for (int m = 0; m < 4; ++m) _Pragma("unroll") for (int k = 0; k < 2; ++k) dst[m][k] = *(const LAS bf16x8*)(lds + PG8_SA(b, h) + aoff + m * 2048 + k * 1024); } while (0)
; #define PG8_WAIT_V(n) asm volatile("s_waitcnt vmcnt(" #n ")" ::: "memory")
; #define PG8_WAIT_L(n) asm volatile("s_waitcnt lgkmcnt(" #n ")" ::: "memory")
; #define PG8_BAR __builtin_amdgcn_s_barrier()
; #define PG8_SCHED __builtin_amdgcn_sched_barrier(0)
; template <class Epi, class Sched, class Prob>
; __device__ __forceinline__ void gemm_phase(LAS unsigned char* lds, LAS unsigned char* lds_epi, const Prob g, const Sched& S, const Epi& E, int wid) {
;     ...
;             PG8_LDA(At, 1, 1); PG8_STAGE(PG8_SB(1, 0), b3, vB0, vB1); PG8_STAGE(PG8_SB(1, 1), b3 + hstepB, vB0, vB1); PG8_STAGE(PG8_SA(1, 0), a3, cA00, cA01);
;             PG8_WAIT_V(8); PG8_WAIT_L(0); PG8_BAR; PG8_MMA(1, 0, At, B0); PG8_MMA(1, 1, At, B1); PG8_BAR; PG8_SCHED;
;         }
;         if constexpr (Prob::FP8) asm volatile("s_nop 7\n\ts_nop 7\n\ts_nop 7" ::: "memory");
;         if (wr == 0) PG8_BAR;
	s_add_i32 s10, s10, s97
	v_lshl_add_u64 v[210:211], v[210:211], 0, s[24:25]
	s_mov_b32 m0, s10
	ds_read_b128 v[178:181], v242 offset:49152
	ds_read_b128 v[182:185], v242 offset:50176
	ds_read_b128 v[186:189], v242 offset:51200
	ds_read_b128 v[190:193], v242 offset:52224
	ds_read_b128 v[194:197], v242 offset:53248
	ds_read_b128 v[198:201], v242 offset:54272
	ds_read_b128 v[202:205], v242 offset:55296
	ds_read_b128 v[206:209], v242 offset:56320
	global_load_lds_dwordx4 v[210:211], off
	s_add_i32 m0, s10, 0x2000
	s_add_u32 s10, s48, 0x80080
	v_lshl_add_u64 v[210:211], v[212:213], 0, s[24:25]
	s_addc_u32 s11, s49, 0
	s_add_i32 s48, s88, s97
	global_load_lds_dwordx4 v[210:211], off
	v_lshl_add_u64 v[210:211], s[10:11], 0, v[128:129]
	s_mov_b32 m0, s48
	s_nop 0
	global_load_lds_dwordx4 v[210:211], off
	v_lshl_add_u64 v[210:211], s[10:11], 0, v[130:131]
	s_add_i32 m0, s48, 0x2000
	s_nop 0
	global_load_lds_dwordx4 v[210:211], off
	v_lshl_add_u64 v[210:211], v[214:215], 0, s[24:25]
	s_mov_b32 m0, s78
	s_nop 0
	global_load_lds_dwordx4 v[210:211], off
	v_lshl_add_u64 v[210:211], v[216:217], 0, s[24:25]
	s_mov_b32 m0, s79
	s_nop 0
	global_load_lds_dwordx4 v[210:211], off
	s_waitcnt vmcnt(8)
	s_waitcnt lgkmcnt(0)
	s_barrier
	s_waitcnt lgkmcnt(0)
	v_mfma_f32_16x16x32_bf16 v[60:63], v[146:149], v[178:181], v[60:63]
	v_mfma_f32_16x16x32_bf16 v[56:59], v[154:157], v[178:181], v[56:59]
	v_mfma_f32_16x16x32_bf16 v[52:55], v[146:149], v[186:189], v[52:55]
	v_mfma_f32_16x16x32_bf16 v[48:51], v[154:157], v[186:189], v[48:51]
	v_mfma_f32_16x16x32_bf16 v[36:39], v[146:149], v[194:197], v[36:39]
	v_mfma_f32_16x16x32_bf16 v[32:35], v[154:157], v[194:197], v[32:35]
	v_mfma_f32_16x16x32_bf16 v[20:23], v[146:149], v[202:205], v[20:23]
	v_mfma_f32_16x16x32_bf16 v[16:19], v[154:157], v[202:205], v[16:19]
	v_mfma_f32_16x16x32_bf16 v[60:63], v[150:153], v[182:185], v[60:63]
	v_mfma_f32_16x16x32_bf16 v[56:59], v[158:161], v[182:185], v[56:59]
	v_mfma_f32_16x16x32_bf16 v[52:55], v[150:153], v[190:193], v[52:55]
	v_mfma_f32_16x16x32_bf16 v[48:51], v[158:161], v[190:193], v[48:51]
	v_mfma_f32_16x16x32_bf16 v[36:39], v[150:153], v[198:201], v[36:39]
	v_mfma_f32_16x16x32_bf16 v[32:35], v[158:161], v[198:201], v[32:35]
	v_mfma_f32_16x16x32_bf16 v[20:23], v[150:153], v[206:209], v[20:23]
	v_mfma_f32_16x16x32_bf16 v[16:19], v[158:161], v[206:209], v[16:19]
	v_mfma_f32_16x16x32_bf16 v[44:47], v[162:165], v[178:181], v[44:47]
	v_mfma_f32_16x16x32_bf16 v[40:43], v[170:173], v[178:181], v[40:43]
	v_mfma_f32_16x16x32_bf16 v[28:31], v[162:165], v[186:189], v[28:31]
	v_mfma_f32_16x16x32_bf16 v[24:27], v[170:173], v[186:189], v[24:27]
	v_mfma_f32_16x16x32_bf16 v[12:15], v[162:165], v[194:197], v[12:15]
	v_mfma_f32_16x16x32_bf16 v[8:11], v[170:173], v[194:197], v[8:11]
	v_mfma_f32_16x16x32_bf16 v[4:7], v[162:165], v[202:205], v[4:7]
	v_mfma_f32_16x16x32_bf16 v[0:3], v[170:173], v[202:205], v[0:3]
	v_mfma_f32_16x16x32_bf16 v[44:47], v[166:169], v[182:185], v[44:47]
	v_mfma_f32_16x16x32_bf16 v[40:43], v[174:177], v[182:185], v[40:43]
	v_mfma_f32_16x16x32_bf16 v[28:31], v[166:169], v[190:193], v[28:31]
	v_mfma_f32_16x16x32_bf16 v[24:27], v[174:177], v[190:193], v[24:27]
	v_mfma_f32_16x16x32_bf16 v[12:15], v[166:169], v[198:201], v[12:15]
	v_mfma_f32_16x16x32_bf16 v[8:11], v[174:177], v[198:201], v[8:11]
	v_mfma_f32_16x16x32_bf16 v[4:7], v[166:169], v[206:209], v[4:7]
	v_mfma_f32_16x16x32_bf16 v[0:3], v[174:177], v[206:209], v[0:3]
	s_barrier
	s_add_i32 s87, s87, 2
	s_add_u32 s54, s54, 0x100
	s_addc_u32 s55, s55, 0
	s_cmp_gt_u32 s87, 29
	s_mov_b64 s[10:11], s[46:47]
	s_cbranch_scc0 .LBB0_1434
	s_setprio 0
	v_readlane_b32 s10, v254, 27
	v_readlane_b32 s11, v254, 28
	s_and_b64 vcc, exec, s[10:11]
	s_cbranch_vccz .LBB0_1437
	s_barrier

; #define PG8_STAGE(bufoff, gbase, o0, o1) do { \
;         __builtin_amdgcn_global_load_lds((const unsigned*)((const char*)(gbase) + (o0)), (LAS unsigned*)(lds + (bufoff) + ldsw), 16, 0, 0); \
;         __builtin_amdgcn_global_load_lds((const unsigned*)((const char*)(gbase) + (o1)), (LAS unsigned*)(lds + (bufoff) + ldsw + 8192), 16, 0, 0); } while (0)
; #define PG8_LDA(dst, b, h) do { _Pragma("unroll") for (int m = 0; m < 4; ++m) _Pragma("unroll") for (int k = 0; k < 2; ++k) dst[m][k] = *(const LAS bf16x8*)(lds + PG8_SA(b, h) + aoff + m * 2048 + k * 1024); } while (0)
; #define PG8_LDB(dst, b, h) do { _Pragma("unroll") for (int n = 0; n < 2; ++n) _Pragma("unroll") for (int k = 0; k < 2; ++k) dst[n][k] = *(const LAS bf16x8*)(lds + PG8_SB(b, h) + boff + n * 2048 + k * 1024); } while (0)
; #define PG8_WAIT_V(n) asm volatile("s_waitcnt vmcnt(" #n ")" ::: "memory")
; #define PG8_WAIT_L(n) asm volatile("s_waitcnt lgkmcnt(" #n ")" ::: "memory")
; #define PG8_BAR __builtin_amdgcn_s_barrier()
; #define PG8_SCHED __builtin_amdgcn_sched_barrier(0)
; template <class Epi, class Sched, class Prob>
; __device__ __forceinline__ void gemm_phase(LAS unsigned char* lds, LAS unsigned char* lds_epi, const Prob g, const Sched& S, const Epi& E, int wid) {
;     ...
;         const bool has_next = S.next(ui + 1, nxt);
;         const char* nA = has_next ? g.a_base(nxt) : cA; const char* nB = has_next ? g.b_base(nxt) : cB;
; _Pragma("clang loop unroll(disable)")
;         for (int t = 0; t < nt; t += 2) {
;             const bool last = (t == nt - 2);
;             const char* a1 = cA + (size_t)(t + 1) * kstep;
;             const char* a2 = last ? nA : cA + (size_t)(t + 2) * kstep; const char* b2 = last ? nB : cB + (size_t)(t + 2) * kstep;
;             const char* a3 = a2 + kstep; const char* b3 = b2 + kstep;
;             PG8_LDB(B0, 0, 0); PG8_LDB(B1, 0, 1); PG8_SCHED; PG8_LDA(At, 0, 0); PG8_STAGE(PG8_SA(1, 1), a1, cA10, cA11);
;             PG8_WAIT_V(8); PG8_WAIT_L(0); PG8_BAR; PG8_MMA(0, 0, At, B0); PG8_MMA(0, 1, At, B1); PG8_BAR; PG8_SCHED;
;             PG8_LDA(At, 0, 1); PG8_STAGE(PG8_SB(0, 0), b2, vB0, vB1); PG8_STAGE(PG8_SB(0, 1), b2 + hstepB, vB0, vB1); PG8_STAGE(PG8_SA(0, 0), a2, cA00, cA01);
;             PG8_WAIT_V(8); PG8_WAIT_L(0); PG8_BAR; PG8_MMA(1, 0, At, B0); PG8_MMA(1, 1, At, B1); PG8_BAR; PG8_SCHED;
.LBB0_1594:
	s_ashr_i32 s65, s64, 31
	s_lshl_b64 s[14:15], s[64:65], 20
	s_add_u32 s17, s40, s14
	s_addc_u32 s19, s41, s15
	s_ashr_i32 s14, s62, 1
	s_ashr_i32 s15, s14, 31
	s_lshl_b64 s[14:15], s[14:15], 9
	s_add_u32 s68, s17, s14
	s_addc_u32 s69, s19, s15
	s_and_b64 s[14:15], s[66:67], exec
	s_cselect_b32 s17, s69, s9
	s_cselect_b32 s19, s68, s8
	s_ashr_i32 s63, s62, 31
	s_lshl_b64 s[14:15], s[62:63], 17
	s_add_u32 s70, s33, s14
	s_addc_u32 s71, s76, s15
	s_and_b64 s[14:15], s[66:67], exec
	v_mov_b32_e32 v0, 0
	s_cselect_b32 s26, s71, s11
	s_cselect_b32 s27, s70, s10
	s_mov_b64 s[20:21], -1
	s_mov_b64 s[14:15], 0
	s_cmp_lt_u32 s91, 0x100
	s_cbranch_scc1 .Lyoung_5
	s_setprio 1
.Lyoung_5:
	s_add_u32 s24, s8, s14
	s_addc_u32 s25, s9, s15
	s_add_u32 s22, s24, 0x100
	s_addc_u32 s23, s25, 0
	v_cndmask_b32_e64 v56, 0, 1, s[20:21]
	s_and_b64 s[20:21], s[12:13], exec
	s_cselect_b32 s20, s19, s22
	s_cselect_b32 s21, s17, s23
	s_add_u32 s14, s10, s14
	s_addc_u32 s15, s11, s15
	s_add_u32 s14, s14, 0x100
	v_cmp_ne_u32_e32 vcc, 1, v56
	ds_read_b128 v[56:59], v221
	ds_read_b128 v[68:71], v221 offset:1024
	ds_read_b128 v[72:75], v221 offset:2048
	ds_read_b128 v[88:91], v221 offset:3072
	ds_read_b128 v[100:103], v222
	ds_read_b128 v[104:107], v222 offset:1024
	ds_read_b128 v[166:169], v222 offset:2048
	ds_read_b128 v[170:173], v222 offset:3072
	s_addc_u32 s15, s15, 0
	s_and_b64 s[12:13], s[12:13], exec
	s_cselect_b32 s15, s26, s15
	s_cselect_b32 s14, s27, s14
	s_add_i32 s65, s85, s97
	s_add_i32 m0, s77, 0xc000
	s_add_i32 s72, s77, 0xe000
	s_add_i32 s36, s65, 0x2000
	s_add_u32 s22, s14, 0x10000
	s_addc_u32 s23, s15, 0
	s_add_i32 s35, 0, 0x18000
	s_add_i32 s63, s86, s97
	s_add_i32 s31, s35, s97
	s_add_i32 s37, s63, 0x2000
	s_add_i32 s34, 0, 0x1c000
	s_add_i32 s29, s31, 0x2000
	s_add_u32 s12, s14, 0x10080
	s_addc_u32 s13, s15, 0
	s_add_i32 s30, s34, s97
	s_add_i32 s28, s30, 0x2000
	v_lshl_add_u64 v[206:207], s[24:25], 0, v[158:159]
	v_lshl_add_u64 v[206:207], v[206:207], 0, s[54:55]
	ds_read_b128 v[174:177], v223
	ds_read_b128 v[178:181], v223 offset:1024
	ds_read_b128 v[182:185], v223 offset:2048
	ds_read_b128 v[186:189], v223 offset:3072
	ds_read_b128 v[190:193], v223 offset:4096
	ds_read_b128 v[194:197], v223 offset:5120
	ds_read_b128 v[198:201], v223 offset:6144
	ds_read_b128 v[202:205], v223 offset:7168
	global_load_lds_dwordx4 v[206:207], off
	v_lshl_add_u64 v[206:207], s[24:25], 0, v[162:163]
	v_lshl_add_u64 v[206:207], v[206:207], 0, s[54:55]
	s_mov_b32 m0, s72
	s_nop 0
	global_load_lds_dwordx4 v[206:207], off
	s_waitcnt vmcnt(8)
	s_waitcnt lgkmcnt(0)
	s_barrier
	s_waitcnt lgkmcnt(0)
	v_mfma_f32_16x16x32_bf16 v[148:151], v[56:59], v[174:177], 0
	v_mfma_f32_16x16x32_bf16 v[116:119], v[72:75], v[174:177], 0
	v_mfma_f32_16x16x32_bf16 v[144:147], v[56:59], v[182:185], 0
	v_mfma_f32_16x16x32_bf16 v[112:115], v[72:75], v[182:185], 0
	v_mfma_f32_16x16x32_bf16 v[140:143], v[56:59], v[190:193], 0
	v_mfma_f32_16x16x32_bf16 v[108:111], v[72:75], v[190:193], 0
	v_mfma_f32_16x16x32_bf16 v[136:139], v[56:59], v[198:201], 0
	v_mfma_f32_16x16x32_bf16 v[96:99], v[72:75], v[198:201], 0
	v_mfma_f32_16x16x32_bf16 v[148:151], v[68:71], v[178:181], v[148:151]
	v_mfma_f32_16x16x32_bf16 v[116:119], v[88:91], v[178:181], v[116:119]
	v_mfma_f32_16x16x32_bf16 v[144:147], v[68:71], v[186:189], v[144:147]
	v_mfma_f32_16x16x32_bf16 v[112:115], v[88:91], v[186:189], v[112:115]
	v_mfma_f32_16x16x32_bf16 v[140:143], v[68:71], v[194:197], v[140:143]
	v_mfma_f32_16x16x32_bf16 v[108:111], v[88:91], v[194:197], v[108:111]
	v_mfma_f32_16x16x32_bf16 v[136:139], v[68:71], v[202:205], v[136:139]
	v_mfma_f32_16x16x32_bf16 v[96:99], v[88:91], v[202:205], v[96:99]
	v_mfma_f32_16x16x32_bf16 v[132:135], v[100:103], v[174:177], 0
	v_mfma_f32_16x16x32_bf16 v[92:95], v[166:169], v[174:177], 0
	v_mfma_f32_16x16x32_bf16 v[128:131], v[100:103], v[182:185], 0
	v_mfma_f32_16x16x32_bf16 v[84:87], v[166:169], v[182:185], 0
	v_mfma_f32_16x16x32_bf16 v[124:127], v[100:103], v[190:193], 0
	v_mfma_f32_16x16x32_bf16 v[80:83], v[166:169], v[190:193], 0
	v_mfma_f32_16x16x32_bf16 v[120:123], v[100:103], v[198:201], 0
	v_mfma_f32_16x16x32_bf16 v[76:79], v[166:169], v[198:201], 0
	v_mfma_f32_16x16x32_bf16 v[132:135], v[104:107], v[178:181], v[132:135]
	v_mfma_f32_16x16x32_bf16 v[92:95], v[170:173], v[178:181], v[92:95]
	v_mfma_f32_16x16x32_bf16 v[128:131], v[104:107], v[186:189], v[128:131]
	v_mfma_f32_16x16x32_bf16 v[84:87], v[170:173], v[186:189], v[84:87]
	v_mfma_f32_16x16x32_bf16 v[124:127], v[104:107], v[194:197], v[124:127]
	v_mfma_f32_16x16x32_bf16 v[80:83], v[170:173], v[194:197], v[80:83]
	v_mfma_f32_16x16x32_bf16 v[120:123], v[104:107], v[202:205], v[120:123]
	v_mfma_f32_16x16x32_bf16 v[76:79], v[170:173], v[202:205], v[76:79]
	s_barrier
	s_mov_b32 m0, s65
	v_lshl_add_u64 v[206:207], s[14:15], 0, v[152:153]
	ds_read_b128 v[174:177], v223 offset:16384
	ds_read_b128 v[178:181], v223 offset:17408
	ds_read_b128 v[182:185], v223 offset:18432
	ds_read_b128 v[186:189], v223 offset:19456
	ds_read_b128 v[190:193], v223 offset:20480
	ds_read_b128 v[194:197], v223 offset:21504
	ds_read_b128 v[198:201], v223 offset:22528
	ds_read_b128 v[202:205], v223 offset:23552
	global_load_lds_dwordx4 v[206:207], off
	v_lshl_add_u64 v[208:209], s[14:15], 0, v[154:155]
	s_mov_b32 m0, s36
	v_lshl_add_u64 v[210:211], s[22:23], 0, v[152:153]
	global_load_lds_dwordx4 v[208:209], off
	s_mov_b32 m0, s63
	v_lshl_add_u64 v[212:213], s[20:21], 0, v[160:161]
	global_load_lds_dwordx4 v[210:211], off
	v_lshl_add_u64 v[210:211], s[22:23], 0, v[154:155]
	s_mov_b32 m0, s37
	s_nop 0
	global_load_lds_dwordx4 v[210:211], off
	v_lshl_add_u64 v[210:211], s[20:21], 0, v[156:157]
	s_mov_b32 m0, s77
	s_nop 0
	global_load_lds_dwordx4 v[210:211], off
	s_mov_b32 m0, s78
	s_nop 0
	global_load_lds_dwordx4 v[212:213], off
	s_waitcnt vmcnt(8)
	s_waitcnt lgkmcnt(0)
	s_barrier
; #define PG8_STAGE(bufoff, gbase, o0, o1) do { \
;         __builtin_amdgcn_global_load_lds((const unsigned*)((const char*)(gbase) + (o0)), (LAS unsigned*)(lds + (bufoff) + ldsw), 16, 0, 0); \
;         __builtin_amdgcn_global_load_lds((const unsigned*)((const char*)(gbase) + (o1)), (LAS unsigned*)(lds + (bufoff) + ldsw + 8192), 16, 0, 0); } while (0)
; #define PG8_LDA(dst, b, h) do { _Pragma("unroll") for (int m = 0; m < 4; ++m) _Pragma("unroll") for (int k = 0; k < 2; ++k) dst[m][k] = *(const LAS bf16x8*)(lds + PG8_SA(b, h) + aoff + m * 2048 + k * 1024); } while (0)
; #define PG8_LDB(dst, b, h) do { _Pragma("unroll") for (int n = 0; n < 2; ++n) _Pragma("unroll") for (int k = 0; k < 2; ++k) dst[n][k] = *(const LAS bf16x8*)(lds + PG8_SB(b, h) + boff + n * 2048 + k * 1024); } while (0)
; template <class Epi, class Sched, class Prob>
; __device__ __forceinline__ void gemm_phase(LAS unsigned char* lds, LAS unsigned char* lds_epi, const Prob g, const Sched& S, const Epi& E, int wid) {
;     ...
;         for (int t = 0; t < nt; t += 2) {
;             const bool last = (t == nt - 2);
;             const char* a1 = cA + (size_t)(t + 1) * kstep;
;             const char* a2 = last ? nA : cA + (size_t)(t + 2) * kstep; const char* b2 = last ? nB : cB + (size_t)(t + 2) * kstep;
;             const char* a3 = a2 + kstep; const char* b3 = b2 + kstep;
;             PG8_LDB(B0, 0, 0); PG8_LDB(B1, 0, 1); PG8_SCHED; PG8_LDA(At, 0, 0); PG8_STAGE(PG8_SA(1, 1), a1, cA10, cA11);
;             PG8_WAIT_V(8); PG8_WAIT_L(0); PG8_BAR; PG8_MMA(0, 0, At, B0); PG8_MMA(0, 1, At, B1); PG8_BAR; PG8_SCHED;
;             PG8_LDA(At, 0, 1); PG8_STAGE(PG8_SB(0, 0), b2, vB0, vB1); PG8_STAGE(PG8_SB(0, 1), b2 + hstepB, vB0, vB1); PG8_STAGE(PG8_SA(0, 0), a2, cA00, cA01);
;             PG8_WAIT_V(8); PG8_WAIT_L(0); PG8_BAR; PG8_MMA(1, 0, At, B0); PG8_MMA(1, 1, At, B1); PG8_BAR; PG8_SCHED;
;             PG8_LDB(B0, 1, 0); PG8_LDB(B1, 1, 1); PG8_SCHED; PG8_LDA(At, 1, 0); PG8_STAGE(PG8_SA(0, 1), a2, cA10, cA11);
;             PG8_WAIT_V(8); PG8_WAIT_L(0); PG8_BAR; PG8_MMA(0, 0, At, B0); PG8_MMA(0, 1, At, B1); PG8_BAR; PG8_SCHED;
;             PG8_LDA(At, 1, 1); PG8_STAGE(PG8_SB(1, 0), b3, vB0, vB1); PG8_STAGE(PG8_SB(1, 1), b3 + hstepB, vB0, vB1); PG8_STAGE(PG8_SA(1, 0), a3, cA00, cA01);
;             PG8_WAIT_V(8); PG8_WAIT_L(0); PG8_BAR; PG8_MMA(1, 0, At, B0); PG8_MMA(1, 1, At, B1); PG8_BAR; PG8_SCHED;
	s_waitcnt lgkmcnt(0)
	v_mfma_f32_16x16x32_bf16 v[64:67], v[56:59], v[174:177], 0
	v_mfma_f32_16x16x32_bf16 v[28:31], v[72:75], v[174:177], 0
	v_mfma_f32_16x16x32_bf16 v[60:63], v[56:59], v[182:185], 0
	v_mfma_f32_16x16x32_bf16 v[24:27], v[72:75], v[182:185], 0
	v_mfma_f32_16x16x32_bf16 v[52:55], v[56:59], v[190:193], 0
	v_mfma_f32_16x16x32_bf16 v[20:23], v[72:75], v[190:193], 0
	v_mfma_f32_16x16x32_bf16 v[48:51], v[56:59], v[198:201], 0
	v_mfma_f32_16x16x32_bf16 v[16:19], v[72:75], v[198:201], 0
	v_mfma_f32_16x16x32_bf16 v[64:67], v[68:71], v[178:181], v[64:67]
	v_mfma_f32_16x16x32_bf16 v[28:31], v[88:91], v[178:181], v[28:31]
	v_mfma_f32_16x16x32_bf16 v[60:63], v[68:71], v[186:189], v[60:63]
	v_mfma_f32_16x16x32_bf16 v[24:27], v[88:91], v[186:189], v[24:27]
	v_mfma_f32_16x16x32_bf16 v[52:55], v[68:71], v[194:197], v[52:55]
	v_mfma_f32_16x16x32_bf16 v[20:23], v[88:91], v[194:197], v[20:23]
	v_mfma_f32_16x16x32_bf16 v[48:51], v[68:71], v[202:205], v[48:51]
	v_mfma_f32_16x16x32_bf16 v[16:19], v[88:91], v[202:205], v[16:19]
	v_mfma_f32_16x16x32_bf16 v[44:47], v[100:103], v[174:177], 0
	v_mfma_f32_16x16x32_bf16 v[12:15], v[166:169], v[174:177], 0
	v_mfma_f32_16x16x32_bf16 v[40:43], v[100:103], v[182:185], 0
	v_mfma_f32_16x16x32_bf16 v[8:11], v[166:169], v[182:185], 0
	v_mfma_f32_16x16x32_bf16 v[36:39], v[100:103], v[190:193], 0
	v_mfma_f32_16x16x32_bf16 v[4:7], v[166:169], v[190:193], 0
	v_mfma_f32_16x16x32_bf16 v[32:35], v[100:103], v[198:201], 0
	v_mfma_f32_16x16x32_bf16 v[0:3], v[166:169], v[198:201], 0
	v_mfma_f32_16x16x32_bf16 v[44:47], v[104:107], v[178:181], v[44:47]
	v_mfma_f32_16x16x32_bf16 v[12:15], v[170:173], v[178:181], v[12:15]
	v_mfma_f32_16x16x32_bf16 v[40:43], v[104:107], v[186:189], v[40:43]
	v_mfma_f32_16x16x32_bf16 v[8:11], v[170:173], v[186:189], v[8:11]
	v_mfma_f32_16x16x32_bf16 v[36:39], v[104:107], v[194:197], v[36:39]
	v_mfma_f32_16x16x32_bf16 v[4:7], v[170:173], v[194:197], v[4:7]
	v_mfma_f32_16x16x32_bf16 v[32:35], v[104:107], v[202:205], v[32:35]
	v_mfma_f32_16x16x32_bf16 v[0:3], v[170:173], v[202:205], v[0:3]
	s_barrier
	v_add_u32_e32 v88, s35, v220
	v_add_u32_e32 v170, s34, v220
	ds_read_b128 v[56:59], v88
	ds_read_b128 v[68:71], v88 offset:1024
	ds_read_b128 v[72:75], v88 offset:2048
	ds_read_b128 v[88:91], v88 offset:3072
	ds_read_b128 v[100:103], v170
	ds_read_b128 v[104:107], v170 offset:1024
	ds_read_b128 v[166:169], v170 offset:2048
	ds_read_b128 v[170:173], v170 offset:3072
	s_mov_b32 m0, s79
	v_lshl_add_u64 v[214:215], s[20:21], 0, v[158:159]
	ds_read_b128 v[174:177], v223 offset:32768
	ds_read_b128 v[178:181], v223 offset:33792
	ds_read_b128 v[182:185], v223 offset:34816
	ds_read_b128 v[186:189], v223 offset:35840
	ds_read_b128 v[190:193], v223 offset:36864
	ds_read_b128 v[194:197], v223 offset:37888
	ds_read_b128 v[198:201], v223 offset:38912
	ds_read_b128 v[202:205], v223 offset:39936
	global_load_lds_dwordx4 v[214:215], off
	v_lshl_add_u64 v[214:215], s[20:21], 0, v[162:163]
	s_mov_b32 m0, s80
	s_nop 0
	global_load_lds_dwordx4 v[214:215], off
	s_waitcnt vmcnt(8)
	s_waitcnt lgkmcnt(0)
	s_barrier
	s_waitcnt lgkmcnt(0)
	v_mfma_f32_16x16x32_bf16 v[148:151], v[56:59], v[174:177], v[148:151]
	v_mfma_f32_16x16x32_bf16 v[116:119], v[72:75], v[174:177], v[116:119]
	v_mfma_f32_16x16x32_bf16 v[144:147], v[56:59], v[182:185], v[144:147]
	v_mfma_f32_16x16x32_bf16 v[112:115], v[72:75], v[182:185], v[112:115]
	v_mfma_f32_16x16x32_bf16 v[140:143], v[56:59], v[190:193], v[140:143]
	v_mfma_f32_16x16x32_bf16 v[108:111], v[72:75], v[190:193], v[108:111]
	v_mfma_f32_16x16x32_bf16 v[136:139], v[56:59], v[198:201], v[136:139]
	v_mfma_f32_16x16x32_bf16 v[96:99], v[72:75], v[198:201], v[96:99]
	v_mfma_f32_16x16x32_bf16 v[148:151], v[68:71], v[178:181], v[148:151]
	v_mfma_f32_16x16x32_bf16 v[116:119], v[88:91], v[178:181], v[116:119]
	v_mfma_f32_16x16x32_bf16 v[144:147], v[68:71], v[186:189], v[144:147]
	v_mfma_f32_16x16x32_bf16 v[112:115], v[88:91], v[186:189], v[112:115]
	v_mfma_f32_16x16x32_bf16 v[140:143], v[68:71], v[194:197], v[140:143]
	v_mfma_f32_16x16x32_bf16 v[108:111], v[88:91], v[194:197], v[108:111]
	v_mfma_f32_16x16x32_bf16 v[136:139], v[68:71], v[202:205], v[136:139]
	v_mfma_f32_16x16x32_bf16 v[96:99], v[88:91], v[202:205], v[96:99]
	v_mfma_f32_16x16x32_bf16 v[132:135], v[100:103], v[174:177], v[132:135]
	v_mfma_f32_16x16x32_bf16 v[92:95], v[166:169], v[174:177], v[92:95]
	v_mfma_f32_16x16x32_bf16 v[128:131], v[100:103], v[182:185], v[128:131]
	v_mfma_f32_16x16x32_bf16 v[84:87], v[166:169], v[182:185], v[84:87]
	v_mfma_f32_16x16x32_bf16 v[124:127], v[100:103], v[190:193], v[124:127]
	v_mfma_f32_16x16x32_bf16 v[80:83], v[166:169], v[190:193], v[80:83]
	v_mfma_f32_16x16x32_bf16 v[120:123], v[100:103], v[198:201], v[120:123]
	v_mfma_f32_16x16x32_bf16 v[76:79], v[166:169], v[198:201], v[76:79]
	v_mfma_f32_16x16x32_bf16 v[132:135], v[104:107], v[178:181], v[132:135]
	v_mfma_f32_16x16x32_bf16 v[92:95], v[170:173], v[178:181], v[92:95]
	v_mfma_f32_16x16x32_bf16 v[128:131], v[104:107], v[186:189], v[128:131]
	v_mfma_f32_16x16x32_bf16 v[84:87], v[170:173], v[186:189], v[84:87]
	v_mfma_f32_16x16x32_bf16 v[124:127], v[104:107], v[194:197], v[124:127]
	v_mfma_f32_16x16x32_bf16 v[80:83], v[170:173], v[194:197], v[80:83]
	v_mfma_f32_16x16x32_bf16 v[120:123], v[104:107], v[202:205], v[120:123]
	v_mfma_f32_16x16x32_bf16 v[76:79], v[170:173], v[202:205], v[76:79]
	s_barrier
; #define PG8_STAGE(bufoff, gbase, o0, o1) do { \
;         __builtin_amdgcn_global_load_lds((const unsigned*)((const char*)(gbase) + (o0)), (LAS unsigned*)(lds + (bufoff) + ldsw), 16, 0, 0); \
;         __builtin_amdgcn_global_load_lds((const unsigned*)((const char*)(gbase) + (o1)), (LAS unsigned*)(lds + (bufoff) + ldsw + 8192), 16, 0, 0); } while (0)
; #define PG8_LDA(dst, b, h) do { _Pragma("unroll") for (int m = 0; m < 4; ++m) _Pragma("unroll") for (int k = 0; k < 2; ++k) dst[m][k] = *(const LAS bf16x8*)(lds + PG8_SA(b, h) + aoff + m * 2048 + k * 1024); } while (0)
; #define PG8_LDB(dst, b, h) do { _Pragma("unroll") for (int n = 0; n < 2; ++n) _Pragma("unroll") for (int k = 0; k < 2; ++k) dst[n][k] = *(const LAS bf16x8*)(lds + PG8_SB(b, h) + boff + n * 2048 + k * 1024); } while (0)
; #define PG8_WAIT_V(n) asm volatile("s_waitcnt vmcnt(" #n ")" ::: "memory")
; #define PG8_WAIT_L(n) asm volatile("s_waitcnt lgkmcnt(" #n ")" ::: "memory")
; #define PG8_BAR __builtin_amdgcn_s_barrier()
; #define PG8_SCHED __builtin_amdgcn_sched_barrier(0)
; template <class Epi, class Sched, class Prob>
; __device__ __forceinline__ void gemm_phase(LAS unsigned char* lds, LAS unsigned char* lds_epi, const Prob g, const Sched& S, const Epi& E, int wid) {
;     ...
;             PG8_LDB(B0, 0, 0); PG8_LDB(B1, 0, 1); PG8_SCHED; PG8_LDA(At, 0, 0); PG8_STAGE(PG8_SA(1, 1), a1, cA10, cA11);
;             PG8_WAIT_V(8); PG8_WAIT_L(0); PG8_BAR; PG8_MMA(0, 0, At, B0); PG8_MMA(0, 1, At, B1); PG8_BAR; PG8_SCHED;
;             PG8_LDA(At, 0, 1); PG8_STAGE(PG8_SB(0, 0), b2, vB0, vB1); PG8_STAGE(PG8_SB(0, 1), b2 + hstepB, vB0, vB1); PG8_STAGE(PG8_SA(0, 0), a2, cA00, cA01);
;             PG8_WAIT_V(8); PG8_WAIT_L(0); PG8_BAR; PG8_MMA(1, 0, At, B0); PG8_MMA(1, 1, At, B1); PG8_BAR; PG8_SCHED;
;             PG8_LDB(B0, 1, 0); PG8_LDB(B1, 1, 1); PG8_SCHED; PG8_LDA(At, 1, 0); PG8_STAGE(PG8_SA(0, 1), a2, cA10, cA11);
;             PG8_WAIT_V(8); PG8_WAIT_L(0); PG8_BAR; PG8_MMA(0, 0, At, B0); PG8_MMA(0, 1, At, B1); PG8_BAR; PG8_SCHED;
;             PG8_LDA(At, 1, 1); PG8_STAGE(PG8_SB(1, 0), b3, vB0, vB1); PG8_STAGE(PG8_SB(1, 1), b3 + hstepB, vB0, vB1); PG8_STAGE(PG8_SA(1, 0), a3, cA00, cA01);
;             PG8_WAIT_V(8); PG8_WAIT_L(0); PG8_BAR; PG8_MMA(1, 0, At, B0); PG8_MMA(1, 1, At, B1); PG8_BAR; PG8_SCHED;
	s_mov_b32 m0, s31
	v_lshl_add_u64 v[206:207], v[206:207], 0, s[54:55]
	ds_read_b128 v[174:177], v223 offset:49152
	ds_read_b128 v[178:181], v223 offset:50176
	ds_read_b128 v[182:185], v223 offset:51200
	ds_read_b128 v[186:189], v223 offset:52224
	ds_read_b128 v[190:193], v223 offset:53248
	ds_read_b128 v[194:197], v223 offset:54272
	ds_read_b128 v[198:201], v223 offset:55296
	ds_read_b128 v[202:205], v223 offset:56320
	global_load_lds_dwordx4 v[206:207], off
	v_lshl_add_u64 v[206:207], v[208:209], 0, s[54:55]
	s_mov_b32 m0, s29
	s_nop 0
	global_load_lds_dwordx4 v[206:207], off
	v_lshl_add_u64 v[206:207], s[12:13], 0, v[152:153]
	s_mov_b32 m0, s30
	s_nop 0
	global_load_lds_dwordx4 v[206:207], off
	v_lshl_add_u64 v[206:207], s[12:13], 0, v[154:155]
	s_mov_b32 m0, s28
	s_nop 0
	global_load_lds_dwordx4 v[206:207], off
	v_lshl_add_u64 v[206:207], v[210:211], 0, s[54:55]
	s_mov_b32 m0, s83
	s_nop 0
	global_load_lds_dwordx4 v[206:207], off
	v_lshl_add_u64 v[206:207], v[212:213], 0, s[54:55]
	s_mov_b32 m0, s84
	s_nop 0
	global_load_lds_dwordx4 v[206:207], off
	s_waitcnt vmcnt(8)
	s_waitcnt lgkmcnt(0)
	s_barrier
	s_waitcnt lgkmcnt(0)
	v_mfma_f32_16x16x32_bf16 v[64:67], v[56:59], v[174:177], v[64:67]
	v_mfma_f32_16x16x32_bf16 v[28:31], v[72:75], v[174:177], v[28:31]
	v_mfma_f32_16x16x32_bf16 v[60:63], v[56:59], v[182:185], v[60:63]
	v_mfma_f32_16x16x32_bf16 v[24:27], v[72:75], v[182:185], v[24:27]
	v_mfma_f32_16x16x32_bf16 v[52:55], v[56:59], v[190:193], v[52:55]
	v_mfma_f32_16x16x32_bf16 v[20:23], v[72:75], v[190:193], v[20:23]
	v_mfma_f32_16x16x32_bf16 v[48:51], v[56:59], v[198:201], v[48:51]
	v_mfma_f32_16x16x32_bf16 v[16:19], v[72:75], v[198:201], v[16:19]
	v_mfma_f32_16x16x32_bf16 v[64:67], v[68:71], v[178:181], v[64:67]
	v_mfma_f32_16x16x32_bf16 v[28:31], v[88:91], v[178:181], v[28:31]
	v_mfma_f32_16x16x32_bf16 v[60:63], v[68:71], v[186:189], v[60:63]
	v_mfma_f32_16x16x32_bf16 v[24:27], v[88:91], v[186:189], v[24:27]
	v_mfma_f32_16x16x32_bf16 v[52:55], v[68:71], v[194:197], v[52:55]
	v_mfma_f32_16x16x32_bf16 v[20:23], v[88:91], v[194:197], v[20:23]
	v_mfma_f32_16x16x32_bf16 v[48:51], v[68:71], v[202:205], v[48:51]
	v_mfma_f32_16x16x32_bf16 v[16:19], v[88:91], v[202:205], v[16:19]
	v_mfma_f32_16x16x32_bf16 v[44:47], v[100:103], v[174:177], v[44:47]
	v_mfma_f32_16x16x32_bf16 v[12:15], v[166:169], v[174:177], v[12:15]
	v_mfma_f32_16x16x32_bf16 v[40:43], v[100:103], v[182:185], v[40:43]
	v_mfma_f32_16x16x32_bf16 v[8:11], v[166:169], v[182:185], v[8:11]
	v_mfma_f32_16x16x32_bf16 v[36:39], v[100:103], v[190:193], v[36:39]
	v_mfma_f32_16x16x32_bf16 v[4:7], v[166:169], v[190:193], v[4:7]
	v_mfma_f32_16x16x32_bf16 v[32:35], v[100:103], v[198:201], v[32:35]
	v_mfma_f32_16x16x32_bf16 v[0:3], v[166:169], v[198:201], v[0:3]
	v_mfma_f32_16x16x32_bf16 v[44:47], v[104:107], v[178:181], v[44:47]
	v_mfma_f32_16x16x32_bf16 v[12:15], v[170:173], v[178:181], v[12:15]
	v_mfma_f32_16x16x32_bf16 v[40:43], v[104:107], v[186:189], v[40:43]
	v_mfma_f32_16x16x32_bf16 v[8:11], v[170:173], v[186:189], v[8:11]
	v_mfma_f32_16x16x32_bf16 v[36:39], v[104:107], v[194:197], v[36:39]
	v_mfma_f32_16x16x32_bf16 v[4:7], v[170:173], v[194:197], v[4:7]
	v_mfma_f32_16x16x32_bf16 v[32:35], v[104:107], v[202:205], v[32:35]
	v_mfma_f32_16x16x32_bf16 v[0:3], v[170:173], v[202:205], v[0:3]
	s_barrier
	s_mov_b64 s[20:21], 0
	s_mov_b64 s[12:13], -1
	s_mov_b64 s[14:15], 0x100
.LBB0_1595:
	s_add_u32 s24, s8, s14
	s_addc_u32 s25, s9, s15
	s_add_u32 s22, s24, 0x100
	s_addc_u32 s23, s25, 0
	v_cndmask_b32_e64 v56, 0, 1, s[20:21]
	s_and_b64 s[20:21], s[12:13], exec
	s_cselect_b32 s20, s19, s22
	s_cselect_b32 s21, s17, s23
	s_add_u32 s14, s10, s14
	s_addc_u32 s15, s11, s15
	s_add_u32 s14, s14, 0x100
	v_cmp_ne_u32_e32 vcc, 1, v56
	ds_read_b128 v[56:59], v221
	ds_read_b128 v[68:71], v221 offset:1024
	ds_read_b128 v[72:75], v221 offset:2048
	ds_read_b128 v[88:91], v221 offset:3072
	ds_read_b128 v[100:103], v222
	ds_read_b128 v[104:107], v222 offset:1024
	ds_read_b128 v[166:169], v222 offset:2048
	ds_read_b128 v[170:173], v222 offset:3072
	s_addc_u32 s15, s15, 0
	s_and_b64 s[12:13], s[12:13], exec
	s_cselect_b32 s15, s26, s15
	s_cselect_b32 s14, s27, s14
	s_add_i32 s65, s85, s97
	s_add_i32 m0, s77, 0xc000
	s_add_i32 s72, s77, 0xe000
	s_add_i32 s36, s65, 0x2000
	s_add_u32 s22, s14, 0x10000
	s_addc_u32 s23, s15, 0
	s_add_i32 s35, 0, 0x18000
	s_add_i32 s63, s86, s97
	s_add_i32 s31, s35, s97
	s_add_i32 s37, s63, 0x2000
	s_add_i32 s34, 0, 0x1c000
	s_add_i32 s29, s31, 0x2000
	s_add_u32 s12, s14, 0x10080
	s_addc_u32 s13, s15, 0
	s_add_i32 s30, s34, s97
	s_add_i32 s28, s30, 0x2000
	v_lshl_add_u64 v[206:207], s[24:25], 0, v[158:159]
	v_lshl_add_u64 v[206:207], v[206:207], 0, s[54:55]
	ds_read_b128 v[174:177], v223
	ds_read_b128 v[178:181], v223 offset:1024
	ds_read_b128 v[182:185], v223 offset:2048
	ds_read_b128 v[186:189], v223 offset:3072
	ds_read_b128 v[190:193], v223 offset:4096
	ds_read_b128 v[194:197], v223 offset:5120
	ds_read_b128 v[198:201], v223 offset:6144
	ds_read_b128 v[202:205], v223 offset:7168
	global_load_lds_dwordx4 v[206:207], off
	v_lshl_add_u64 v[206:207], s[24:25], 0, v[162:163]
	v_lshl_add_u64 v[206:207], v[206:207], 0, s[54:55]
	s_mov_b32 m0, s72
	s_nop 0
	global_load_lds_dwordx4 v[206:207], off
	s_waitcnt vmcnt(8)
	s_waitcnt lgkmcnt(0)
	s_barrier
; #define PG8_STAGE(bufoff, gbase, o0, o1) do { \
;         __builtin_amdgcn_global_load_lds((const unsigned*)((const char*)(gbase) + (o0)), (LAS unsigned*)(lds + (bufoff) + ldsw), 16, 0, 0); \
;         __builtin_amdgcn_global_load_lds((const unsigned*)((const char*)(gbase) + (o1)), (LAS unsigned*)(lds + (bufoff) + ldsw + 8192), 16, 0, 0); } while (0)
; #define PG8_LDA(dst, b, h) do { _Pragma("unroll") for (int m = 0; m < 4; ++m) _Pragma("unroll") for (int k = 0; k < 2; ++k) dst[m][k] = *(const LAS bf16x8*)(lds + PG8_SA(b, h) + aoff + m * 2048 + k * 1024); } while (0)
; #define PG8_LDB(dst, b, h) do { _Pragma("unroll") for (int n = 0; n < 2; ++n) _Pragma("unroll") for (int k = 0; k < 2; ++k) dst[n][k] = *(const LAS bf16x8*)(lds + PG8_SB(b, h) + boff + n * 2048 + k * 1024); } while (0)
; #define PG8_WAIT_V(n) asm volatile("s_waitcnt vmcnt(" #n ")" ::: "memory")
; #define PG8_WAIT_L(n) asm volatile("s_waitcnt lgkmcnt(" #n ")" ::: "memory")
; #define PG8_BAR __builtin_amdgcn_s_barrier()
; #define PG8_SCHED __builtin_amdgcn_sched_barrier(0)
; template <class Epi, class Sched, class Prob>
; __device__ __forceinline__ void gemm_phase(LAS unsigned char* lds, LAS unsigned char* lds_epi, const Prob g, const Sched& S, const Epi& E, int wid) {
;     ...
;             PG8_LDB(B0, 0, 0); PG8_LDB(B1, 0, 1); PG8_SCHED; PG8_LDA(At, 0, 0); PG8_STAGE(PG8_SA(1, 1), a1, cA10, cA11);
;             PG8_WAIT_V(8); PG8_WAIT_L(0); PG8_BAR; PG8_MMA(0, 0, At, B0); PG8_MMA(0, 1, At, B1); PG8_BAR; PG8_SCHED;
;             PG8_LDA(At, 0, 1); PG8_STAGE(PG8_SB(0, 0), b2, vB0, vB1); PG8_STAGE(PG8_SB(0, 1), b2 + hstepB, vB0, vB1); PG8_STAGE(PG8_SA(0, 0), a2, cA00, cA01);
;             PG8_WAIT_V(8); PG8_WAIT_L(0); PG8_BAR; PG8_MMA(1, 0, At, B0); PG8_MMA(1, 1, At, B1); PG8_BAR; PG8_SCHED;
;             PG8_LDB(B0, 1, 0); PG8_LDB(B1, 1, 1); PG8_SCHED; PG8_LDA(At, 1, 0); PG8_STAGE(PG8_SA(0, 1), a2, cA10, cA11);
;             PG8_WAIT_V(8); PG8_WAIT_L(0); PG8_BAR; PG8_MMA(0, 0, At, B0); PG8_MMA(0, 1, At, B1); PG8_BAR; PG8_SCHED;
;             PG8_LDA(At, 1, 1); PG8_STAGE(PG8_SB(1, 0), b3, vB0, vB1); PG8_STAGE(PG8_SB(1, 1), b3 + hstepB, vB0, vB1); PG8_STAGE(PG8_SA(1, 0), a3, cA00, cA01);
;             PG8_WAIT_V(8); PG8_WAIT_L(0); PG8_BAR; PG8_MMA(1, 0, At, B0); PG8_MMA(1, 1, At, B1); PG8_BAR; PG8_SCHED;
	s_waitcnt lgkmcnt(0)
	v_mfma_f32_16x16x32_bf16 v[148:151], v[56:59], v[174:177], v[148:151]
	v_mfma_f32_16x16x32_bf16 v[116:119], v[72:75], v[174:177], v[116:119]
	v_mfma_f32_16x16x32_bf16 v[144:147], v[56:59], v[182:185], v[144:147]
	v_mfma_f32_16x16x32_bf16 v[112:115], v[72:75], v[182:185], v[112:115]
	v_mfma_f32_16x16x32_bf16 v[140:143], v[56:59], v[190:193], v[140:143]
	v_mfma_f32_16x16x32_bf16 v[108:111], v[72:75], v[190:193], v[108:111]
	v_mfma_f32_16x16x32_bf16 v[136:139], v[56:59], v[198:201], v[136:139]
	v_mfma_f32_16x16x32_bf16 v[96:99], v[72:75], v[198:201], v[96:99]
	v_mfma_f32_16x16x32_bf16 v[148:151], v[68:71], v[178:181], v[148:151]
	v_mfma_f32_16x16x32_bf16 v[116:119], v[88:91], v[178:181], v[116:119]
	v_mfma_f32_16x16x32_bf16 v[144:147], v[68:71], v[186:189], v[144:147]
	v_mfma_f32_16x16x32_bf16 v[112:115], v[88:91], v[186:189], v[112:115]
	v_mfma_f32_16x16x32_bf16 v[140:143], v[68:71], v[194:197], v[140:143]
	v_mfma_f32_16x16x32_bf16 v[108:111], v[88:91], v[194:197], v[108:111]
	v_mfma_f32_16x16x32_bf16 v[136:139], v[68:71], v[202:205], v[136:139]
	v_mfma_f32_16x16x32_bf16 v[96:99], v[88:91], v[202:205], v[96:99]
	v_mfma_f32_16x16x32_bf16 v[132:135], v[100:103], v[174:177], v[132:135]
	v_mfma_f32_16x16x32_bf16 v[92:95], v[166:169], v[174:177], v[92:95]
	v_mfma_f32_16x16x32_bf16 v[128:131], v[100:103], v[182:185], v[128:131]
	v_mfma_f32_16x16x32_bf16 v[84:87], v[166:169], v[182:185], v[84:87]
	v_mfma_f32_16x16x32_bf16 v[124:127], v[100:103], v[190:193], v[124:127]
	v_mfma_f32_16x16x32_bf16 v[80:83], v[166:169], v[190:193], v[80:83]
	v_mfma_f32_16x16x32_bf16 v[120:123], v[100:103], v[198:201], v[120:123]
	v_mfma_f32_16x16x32_bf16 v[76:79], v[166:169], v[198:201], v[76:79]
	v_mfma_f32_16x16x32_bf16 v[132:135], v[104:107], v[178:181], v[132:135]
	v_mfma_f32_16x16x32_bf16 v[92:95], v[170:173], v[178:181], v[92:95]
	v_mfma_f32_16x16x32_bf16 v[128:131], v[104:107], v[186:189], v[128:131]
	v_mfma_f32_16x16x32_bf16 v[84:87], v[170:173], v[186:189], v[84:87]
	v_mfma_f32_16x16x32_bf16 v[124:127], v[104:107], v[194:197], v[124:127]
	v_mfma_f32_16x16x32_bf16 v[80:83], v[170:173], v[194:197], v[80:83]
	v_mfma_f32_16x16x32_bf16 v[120:123], v[104:107], v[202:205], v[120:123]
	v_mfma_f32_16x16x32_bf16 v[76:79], v[170:173], v[202:205], v[76:79]
	s_barrier
	s_mov_b32 m0, s65
	v_lshl_add_u64 v[206:207], s[14:15], 0, v[152:153]
	ds_read_b128 v[174:177], v223 offset:16384
	ds_read_b128 v[178:181], v223 offset:17408
	ds_read_b128 v[182:185], v223 offset:18432
	ds_read_b128 v[186:189], v223 offset:19456
	ds_read_b128 v[190:193], v223 offset:20480
	ds_read_b128 v[194:197], v223 offset:21504
	ds_read_b128 v[198:201], v223 offset:22528
	ds_read_b128 v[202:205], v223 offset:23552
	global_load_lds_dwordx4 v[206:207], off
	v_lshl_add_u64 v[208:209], s[14:15], 0, v[154:155]
	s_mov_b32 m0, s36
	v_lshl_add_u64 v[210:211], s[22:23], 0, v[152:153]
	global_load_lds_dwordx4 v[208:209], off
	s_mov_b32 m0, s63
	v_lshl_add_u64 v[212:213], s[20:21], 0, v[160:161]
	global_load_lds_dwordx4 v[210:211], off
	v_lshl_add_u64 v[210:211], s[22:23], 0, v[154:155]
	s_mov_b32 m0, s37
	s_nop 0
	global_load_lds_dwordx4 v[210:211], off
	v_lshl_add_u64 v[210:211], s[20:21], 0, v[156:157]
	s_mov_b32 m0, s77
	s_nop 0
	global_load_lds_dwordx4 v[210:211], off
	s_mov_b32 m0, s78
	s_nop 0
	global_load_lds_dwordx4 v[212:213], off
	s_waitcnt vmcnt(8)
	s_waitcnt lgkmcnt(0)
	s_barrier
	s_waitcnt lgkmcnt(0)
	v_mfma_f32_16x16x32_bf16 v[64:67], v[56:59], v[174:177], v[64:67]
	v_mfma_f32_16x16x32_bf16 v[28:31], v[72:75], v[174:177], v[28:31]
	v_mfma_f32_16x16x32_bf16 v[60:63], v[56:59], v[182:185], v[60:63]
	v_mfma_f32_16x16x32_bf16 v[24:27], v[72:75], v[182:185], v[24:27]
	v_mfma_f32_16x16x32_bf16 v[52:55], v[56:59], v[190:193], v[52:55]
	v_mfma_f32_16x16x32_bf16 v[20:23], v[72:75], v[190:193], v[20:23]
	v_mfma_f32_16x16x32_bf16 v[48:51], v[56:59], v[198:201], v[48:51]
	v_mfma_f32_16x16x32_bf16 v[16:19], v[72:75], v[198:201], v[16:19]
	v_mfma_f32_16x16x32_bf16 v[64:67], v[68:71], v[178:181], v[64:67]
	v_mfma_f32_16x16x32_bf16 v[28:31], v[88:91], v[178:181], v[28:31]
	v_mfma_f32_16x16x32_bf16 v[60:63], v[68:71], v[186:189], v[60:63]
	v_mfma_f32_16x16x32_bf16 v[24:27], v[88:91], v[186:189], v[24:27]
	v_mfma_f32_16x16x32_bf16 v[52:55], v[68:71], v[194:197], v[52:55]
	v_mfma_f32_16x16x32_bf16 v[20:23], v[88:91], v[194:197], v[20:23]
	v_mfma_f32_16x16x32_bf16 v[48:51], v[68:71], v[202:205], v[48:51]
	v_mfma_f32_16x16x32_bf16 v[16:19], v[88:91], v[202:205], v[16:19]
	v_mfma_f32_16x16x32_bf16 v[44:47], v[100:103], v[174:177], v[44:47]
	v_mfma_f32_16x16x32_bf16 v[12:15], v[166:169], v[174:177], v[12:15]
	v_mfma_f32_16x16x32_bf16 v[40:43], v[100:103], v[182:185], v[40:43]
	v_mfma_f32_16x16x32_bf16 v[8:11], v[166:169], v[182:185], v[8:11]
	v_mfma_f32_16x16x32_bf16 v[36:39], v[100:103], v[190:193], v[36:39]
	v_mfma_f32_16x16x32_bf16 v[4:7], v[166:169], v[190:193], v[4:7]
	v_mfma_f32_16x16x32_bf16 v[32:35], v[100:103], v[198:201], v[32:35]
	v_mfma_f32_16x16x32_bf16 v[0:3], v[166:169], v[198:201], v[0:3]
	v_mfma_f32_16x16x32_bf16 v[44:47], v[104:107], v[178:181], v[44:47]
	v_mfma_f32_16x16x32_bf16 v[12:15], v[170:173], v[178:181], v[12:15]
	v_mfma_f32_16x16x32_bf16 v[40:43], v[104:107], v[186:189], v[40:43]
	v_mfma_f32_16x16x32_bf16 v[8:11], v[170:173], v[186:189], v[8:11]
	v_mfma_f32_16x16x32_bf16 v[36:39], v[104:107], v[194:197], v[36:39]
	v_mfma_f32_16x16x32_bf16 v[4:7], v[170:173], v[194:197], v[4:7]
	v_mfma_f32_16x16x32_bf16 v[32:35], v[104:107], v[202:205], v[32:35]
	v_mfma_f32_16x16x32_bf16 v[0:3], v[170:173], v[202:205], v[0:3]
	s_barrier
; #define PG8_STAGE(bufoff, gbase, o0, o1) do { \
;         __builtin_amdgcn_global_load_lds((const unsigned*)((const char*)(gbase) + (o0)), (LAS unsigned*)(lds + (bufoff) + ldsw), 16, 0, 0); \
;         __builtin_amdgcn_global_load_lds((const unsigned*)((const char*)(gbase) + (o1)), (LAS unsigned*)(lds + (bufoff) + ldsw + 8192), 16, 0, 0); } while (0)
; #define PG8_LDA(dst, b, h) do { _Pragma("unroll") for (int m = 0; m < 4; ++m) _Pragma("unroll") for (int k = 0; k < 2; ++k) dst[m][k] = *(const LAS bf16x8*)(lds + PG8_SA(b, h) + aoff + m * 2048 + k * 1024); } while (0)
; #define PG8_LDB(dst, b, h) do { _Pragma("unroll") for (int n = 0; n < 2; ++n) _Pragma("unroll") for (int k = 0; k < 2; ++k) dst[n][k] = *(const LAS bf16x8*)(lds + PG8_SB(b, h) + boff + n * 2048 + k * 1024); } while (0)
; #define PG8_WAIT_V(n) asm volatile("s_waitcnt vmcnt(" #n ")" ::: "memory")
; #define PG8_WAIT_L(n) asm volatile("s_waitcnt lgkmcnt(" #n ")" ::: "memory")
; #define PG8_BAR __builtin_amdgcn_s_barrier()
; #define PG8_SCHED __builtin_amdgcn_sched_barrier(0)
; template <class Epi, class Sched, class Prob>
; __device__ __forceinline__ void gemm_phase(LAS unsigned char* lds, LAS unsigned char* lds_epi, const Prob g, const Sched& S, const Epi& E, int wid) {
;     ...
;             PG8_LDB(B0, 1, 0); PG8_LDB(B1, 1, 1); PG8_SCHED; PG8_LDA(At, 1, 0); PG8_STAGE(PG8_SA(0, 1), a2, cA10, cA11);
;             PG8_WAIT_V(8); PG8_WAIT_L(0); PG8_BAR; PG8_MMA(0, 0, At, B0); PG8_MMA(0, 1, At, B1); PG8_BAR; PG8_SCHED;
;             PG8_LDA(At, 1, 1); PG8_STAGE(PG8_SB(1, 0), b3, vB0, vB1); PG8_STAGE(PG8_SB(1, 1), b3 + hstepB, vB0, vB1); PG8_STAGE(PG8_SA(1, 0), a3, cA00, cA01);
;             PG8_WAIT_V(8); PG8_WAIT_L(0); PG8_BAR; PG8_MMA(1, 0, At, B0); PG8_MMA(1, 1, At, B1); PG8_BAR; PG8_SCHED;
;         }
;         if constexpr (Prob::FP8) asm volatile("s_nop 7\n\ts_nop 7\n\ts_nop 7" ::: "memory");
;         if (wr == 0) PG8_BAR;
	v_add_u32_e32 v88, s35, v220
	v_add_u32_e32 v170, s34, v220
	ds_read_b128 v[56:59], v88
	ds_read_b128 v[68:71], v88 offset:1024
	ds_read_b128 v[72:75], v88 offset:2048
	ds_read_b128 v[88:91], v88 offset:3072
	ds_read_b128 v[100:103], v170
	ds_read_b128 v[104:107], v170 offset:1024
	ds_read_b128 v[166:169], v170 offset:2048
	ds_read_b128 v[170:173], v170 offset:3072
	s_mov_b32 m0, s79
	v_lshl_add_u64 v[214:215], s[20:21], 0, v[158:159]
	ds_read_b128 v[174:177], v223 offset:32768
	ds_read_b128 v[178:181], v223 offset:33792
	ds_read_b128 v[182:185], v223 offset:34816
	ds_read_b128 v[186:189], v223 offset:35840
	ds_read_b128 v[190:193], v223 offset:36864
	ds_read_b128 v[194:197], v223 offset:37888
	ds_read_b128 v[198:201], v223 offset:38912
	ds_read_b128 v[202:205], v223 offset:39936
	global_load_lds_dwordx4 v[214:215], off
	v_lshl_add_u64 v[214:215], s[20:21], 0, v[162:163]
	s_mov_b32 m0, s80
	s_nop 0
	global_load_lds_dwordx4 v[214:215], off
	s_waitcnt vmcnt(8)
	s_waitcnt lgkmcnt(0)
	s_barrier
	s_waitcnt lgkmcnt(0)
	v_mfma_f32_16x16x32_bf16 v[148:151], v[56:59], v[174:177], v[148:151]
	v_mfma_f32_16x16x32_bf16 v[116:119], v[72:75], v[174:177], v[116:119]
	v_mfma_f32_16x16x32_bf16 v[144:147], v[56:59], v[182:185], v[144:147]
	v_mfma_f32_16x16x32_bf16 v[112:115], v[72:75], v[182:185], v[112:115]
	v_mfma_f32_16x16x32_bf16 v[140:143], v[56:59], v[190:193], v[140:143]
	v_mfma_f32_16x16x32_bf16 v[108:111], v[72:75], v[190:193], v[108:111]
	v_mfma_f32_16x16x32_bf16 v[136:139], v[56:59], v[198:201], v[136:139]
	v_mfma_f32_16x16x32_bf16 v[96:99], v[72:75], v[198:201], v[96:99]
	v_mfma_f32_16x16x32_bf16 v[148:151], v[68:71], v[178:181], v[148:151]
	v_mfma_f32_16x16x32_bf16 v[116:119], v[88:91], v[178:181], v[116:119]
	v_mfma_f32_16x16x32_bf16 v[144:147], v[68:71], v[186:189], v[144:147]
	v_mfma_f32_16x16x32_bf16 v[112:115], v[88:91], v[186:189], v[112:115]
	v_mfma_f32_16x16x32_bf16 v[140:143], v[68:71], v[194:197], v[140:143]
	v_mfma_f32_16x16x32_bf16 v[108:111], v[88:91], v[194:197], v[108:111]
	v_mfma_f32_16x16x32_bf16 v[136:139], v[68:71], v[202:205], v[136:139]
	v_mfma_f32_16x16x32_bf16 v[96:99], v[88:91], v[202:205], v[96:99]
	v_mfma_f32_16x16x32_bf16 v[132:135], v[100:103], v[174:177], v[132:135]
	v_mfma_f32_16x16x32_bf16 v[92:95], v[166:169], v[174:177], v[92:95]
	v_mfma_f32_16x16x32_bf16 v[128:131], v[100:103], v[182:185], v[128:131]
	v_mfma_f32_16x16x32_bf16 v[84:87], v[166:169], v[182:185], v[84:87]
	v_mfma_f32_16x16x32_bf16 v[124:127], v[100:103], v[190:193], v[124:127]
	v_mfma_f32_16x16x32_bf16 v[80:83], v[166:169], v[190:193], v[80:83]
	v_mfma_f32_16x16x32_bf16 v[120:123], v[100:103], v[198:201], v[120:123]
	v_mfma_f32_16x16x32_bf16 v[76:79], v[166:169], v[198:201], v[76:79]
	v_mfma_f32_16x16x32_bf16 v[132:135], v[104:107], v[178:181], v[132:135]
	v_mfma_f32_16x16x32_bf16 v[92:95], v[170:173], v[178:181], v[92:95]
	v_mfma_f32_16x16x32_bf16 v[128:131], v[104:107], v[186:189], v[128:131]
	v_mfma_f32_16x16x32_bf16 v[84:87], v[170:173], v[186:189], v[84:87]
	v_mfma_f32_16x16x32_bf16 v[124:127], v[104:107], v[194:197], v[124:127]
	v_mfma_f32_16x16x32_bf16 v[80:83], v[170:173], v[194:197], v[80:83]
	v_mfma_f32_16x16x32_bf16 v[120:123], v[104:107], v[202:205], v[120:123]
	v_mfma_f32_16x16x32_bf16 v[76:79], v[170:173], v[202:205], v[76:79]
	s_barrier
	s_mov_b32 m0, s31
	v_lshl_add_u64 v[206:207], v[206:207], 0, s[54:55]
	ds_read_b128 v[174:177], v223 offset:49152
	ds_read_b128 v[178:181], v223 offset:50176
	ds_read_b128 v[182:185], v223 offset:51200
	ds_read_b128 v[186:189], v223 offset:52224
	ds_read_b128 v[190:193], v223 offset:53248
	ds_read_b128 v[194:197], v223 offset:54272
	ds_read_b128 v[198:201], v223 offset:55296
	ds_read_b128 v[202:205], v223 offset:56320
	global_load_lds_dwordx4 v[206:207], off
	v_lshl_add_u64 v[206:207], v[208:209], 0, s[54:55]
	s_mov_b32 m0, s29
	s_nop 0
	global_load_lds_dwordx4 v[206:207], off
	v_lshl_add_u64 v[206:207], s[12:13], 0, v[152:153]
	s_mov_b32 m0, s30
	s_nop 0
	global_load_lds_dwordx4 v[206:207], off
	v_lshl_add_u64 v[206:207], s[12:13], 0, v[154:155]
	s_mov_b32 m0, s28
	s_nop 0
	global_load_lds_dwordx4 v[206:207], off
	v_lshl_add_u64 v[206:207], v[210:211], 0, s[54:55]
	s_mov_b32 m0, s83
	s_nop 0
	global_load_lds_dwordx4 v[206:207], off
	v_lshl_add_u64 v[206:207], v[212:213], 0, s[54:55]
	s_mov_b32 m0, s84
	s_nop 0
	global_load_lds_dwordx4 v[206:207], off
	s_waitcnt vmcnt(8)
	s_waitcnt lgkmcnt(0)
	s_barrier
	s_waitcnt lgkmcnt(0)
	v_mfma_f32_16x16x32_bf16 v[64:67], v[56:59], v[174:177], v[64:67]
	v_mfma_f32_16x16x32_bf16 v[28:31], v[72:75], v[174:177], v[28:31]
	v_mfma_f32_16x16x32_bf16 v[60:63], v[56:59], v[182:185], v[60:63]
	v_mfma_f32_16x16x32_bf16 v[24:27], v[72:75], v[182:185], v[24:27]
	v_mfma_f32_16x16x32_bf16 v[52:55], v[56:59], v[190:193], v[52:55]
	v_mfma_f32_16x16x32_bf16 v[20:23], v[72:75], v[190:193], v[20:23]
	v_mfma_f32_16x16x32_bf16 v[48:51], v[56:59], v[198:201], v[48:51]
	v_mfma_f32_16x16x32_bf16 v[16:19], v[72:75], v[198:201], v[16:19]
	v_mfma_f32_16x16x32_bf16 v[64:67], v[68:71], v[178:181], v[64:67]
	v_mfma_f32_16x16x32_bf16 v[28:31], v[88:91], v[178:181], v[28:31]
	v_mfma_f32_16x16x32_bf16 v[60:63], v[68:71], v[186:189], v[60:63]
	v_mfma_f32_16x16x32_bf16 v[24:27], v[88:91], v[186:189], v[24:27]
	v_mfma_f32_16x16x32_bf16 v[52:55], v[68:71], v[194:197], v[52:55]
	v_mfma_f32_16x16x32_bf16 v[20:23], v[88:91], v[194:197], v[20:23]
	v_mfma_f32_16x16x32_bf16 v[48:51], v[68:71], v[202:205], v[48:51]
	v_mfma_f32_16x16x32_bf16 v[16:19], v[88:91], v[202:205], v[16:19]
	v_mfma_f32_16x16x32_bf16 v[44:47], v[100:103], v[174:177], v[44:47]
	v_mfma_f32_16x16x32_bf16 v[12:15], v[166:169], v[174:177], v[12:15]
	v_mfma_f32_16x16x32_bf16 v[40:43], v[100:103], v[182:185], v[40:43]
	v_mfma_f32_16x16x32_bf16 v[8:11], v[166:169], v[182:185], v[8:11]
	v_mfma_f32_16x16x32_bf16 v[36:39], v[100:103], v[190:193], v[36:39]
	v_mfma_f32_16x16x32_bf16 v[4:7], v[166:169], v[190:193], v[4:7]
	v_mfma_f32_16x16x32_bf16 v[32:35], v[100:103], v[198:201], v[32:35]
	v_mfma_f32_16x16x32_bf16 v[0:3], v[166:169], v[198:201], v[0:3]
	v_mfma_f32_16x16x32_bf16 v[44:47], v[104:107], v[178:181], v[44:47]
	v_mfma_f32_16x16x32_bf16 v[12:15], v[170:173], v[178:181], v[12:15]
	v_mfma_f32_16x16x32_bf16 v[40:43], v[104:107], v[186:189], v[40:43]
	v_mfma_f32_16x16x32_bf16 v[8:11], v[170:173], v[186:189], v[8:11]
	v_mfma_f32_16x16x32_bf16 v[36:39], v[104:107], v[194:197], v[36:39]
	v_mfma_f32_16x16x32_bf16 v[4:7], v[170:173], v[194:197], v[4:7]
	v_mfma_f32_16x16x32_bf16 v[32:35], v[104:107], v[202:205], v[32:35]
	v_mfma_f32_16x16x32_bf16 v[0:3], v[170:173], v[202:205], v[0:3]
	s_barrier
	s_mov_b64 s[20:21], 0
	s_mov_b64 s[12:13], -1
	s_mov_b64 s[14:15], 0x100
	s_cbranch_vccz .LBB0_1595
	s_setprio 0
	v_readlane_b32 s8, v254, 27
	v_readlane_b32 s9, v254, 28
	s_and_b64 vcc, exec, s[8:9]
	s_cbranch_vccz .LBB0_1598
	s_barrier

; #define PG8_STAGE(bufoff, gbase, o0, o1) do { \
;         __builtin_amdgcn_global_load_lds((const unsigned*)((const char*)(gbase) + (o0)), (LAS unsigned*)(lds + (bufoff) + ldsw), 16, 0, 0); \
;         __builtin_amdgcn_global_load_lds((const unsigned*)((const char*)(gbase) + (o1)), (LAS unsigned*)(lds + (bufoff) + ldsw + 8192), 16, 0, 0); } while (0)
; #define PG8_LDA(dst, b, h) do { _Pragma("unroll") for (int m = 0; m < 4; ++m) _Pragma("unroll") for (int k = 0; k < 2; ++k) dst[m][k] = *(const LAS bf16x8*)(lds + PG8_SA(b, h) + aoff + m * 2048 + k * 1024); } while (0)
; #define PG8_LDB(dst, b, h) do { _Pragma("unroll") for (int n = 0; n < 2; ++n) _Pragma("unroll") for (int k = 0; k < 2; ++k) dst[n][k] = *(const LAS bf16x8*)(lds + PG8_SB(b, h) + boff + n * 2048 + k * 1024); } while (0)
; #define PG8_WAIT_V(n) asm volatile("s_waitcnt vmcnt(" #n ")" ::: "memory")
; #define PG8_WAIT_L(n) asm volatile("s_waitcnt lgkmcnt(" #n ")" ::: "memory")
; #define PG8_BAR __builtin_amdgcn_s_barrier()
; #define PG8_SCHED __builtin_amdgcn_sched_barrier(0)
; template <class Epi, class Sched, class Prob>
; __device__ __forceinline__ void gemm_phase(LAS unsigned char* lds, LAS unsigned char* lds_epi, const Prob g, const Sched& S, const Epi& E, int wid) {
;     ...
;     for (;;) {
;         const bool has_next = S.next(ui + 1, nxt);
;         const char* nA = has_next ? g.a_base(nxt) : cA; const char* nB = has_next ? g.b_base(nxt) : cB;
; _Pragma("clang loop unroll(disable)")
;         for (int t = 0; t < nt; t += 2) {
;             const bool last = (t == nt - 2);
;             const char* a1 = cA + (size_t)(t + 1) * kstep;
;             const char* a2 = last ? nA : cA + (size_t)(t + 2) * kstep; const char* b2 = last ? nB : cB + (size_t)(t + 2) * kstep;
;             const char* a3 = a2 + kstep; const char* b3 = b2 + kstep;
;             PG8_LDB(B0, 0, 0); PG8_LDB(B1, 0, 1); PG8_SCHED; PG8_LDA(At, 0, 0); PG8_STAGE(PG8_SA(1, 1), a1, cA10, cA11);
;             PG8_WAIT_V(8); PG8_WAIT_L(0); PG8_BAR; PG8_MMA(0, 0, At, B0); PG8_MMA(0, 1, At, B1); PG8_BAR; PG8_SCHED;
;             PG8_LDA(At, 0, 1); PG8_STAGE(PG8_SB(0, 0), b2, vB0, vB1); PG8_STAGE(PG8_SB(0, 1), b2 + hstepB, vB0, vB1); PG8_STAGE(PG8_SA(0, 0), a2, cA00, cA01);
.LBB0_1748:
	s_ashr_i32 s17, s16, 31
	s_lshl_b64 s[22:23], s[16:17], 20
	s_add_u32 s22, s33, s22
	s_addc_u32 s23, s36, s23
	s_and_b64 s[24:25], s[30:31], exec
	s_cselect_b32 s17, s23, s27
	s_cselect_b32 s19, s22, s26
	s_ashr_i32 s15, s14, 31
	s_lshl_b64 s[24:25], s[14:15], 20
	s_add_u32 s24, s37, s24
	s_addc_u32 s25, s40, s25
	s_and_b64 s[34:35], s[30:31], exec
	s_cselect_b32 s15, s25, s29
	s_cselect_b32 s54, s24, s28
	s_add_u32 s26, s26, 0x80
	s_addc_u32 s27, s27, 0
	s_add_u32 s55, s28, 0x100
	s_addc_u32 s56, s29, 0
	s_mov_b32 s57, -2
	s_cmp_lt_u32 s91, 0x100
	s_cbranch_scc1 .Lyoung_6
	s_setprio 1
.Lyoung_6:
.LBB0_1749:
	v_add_u32_e32 v160, s51, v145
	v_add_u32_e32 v176, s52, v145
	ds_read_b128 v[148:151], v160
	ds_read_b128 v[152:155], v160 offset:1024
	ds_read_b128 v[156:159], v160 offset:2048
	ds_read_b128 v[160:163], v160 offset:3072
	ds_read_b128 v[164:167], v176
	ds_read_b128 v[168:171], v176 offset:1024
	ds_read_b128 v[172:175], v176 offset:2048
	ds_read_b128 v[176:179], v176 offset:3072
	s_add_u32 s28, s26, 0x80
	s_addc_u32 s29, s27, 0
	s_cmp_eq_u32 s57, 28
	s_cselect_b32 s35, s17, s29
	s_cselect_b32 s34, s19, s28
	s_cselect_b32 s29, s15, s56
	s_cselect_b32 s28, s54, s55
	v_lshl_add_u64 v[212:213], s[26:27], 0, v[140:141]
	s_add_i32 m0, s21, 0xc000
	ds_read_b128 v[180:183], v147
	ds_read_b128 v[184:187], v147 offset:1024
	ds_read_b128 v[188:191], v147 offset:2048
	ds_read_b128 v[192:195], v147 offset:3072
	ds_read_b128 v[196:199], v147 offset:4096
	ds_read_b128 v[200:203], v147 offset:5120
	ds_read_b128 v[204:207], v147 offset:6144
	ds_read_b128 v[208:211], v147 offset:7168
	global_load_lds_dwordx4 v[212:213], off
	v_lshl_add_u64 v[212:213], s[26:27], 0, v[138:139]
	s_add_i32 m0, s21, 0xe000
	s_nop 0
	global_load_lds_dwordx4 v[212:213], off
	s_waitcnt vmcnt(8)
	s_waitcnt lgkmcnt(0)
	s_barrier
	s_waitcnt lgkmcnt(0)
	v_mfma_f32_16x16x32_bf16 v[12:15], v[148:151], v[180:183], v[12:15]
	v_mfma_f32_16x16x32_bf16 v[28:31], v[156:159], v[180:183], v[28:31]
	v_mfma_f32_16x16x32_bf16 v[8:11], v[148:151], v[188:191], v[8:11]
	v_mfma_f32_16x16x32_bf16 v[24:27], v[156:159], v[188:191], v[24:27]
	v_mfma_f32_16x16x32_bf16 v[4:7], v[148:151], v[196:199], v[4:7]
	v_mfma_f32_16x16x32_bf16 v[20:23], v[156:159], v[196:199], v[20:23]
	v_mfma_f32_16x16x32_bf16 v[0:3], v[148:151], v[204:207], v[0:3]
	v_mfma_f32_16x16x32_bf16 v[16:19], v[156:159], v[204:207], v[16:19]
	v_mfma_f32_16x16x32_bf16 v[12:15], v[152:155], v[184:187], v[12:15]
	v_mfma_f32_16x16x32_bf16 v[28:31], v[160:163], v[184:187], v[28:31]
	v_mfma_f32_16x16x32_bf16 v[8:11], v[152:155], v[192:195], v[8:11]
	v_mfma_f32_16x16x32_bf16 v[24:27], v[160:163], v[192:195], v[24:27]
	v_mfma_f32_16x16x32_bf16 v[4:7], v[152:155], v[200:203], v[4:7]
	v_mfma_f32_16x16x32_bf16 v[20:23], v[160:163], v[200:203], v[20:23]
	v_mfma_f32_16x16x32_bf16 v[0:3], v[152:155], v[208:211], v[0:3]
	v_mfma_f32_16x16x32_bf16 v[16:19], v[160:163], v[208:211], v[16:19]
	v_mfma_f32_16x16x32_bf16 v[44:47], v[164:167], v[180:183], v[44:47]
	v_mfma_f32_16x16x32_bf16 v[68:71], v[172:175], v[180:183], v[68:71]
	v_mfma_f32_16x16x32_bf16 v[40:43], v[164:167], v[188:191], v[40:43]
	v_mfma_f32_16x16x32_bf16 v[64:67], v[172:175], v[188:191], v[64:67]
	v_mfma_f32_16x16x32_bf16 v[36:39], v[164:167], v[196:199], v[36:39]
	v_mfma_f32_16x16x32_bf16 v[60:63], v[172:175], v[196:199], v[60:63]
	v_mfma_f32_16x16x32_bf16 v[32:35], v[164:167], v[204:207], v[32:35]
	v_mfma_f32_16x16x32_bf16 v[56:59], v[172:175], v[204:207], v[56:59]
	v_mfma_f32_16x16x32_bf16 v[44:47], v[168:171], v[184:187], v[44:47]
	v_mfma_f32_16x16x32_bf16 v[68:71], v[176:179], v[184:187], v[68:71]
	v_mfma_f32_16x16x32_bf16 v[40:43], v[168:171], v[192:195], v[40:43]
	v_mfma_f32_16x16x32_bf16 v[64:67], v[176:179], v[192:195], v[64:67]
	v_mfma_f32_16x16x32_bf16 v[36:39], v[168:171], v[200:203], v[36:39]
	v_mfma_f32_16x16x32_bf16 v[60:63], v[176:179], v[200:203], v[60:63]
	v_mfma_f32_16x16x32_bf16 v[32:35], v[168:171], v[208:211], v[32:35]
	v_mfma_f32_16x16x32_bf16 v[56:59], v[176:179], v[208:211], v[56:59]
	s_barrier
	s_add_i32 s58, s51, s97
	v_lshl_add_u64 v[212:213], s[28:29], 0, v[130:131]
	s_mov_b32 m0, s58
	ds_read_b128 v[180:183], v147 offset:16384
	ds_read_b128 v[184:187], v147 offset:17408
	ds_read_b128 v[188:191], v147 offset:18432
	ds_read_b128 v[192:195], v147 offset:19456
	ds_read_b128 v[196:199], v147 offset:20480
	ds_read_b128 v[200:203], v147 offset:21504
	ds_read_b128 v[204:207], v147 offset:22528
	ds_read_b128 v[208:211], v147 offset:23552
	global_load_lds_dwordx4 v[212:213], off
	s_add_i32 m0, s58, 0x2000
	s_add_u32 s58, s28, 0x80000
	v_lshl_add_u64 v[214:215], s[28:29], 0, v[128:129]
	s_addc_u32 s59, s29, 0
	s_add_i32 s60, s52, s97
	global_load_lds_dwordx4 v[214:215], off
	v_lshl_add_u64 v[216:217], s[58:59], 0, v[130:131]
	s_mov_b32 m0, s60
	v_lshl_add_u64 v[218:219], s[34:35], 0, v[128:129]
	global_load_lds_dwordx4 v[216:217], off
	v_lshl_add_u64 v[216:217], s[58:59], 0, v[128:129]
	s_add_i32 m0, s60, 0x2000
	s_nop 0
	global_load_lds_dwordx4 v[216:217], off
	v_lshl_add_u64 v[216:217], s[34:35], 0, v[130:131]
	s_mov_b32 m0, s21
	s_nop 0
	global_load_lds_dwordx4 v[216:217], off
	s_mov_b32 m0, s46
	s_nop 0
	global_load_lds_dwordx4 v[218:219], off
	s_waitcnt vmcnt(8)
	s_waitcnt lgkmcnt(0)
	s_barrier
; #define PG8_STAGE(bufoff, gbase, o0, o1) do { \
;         __builtin_amdgcn_global_load_lds((const unsigned*)((const char*)(gbase) + (o0)), (LAS unsigned*)(lds + (bufoff) + ldsw), 16, 0, 0); \
;         __builtin_amdgcn_global_load_lds((const unsigned*)((const char*)(gbase) + (o1)), (LAS unsigned*)(lds + (bufoff) + ldsw + 8192), 16, 0, 0); } while (0)
; #define PG8_LDA(dst, b, h) do { _Pragma("unroll") for (int m = 0; m < 4; ++m) _Pragma("unroll") for (int k = 0; k < 2; ++k) dst[m][k] = *(const LAS bf16x8*)(lds + PG8_SA(b, h) + aoff + m * 2048 + k * 1024); } while (0)
; #define PG8_LDB(dst, b, h) do { _Pragma("unroll") for (int n = 0; n < 2; ++n) _Pragma("unroll") for (int k = 0; k < 2; ++k) dst[n][k] = *(const LAS bf16x8*)(lds + PG8_SB(b, h) + boff + n * 2048 + k * 1024); } while (0)
; #define PG8_WAIT_V(n) asm volatile("s_waitcnt vmcnt(" #n ")" ::: "memory")
; #define PG8_WAIT_L(n) asm volatile("s_waitcnt lgkmcnt(" #n ")" ::: "memory")
; #define PG8_BAR __builtin_amdgcn_s_barrier()
; #define PG8_SCHED __builtin_amdgcn_sched_barrier(0)
; template <class Epi, class Sched, class Prob>
; __device__ __forceinline__ void gemm_phase(LAS unsigned char* lds, LAS unsigned char* lds_epi, const Prob g, const Sched& S, const Epi& E, int wid) {
;     ...
;             PG8_WAIT_V(8); PG8_WAIT_L(0); PG8_BAR; PG8_MMA(1, 0, At, B0); PG8_MMA(1, 1, At, B1); PG8_BAR; PG8_SCHED;
;             PG8_LDB(B0, 1, 0); PG8_LDB(B1, 1, 1); PG8_SCHED; PG8_LDA(At, 1, 0); PG8_STAGE(PG8_SA(0, 1), a2, cA10, cA11);
;             PG8_WAIT_V(8); PG8_WAIT_L(0); PG8_BAR; PG8_MMA(0, 0, At, B0); PG8_MMA(0, 1, At, B1); PG8_BAR; PG8_SCHED;
	s_waitcnt lgkmcnt(0)
	v_mfma_f32_16x16x32_bf16 v[52:55], v[148:151], v[180:183], v[52:55]
	v_mfma_f32_16x16x32_bf16 v[76:79], v[156:159], v[180:183], v[76:79]
	v_mfma_f32_16x16x32_bf16 v[48:51], v[148:151], v[188:191], v[48:51]
	v_mfma_f32_16x16x32_bf16 v[72:75], v[156:159], v[188:191], v[72:75]
	v_mfma_f32_16x16x32_bf16 v[100:103], v[148:151], v[196:199], v[100:103]
	v_mfma_f32_16x16x32_bf16 v[108:111], v[156:159], v[196:199], v[108:111]
	v_mfma_f32_16x16x32_bf16 v[96:99], v[148:151], v[204:207], v[96:99]
	v_mfma_f32_16x16x32_bf16 v[104:107], v[156:159], v[204:207], v[104:107]
	v_mfma_f32_16x16x32_bf16 v[52:55], v[152:155], v[184:187], v[52:55]
	v_mfma_f32_16x16x32_bf16 v[76:79], v[160:163], v[184:187], v[76:79]
	v_mfma_f32_16x16x32_bf16 v[48:51], v[152:155], v[192:195], v[48:51]
	v_mfma_f32_16x16x32_bf16 v[72:75], v[160:163], v[192:195], v[72:75]
	v_mfma_f32_16x16x32_bf16 v[100:103], v[152:155], v[200:203], v[100:103]
	v_mfma_f32_16x16x32_bf16 v[108:111], v[160:163], v[200:203], v[108:111]
	v_mfma_f32_16x16x32_bf16 v[96:99], v[152:155], v[208:211], v[96:99]
	v_mfma_f32_16x16x32_bf16 v[104:107], v[160:163], v[208:211], v[104:107]
	v_mfma_f32_16x16x32_bf16 v[84:87], v[164:167], v[180:183], v[84:87]
	v_mfma_f32_16x16x32_bf16 v[92:95], v[172:175], v[180:183], v[92:95]
	v_mfma_f32_16x16x32_bf16 v[80:83], v[164:167], v[188:191], v[80:83]
	v_mfma_f32_16x16x32_bf16 v[88:91], v[172:175], v[188:191], v[88:91]
	v_mfma_f32_16x16x32_bf16 v[116:119], v[164:167], v[196:199], v[116:119]
	v_mfma_f32_16x16x32_bf16 v[124:127], v[172:175], v[196:199], v[124:127]
	v_mfma_f32_16x16x32_bf16 v[112:115], v[164:167], v[204:207], v[112:115]
	v_mfma_f32_16x16x32_bf16 v[120:123], v[172:175], v[204:207], v[120:123]
	v_mfma_f32_16x16x32_bf16 v[84:87], v[168:171], v[184:187], v[84:87]
	v_mfma_f32_16x16x32_bf16 v[92:95], v[176:179], v[184:187], v[92:95]
	v_mfma_f32_16x16x32_bf16 v[80:83], v[168:171], v[192:195], v[80:83]
	v_mfma_f32_16x16x32_bf16 v[88:91], v[176:179], v[192:195], v[88:91]
	v_mfma_f32_16x16x32_bf16 v[116:119], v[168:171], v[200:203], v[116:119]
	v_mfma_f32_16x16x32_bf16 v[124:127], v[176:179], v[200:203], v[124:127]
	v_mfma_f32_16x16x32_bf16 v[112:115], v[168:171], v[208:211], v[112:115]
	v_mfma_f32_16x16x32_bf16 v[120:123], v[176:179], v[208:211], v[120:123]
	s_barrier
	s_add_i32 s58, 0, 0x18000
	s_add_i32 s59, 0, 0x1c000
	v_add_u32_e32 v160, s58, v145
	v_add_u32_e32 v176, s59, v145
	ds_read_b128 v[148:151], v160
	ds_read_b128 v[152:155], v160 offset:1024
	ds_read_b128 v[156:159], v160 offset:2048
	ds_read_b128 v[160:163], v160 offset:3072
	ds_read_b128 v[164:167], v176
	ds_read_b128 v[168:171], v176 offset:1024
	ds_read_b128 v[172:175], v176 offset:2048
	ds_read_b128 v[176:179], v176 offset:3072
	s_mov_b32 m0, s47
	v_lshl_add_u64 v[220:221], s[34:35], 0, v[132:133]
	ds_read_b128 v[180:183], v147 offset:32768
	ds_read_b128 v[184:187], v147 offset:33792
	ds_read_b128 v[188:191], v147 offset:34816
	ds_read_b128 v[192:195], v147 offset:35840
	ds_read_b128 v[196:199], v147 offset:36864
	ds_read_b128 v[200:203], v147 offset:37888
	ds_read_b128 v[204:207], v147 offset:38912
	ds_read_b128 v[208:211], v147 offset:39936
	global_load_lds_dwordx4 v[220:221], off
	v_lshl_add_u64 v[220:221], s[34:35], 0, v[134:135]
	s_mov_b32 m0, s48
	s_nop 0
	global_load_lds_dwordx4 v[220:221], off
	s_waitcnt vmcnt(8)
	s_waitcnt lgkmcnt(0)
	s_barrier
	s_waitcnt lgkmcnt(0)
	v_mfma_f32_16x16x32_bf16 v[12:15], v[148:151], v[180:183], v[12:15]
	v_mfma_f32_16x16x32_bf16 v[28:31], v[156:159], v[180:183], v[28:31]
	v_mfma_f32_16x16x32_bf16 v[8:11], v[148:151], v[188:191], v[8:11]
	v_mfma_f32_16x16x32_bf16 v[24:27], v[156:159], v[188:191], v[24:27]
	v_mfma_f32_16x16x32_bf16 v[4:7], v[148:151], v[196:199], v[4:7]
	v_mfma_f32_16x16x32_bf16 v[20:23], v[156:159], v[196:199], v[20:23]
	v_mfma_f32_16x16x32_bf16 v[0:3], v[148:151], v[204:207], v[0:3]
	v_mfma_f32_16x16x32_bf16 v[16:19], v[156:159], v[204:207], v[16:19]
	v_mfma_f32_16x16x32_bf16 v[12:15], v[152:155], v[184:187], v[12:15]
	v_mfma_f32_16x16x32_bf16 v[28:31], v[160:163], v[184:187], v[28:31]
	v_mfma_f32_16x16x32_bf16 v[8:11], v[152:155], v[192:195], v[8:11]
	v_mfma_f32_16x16x32_bf16 v[24:27], v[160:163], v[192:195], v[24:27]
	v_mfma_f32_16x16x32_bf16 v[4:7], v[152:155], v[200:203], v[4:7]
	v_mfma_f32_16x16x32_bf16 v[20:23], v[160:163], v[200:203], v[20:23]
	v_mfma_f32_16x16x32_bf16 v[0:3], v[152:155], v[208:211], v[0:3]
	v_mfma_f32_16x16x32_bf16 v[16:19], v[160:163], v[208:211], v[16:19]
	v_mfma_f32_16x16x32_bf16 v[44:47], v[164:167], v[180:183], v[44:47]
	v_mfma_f32_16x16x32_bf16 v[68:71], v[172:175], v[180:183], v[68:71]
	v_mfma_f32_16x16x32_bf16 v[40:43], v[164:167], v[188:191], v[40:43]
	v_mfma_f32_16x16x32_bf16 v[64:67], v[172:175], v[188:191], v[64:67]
	v_mfma_f32_16x16x32_bf16 v[36:39], v[164:167], v[196:199], v[36:39]
	v_mfma_f32_16x16x32_bf16 v[60:63], v[172:175], v[196:199], v[60:63]
	v_mfma_f32_16x16x32_bf16 v[32:35], v[164:167], v[204:207], v[32:35]
	v_mfma_f32_16x16x32_bf16 v[56:59], v[172:175], v[204:207], v[56:59]
	v_mfma_f32_16x16x32_bf16 v[44:47], v[168:171], v[184:187], v[44:47]
	v_mfma_f32_16x16x32_bf16 v[68:71], v[176:179], v[184:187], v[68:71]
	v_mfma_f32_16x16x32_bf16 v[40:43], v[168:171], v[192:195], v[40:43]
	v_mfma_f32_16x16x32_bf16 v[64:67], v[176:179], v[192:195], v[64:67]
	v_mfma_f32_16x16x32_bf16 v[36:39], v[168:171], v[200:203], v[36:39]
	v_mfma_f32_16x16x32_bf16 v[60:63], v[176:179], v[200:203], v[60:63]
	v_mfma_f32_16x16x32_bf16 v[32:35], v[168:171], v[208:211], v[32:35]
	v_mfma_f32_16x16x32_bf16 v[56:59], v[176:179], v[208:211], v[56:59]
	s_barrier
; #define PG8_STAGE(bufoff, gbase, o0, o1) do { \
;         __builtin_amdgcn_global_load_lds((const unsigned*)((const char*)(gbase) + (o0)), (LAS unsigned*)(lds + (bufoff) + ldsw), 16, 0, 0); \
;         __builtin_amdgcn_global_load_lds((const unsigned*)((const char*)(gbase) + (o1)), (LAS unsigned*)(lds + (bufoff) + ldsw + 8192), 16, 0, 0); } while (0)
; #define PG8_LDA(dst, b, h) do { _Pragma("unroll") for (int m = 0; m < 4; ++m) _Pragma("unroll") for (int k = 0; k < 2; ++k) dst[m][k] = *(const LAS bf16x8*)(lds + PG8_SA(b, h) + aoff + m * 2048 + k * 1024); } while (0)
; #define PG8_WAIT_V(n) asm volatile("s_waitcnt vmcnt(" #n ")" ::: "memory")
; #define PG8_WAIT_L(n) asm volatile("s_waitcnt lgkmcnt(" #n ")" ::: "memory")
; #define PG8_BAR __builtin_amdgcn_s_barrier()
; #define PG8_SCHED __builtin_amdgcn_sched_barrier(0)
; template <class Epi, class Sched, class Prob>
; __device__ __forceinline__ void gemm_phase(LAS unsigned char* lds, LAS unsigned char* lds_epi, const Prob g, const Sched& S, const Epi& E, int wid) {
;     ...
;             PG8_LDA(At, 1, 1); PG8_STAGE(PG8_SB(1, 0), b3, vB0, vB1); PG8_STAGE(PG8_SB(1, 1), b3 + hstepB, vB0, vB1); PG8_STAGE(PG8_SA(1, 0), a3, cA00, cA01);
;             PG8_WAIT_V(8); PG8_WAIT_L(0); PG8_BAR; PG8_MMA(1, 0, At, B0); PG8_MMA(1, 1, At, B1); PG8_BAR; PG8_SCHED;
;         }
;         if constexpr (Prob::FP8) asm volatile("s_nop 7\n\ts_nop 7\n\ts_nop 7" ::: "memory");
;         if (wr == 0) PG8_BAR;
	s_add_i32 s34, s58, s97
	v_lshl_add_u64 v[212:213], v[212:213], 0, s[8:9]
	s_mov_b32 m0, s34
	ds_read_b128 v[180:183], v147 offset:49152
	ds_read_b128 v[184:187], v147 offset:50176
	ds_read_b128 v[188:191], v147 offset:51200
	ds_read_b128 v[192:195], v147 offset:52224
	ds_read_b128 v[196:199], v147 offset:53248
	ds_read_b128 v[200:203], v147 offset:54272
	ds_read_b128 v[204:207], v147 offset:55296
	ds_read_b128 v[208:211], v147 offset:56320
	global_load_lds_dwordx4 v[212:213], off
	s_add_i32 m0, s34, 0x2000
	s_add_u32 s28, s28, 0x80080
	v_lshl_add_u64 v[212:213], v[214:215], 0, s[8:9]
	s_addc_u32 s29, s29, 0
	s_add_i32 s34, s59, s97
	global_load_lds_dwordx4 v[212:213], off
	v_lshl_add_u64 v[212:213], s[28:29], 0, v[130:131]
	s_mov_b32 m0, s34
	s_nop 0
	global_load_lds_dwordx4 v[212:213], off
	v_lshl_add_u64 v[212:213], s[28:29], 0, v[128:129]
	s_add_i32 m0, s34, 0x2000
	s_nop 0
	global_load_lds_dwordx4 v[212:213], off
	v_lshl_add_u64 v[212:213], v[216:217], 0, s[8:9]
	s_mov_b32 m0, s49
	s_nop 0
	global_load_lds_dwordx4 v[212:213], off
	v_lshl_add_u64 v[212:213], v[218:219], 0, s[8:9]
	s_mov_b32 m0, s50
	s_nop 0
	global_load_lds_dwordx4 v[212:213], off
	s_waitcnt vmcnt(8)
	s_waitcnt lgkmcnt(0)
	s_barrier
	s_waitcnt lgkmcnt(0)
	v_mfma_f32_16x16x32_bf16 v[52:55], v[148:151], v[180:183], v[52:55]
	v_mfma_f32_16x16x32_bf16 v[76:79], v[156:159], v[180:183], v[76:79]
	v_mfma_f32_16x16x32_bf16 v[48:51], v[148:151], v[188:191], v[48:51]
	v_mfma_f32_16x16x32_bf16 v[72:75], v[156:159], v[188:191], v[72:75]
	v_mfma_f32_16x16x32_bf16 v[100:103], v[148:151], v[196:199], v[100:103]
	v_mfma_f32_16x16x32_bf16 v[108:111], v[156:159], v[196:199], v[108:111]
	v_mfma_f32_16x16x32_bf16 v[96:99], v[148:151], v[204:207], v[96:99]
	v_mfma_f32_16x16x32_bf16 v[104:107], v[156:159], v[204:207], v[104:107]
	v_mfma_f32_16x16x32_bf16 v[52:55], v[152:155], v[184:187], v[52:55]
	v_mfma_f32_16x16x32_bf16 v[76:79], v[160:163], v[184:187], v[76:79]
	v_mfma_f32_16x16x32_bf16 v[48:51], v[152:155], v[192:195], v[48:51]
	v_mfma_f32_16x16x32_bf16 v[72:75], v[160:163], v[192:195], v[72:75]
	v_mfma_f32_16x16x32_bf16 v[100:103], v[152:155], v[200:203], v[100:103]
	v_mfma_f32_16x16x32_bf16 v[108:111], v[160:163], v[200:203], v[108:111]
	v_mfma_f32_16x16x32_bf16 v[96:99], v[152:155], v[208:211], v[96:99]
	v_mfma_f32_16x16x32_bf16 v[104:107], v[160:163], v[208:211], v[104:107]
	v_mfma_f32_16x16x32_bf16 v[84:87], v[164:167], v[180:183], v[84:87]
	v_mfma_f32_16x16x32_bf16 v[92:95], v[172:175], v[180:183], v[92:95]
	v_mfma_f32_16x16x32_bf16 v[80:83], v[164:167], v[188:191], v[80:83]
	v_mfma_f32_16x16x32_bf16 v[88:91], v[172:175], v[188:191], v[88:91]
	v_mfma_f32_16x16x32_bf16 v[116:119], v[164:167], v[196:199], v[116:119]
	v_mfma_f32_16x16x32_bf16 v[124:127], v[172:175], v[196:199], v[124:127]
	v_mfma_f32_16x16x32_bf16 v[112:115], v[164:167], v[204:207], v[112:115]
	v_mfma_f32_16x16x32_bf16 v[120:123], v[172:175], v[204:207], v[120:123]
	v_mfma_f32_16x16x32_bf16 v[84:87], v[168:171], v[184:187], v[84:87]
	v_mfma_f32_16x16x32_bf16 v[92:95], v[176:179], v[184:187], v[92:95]
	v_mfma_f32_16x16x32_bf16 v[80:83], v[168:171], v[192:195], v[80:83]
	v_mfma_f32_16x16x32_bf16 v[88:91], v[176:179], v[192:195], v[88:91]
	v_mfma_f32_16x16x32_bf16 v[116:119], v[168:171], v[200:203], v[116:119]
	v_mfma_f32_16x16x32_bf16 v[124:127], v[176:179], v[200:203], v[124:127]
	v_mfma_f32_16x16x32_bf16 v[112:115], v[168:171], v[208:211], v[112:115]
	v_mfma_f32_16x16x32_bf16 v[120:123], v[176:179], v[208:211], v[120:123]
	s_barrier
	s_add_i32 s57, s57, 2
	s_add_u32 s26, s26, 0x100
	s_addc_u32 s27, s27, 0
	s_add_u32 s55, s55, 0x100
	s_addc_u32 s56, s56, 0
	s_cmp_gt_u32 s57, 29
	s_cbranch_scc0 .LBB0_1749
	s_setprio 0
	v_readlane_b32 s26, v254, 27
	v_readlane_b32 s27, v254, 28
	s_and_b64 vcc, exec, s[26:27]
	s_cbranch_vccz .LBB0_1752
	s_barrier

; #define PG8_STAGE(bufoff, gbase, o0, o1) do { \
;         __builtin_amdgcn_global_load_lds((const unsigned*)((const char*)(gbase) + (o0)), (LAS unsigned*)(lds + (bufoff) + ldsw), 16, 0, 0); \
;         __builtin_amdgcn_global_load_lds((const unsigned*)((const char*)(gbase) + (o1)), (LAS unsigned*)(lds + (bufoff) + ldsw + 8192), 16, 0, 0); } while (0)
; #define PG8_LDA(dst, b, h) do { _Pragma("unroll") for (int m = 0; m < 4; ++m) _Pragma("unroll") for (int k = 0; k < 2; ++k) dst[m][k] = *(const LAS bf16x8*)(lds + PG8_SA(b, h) + aoff + m * 2048 + k * 1024); } while (0)
; #define PG8_LDB(dst, b, h) do { _Pragma("unroll") for (int n = 0; n < 2; ++n) _Pragma("unroll") for (int k = 0; k < 2; ++k) dst[n][k] = *(const LAS bf16x8*)(lds + PG8_SB(b, h) + boff + n * 2048 + k * 1024); } while (0)
; #define PG8_WAIT_V(n) asm volatile("s_waitcnt vmcnt(" #n ")" ::: "memory")
; #define PG8_WAIT_L(n) asm volatile("s_waitcnt lgkmcnt(" #n ")" ::: "memory")
; template <class Epi, class Sched, class Prob>
; __device__ __forceinline__ void gemm_phase(LAS unsigned char* lds, LAS unsigned char* lds_epi, const Prob g, const Sched& S, const Epi& E, int wid) {
;     ...
;     for (;;) {
;         const bool has_next = S.next(ui + 1, nxt);
;         const char* nA = has_next ? g.a_base(nxt) : cA; const char* nB = has_next ? g.b_base(nxt) : cB;
; _Pragma("clang loop unroll(disable)")
;         for (int t = 0; t < nt; t += 2) {
;             const bool last = (t == nt - 2);
;             const char* a1 = cA + (size_t)(t + 1) * kstep;
;             const char* a2 = last ? nA : cA + (size_t)(t + 2) * kstep; const char* b2 = last ? nB : cB + (size_t)(t + 2) * kstep;
;             const char* a3 = a2 + kstep; const char* b3 = b2 + kstep;
;             PG8_LDB(B0, 0, 0); PG8_LDB(B1, 0, 1); PG8_SCHED; PG8_LDA(At, 0, 0); PG8_STAGE(PG8_SA(1, 1), a1, cA10, cA11);
;             PG8_WAIT_V(8); PG8_WAIT_L(0); PG8_BAR; PG8_MMA(0, 0, At, B0); PG8_MMA(0, 1, At, B1); PG8_BAR; PG8_SCHED;
;             PG8_LDA(At, 0, 1); PG8_STAGE(PG8_SB(0, 0), b2, vB0, vB1); PG8_STAGE(PG8_SB(0, 1), b2 + hstepB, vB0, vB1); PG8_STAGE(PG8_SA(0, 0), a2, cA00, cA01);
;             PG8_WAIT_V(8); PG8_WAIT_L(0); PG8_BAR; PG8_MMA(1, 0, At, B0); PG8_MMA(1, 1, At, B1); PG8_BAR; PG8_SCHED;
;             PG8_LDB(B0, 1, 0); PG8_LDB(B1, 1, 1); PG8_SCHED; PG8_LDA(At, 1, 0); PG8_STAGE(PG8_SA(0, 1), a2, cA10, cA11);
.LBB0_2090:
	s_ashr_i32 s11, s10, 31
	s_lshl_b64 s[30:31], s[10:11], 19
	s_add_u32 s30, s51, s30
	s_addc_u32 s31, s52, s31
	s_and_b64 s[40:41], s[40:41], exec
	s_cselect_b32 s11, s31, s37
	s_cselect_b32 s29, s30, s36
	s_add_u32 s36, s36, 0x80
	v_mov_b32_e32 v32, 0
	s_addc_u32 s37, s37, 0
	v_lshl_add_u64 v[182:183], v[0:1], 0, s[22:23]
	s_mov_b32 s69, -2
	s_cmp_lt_u32 s91, 0x100
	s_cbranch_scc1 .Lyoung_7
	s_setprio 1
.Lyoung_7:
	ds_read_b128 v[24:27], v199
	ds_read_b128 v[28:31], v199 offset:1024
	ds_read_b128 v[16:19], v199 offset:2048
	ds_read_b128 v[20:23], v199 offset:3072
	ds_read_b128 v[8:11], v200
	ds_read_b128 v[12:15], v200 offset:1024
	ds_read_b128 v[0:3], v200 offset:2048
	ds_read_b128 v[4:7], v200 offset:3072
	s_add_u32 s40, s36, 0x80
	s_addc_u32 s41, s37, 0
	s_cmp_eq_u32 s69, 12
	s_cselect_b64 vcc, -1, 0
	s_cselect_b32 s41, s11, s41
	s_cselect_b32 s40, s29, s40
	v_cndmask_b32_e32 v185, v183, v181, vcc
	v_cndmask_b32_e32 v184, v182, v180, vcc
	v_lshl_add_u64 v[228:229], s[36:37], 0, v[176:177]
	s_add_i32 m0, s35, 0xc000
	ds_read_b128 v[186:189], v201
	ds_read_b128 v[190:193], v201 offset:1024
	ds_read_b128 v[204:207], v201 offset:2048
	ds_read_b128 v[208:211], v201 offset:3072
	ds_read_b128 v[212:215], v201 offset:4096
	ds_read_b128 v[216:219], v201 offset:5120
	ds_read_b128 v[220:223], v201 offset:6144
	ds_read_b128 v[224:227], v201 offset:7168
	global_load_lds_dwordx4 v[228:229], off
	v_lshl_add_u64 v[228:229], s[36:37], 0, v[174:175]
	s_add_i32 m0, s35, 0xe000
	s_nop 0
	global_load_lds_dwordx4 v[228:229], off
	s_waitcnt vmcnt(8)
	s_waitcnt lgkmcnt(0)
	s_barrier
	s_waitcnt lgkmcnt(0)
	v_mfma_f32_16x16x128_f8f6f4 v[156:159], v[24:31], v[186:193], 0
	v_mfma_f32_16x16x128_f8f6f4 v[152:155], v[16:23], v[186:193], 0
	v_mfma_f32_16x16x128_f8f6f4 v[140:143], v[24:31], v[204:211], 0
	v_mfma_f32_16x16x128_f8f6f4 v[136:139], v[16:23], v[204:211], 0
	v_mfma_f32_16x16x128_f8f6f4 v[124:127], v[24:31], v[212:219], 0
	v_mfma_f32_16x16x128_f8f6f4 v[120:123], v[16:23], v[212:219], 0
	v_mfma_f32_16x16x128_f8f6f4 v[108:111], v[24:31], v[220:227], 0
	v_mfma_f32_16x16x128_f8f6f4 v[104:107], v[16:23], v[220:227], 0
	v_mfma_f32_16x16x128_f8f6f4 v[148:151], v[8:15], v[186:193], 0
	v_mfma_f32_16x16x128_f8f6f4 v[144:147], v[0:7], v[186:193], 0
	v_mfma_f32_16x16x128_f8f6f4 v[132:135], v[8:15], v[204:211], 0
	v_mfma_f32_16x16x128_f8f6f4 v[128:131], v[0:7], v[204:211], 0
	v_mfma_f32_16x16x128_f8f6f4 v[116:119], v[8:15], v[212:219], 0
	v_mfma_f32_16x16x128_f8f6f4 v[112:115], v[0:7], v[212:219], 0
	v_mfma_f32_16x16x128_f8f6f4 v[100:103], v[8:15], v[220:227], 0
	v_mfma_f32_16x16x128_f8f6f4 v[96:99], v[0:7], v[220:227], 0
	s_barrier
	s_add_i32 s70, s63, s97
	v_lshl_add_u64 v[186:187], v[184:185], 0, v[160:161]
	s_mov_b32 m0, s70
	ds_read_b128 v[204:207], v201 offset:16384
	ds_read_b128 v[208:211], v201 offset:17408
	ds_read_b128 v[212:215], v201 offset:18432
	ds_read_b128 v[216:219], v201 offset:19456
	ds_read_b128 v[220:223], v201 offset:20480
	ds_read_b128 v[224:227], v201 offset:21504
	ds_read_b128 v[228:231], v201 offset:22528
	ds_read_b128 v[232:235], v201 offset:23552
	global_load_lds_dwordx4 v[186:187], off
	v_lshl_add_u64 v[188:189], v[184:185], 0, v[162:163]
	s_add_i32 m0, s70, 0x2000
	v_lshl_add_u64 v[190:191], v[184:185], 0, s[12:13]
	s_add_i32 s70, s64, s97
	global_load_lds_dwordx4 v[188:189], off
	v_lshl_add_u64 v[192:193], v[190:191], 0, v[160:161]
	s_mov_b32 m0, s70
	v_lshl_add_u64 v[190:191], v[190:191], 0, v[162:163]
	global_load_lds_dwordx4 v[192:193], off
	s_add_i32 m0, s70, 0x2000
	v_lshl_add_u64 v[192:193], s[40:41], 0, v[168:169]
	global_load_lds_dwordx4 v[190:191], off
	v_lshl_add_u64 v[190:191], s[40:41], 0, v[164:165]
	s_mov_b32 m0, s35
	s_nop 0
	global_load_lds_dwordx4 v[190:191], off
	s_mov_b32 m0, s58
	s_nop 0
	global_load_lds_dwordx4 v[192:193], off
	s_waitcnt vmcnt(8)
	s_waitcnt lgkmcnt(0)
	s_barrier
	s_waitcnt lgkmcnt(0)
	v_mfma_f32_16x16x128_f8f6f4 v[92:95], v[24:31], v[204:211], 0
	v_mfma_f32_16x16x128_f8f6f4 v[88:91], v[16:23], v[204:211], 0
	v_mfma_f32_16x16x128_f8f6f4 v[76:79], v[24:31], v[212:219], 0
	v_mfma_f32_16x16x128_f8f6f4 v[72:75], v[16:23], v[212:219], 0
	v_mfma_f32_16x16x128_f8f6f4 v[60:63], v[24:31], v[220:227], 0
	v_mfma_f32_16x16x128_f8f6f4 v[56:59], v[16:23], v[220:227], 0
	v_mfma_f32_16x16x128_f8f6f4 v[44:47], v[24:31], v[228:235], 0
	v_mfma_f32_16x16x128_f8f6f4 v[40:43], v[16:23], v[228:235], 0
	v_mfma_f32_16x16x128_f8f6f4 v[84:87], v[8:15], v[204:211], 0
	v_mfma_f32_16x16x128_f8f6f4 v[80:83], v[0:7], v[204:211], 0
	v_mfma_f32_16x16x128_f8f6f4 v[68:71], v[8:15], v[212:219], 0
	v_mfma_f32_16x16x128_f8f6f4 v[64:67], v[0:7], v[212:219], 0
	v_mfma_f32_16x16x128_f8f6f4 v[52:55], v[8:15], v[220:227], 0
	v_mfma_f32_16x16x128_f8f6f4 v[48:51], v[0:7], v[220:227], 0
	v_mfma_f32_16x16x128_f8f6f4 v[36:39], v[8:15], v[228:235], 0
	v_mfma_f32_16x16x128_f8f6f4 v[32:35], v[0:7], v[228:235], 0
	s_barrier
	s_add_i32 s70, 0, 0x18000
	s_add_i32 s71, 0, 0x1c000
	v_add_u32_e32 v12, s70, v195
	v_add_u32_e32 v28, s71, v195
	ds_read_b128 v[0:3], v12
	ds_read_b128 v[4:7], v12 offset:1024
	ds_read_b128 v[8:11], v12 offset:2048
	ds_read_b128 v[12:15], v12 offset:3072
	ds_read_b128 v[16:19], v28
	ds_read_b128 v[20:23], v28 offset:1024
	ds_read_b128 v[24:27], v28 offset:2048
	ds_read_b128 v[28:31], v28 offset:3072
	s_mov_b32 m0, s59
	v_lshl_add_u64 v[236:237], s[40:41], 0, v[166:167]
	ds_read_b128 v[204:207], v201 offset:32768
	ds_read_b128 v[208:211], v201 offset:33792
	ds_read_b128 v[212:215], v201 offset:34816
	ds_read_b128 v[216:219], v201 offset:35840
	ds_read_b128 v[220:223], v201 offset:36864
	ds_read_b128 v[224:227], v201 offset:37888
	ds_read_b128 v[228:231], v201 offset:38912
	ds_read_b128 v[232:235], v201 offset:39936
	global_load_lds_dwordx4 v[236:237], off
	v_lshl_add_u64 v[236:237], s[40:41], 0, v[170:171]
	s_mov_b32 m0, s60
	s_nop 0
	global_load_lds_dwordx4 v[236:237], off
	s_waitcnt vmcnt(8)
	s_waitcnt lgkmcnt(0)
	s_barrier
; #define PG8_STAGE(bufoff, gbase, o0, o1) do { \
;         __builtin_amdgcn_global_load_lds((const unsigned*)((const char*)(gbase) + (o0)), (LAS unsigned*)(lds + (bufoff) + ldsw), 16, 0, 0); \
;         __builtin_amdgcn_global_load_lds((const unsigned*)((const char*)(gbase) + (o1)), (LAS unsigned*)(lds + (bufoff) + ldsw + 8192), 16, 0, 0); } while (0)
; #define PG8_LDA(dst, b, h) do { _Pragma("unroll") for (int m = 0; m < 4; ++m) _Pragma("unroll") for (int k = 0; k < 2; ++k) dst[m][k] = *(const LAS bf16x8*)(lds + PG8_SA(b, h) + aoff + m * 2048 + k * 1024); } while (0)
; #define PG8_LDB(dst, b, h) do { _Pragma("unroll") for (int n = 0; n < 2; ++n) _Pragma("unroll") for (int k = 0; k < 2; ++k) dst[n][k] = *(const LAS bf16x8*)(lds + PG8_SB(b, h) + boff + n * 2048 + k * 1024); } while (0)
; #define PG8_WAIT_V(n) asm volatile("s_waitcnt vmcnt(" #n ")" ::: "memory")
; #define PG8_WAIT_L(n) asm volatile("s_waitcnt lgkmcnt(" #n ")" ::: "memory")
; #define PG8_BAR __builtin_amdgcn_s_barrier()
; #define PG8_SCHED __builtin_amdgcn_sched_barrier(0)
; template <class Epi, class Sched, class Prob>
; __device__ __forceinline__ void gemm_phase(LAS unsigned char* lds, LAS unsigned char* lds_epi, const Prob g, const Sched& S, const Epi& E, int wid) {
;     ...
;             PG8_LDB(B0, 0, 0); PG8_LDB(B1, 0, 1); PG8_SCHED; PG8_LDA(At, 0, 0); PG8_STAGE(PG8_SA(1, 1), a1, cA10, cA11);
;             PG8_WAIT_V(8); PG8_WAIT_L(0); PG8_BAR; PG8_MMA(0, 0, At, B0); PG8_MMA(0, 1, At, B1); PG8_BAR; PG8_SCHED;
;             PG8_LDA(At, 0, 1); PG8_STAGE(PG8_SB(0, 0), b2, vB0, vB1); PG8_STAGE(PG8_SB(0, 1), b2 + hstepB, vB0, vB1); PG8_STAGE(PG8_SA(0, 0), a2, cA00, cA01);
;             PG8_WAIT_V(8); PG8_WAIT_L(0); PG8_BAR; PG8_MMA(1, 0, At, B0); PG8_MMA(1, 1, At, B1); PG8_BAR; PG8_SCHED;
;             PG8_LDB(B0, 1, 0); PG8_LDB(B1, 1, 1); PG8_SCHED; PG8_LDA(At, 1, 0); PG8_STAGE(PG8_SA(0, 1), a2, cA10, cA11);
;             PG8_WAIT_V(8); PG8_WAIT_L(0); PG8_BAR; PG8_MMA(0, 0, At, B0); PG8_MMA(0, 1, At, B1); PG8_BAR; PG8_SCHED;
;             PG8_LDA(At, 1, 1); PG8_STAGE(PG8_SB(1, 0), b3, vB0, vB1); PG8_STAGE(PG8_SB(1, 1), b3 + hstepB, vB0, vB1); PG8_STAGE(PG8_SA(1, 0), a3, cA00, cA01);
;             PG8_WAIT_V(8); PG8_WAIT_L(0); PG8_BAR; PG8_MMA(1, 0, At, B0); PG8_MMA(1, 1, At, B1); PG8_BAR; PG8_SCHED;
	s_waitcnt lgkmcnt(0)
	v_mfma_f32_16x16x128_f8f6f4 v[156:159], v[0:7], v[204:211], v[156:159]
	v_mfma_f32_16x16x128_f8f6f4 v[152:155], v[8:15], v[204:211], v[152:155]
	v_mfma_f32_16x16x128_f8f6f4 v[140:143], v[0:7], v[212:219], v[140:143]
	v_mfma_f32_16x16x128_f8f6f4 v[136:139], v[8:15], v[212:219], v[136:139]
	v_mfma_f32_16x16x128_f8f6f4 v[124:127], v[0:7], v[220:227], v[124:127]
	v_mfma_f32_16x16x128_f8f6f4 v[120:123], v[8:15], v[220:227], v[120:123]
	v_mfma_f32_16x16x128_f8f6f4 v[108:111], v[0:7], v[228:235], v[108:111]
	v_mfma_f32_16x16x128_f8f6f4 v[104:107], v[8:15], v[228:235], v[104:107]
	v_mfma_f32_16x16x128_f8f6f4 v[148:151], v[16:23], v[204:211], v[148:151]
	v_mfma_f32_16x16x128_f8f6f4 v[144:147], v[24:31], v[204:211], v[144:147]
	v_mfma_f32_16x16x128_f8f6f4 v[132:135], v[16:23], v[212:219], v[132:135]
	v_mfma_f32_16x16x128_f8f6f4 v[128:131], v[24:31], v[212:219], v[128:131]
	v_mfma_f32_16x16x128_f8f6f4 v[116:119], v[16:23], v[220:227], v[116:119]
	v_mfma_f32_16x16x128_f8f6f4 v[112:115], v[24:31], v[220:227], v[112:115]
	v_mfma_f32_16x16x128_f8f6f4 v[100:103], v[16:23], v[228:235], v[100:103]
	v_mfma_f32_16x16x128_f8f6f4 v[96:99], v[24:31], v[228:235], v[96:99]
	s_barrier
	s_add_i32 s40, s70, s97
	v_lshl_add_u64 v[186:187], v[186:187], 0, s[18:19]
	s_mov_b32 m0, s40
	ds_read_b128 v[204:207], v201 offset:49152
	ds_read_b128 v[208:211], v201 offset:50176
	ds_read_b128 v[212:215], v201 offset:51200
	ds_read_b128 v[216:219], v201 offset:52224
	ds_read_b128 v[220:223], v201 offset:53248
	ds_read_b128 v[224:227], v201 offset:54272
	ds_read_b128 v[228:231], v201 offset:55296
	ds_read_b128 v[232:235], v201 offset:56320
	global_load_lds_dwordx4 v[186:187], off
	v_lshl_add_u64 v[186:187], v[188:189], 0, s[18:19]
	s_add_i32 m0, s40, 0x2000
	v_lshl_add_u64 v[184:185], v[184:185], 0, s[20:21]
	s_add_i32 s40, s71, s97
	global_load_lds_dwordx4 v[186:187], off
	v_lshl_add_u64 v[186:187], v[184:185], 0, v[160:161]
	s_mov_b32 m0, s40
	v_lshl_add_u64 v[184:185], v[184:185], 0, v[162:163]
	global_load_lds_dwordx4 v[186:187], off
	s_add_i32 m0, s40, 0x2000
	s_nop 0
	global_load_lds_dwordx4 v[184:185], off
	v_lshl_add_u64 v[184:185], v[190:191], 0, s[18:19]
	s_mov_b32 m0, s61
	s_nop 0
	global_load_lds_dwordx4 v[184:185], off
	v_lshl_add_u64 v[184:185], v[192:193], 0, s[18:19]
	s_mov_b32 m0, s62
	s_nop 0
	global_load_lds_dwordx4 v[184:185], off
	s_waitcnt vmcnt(8)
	s_waitcnt lgkmcnt(0)
	s_barrier
	s_waitcnt lgkmcnt(0)
	v_mfma_f32_16x16x128_f8f6f4 v[92:95], v[0:7], v[204:211], v[92:95]
	v_mfma_f32_16x16x128_f8f6f4 v[88:91], v[8:15], v[204:211], v[88:91]
	v_mfma_f32_16x16x128_f8f6f4 v[76:79], v[0:7], v[212:219], v[76:79]
	v_mfma_f32_16x16x128_f8f6f4 v[72:75], v[8:15], v[212:219], v[72:75]
	v_mfma_f32_16x16x128_f8f6f4 v[60:63], v[0:7], v[220:227], v[60:63]
	v_mfma_f32_16x16x128_f8f6f4 v[56:59], v[8:15], v[220:227], v[56:59]
	v_mfma_f32_16x16x128_f8f6f4 v[44:47], v[0:7], v[228:235], v[44:47]
	v_mfma_f32_16x16x128_f8f6f4 v[40:43], v[8:15], v[228:235], v[40:43]
	v_mfma_f32_16x16x128_f8f6f4 v[84:87], v[16:23], v[204:211], v[84:87]
	v_mfma_f32_16x16x128_f8f6f4 v[80:83], v[24:31], v[204:211], v[80:83]
	v_mfma_f32_16x16x128_f8f6f4 v[68:71], v[16:23], v[212:219], v[68:71]
	v_mfma_f32_16x16x128_f8f6f4 v[64:67], v[24:31], v[212:219], v[64:67]
	v_mfma_f32_16x16x128_f8f6f4 v[52:55], v[16:23], v[220:227], v[52:55]
	v_mfma_f32_16x16x128_f8f6f4 v[48:51], v[24:31], v[220:227], v[48:51]
	v_mfma_f32_16x16x128_f8f6f4 v[36:39], v[16:23], v[228:235], v[36:39]
	v_mfma_f32_16x16x128_f8f6f4 v[32:35], v[24:31], v[228:235], v[32:35]
	s_barrier
	s_add_i32 s69, s69, 2
	s_add_u32 s36, s36, 0x100
	s_addc_u32 s37, s37, 0
	s_cmp_gt_u32 s69, 13
	v_lshl_add_u64 v[182:183], v[182:183], 0, s[22:23]
.LBB0_2091:
	ds_read_b128 v[24:27], v199
	ds_read_b128 v[28:31], v199 offset:1024
	ds_read_b128 v[16:19], v199 offset:2048
	ds_read_b128 v[20:23], v199 offset:3072
	ds_read_b128 v[8:11], v200
	ds_read_b128 v[12:15], v200 offset:1024
	ds_read_b128 v[0:3], v200 offset:2048
	ds_read_b128 v[4:7], v200 offset:3072
	s_add_u32 s40, s36, 0x80
	s_addc_u32 s41, s37, 0
	s_cmp_eq_u32 s69, 12
	s_cselect_b64 vcc, -1, 0
	s_cselect_b32 s41, s11, s41
	s_cselect_b32 s40, s29, s40
	v_cndmask_b32_e32 v185, v183, v181, vcc
	v_cndmask_b32_e32 v184, v182, v180, vcc
	v_lshl_add_u64 v[228:229], s[36:37], 0, v[176:177]
	s_add_i32 m0, s35, 0xc000
	ds_read_b128 v[186:189], v201
	ds_read_b128 v[190:193], v201 offset:1024
	ds_read_b128 v[204:207], v201 offset:2048
	ds_read_b128 v[208:211], v201 offset:3072
	ds_read_b128 v[212:215], v201 offset:4096
	ds_read_b128 v[216:219], v201 offset:5120
	ds_read_b128 v[220:223], v201 offset:6144
	ds_read_b128 v[224:227], v201 offset:7168
	global_load_lds_dwordx4 v[228:229], off
	v_lshl_add_u64 v[228:229], s[36:37], 0, v[174:175]
	s_add_i32 m0, s35, 0xe000
	s_nop 0
	global_load_lds_dwordx4 v[228:229], off
	s_waitcnt vmcnt(8)
	s_waitcnt lgkmcnt(0)
	s_barrier
	s_waitcnt lgkmcnt(0)
	v_mfma_f32_16x16x128_f8f6f4 v[156:159], v[24:31], v[186:193], v[156:159]
	v_mfma_f32_16x16x128_f8f6f4 v[152:155], v[16:23], v[186:193], v[152:155]
	v_mfma_f32_16x16x128_f8f6f4 v[140:143], v[24:31], v[204:211], v[140:143]
	v_mfma_f32_16x16x128_f8f6f4 v[136:139], v[16:23], v[204:211], v[136:139]
	v_mfma_f32_16x16x128_f8f6f4 v[124:127], v[24:31], v[212:219], v[124:127]
	v_mfma_f32_16x16x128_f8f6f4 v[120:123], v[16:23], v[212:219], v[120:123]
	v_mfma_f32_16x16x128_f8f6f4 v[108:111], v[24:31], v[220:227], v[108:111]
	v_mfma_f32_16x16x128_f8f6f4 v[104:107], v[16:23], v[220:227], v[104:107]
	v_mfma_f32_16x16x128_f8f6f4 v[148:151], v[8:15], v[186:193], v[148:151]
	v_mfma_f32_16x16x128_f8f6f4 v[144:147], v[0:7], v[186:193], v[144:147]
	v_mfma_f32_16x16x128_f8f6f4 v[132:135], v[8:15], v[204:211], v[132:135]
	v_mfma_f32_16x16x128_f8f6f4 v[128:131], v[0:7], v[204:211], v[128:131]
	v_mfma_f32_16x16x128_f8f6f4 v[116:119], v[8:15], v[212:219], v[116:119]
	v_mfma_f32_16x16x128_f8f6f4 v[112:115], v[0:7], v[212:219], v[112:115]
	v_mfma_f32_16x16x128_f8f6f4 v[100:103], v[8:15], v[220:227], v[100:103]
	v_mfma_f32_16x16x128_f8f6f4 v[96:99], v[0:7], v[220:227], v[96:99]
	s_barrier
; #define PG8_STAGE(bufoff, gbase, o0, o1) do { \
;         __builtin_amdgcn_global_load_lds((const unsigned*)((const char*)(gbase) + (o0)), (LAS unsigned*)(lds + (bufoff) + ldsw), 16, 0, 0); \
;         __builtin_amdgcn_global_load_lds((const unsigned*)((const char*)(gbase) + (o1)), (LAS unsigned*)(lds + (bufoff) + ldsw + 8192), 16, 0, 0); } while (0)
; #define PG8_LDA(dst, b, h) do { _Pragma("unroll") for (int m = 0; m < 4; ++m) _Pragma("unroll") for (int k = 0; k < 2; ++k) dst[m][k] = *(const LAS bf16x8*)(lds + PG8_SA(b, h) + aoff + m * 2048 + k * 1024); } while (0)
; #define PG8_LDB(dst, b, h) do { _Pragma("unroll") for (int n = 0; n < 2; ++n) _Pragma("unroll") for (int k = 0; k < 2; ++k) dst[n][k] = *(const LAS bf16x8*)(lds + PG8_SB(b, h) + boff + n * 2048 + k * 1024); } while (0)
; #define PG8_WAIT_V(n) asm volatile("s_waitcnt vmcnt(" #n ")" ::: "memory")
; #define PG8_WAIT_L(n) asm volatile("s_waitcnt lgkmcnt(" #n ")" ::: "memory")
; #define PG8_BAR __builtin_amdgcn_s_barrier()
; #define PG8_SCHED __builtin_amdgcn_sched_barrier(0)
; template <class Epi, class Sched, class Prob>
; __device__ __forceinline__ void gemm_phase(LAS unsigned char* lds, LAS unsigned char* lds_epi, const Prob g, const Sched& S, const Epi& E, int wid) {
;     ...
;             PG8_LDA(At, 0, 1); PG8_STAGE(PG8_SB(0, 0), b2, vB0, vB1); PG8_STAGE(PG8_SB(0, 1), b2 + hstepB, vB0, vB1); PG8_STAGE(PG8_SA(0, 0), a2, cA00, cA01);
;             PG8_WAIT_V(8); PG8_WAIT_L(0); PG8_BAR; PG8_MMA(1, 0, At, B0); PG8_MMA(1, 1, At, B1); PG8_BAR; PG8_SCHED;
;             PG8_LDB(B0, 1, 0); PG8_LDB(B1, 1, 1); PG8_SCHED; PG8_LDA(At, 1, 0); PG8_STAGE(PG8_SA(0, 1), a2, cA10, cA11);
	s_add_i32 s70, s63, s97
	v_lshl_add_u64 v[186:187], v[184:185], 0, v[160:161]
	s_mov_b32 m0, s70
	ds_read_b128 v[204:207], v201 offset:16384
	ds_read_b128 v[208:211], v201 offset:17408
	ds_read_b128 v[212:215], v201 offset:18432
	ds_read_b128 v[216:219], v201 offset:19456
	ds_read_b128 v[220:223], v201 offset:20480
	ds_read_b128 v[224:227], v201 offset:21504
	ds_read_b128 v[228:231], v201 offset:22528
	ds_read_b128 v[232:235], v201 offset:23552
	global_load_lds_dwordx4 v[186:187], off
	v_lshl_add_u64 v[188:189], v[184:185], 0, v[162:163]
	s_add_i32 m0, s70, 0x2000
	v_lshl_add_u64 v[190:191], v[184:185], 0, s[12:13]
	s_add_i32 s70, s64, s97
	global_load_lds_dwordx4 v[188:189], off
	v_lshl_add_u64 v[192:193], v[190:191], 0, v[160:161]
	s_mov_b32 m0, s70
	v_lshl_add_u64 v[190:191], v[190:191], 0, v[162:163]
	global_load_lds_dwordx4 v[192:193], off
	s_add_i32 m0, s70, 0x2000
	v_lshl_add_u64 v[192:193], s[40:41], 0, v[168:169]
	global_load_lds_dwordx4 v[190:191], off
	v_lshl_add_u64 v[190:191], s[40:41], 0, v[164:165]
	s_mov_b32 m0, s35
	s_nop 0
	global_load_lds_dwordx4 v[190:191], off
	s_mov_b32 m0, s58
	s_nop 0
	global_load_lds_dwordx4 v[192:193], off
	s_waitcnt vmcnt(8)
	s_waitcnt lgkmcnt(0)
	s_barrier
	s_waitcnt lgkmcnt(0)
	v_mfma_f32_16x16x128_f8f6f4 v[92:95], v[24:31], v[204:211], v[92:95]
	v_mfma_f32_16x16x128_f8f6f4 v[88:91], v[16:23], v[204:211], v[88:91]
	v_mfma_f32_16x16x128_f8f6f4 v[76:79], v[24:31], v[212:219], v[76:79]
	v_mfma_f32_16x16x128_f8f6f4 v[72:75], v[16:23], v[212:219], v[72:75]
	v_mfma_f32_16x16x128_f8f6f4 v[60:63], v[24:31], v[220:227], v[60:63]
	v_mfma_f32_16x16x128_f8f6f4 v[56:59], v[16:23], v[220:227], v[56:59]
	v_mfma_f32_16x16x128_f8f6f4 v[44:47], v[24:31], v[228:235], v[44:47]
	v_mfma_f32_16x16x128_f8f6f4 v[40:43], v[16:23], v[228:235], v[40:43]
	v_mfma_f32_16x16x128_f8f6f4 v[84:87], v[8:15], v[204:211], v[84:87]
	v_mfma_f32_16x16x128_f8f6f4 v[80:83], v[0:7], v[204:211], v[80:83]
	v_mfma_f32_16x16x128_f8f6f4 v[68:71], v[8:15], v[212:219], v[68:71]
	v_mfma_f32_16x16x128_f8f6f4 v[64:67], v[0:7], v[212:219], v[64:67]
	v_mfma_f32_16x16x128_f8f6f4 v[52:55], v[8:15], v[220:227], v[52:55]
	v_mfma_f32_16x16x128_f8f6f4 v[48:51], v[0:7], v[220:227], v[48:51]
	v_mfma_f32_16x16x128_f8f6f4 v[36:39], v[8:15], v[228:235], v[36:39]
	v_mfma_f32_16x16x128_f8f6f4 v[32:35], v[0:7], v[228:235], v[32:35]
	s_barrier
	s_add_i32 s70, 0, 0x18000
	s_add_i32 s71, 0, 0x1c000
	v_add_u32_e32 v12, s70, v195
	v_add_u32_e32 v28, s71, v195
	ds_read_b128 v[0:3], v12
	ds_read_b128 v[4:7], v12 offset:1024
	ds_read_b128 v[8:11], v12 offset:2048
	ds_read_b128 v[12:15], v12 offset:3072
	ds_read_b128 v[16:19], v28
	ds_read_b128 v[20:23], v28 offset:1024
	ds_read_b128 v[24:27], v28 offset:2048
	ds_read_b128 v[28:31], v28 offset:3072
	s_mov_b32 m0, s59
	v_lshl_add_u64 v[236:237], s[40:41], 0, v[166:167]
	ds_read_b128 v[204:207], v201 offset:32768
	ds_read_b128 v[208:211], v201 offset:33792
	ds_read_b128 v[212:215], v201 offset:34816
	ds_read_b128 v[216:219], v201 offset:35840
	ds_read_b128 v[220:223], v201 offset:36864
	ds_read_b128 v[224:227], v201 offset:37888
	ds_read_b128 v[228:231], v201 offset:38912
	ds_read_b128 v[232:235], v201 offset:39936
	global_load_lds_dwordx4 v[236:237], off
	v_lshl_add_u64 v[236:237], s[40:41], 0, v[170:171]
	s_mov_b32 m0, s60
	s_nop 0
	global_load_lds_dwordx4 v[236:237], off
	s_waitcnt vmcnt(8)
	s_waitcnt lgkmcnt(0)
	s_barrier
; #define PG8_STAGE(bufoff, gbase, o0, o1) do { \
;         __builtin_amdgcn_global_load_lds((const unsigned*)((const char*)(gbase) + (o0)), (LAS unsigned*)(lds + (bufoff) + ldsw), 16, 0, 0); \
;         __builtin_amdgcn_global_load_lds((const unsigned*)((const char*)(gbase) + (o1)), (LAS unsigned*)(lds + (bufoff) + ldsw + 8192), 16, 0, 0); } while (0)
; #define PG8_LDA(dst, b, h) do { _Pragma("unroll") for (int m = 0; m < 4; ++m) _Pragma("unroll") for (int k = 0; k < 2; ++k) dst[m][k] = *(const LAS bf16x8*)(lds + PG8_SA(b, h) + aoff + m * 2048 + k * 1024); } while (0)
; #define PG8_WAIT_V(n) asm volatile("s_waitcnt vmcnt(" #n ")" ::: "memory")
; #define PG8_WAIT_L(n) asm volatile("s_waitcnt lgkmcnt(" #n ")" ::: "memory")
; #define PG8_BAR __builtin_amdgcn_s_barrier()
; #define PG8_SCHED __builtin_amdgcn_sched_barrier(0)
; template <class Epi, class Sched, class Prob>
; __device__ __forceinline__ void gemm_phase(LAS unsigned char* lds, LAS unsigned char* lds_epi, const Prob g, const Sched& S, const Epi& E, int wid) {
;     ...
;             PG8_WAIT_V(8); PG8_WAIT_L(0); PG8_BAR; PG8_MMA(0, 0, At, B0); PG8_MMA(0, 1, At, B1); PG8_BAR; PG8_SCHED;
;             PG8_LDA(At, 1, 1); PG8_STAGE(PG8_SB(1, 0), b3, vB0, vB1); PG8_STAGE(PG8_SB(1, 1), b3 + hstepB, vB0, vB1); PG8_STAGE(PG8_SA(1, 0), a3, cA00, cA01);
;             PG8_WAIT_V(8); PG8_WAIT_L(0); PG8_BAR; PG8_MMA(1, 0, At, B0); PG8_MMA(1, 1, At, B1); PG8_BAR; PG8_SCHED;
;         }
;         if constexpr (Prob::FP8) asm volatile("s_nop 7\n\ts_nop 7\n\ts_nop 7" ::: "memory");
;         if (wr == 0) PG8_BAR;
	s_waitcnt lgkmcnt(0)
	v_mfma_f32_16x16x128_f8f6f4 v[156:159], v[0:7], v[204:211], v[156:159]
	v_mfma_f32_16x16x128_f8f6f4 v[152:155], v[8:15], v[204:211], v[152:155]
	v_mfma_f32_16x16x128_f8f6f4 v[140:143], v[0:7], v[212:219], v[140:143]
	v_mfma_f32_16x16x128_f8f6f4 v[136:139], v[8:15], v[212:219], v[136:139]
	v_mfma_f32_16x16x128_f8f6f4 v[124:127], v[0:7], v[220:227], v[124:127]
	v_mfma_f32_16x16x128_f8f6f4 v[120:123], v[8:15], v[220:227], v[120:123]
	v_mfma_f32_16x16x128_f8f6f4 v[108:111], v[0:7], v[228:235], v[108:111]
	v_mfma_f32_16x16x128_f8f6f4 v[104:107], v[8:15], v[228:235], v[104:107]
	v_mfma_f32_16x16x128_f8f6f4 v[148:151], v[16:23], v[204:211], v[148:151]
	v_mfma_f32_16x16x128_f8f6f4 v[144:147], v[24:31], v[204:211], v[144:147]
	v_mfma_f32_16x16x128_f8f6f4 v[132:135], v[16:23], v[212:219], v[132:135]
	v_mfma_f32_16x16x128_f8f6f4 v[128:131], v[24:31], v[212:219], v[128:131]
	v_mfma_f32_16x16x128_f8f6f4 v[116:119], v[16:23], v[220:227], v[116:119]
	v_mfma_f32_16x16x128_f8f6f4 v[112:115], v[24:31], v[220:227], v[112:115]
	v_mfma_f32_16x16x128_f8f6f4 v[100:103], v[16:23], v[228:235], v[100:103]
	v_mfma_f32_16x16x128_f8f6f4 v[96:99], v[24:31], v[228:235], v[96:99]
	s_barrier
	s_add_i32 s40, s70, s97
	v_lshl_add_u64 v[186:187], v[186:187], 0, s[18:19]
	s_mov_b32 m0, s40
	ds_read_b128 v[204:207], v201 offset:49152
	ds_read_b128 v[208:211], v201 offset:50176
	ds_read_b128 v[212:215], v201 offset:51200
	ds_read_b128 v[216:219], v201 offset:52224
	ds_read_b128 v[220:223], v201 offset:53248
	ds_read_b128 v[224:227], v201 offset:54272
	ds_read_b128 v[228:231], v201 offset:55296
	ds_read_b128 v[232:235], v201 offset:56320
	global_load_lds_dwordx4 v[186:187], off
	v_lshl_add_u64 v[186:187], v[188:189], 0, s[18:19]
	s_add_i32 m0, s40, 0x2000
	v_lshl_add_u64 v[184:185], v[184:185], 0, s[20:21]
	s_add_i32 s40, s71, s97
	global_load_lds_dwordx4 v[186:187], off
	v_lshl_add_u64 v[186:187], v[184:185], 0, v[160:161]
	s_mov_b32 m0, s40
	v_lshl_add_u64 v[184:185], v[184:185], 0, v[162:163]
	global_load_lds_dwordx4 v[186:187], off
	s_add_i32 m0, s40, 0x2000
	s_nop 0
	global_load_lds_dwordx4 v[184:185], off
	v_lshl_add_u64 v[184:185], v[190:191], 0, s[18:19]
	s_mov_b32 m0, s61
	s_nop 0
	global_load_lds_dwordx4 v[184:185], off
	v_lshl_add_u64 v[184:185], v[192:193], 0, s[18:19]
	s_mov_b32 m0, s62
	s_nop 0
	global_load_lds_dwordx4 v[184:185], off
	s_waitcnt vmcnt(8)
	s_waitcnt lgkmcnt(0)
	s_barrier
	s_waitcnt lgkmcnt(0)
	v_mfma_f32_16x16x128_f8f6f4 v[92:95], v[0:7], v[204:211], v[92:95]
	v_mfma_f32_16x16x128_f8f6f4 v[88:91], v[8:15], v[204:211], v[88:91]
	v_mfma_f32_16x16x128_f8f6f4 v[76:79], v[0:7], v[212:219], v[76:79]
	v_mfma_f32_16x16x128_f8f6f4 v[72:75], v[8:15], v[212:219], v[72:75]
	v_mfma_f32_16x16x128_f8f6f4 v[60:63], v[0:7], v[220:227], v[60:63]
	v_mfma_f32_16x16x128_f8f6f4 v[56:59], v[8:15], v[220:227], v[56:59]
	v_mfma_f32_16x16x128_f8f6f4 v[44:47], v[0:7], v[228:235], v[44:47]
	v_mfma_f32_16x16x128_f8f6f4 v[40:43], v[8:15], v[228:235], v[40:43]
	v_mfma_f32_16x16x128_f8f6f4 v[84:87], v[16:23], v[204:211], v[84:87]
	v_mfma_f32_16x16x128_f8f6f4 v[80:83], v[24:31], v[204:211], v[80:83]
	v_mfma_f32_16x16x128_f8f6f4 v[68:71], v[16:23], v[212:219], v[68:71]
	v_mfma_f32_16x16x128_f8f6f4 v[64:67], v[24:31], v[212:219], v[64:67]
	v_mfma_f32_16x16x128_f8f6f4 v[52:55], v[16:23], v[220:227], v[52:55]
	v_mfma_f32_16x16x128_f8f6f4 v[48:51], v[24:31], v[220:227], v[48:51]
	v_mfma_f32_16x16x128_f8f6f4 v[36:39], v[16:23], v[228:235], v[36:39]
	v_mfma_f32_16x16x128_f8f6f4 v[32:35], v[24:31], v[228:235], v[32:35]
	s_barrier
	s_add_i32 s69, s69, 2
	s_add_u32 s36, s36, 0x100
	s_addc_u32 s37, s37, 0
	s_cmp_gt_u32 s69, 13
	v_lshl_add_u64 v[182:183], v[182:183], 0, s[22:23]
	s_cbranch_scc0 .LBB0_2091
	s_setprio 0
	v_readlane_b32 s36, v254, 27
	v_readlane_b32 s37, v254, 28
	s_and_b64 vcc, exec, s[36:37]
	s_cbranch_vccz .LBB0_2094
	s_barrier

; #define PG8_STAGE(bufoff, gbase, o0, o1) do { \
;         __builtin_amdgcn_global_load_lds((const unsigned*)((const char*)(gbase) + (o0)), (LAS unsigned*)(lds + (bufoff) + ldsw), 16, 0, 0); \
;         __builtin_amdgcn_global_load_lds((const unsigned*)((const char*)(gbase) + (o1)), (LAS unsigned*)(lds + (bufoff) + ldsw + 8192), 16, 0, 0); } while (0)
; #define PG8_LDA(dst, b, h) do { _Pragma("unroll") for (int m = 0; m < 4; ++m) _Pragma("unroll") for (int k = 0; k < 2; ++k) dst[m][k] = *(const LAS bf16x8*)(lds + PG8_SA(b, h) + aoff + m * 2048 + k * 1024); } while (0)
; #define PG8_LDB(dst, b, h) do { _Pragma("unroll") for (int n = 0; n < 2; ++n) _Pragma("unroll") for (int k = 0; k < 2; ++k) dst[n][k] = *(const LAS bf16x8*)(lds + PG8_SB(b, h) + boff + n * 2048 + k * 1024); } while (0)
; #define PG8_WAIT_V(n) asm volatile("s_waitcnt vmcnt(" #n ")" ::: "memory")
; #define PG8_WAIT_L(n) asm volatile("s_waitcnt lgkmcnt(" #n ")" ::: "memory")
; template <class Epi, class Sched, class Prob>
; __device__ __forceinline__ void gemm_phase(LAS unsigned char* lds, LAS unsigned char* lds_epi, const Prob g, const Sched& S, const Epi& E, int wid) {
;     ...
;     for (;;) {
;         const bool has_next = S.next(ui + 1, nxt);
;         const char* nA = has_next ? g.a_base(nxt) : cA; const char* nB = has_next ? g.b_base(nxt) : cB;
; _Pragma("clang loop unroll(disable)")
;         for (int t = 0; t < nt; t += 2) {
;             const bool last = (t == nt - 2);
;             const char* a1 = cA + (size_t)(t + 1) * kstep;
;             const char* a2 = last ? nA : cA + (size_t)(t + 2) * kstep; const char* b2 = last ? nB : cB + (size_t)(t + 2) * kstep;
;             const char* a3 = a2 + kstep; const char* b3 = b2 + kstep;
;             PG8_LDB(B0, 0, 0); PG8_LDB(B1, 0, 1); PG8_SCHED; PG8_LDA(At, 0, 0); PG8_STAGE(PG8_SA(1, 1), a1, cA10, cA11);
;             PG8_WAIT_V(8); PG8_WAIT_L(0); PG8_BAR; PG8_MMA(0, 0, At, B0); PG8_MMA(0, 1, At, B1); PG8_BAR; PG8_SCHED;
;             PG8_LDA(At, 0, 1); PG8_STAGE(PG8_SB(0, 0), b2, vB0, vB1); PG8_STAGE(PG8_SB(0, 1), b2 + hstepB, vB0, vB1); PG8_STAGE(PG8_SA(0, 0), a2, cA00, cA01);
;             PG8_WAIT_V(8); PG8_WAIT_L(0); PG8_BAR; PG8_MMA(1, 0, At, B0); PG8_MMA(1, 1, At, B1); PG8_BAR; PG8_SCHED;
;             PG8_LDB(B0, 1, 0); PG8_LDB(B1, 1, 1); PG8_SCHED; PG8_LDA(At, 1, 0); PG8_STAGE(PG8_SA(0, 1), a2, cA10, cA11);
.LBB0_2172:
	s_add_u32 s36, s36, 0x80
	v_mov_b32_e32 v32, 0
	s_addc_u32 s37, s37, 0
	v_lshl_add_u64 v[186:187], v[0:1], 0, s[22:23]
	s_mov_b32 s64, -2
	s_cmp_lt_u32 s91, 0x100
	s_cbranch_scc1 .Lyoung_8
	s_setprio 1
.Lyoung_8:
	ds_read_b128 v[24:27], v161
	ds_read_b128 v[28:31], v161 offset:1024
	ds_read_b128 v[16:19], v161 offset:2048
	ds_read_b128 v[20:23], v161 offset:3072
	ds_read_b128 v[8:11], v207
	ds_read_b128 v[12:15], v207 offset:1024
	ds_read_b128 v[0:3], v207 offset:2048
	ds_read_b128 v[4:7], v207 offset:3072
	s_add_u32 s40, s36, 0x80
	s_addc_u32 s41, s37, 0
	s_cmp_eq_u32 s64, 52
	s_cselect_b64 vcc, -1, 0
	s_cselect_b32 s41, s31, s41
	s_cselect_b32 s40, s30, s40
	v_cndmask_b32_e32 v189, v187, v185, vcc
	v_cndmask_b32_e32 v188, v186, v184, vcc
	v_lshl_add_u64 v[212:213], s[36:37], 0, v[182:183]
	s_add_i32 m0, s33, 0xc000
	ds_read_b128 v[190:193], v208
	ds_read_b128 v[194:197], v208 offset:1024
	ds_read_b128 v[216:219], v208 offset:2048
	ds_read_b128 v[220:223], v208 offset:3072
	ds_read_b128 v[224:227], v208 offset:4096
	ds_read_b128 v[228:231], v208 offset:5120
	ds_read_b128 v[238:241], v208 offset:6144
	ds_read_b128 v[242:245], v208 offset:7168
	global_load_lds_dwordx4 v[212:213], off
	v_lshl_add_u64 v[212:213], s[36:37], 0, v[180:181]
	s_add_i32 m0, s33, 0xe000
	s_nop 0
	global_load_lds_dwordx4 v[212:213], off
	s_waitcnt vmcnt(8)
	s_waitcnt lgkmcnt(0)
	s_barrier
	s_waitcnt lgkmcnt(0)
	v_mfma_f32_16x16x128_f8f6f4 v[156:159], v[24:31], v[190:197], 0
	v_mfma_f32_16x16x128_f8f6f4 v[152:155], v[16:23], v[190:197], 0
	v_mfma_f32_16x16x128_f8f6f4 v[140:143], v[24:31], v[216:223], 0
	v_mfma_f32_16x16x128_f8f6f4 v[136:139], v[16:23], v[216:223], 0
	v_mfma_f32_16x16x128_f8f6f4 v[124:127], v[24:31], v[224:231], 0
	v_mfma_f32_16x16x128_f8f6f4 v[120:123], v[16:23], v[224:231], 0
	v_mfma_f32_16x16x128_f8f6f4 v[108:111], v[24:31], v[238:245], 0
	v_mfma_f32_16x16x128_f8f6f4 v[104:107], v[16:23], v[238:245], 0
	v_mfma_f32_16x16x128_f8f6f4 v[148:151], v[8:15], v[190:197], 0
	v_mfma_f32_16x16x128_f8f6f4 v[144:147], v[0:7], v[190:197], 0
	v_mfma_f32_16x16x128_f8f6f4 v[132:135], v[8:15], v[216:223], 0
	v_mfma_f32_16x16x128_f8f6f4 v[128:131], v[0:7], v[216:223], 0
	v_mfma_f32_16x16x128_f8f6f4 v[116:119], v[8:15], v[224:231], 0
	v_mfma_f32_16x16x128_f8f6f4 v[112:115], v[0:7], v[224:231], 0
	v_mfma_f32_16x16x128_f8f6f4 v[100:103], v[8:15], v[238:245], 0
	v_mfma_f32_16x16x128_f8f6f4 v[96:99], v[0:7], v[238:245], 0
	s_barrier
	s_add_i32 s65, s58, s97
	v_lshl_add_u64 v[190:191], v[188:189], 0, v[162:163]
	s_mov_b32 m0, s65
	ds_read_b128 v[216:219], v208 offset:16384
	ds_read_b128 v[220:223], v208 offset:17408
	ds_read_b128 v[224:227], v208 offset:18432
	ds_read_b128 v[228:231], v208 offset:19456
	ds_read_b128 v[238:241], v208 offset:20480
	ds_read_b128 v[242:245], v208 offset:21504
	ds_read_b128 v[246:249], v208 offset:22528
	ds_read_b128 v[250:253], v208 offset:23552
	global_load_lds_dwordx4 v[190:191], off
	v_lshl_add_u64 v[192:193], v[188:189], 0, v[164:165]
	s_add_i32 m0, s65, 0x2000
	v_lshl_add_u64 v[194:195], v[188:189], 0, s[16:17]
	s_add_i32 s65, s59, s97
	global_load_lds_dwordx4 v[192:193], off
	v_lshl_add_u64 v[196:197], v[194:195], 0, v[162:163]
	s_mov_b32 m0, s65
	v_lshl_add_u64 v[194:195], v[194:195], 0, v[164:165]
	global_load_lds_dwordx4 v[196:197], off
	s_add_i32 m0, s65, 0x2000
	v_lshl_add_u64 v[196:197], s[40:41], 0, v[174:175]
	global_load_lds_dwordx4 v[194:195], off
	v_lshl_add_u64 v[194:195], s[40:41], 0, v[170:171]
	s_mov_b32 m0, s33
	s_nop 0
	global_load_lds_dwordx4 v[194:195], off
	s_mov_b32 m0, s35
	s_nop 0
	global_load_lds_dwordx4 v[196:197], off
	s_waitcnt vmcnt(8)
	s_waitcnt lgkmcnt(0)
	s_barrier
	s_waitcnt lgkmcnt(0)
	v_mfma_f32_16x16x128_f8f6f4 v[92:95], v[24:31], v[216:223], 0
	v_mfma_f32_16x16x128_f8f6f4 v[88:91], v[16:23], v[216:223], 0
	v_mfma_f32_16x16x128_f8f6f4 v[76:79], v[24:31], v[224:231], 0
	v_mfma_f32_16x16x128_f8f6f4 v[72:75], v[16:23], v[224:231], 0
	v_mfma_f32_16x16x128_f8f6f4 v[60:63], v[24:31], v[238:245], 0
	v_mfma_f32_16x16x128_f8f6f4 v[56:59], v[16:23], v[238:245], 0
	v_mfma_f32_16x16x128_f8f6f4 v[44:47], v[24:31], v[246:253], 0
	v_mfma_f32_16x16x128_f8f6f4 v[40:43], v[16:23], v[246:253], 0
	v_mfma_f32_16x16x128_f8f6f4 v[84:87], v[8:15], v[216:223], 0
	v_mfma_f32_16x16x128_f8f6f4 v[80:83], v[0:7], v[216:223], 0
	v_mfma_f32_16x16x128_f8f6f4 v[68:71], v[8:15], v[224:231], 0
	v_mfma_f32_16x16x128_f8f6f4 v[64:67], v[0:7], v[224:231], 0
	v_mfma_f32_16x16x128_f8f6f4 v[52:55], v[8:15], v[238:245], 0
	v_mfma_f32_16x16x128_f8f6f4 v[48:51], v[0:7], v[238:245], 0
	v_mfma_f32_16x16x128_f8f6f4 v[36:39], v[8:15], v[246:253], 0
	v_mfma_f32_16x16x128_f8f6f4 v[32:35], v[0:7], v[246:253], 0
	s_barrier
	s_add_i32 s65, 0, 0x18000
	s_add_i32 s66, 0, 0x1c000
	v_add_u32_e32 v12, s65, v204
	v_add_u32_e32 v28, s66, v204
	ds_read_b128 v[0:3], v12
	ds_read_b128 v[4:7], v12 offset:1024
	ds_read_b128 v[8:11], v12 offset:2048
	ds_read_b128 v[12:15], v12 offset:3072
	ds_read_b128 v[16:19], v28
	ds_read_b128 v[20:23], v28 offset:1024
	ds_read_b128 v[24:27], v28 offset:2048
	ds_read_b128 v[28:31], v28 offset:3072
	s_mov_b32 m0, s48
	v_lshl_add_u64 v[212:213], s[40:41], 0, v[172:173]
	ds_read_b128 v[216:219], v208 offset:32768
	ds_read_b128 v[220:223], v208 offset:33792
	ds_read_b128 v[224:227], v208 offset:34816
	ds_read_b128 v[228:231], v208 offset:35840
	ds_read_b128 v[238:241], v208 offset:36864
	ds_read_b128 v[242:245], v208 offset:37888
	ds_read_b128 v[246:249], v208 offset:38912
	ds_read_b128 v[250:253], v208 offset:39936
	global_load_lds_dwordx4 v[212:213], off
	v_lshl_add_u64 v[212:213], s[40:41], 0, v[176:177]
	s_mov_b32 m0, s52
	s_nop 0
	global_load_lds_dwordx4 v[212:213], off
	s_waitcnt vmcnt(8)
	s_waitcnt lgkmcnt(0)
	s_barrier
; #define PG8_STAGE(bufoff, gbase, o0, o1) do { \
;         __builtin_amdgcn_global_load_lds((const unsigned*)((const char*)(gbase) + (o0)), (LAS unsigned*)(lds + (bufoff) + ldsw), 16, 0, 0); \
;         __builtin_amdgcn_global_load_lds((const unsigned*)((const char*)(gbase) + (o1)), (LAS unsigned*)(lds + (bufoff) + ldsw + 8192), 16, 0, 0); } while (0)
; #define PG8_LDA(dst, b, h) do { _Pragma("unroll") for (int m = 0; m < 4; ++m) _Pragma("unroll") for (int k = 0; k < 2; ++k) dst[m][k] = *(const LAS bf16x8*)(lds + PG8_SA(b, h) + aoff + m * 2048 + k * 1024); } while (0)
; #define PG8_LDB(dst, b, h) do { _Pragma("unroll") for (int n = 0; n < 2; ++n) _Pragma("unroll") for (int k = 0; k < 2; ++k) dst[n][k] = *(const LAS bf16x8*)(lds + PG8_SB(b, h) + boff + n * 2048 + k * 1024); } while (0)
; #define PG8_WAIT_V(n) asm volatile("s_waitcnt vmcnt(" #n ")" ::: "memory")
; #define PG8_WAIT_L(n) asm volatile("s_waitcnt lgkmcnt(" #n ")" ::: "memory")
; #define PG8_BAR __builtin_amdgcn_s_barrier()
; #define PG8_SCHED __builtin_amdgcn_sched_barrier(0)
; template <class Epi, class Sched, class Prob>
; __device__ __forceinline__ void gemm_phase(LAS unsigned char* lds, LAS unsigned char* lds_epi, const Prob g, const Sched& S, const Epi& E, int wid) {
;     ...
;             PG8_LDB(B0, 0, 0); PG8_LDB(B1, 0, 1); PG8_SCHED; PG8_LDA(At, 0, 0); PG8_STAGE(PG8_SA(1, 1), a1, cA10, cA11);
;             PG8_WAIT_V(8); PG8_WAIT_L(0); PG8_BAR; PG8_MMA(0, 0, At, B0); PG8_MMA(0, 1, At, B1); PG8_BAR; PG8_SCHED;
;             PG8_LDA(At, 0, 1); PG8_STAGE(PG8_SB(0, 0), b2, vB0, vB1); PG8_STAGE(PG8_SB(0, 1), b2 + hstepB, vB0, vB1); PG8_STAGE(PG8_SA(0, 0), a2, cA00, cA01);
;             PG8_WAIT_V(8); PG8_WAIT_L(0); PG8_BAR; PG8_MMA(1, 0, At, B0); PG8_MMA(1, 1, At, B1); PG8_BAR; PG8_SCHED;
;             PG8_LDB(B0, 1, 0); PG8_LDB(B1, 1, 1); PG8_SCHED; PG8_LDA(At, 1, 0); PG8_STAGE(PG8_SA(0, 1), a2, cA10, cA11);
;             PG8_WAIT_V(8); PG8_WAIT_L(0); PG8_BAR; PG8_MMA(0, 0, At, B0); PG8_MMA(0, 1, At, B1); PG8_BAR; PG8_SCHED;
;             PG8_LDA(At, 1, 1); PG8_STAGE(PG8_SB(1, 0), b3, vB0, vB1); PG8_STAGE(PG8_SB(1, 1), b3 + hstepB, vB0, vB1); PG8_STAGE(PG8_SA(1, 0), a3, cA00, cA01);
;             PG8_WAIT_V(8); PG8_WAIT_L(0); PG8_BAR; PG8_MMA(1, 0, At, B0); PG8_MMA(1, 1, At, B1); PG8_BAR; PG8_SCHED;
	s_waitcnt lgkmcnt(0)
	v_mfma_f32_16x16x128_f8f6f4 v[156:159], v[0:7], v[216:223], v[156:159]
	v_mfma_f32_16x16x128_f8f6f4 v[152:155], v[8:15], v[216:223], v[152:155]
	v_mfma_f32_16x16x128_f8f6f4 v[140:143], v[0:7], v[224:231], v[140:143]
	v_mfma_f32_16x16x128_f8f6f4 v[136:139], v[8:15], v[224:231], v[136:139]
	v_mfma_f32_16x16x128_f8f6f4 v[124:127], v[0:7], v[238:245], v[124:127]
	v_mfma_f32_16x16x128_f8f6f4 v[120:123], v[8:15], v[238:245], v[120:123]
	v_mfma_f32_16x16x128_f8f6f4 v[108:111], v[0:7], v[246:253], v[108:111]
	v_mfma_f32_16x16x128_f8f6f4 v[104:107], v[8:15], v[246:253], v[104:107]
	v_mfma_f32_16x16x128_f8f6f4 v[148:151], v[16:23], v[216:223], v[148:151]
	v_mfma_f32_16x16x128_f8f6f4 v[144:147], v[24:31], v[216:223], v[144:147]
	v_mfma_f32_16x16x128_f8f6f4 v[132:135], v[16:23], v[224:231], v[132:135]
	v_mfma_f32_16x16x128_f8f6f4 v[128:131], v[24:31], v[224:231], v[128:131]
	v_mfma_f32_16x16x128_f8f6f4 v[116:119], v[16:23], v[238:245], v[116:119]
	v_mfma_f32_16x16x128_f8f6f4 v[112:115], v[24:31], v[238:245], v[112:115]
	v_mfma_f32_16x16x128_f8f6f4 v[100:103], v[16:23], v[246:253], v[100:103]
	v_mfma_f32_16x16x128_f8f6f4 v[96:99], v[24:31], v[246:253], v[96:99]
	s_barrier
	s_add_i32 s40, s65, s97
	v_lshl_add_u64 v[190:191], v[190:191], 0, s[18:19]
	s_mov_b32 m0, s40
	ds_read_b128 v[216:219], v208 offset:49152
	ds_read_b128 v[220:223], v208 offset:50176
	ds_read_b128 v[224:227], v208 offset:51200
	ds_read_b128 v[228:231], v208 offset:52224
	ds_read_b128 v[238:241], v208 offset:53248
	ds_read_b128 v[242:245], v208 offset:54272
	ds_read_b128 v[246:249], v208 offset:55296
	ds_read_b128 v[250:253], v208 offset:56320
	global_load_lds_dwordx4 v[190:191], off
	v_lshl_add_u64 v[190:191], v[192:193], 0, s[18:19]
	s_add_i32 m0, s40, 0x2000
	v_lshl_add_u64 v[188:189], v[188:189], 0, s[20:21]
	s_add_i32 s40, s66, s97
	global_load_lds_dwordx4 v[190:191], off
	v_lshl_add_u64 v[190:191], v[188:189], 0, v[162:163]
	s_mov_b32 m0, s40
	v_lshl_add_u64 v[188:189], v[188:189], 0, v[164:165]
	global_load_lds_dwordx4 v[190:191], off
	s_add_i32 m0, s40, 0x2000
	s_nop 0
	global_load_lds_dwordx4 v[188:189], off
	v_lshl_add_u64 v[188:189], v[194:195], 0, s[18:19]
	s_mov_b32 m0, s54
	s_nop 0
	global_load_lds_dwordx4 v[188:189], off
	v_lshl_add_u64 v[188:189], v[196:197], 0, s[18:19]
	s_mov_b32 m0, s55
	s_nop 0
	global_load_lds_dwordx4 v[188:189], off
	s_waitcnt vmcnt(8)
	s_waitcnt lgkmcnt(0)
	s_barrier
	s_waitcnt lgkmcnt(0)
	v_mfma_f32_16x16x128_f8f6f4 v[92:95], v[0:7], v[216:223], v[92:95]
	v_mfma_f32_16x16x128_f8f6f4 v[88:91], v[8:15], v[216:223], v[88:91]
	v_mfma_f32_16x16x128_f8f6f4 v[76:79], v[0:7], v[224:231], v[76:79]
	v_mfma_f32_16x16x128_f8f6f4 v[72:75], v[8:15], v[224:231], v[72:75]
	v_mfma_f32_16x16x128_f8f6f4 v[60:63], v[0:7], v[238:245], v[60:63]
	v_mfma_f32_16x16x128_f8f6f4 v[56:59], v[8:15], v[238:245], v[56:59]
	v_mfma_f32_16x16x128_f8f6f4 v[44:47], v[0:7], v[246:253], v[44:47]
	v_mfma_f32_16x16x128_f8f6f4 v[40:43], v[8:15], v[246:253], v[40:43]
	v_mfma_f32_16x16x128_f8f6f4 v[84:87], v[16:23], v[216:223], v[84:87]
	v_mfma_f32_16x16x128_f8f6f4 v[80:83], v[24:31], v[216:223], v[80:83]
	v_mfma_f32_16x16x128_f8f6f4 v[68:71], v[16:23], v[224:231], v[68:71]
	v_mfma_f32_16x16x128_f8f6f4 v[64:67], v[24:31], v[224:231], v[64:67]
	v_mfma_f32_16x16x128_f8f6f4 v[52:55], v[16:23], v[238:245], v[52:55]
	v_mfma_f32_16x16x128_f8f6f4 v[48:51], v[24:31], v[238:245], v[48:51]
	v_mfma_f32_16x16x128_f8f6f4 v[36:39], v[16:23], v[246:253], v[36:39]
	v_mfma_f32_16x16x128_f8f6f4 v[32:35], v[24:31], v[246:253], v[32:35]
	s_barrier
	s_add_i32 s64, s64, 2
	s_add_u32 s36, s36, 0x100
	s_addc_u32 s37, s37, 0
	s_cmp_gt_u32 s64, 53
	v_lshl_add_u64 v[186:187], v[186:187], 0, s[22:23]
.LBB0_2173:
	ds_read_b128 v[24:27], v161
	ds_read_b128 v[28:31], v161 offset:1024
	ds_read_b128 v[16:19], v161 offset:2048
	ds_read_b128 v[20:23], v161 offset:3072
	ds_read_b128 v[8:11], v207
	ds_read_b128 v[12:15], v207 offset:1024
	ds_read_b128 v[0:3], v207 offset:2048
	ds_read_b128 v[4:7], v207 offset:3072
	s_add_u32 s40, s36, 0x80
	s_addc_u32 s41, s37, 0
	s_cmp_eq_u32 s64, 52
	s_cselect_b64 vcc, -1, 0
	s_cselect_b32 s41, s31, s41
	s_cselect_b32 s40, s30, s40
	v_cndmask_b32_e32 v189, v187, v185, vcc
	v_cndmask_b32_e32 v188, v186, v184, vcc
	v_lshl_add_u64 v[212:213], s[36:37], 0, v[182:183]
	s_add_i32 m0, s33, 0xc000
	ds_read_b128 v[190:193], v208
	ds_read_b128 v[194:197], v208 offset:1024
	ds_read_b128 v[216:219], v208 offset:2048
	ds_read_b128 v[220:223], v208 offset:3072
	ds_read_b128 v[224:227], v208 offset:4096
	ds_read_b128 v[228:231], v208 offset:5120
	ds_read_b128 v[238:241], v208 offset:6144
	ds_read_b128 v[242:245], v208 offset:7168
	global_load_lds_dwordx4 v[212:213], off
	v_lshl_add_u64 v[212:213], s[36:37], 0, v[180:181]
	s_add_i32 m0, s33, 0xe000
	s_nop 0
	global_load_lds_dwordx4 v[212:213], off
	s_waitcnt vmcnt(8)
	s_waitcnt lgkmcnt(0)
	s_barrier
	s_waitcnt lgkmcnt(0)
	v_mfma_f32_16x16x128_f8f6f4 v[156:159], v[24:31], v[190:197], v[156:159]
	v_mfma_f32_16x16x128_f8f6f4 v[152:155], v[16:23], v[190:197], v[152:155]
	v_mfma_f32_16x16x128_f8f6f4 v[140:143], v[24:31], v[216:223], v[140:143]
	v_mfma_f32_16x16x128_f8f6f4 v[136:139], v[16:23], v[216:223], v[136:139]
	v_mfma_f32_16x16x128_f8f6f4 v[124:127], v[24:31], v[224:231], v[124:127]
	v_mfma_f32_16x16x128_f8f6f4 v[120:123], v[16:23], v[224:231], v[120:123]
	v_mfma_f32_16x16x128_f8f6f4 v[108:111], v[24:31], v[238:245], v[108:111]
	v_mfma_f32_16x16x128_f8f6f4 v[104:107], v[16:23], v[238:245], v[104:107]
	v_mfma_f32_16x16x128_f8f6f4 v[148:151], v[8:15], v[190:197], v[148:151]
	v_mfma_f32_16x16x128_f8f6f4 v[144:147], v[0:7], v[190:197], v[144:147]
	v_mfma_f32_16x16x128_f8f6f4 v[132:135], v[8:15], v[216:223], v[132:135]
	v_mfma_f32_16x16x128_f8f6f4 v[128:131], v[0:7], v[216:223], v[128:131]
	v_mfma_f32_16x16x128_f8f6f4 v[116:119], v[8:15], v[224:231], v[116:119]
	v_mfma_f32_16x16x128_f8f6f4 v[112:115], v[0:7], v[224:231], v[112:115]
	v_mfma_f32_16x16x128_f8f6f4 v[100:103], v[8:15], v[238:245], v[100:103]
	v_mfma_f32_16x16x128_f8f6f4 v[96:99], v[0:7], v[238:245], v[96:99]
	s_barrier
; #define PG8_STAGE(bufoff, gbase, o0, o1) do { \
;         __builtin_amdgcn_global_load_lds((const unsigned*)((const char*)(gbase) + (o0)), (LAS unsigned*)(lds + (bufoff) + ldsw), 16, 0, 0); \
;         __builtin_amdgcn_global_load_lds((const unsigned*)((const char*)(gbase) + (o1)), (LAS unsigned*)(lds + (bufoff) + ldsw + 8192), 16, 0, 0); } while (0)
; #define PG8_LDA(dst, b, h) do { _Pragma("unroll") for (int m = 0; m < 4; ++m) _Pragma("unroll") for (int k = 0; k < 2; ++k) dst[m][k] = *(const LAS bf16x8*)(lds + PG8_SA(b, h) + aoff + m * 2048 + k * 1024); } while (0)
; #define PG8_LDB(dst, b, h) do { _Pragma("unroll") for (int n = 0; n < 2; ++n) _Pragma("unroll") for (int k = 0; k < 2; ++k) dst[n][k] = *(const LAS bf16x8*)(lds + PG8_SB(b, h) + boff + n * 2048 + k * 1024); } while (0)
; #define PG8_WAIT_V(n) asm volatile("s_waitcnt vmcnt(" #n ")" ::: "memory")
; #define PG8_WAIT_L(n) asm volatile("s_waitcnt lgkmcnt(" #n ")" ::: "memory")
; #define PG8_BAR __builtin_amdgcn_s_barrier()
; #define PG8_SCHED __builtin_amdgcn_sched_barrier(0)
; template <class Epi, class Sched, class Prob>
; __device__ __forceinline__ void gemm_phase(LAS unsigned char* lds, LAS unsigned char* lds_epi, const Prob g, const Sched& S, const Epi& E, int wid) {
;     ...
;             PG8_LDA(At, 0, 1); PG8_STAGE(PG8_SB(0, 0), b2, vB0, vB1); PG8_STAGE(PG8_SB(0, 1), b2 + hstepB, vB0, vB1); PG8_STAGE(PG8_SA(0, 0), a2, cA00, cA01);
;             PG8_WAIT_V(8); PG8_WAIT_L(0); PG8_BAR; PG8_MMA(1, 0, At, B0); PG8_MMA(1, 1, At, B1); PG8_BAR; PG8_SCHED;
;             PG8_LDB(B0, 1, 0); PG8_LDB(B1, 1, 1); PG8_SCHED; PG8_LDA(At, 1, 0); PG8_STAGE(PG8_SA(0, 1), a2, cA10, cA11);
	s_add_i32 s65, s58, s97
	v_lshl_add_u64 v[190:191], v[188:189], 0, v[162:163]
	s_mov_b32 m0, s65
	ds_read_b128 v[216:219], v208 offset:16384
	ds_read_b128 v[220:223], v208 offset:17408
	ds_read_b128 v[224:227], v208 offset:18432
	ds_read_b128 v[228:231], v208 offset:19456
	ds_read_b128 v[238:241], v208 offset:20480
	ds_read_b128 v[242:245], v208 offset:21504
	ds_read_b128 v[246:249], v208 offset:22528
	ds_read_b128 v[250:253], v208 offset:23552
	global_load_lds_dwordx4 v[190:191], off
	v_lshl_add_u64 v[192:193], v[188:189], 0, v[164:165]
	s_add_i32 m0, s65, 0x2000
	v_lshl_add_u64 v[194:195], v[188:189], 0, s[16:17]
	s_add_i32 s65, s59, s97
	global_load_lds_dwordx4 v[192:193], off
	v_lshl_add_u64 v[196:197], v[194:195], 0, v[162:163]
	s_mov_b32 m0, s65
	v_lshl_add_u64 v[194:195], v[194:195], 0, v[164:165]
	global_load_lds_dwordx4 v[196:197], off
	s_add_i32 m0, s65, 0x2000
	v_lshl_add_u64 v[196:197], s[40:41], 0, v[174:175]
	global_load_lds_dwordx4 v[194:195], off
	v_lshl_add_u64 v[194:195], s[40:41], 0, v[170:171]
	s_mov_b32 m0, s33
	s_nop 0
	global_load_lds_dwordx4 v[194:195], off
	s_mov_b32 m0, s35
	s_nop 0
	global_load_lds_dwordx4 v[196:197], off
	s_waitcnt vmcnt(8)
	s_waitcnt lgkmcnt(0)
	s_barrier
	s_waitcnt lgkmcnt(0)
	v_mfma_f32_16x16x128_f8f6f4 v[92:95], v[24:31], v[216:223], v[92:95]
	v_mfma_f32_16x16x128_f8f6f4 v[88:91], v[16:23], v[216:223], v[88:91]
	v_mfma_f32_16x16x128_f8f6f4 v[76:79], v[24:31], v[224:231], v[76:79]
	v_mfma_f32_16x16x128_f8f6f4 v[72:75], v[16:23], v[224:231], v[72:75]
	v_mfma_f32_16x16x128_f8f6f4 v[60:63], v[24:31], v[238:245], v[60:63]
	v_mfma_f32_16x16x128_f8f6f4 v[56:59], v[16:23], v[238:245], v[56:59]
	v_mfma_f32_16x16x128_f8f6f4 v[44:47], v[24:31], v[246:253], v[44:47]
	v_mfma_f32_16x16x128_f8f6f4 v[40:43], v[16:23], v[246:253], v[40:43]
	v_mfma_f32_16x16x128_f8f6f4 v[84:87], v[8:15], v[216:223], v[84:87]
	v_mfma_f32_16x16x128_f8f6f4 v[80:83], v[0:7], v[216:223], v[80:83]
	v_mfma_f32_16x16x128_f8f6f4 v[68:71], v[8:15], v[224:231], v[68:71]
	v_mfma_f32_16x16x128_f8f6f4 v[64:67], v[0:7], v[224:231], v[64:67]
	v_mfma_f32_16x16x128_f8f6f4 v[52:55], v[8:15], v[238:245], v[52:55]
	v_mfma_f32_16x16x128_f8f6f4 v[48:51], v[0:7], v[238:245], v[48:51]
	v_mfma_f32_16x16x128_f8f6f4 v[36:39], v[8:15], v[246:253], v[36:39]
	v_mfma_f32_16x16x128_f8f6f4 v[32:35], v[0:7], v[246:253], v[32:35]
	s_barrier
	s_add_i32 s65, 0, 0x18000
	s_add_i32 s66, 0, 0x1c000
	v_add_u32_e32 v12, s65, v204
	v_add_u32_e32 v28, s66, v204
	ds_read_b128 v[0:3], v12
	ds_read_b128 v[4:7], v12 offset:1024
	ds_read_b128 v[8:11], v12 offset:2048
	ds_read_b128 v[12:15], v12 offset:3072
	ds_read_b128 v[16:19], v28
	ds_read_b128 v[20:23], v28 offset:1024
	ds_read_b128 v[24:27], v28 offset:2048
	ds_read_b128 v[28:31], v28 offset:3072
	s_mov_b32 m0, s48
	v_lshl_add_u64 v[212:213], s[40:41], 0, v[172:173]
	ds_read_b128 v[216:219], v208 offset:32768
	ds_read_b128 v[220:223], v208 offset:33792
	ds_read_b128 v[224:227], v208 offset:34816
	ds_read_b128 v[228:231], v208 offset:35840
	ds_read_b128 v[238:241], v208 offset:36864
	ds_read_b128 v[242:245], v208 offset:37888
	ds_read_b128 v[246:249], v208 offset:38912
	ds_read_b128 v[250:253], v208 offset:39936
	global_load_lds_dwordx4 v[212:213], off
	v_lshl_add_u64 v[212:213], s[40:41], 0, v[176:177]
	s_mov_b32 m0, s52
	s_nop 0
	global_load_lds_dwordx4 v[212:213], off
	s_waitcnt vmcnt(8)
	s_waitcnt lgkmcnt(0)
	s_barrier
; #define PG8_STAGE(bufoff, gbase, o0, o1) do { \
;         __builtin_amdgcn_global_load_lds((const unsigned*)((const char*)(gbase) + (o0)), (LAS unsigned*)(lds + (bufoff) + ldsw), 16, 0, 0); \
;         __builtin_amdgcn_global_load_lds((const unsigned*)((const char*)(gbase) + (o1)), (LAS unsigned*)(lds + (bufoff) + ldsw + 8192), 16, 0, 0); } while (0)
; #define PG8_LDA(dst, b, h) do { _Pragma("unroll") for (int m = 0; m < 4; ++m) _Pragma("unroll") for (int k = 0; k < 2; ++k) dst[m][k] = *(const LAS bf16x8*)(lds + PG8_SA(b, h) + aoff + m * 2048 + k * 1024); } while (0)
; #define PG8_WAIT_V(n) asm volatile("s_waitcnt vmcnt(" #n ")" ::: "memory")
; #define PG8_WAIT_L(n) asm volatile("s_waitcnt lgkmcnt(" #n ")" ::: "memory")
; #define PG8_BAR __builtin_amdgcn_s_barrier()
; #define PG8_SCHED __builtin_amdgcn_sched_barrier(0)
; template <class Epi, class Sched, class Prob>
; __device__ __forceinline__ void gemm_phase(LAS unsigned char* lds, LAS unsigned char* lds_epi, const Prob g, const Sched& S, const Epi& E, int wid) {
;     ...
;             PG8_WAIT_V(8); PG8_WAIT_L(0); PG8_BAR; PG8_MMA(0, 0, At, B0); PG8_MMA(0, 1, At, B1); PG8_BAR; PG8_SCHED;
;             PG8_LDA(At, 1, 1); PG8_STAGE(PG8_SB(1, 0), b3, vB0, vB1); PG8_STAGE(PG8_SB(1, 1), b3 + hstepB, vB0, vB1); PG8_STAGE(PG8_SA(1, 0), a3, cA00, cA01);
;             PG8_WAIT_V(8); PG8_WAIT_L(0); PG8_BAR; PG8_MMA(1, 0, At, B0); PG8_MMA(1, 1, At, B1); PG8_BAR; PG8_SCHED;
;         }
;         if constexpr (Prob::FP8) asm volatile("s_nop 7\n\ts_nop 7\n\ts_nop 7" ::: "memory");
;         if (wr == 0) PG8_BAR;
	s_waitcnt lgkmcnt(0)
	v_mfma_f32_16x16x128_f8f6f4 v[156:159], v[0:7], v[216:223], v[156:159]
	v_mfma_f32_16x16x128_f8f6f4 v[152:155], v[8:15], v[216:223], v[152:155]
	v_mfma_f32_16x16x128_f8f6f4 v[140:143], v[0:7], v[224:231], v[140:143]
	v_mfma_f32_16x16x128_f8f6f4 v[136:139], v[8:15], v[224:231], v[136:139]
	v_mfma_f32_16x16x128_f8f6f4 v[124:127], v[0:7], v[238:245], v[124:127]
	v_mfma_f32_16x16x128_f8f6f4 v[120:123], v[8:15], v[238:245], v[120:123]
	v_mfma_f32_16x16x128_f8f6f4 v[108:111], v[0:7], v[246:253], v[108:111]
	v_mfma_f32_16x16x128_f8f6f4 v[104:107], v[8:15], v[246:253], v[104:107]
	v_mfma_f32_16x16x128_f8f6f4 v[148:151], v[16:23], v[216:223], v[148:151]
	v_mfma_f32_16x16x128_f8f6f4 v[144:147], v[24:31], v[216:223], v[144:147]
	v_mfma_f32_16x16x128_f8f6f4 v[132:135], v[16:23], v[224:231], v[132:135]
	v_mfma_f32_16x16x128_f8f6f4 v[128:131], v[24:31], v[224:231], v[128:131]
	v_mfma_f32_16x16x128_f8f6f4 v[116:119], v[16:23], v[238:245], v[116:119]
	v_mfma_f32_16x16x128_f8f6f4 v[112:115], v[24:31], v[238:245], v[112:115]
	v_mfma_f32_16x16x128_f8f6f4 v[100:103], v[16:23], v[246:253], v[100:103]
	v_mfma_f32_16x16x128_f8f6f4 v[96:99], v[24:31], v[246:253], v[96:99]
	s_barrier
	s_add_i32 s40, s65, s97
	v_lshl_add_u64 v[190:191], v[190:191], 0, s[18:19]
	s_mov_b32 m0, s40
	ds_read_b128 v[216:219], v208 offset:49152
	ds_read_b128 v[220:223], v208 offset:50176
	ds_read_b128 v[224:227], v208 offset:51200
	ds_read_b128 v[228:231], v208 offset:52224
	ds_read_b128 v[238:241], v208 offset:53248
	ds_read_b128 v[242:245], v208 offset:54272
	ds_read_b128 v[246:249], v208 offset:55296
	ds_read_b128 v[250:253], v208 offset:56320
	global_load_lds_dwordx4 v[190:191], off
	v_lshl_add_u64 v[190:191], v[192:193], 0, s[18:19]
	s_add_i32 m0, s40, 0x2000
	v_lshl_add_u64 v[188:189], v[188:189], 0, s[20:21]
	s_add_i32 s40, s66, s97
	global_load_lds_dwordx4 v[190:191], off
	v_lshl_add_u64 v[190:191], v[188:189], 0, v[162:163]
	s_mov_b32 m0, s40
	v_lshl_add_u64 v[188:189], v[188:189], 0, v[164:165]
	global_load_lds_dwordx4 v[190:191], off
	s_add_i32 m0, s40, 0x2000
	s_nop 0
	global_load_lds_dwordx4 v[188:189], off
	v_lshl_add_u64 v[188:189], v[194:195], 0, s[18:19]
	s_mov_b32 m0, s54
	s_nop 0
	global_load_lds_dwordx4 v[188:189], off
	v_lshl_add_u64 v[188:189], v[196:197], 0, s[18:19]
	s_mov_b32 m0, s55
	s_nop 0
	global_load_lds_dwordx4 v[188:189], off
	s_waitcnt vmcnt(8)
	s_waitcnt lgkmcnt(0)
	s_barrier
	s_waitcnt lgkmcnt(0)
	v_mfma_f32_16x16x128_f8f6f4 v[92:95], v[0:7], v[216:223], v[92:95]
	v_mfma_f32_16x16x128_f8f6f4 v[88:91], v[8:15], v[216:223], v[88:91]
	v_mfma_f32_16x16x128_f8f6f4 v[76:79], v[0:7], v[224:231], v[76:79]
	v_mfma_f32_16x16x128_f8f6f4 v[72:75], v[8:15], v[224:231], v[72:75]
	v_mfma_f32_16x16x128_f8f6f4 v[60:63], v[0:7], v[238:245], v[60:63]
	v_mfma_f32_16x16x128_f8f6f4 v[56:59], v[8:15], v[238:245], v[56:59]
	v_mfma_f32_16x16x128_f8f6f4 v[44:47], v[0:7], v[246:253], v[44:47]
	v_mfma_f32_16x16x128_f8f6f4 v[40:43], v[8:15], v[246:253], v[40:43]
	v_mfma_f32_16x16x128_f8f6f4 v[84:87], v[16:23], v[216:223], v[84:87]
	v_mfma_f32_16x16x128_f8f6f4 v[80:83], v[24:31], v[216:223], v[80:83]
	v_mfma_f32_16x16x128_f8f6f4 v[68:71], v[16:23], v[224:231], v[68:71]
	v_mfma_f32_16x16x128_f8f6f4 v[64:67], v[24:31], v[224:231], v[64:67]
	v_mfma_f32_16x16x128_f8f6f4 v[52:55], v[16:23], v[238:245], v[52:55]
	v_mfma_f32_16x16x128_f8f6f4 v[48:51], v[24:31], v[238:245], v[48:51]
	v_mfma_f32_16x16x128_f8f6f4 v[36:39], v[16:23], v[246:253], v[36:39]
	v_mfma_f32_16x16x128_f8f6f4 v[32:35], v[24:31], v[246:253], v[32:35]
	s_barrier
	s_add_i32 s64, s64, 2
	s_add_u32 s36, s36, 0x100
	s_addc_u32 s37, s37, 0
	s_cmp_gt_u32 s64, 53
	v_lshl_add_u64 v[186:187], v[186:187], 0, s[22:23]
	s_cbranch_scc0 .LBB0_2173
	s_setprio 0
	s_nop 7
	s_nop 7
	s_nop 7
	v_readlane_b32 s36, v254, 27
	v_readlane_b32 s37, v254, 28
	s_and_b64 vcc, exec, s[36:37]
	s_cbranch_vccz .LBB0_2176
	s_barrier

; #define PG8_STAGE(bufoff, gbase, o0, o1) do { \
;         __builtin_amdgcn_global_load_lds((const unsigned*)((const char*)(gbase) + (o0)), (LAS unsigned*)(lds + (bufoff) + ldsw), 16, 0, 0); \
;         __builtin_amdgcn_global_load_lds((const unsigned*)((const char*)(gbase) + (o1)), (LAS unsigned*)(lds + (bufoff) + ldsw + 8192), 16, 0, 0); } while (0)
; #define PG8_WAIT_V(n) asm volatile("s_waitcnt vmcnt(" #n ")" ::: "memory")
; #define PG8_BAR __builtin_amdgcn_s_barrier()
; #define PG8_ACC_INIT(unit) do { if constexpr (Epi::ACC_INIT) { E.init(acc, unit, wr, wc, fr, fq); } else { \
;         _Pragma("unroll") for (int a = 0; a < 2; ++a) _Pragma("unroll") for (int b = 0; b < 2; ++b) _Pragma("unroll") for (int m = 0; m < 4; ++m) _Pragma("unroll") for (int n = 0; n < 2; ++n) acc[a][b][m][n] = (f32x4){0.f, 0.f, 0.f, 0.f}; } } while (0)
; template <class Epi, class Sched, class Prob>
; __device__ __forceinline__ void gemm_phase(LAS unsigned char* lds, LAS unsigned char* lds_epi, const Prob g, const Sched& S, const Epi& E, int wid) {
;     ...
;     const unsigned cA00 = (unsigned)Ra0 * lda2 + (unsigned)C0 * 2u, cA01 = (unsigned)Ra1 * lda2 + (unsigned)C1 * 2u, cA10 = cA00 + (unsigned)HALF * lda2, cA11 = cA01 + (unsigned)HALF * lda2;
;     f32x4 acc[2][2][4][2];
;     ...
;     PG8_ACC_INIT(cur);
;     bf16x8 At[4][2], B0[2][2], B1[2][2];
;     const char* cA = g.a_base(cur); const char* cB = g.b_base(cur);
;     PG8_STAGE(PG8_SB(0, 0), cB, vB0, vB1); PG8_STAGE(PG8_SB(0, 1), cB + hstepB, vB0, vB1); PG8_STAGE(PG8_SA(0, 0), cA, cA00, cA01); PG8_STAGE(PG8_SA(0, 1), cA, cA10, cA11);
;     if (wr == 1) PG8_BAR;
;     PG8_WAIT_V(2); PG8_BAR;
;     PG8_STAGE(PG8_SB(1, 0), cB + kstep, vB0, vB1); PG8_STAGE(PG8_SA(1, 0), cA + kstep, cA00, cA01); PG8_STAGE(PG8_SB(1, 1), cB + hstepB + kstep, vB0, vB1);
;     PG8_WAIT_V(6); PG8_BAR;
;     for (;;) {
.LBB0_2190:
	s_mov_b64 s[12:13], 0x80
	v_lshl_add_u64 v[6:7], v[6:7], 0, s[12:13]
	s_add_i32 m0, s25, 0x18000
	s_waitcnt vmcnt(2)
	s_barrier
	global_load_lds_dwordx4 v[6:7], off
	v_lshl_add_u64 v[2:3], v[2:3], 0, s[12:13]
	s_add_i32 m0, s25, 0x1a000
	s_add_i32 s29, s25, 0x8000
	s_add_i32 s30, s25, 0xa000
	global_load_lds_dwordx4 v[2:3], off
	v_lshl_add_u64 v[0:1], v[0:1], 0, s[12:13]
	s_mov_b32 m0, s29
	s_add_u32 s36, s10, 0xe0080
	global_load_lds_dwordx4 v[0:1], off
	v_lshl_add_u64 v[0:1], v[4:5], 0, s[12:13]
	s_mov_b32 m0, s30
	s_addc_u32 s37, s11, 0
	global_load_lds_dwordx4 v[0:1], off
	v_lshl_add_u64 v[0:1], s[36:37], 0, v[162:163]
	s_add_i32 m0, s25, 0x1c000
	s_mov_b32 s40, 0x1c000
	global_load_lds_dwordx4 v[0:1], off
	v_lshl_add_u64 v[0:1], s[36:37], 0, v[164:165]
	s_add_i32 m0, s25, 0x1e000
	s_add_u32 s36, s15, s21
	global_load_lds_dwordx4 v[0:1], off
	v_lshrrev_b32_e32 v1, 1, v200
	v_mul_lo_u32 v0, v203, s31
	s_addc_u32 s37, s14, 0
	v_mad_u64_u32 v[0:1], s[14:15], v1, s40, v[0:1]
	s_add_u32 s14, s8, s36
	s_addc_u32 s15, s9, s37
	s_add_i32 s17, s17, s18
	s_add_i32 s17, s17, s19
	v_and_b32_e32 v1, 1, v200
	s_add_i32 s17, s17, s20
	v_lshl_or_b32 v0, v1, 6, v0
	v_lshlrev_b32_e32 v1, 1, v206
	s_add_i32 s16, s17, s16
	v_add3_u32 v0, v0, v1, s35
	v_mov_b32_e32 v1, v163
	s_mul_hi_u32 s17, s16, 0xe00000
	s_mul_i32 s16, s16, 0xe00000
	v_lshl_add_u64 v[0:1], s[14:15], 0, v[0:1]
	s_mov_b64 s[36:37], 0x41000080
	s_add_u32 s16, s16, s34
	v_lshl_add_u64 v[174:175], v[0:1], 0, s[36:37]
	v_lshrrev_b32_e32 v1, 1, v199
	v_mul_lo_u32 v0, v201, s31
	s_addc_u32 s17, s17, s33
	v_mad_u64_u32 v[0:1], s[40:41], v1, s40, v[0:1]
	s_add_u32 s16, s16, s21
	v_and_b32_e32 v1, 1, v199
	s_addc_u32 s17, s17, 0
	v_lshl_or_b32 v0, v1, 6, v0
	v_lshlrev_b32_e32 v1, 1, v202
	s_add_u32 s16, s8, s16
	v_add3_u32 v0, v0, v1, s35
	v_mov_b32_e32 v1, v163
	s_addc_u32 s17, s9, s17
	v_lshl_add_u64 v[0:1], s[14:15], 0, v[0:1]
	s_add_u32 s31, s16, 0x27000100
	s_waitcnt vmcnt(6)
	v_lshl_add_u64 v[176:177], v[0:1], 0, s[36:37]
	s_addc_u32 s33, s17, 0
	s_add_i32 s37, 0, 0x10000
	s_add_i32 s41, 0, 0x14000
	s_add_i32 s43, 0, 0x18000
	s_add_i32 s45, 0, 0x1c000
	v_add_u32_e32 v161, s37, v204
	v_add_u32_e32 v186, s41, v204
	s_add_i32 s37, s37, s97
	s_add_i32 s41, s41, s97
	v_add_u32_e32 v188, s43, v204
	v_add_u32_e32 v189, s45, v204
	s_add_i32 s43, s43, s97
	s_add_i32 s45, s45, s97
	v_mov_b32_e32 v171, v163
	v_mov_b32_e32 v173, v163
	s_mov_b32 s34, -2
	s_mov_b64 s[16:17], 0
	v_add_u32_e32 v187, 0, v205
	s_add_i32 s35, s25, 0xc000
	s_add_i32 s36, s25, 0xe000
	s_add_i32 s40, s37, 0x2000
	s_add_i32 s42, s41, 0x2000
	s_add_i32 s44, s43, 0x2000
	s_add_i32 s46, s45, 0x2000
	v_mov_b64_e32 v[32:33], 0
	v_mov_b64_e32 v[34:35], 0
	v_mov_b64_e32 v[36:37], 0
	v_mov_b64_e32 v[38:39], 0
	v_mov_b64_e32 v[40:41], 0
	v_mov_b64_e32 v[42:43], 0
	v_mov_b64_e32 v[44:45], 0
	v_mov_b64_e32 v[46:47], 0
	v_mov_b64_e32 v[48:49], 0
	v_mov_b64_e32 v[50:51], 0
	v_mov_b64_e32 v[52:53], 0
	v_mov_b64_e32 v[54:55], 0
	v_mov_b64_e32 v[56:57], 0
	v_mov_b64_e32 v[58:59], 0
	v_mov_b64_e32 v[60:61], 0
	v_mov_b64_e32 v[62:63], 0
	v_mov_b64_e32 v[64:65], 0
	v_mov_b64_e32 v[66:67], 0
	v_mov_b64_e32 v[68:69], 0
	v_mov_b64_e32 v[70:71], 0
	v_mov_b64_e32 v[72:73], 0
	v_mov_b64_e32 v[74:75], 0
	v_mov_b64_e32 v[76:77], 0
	v_mov_b64_e32 v[78:79], 0
	v_mov_b64_e32 v[80:81], 0
	v_mov_b64_e32 v[82:83], 0
	v_mov_b64_e32 v[84:85], 0
	v_mov_b64_e32 v[86:87], 0
	v_mov_b64_e32 v[88:89], 0
	v_mov_b64_e32 v[90:91], 0
	v_mov_b64_e32 v[92:93], 0
	v_mov_b64_e32 v[94:95], 0
	v_mov_b64_e32 v[96:97], 0
	v_mov_b64_e32 v[98:99], 0
	v_mov_b64_e32 v[100:101], 0
	v_mov_b64_e32 v[102:103], 0
	v_mov_b64_e32 v[104:105], 0
	v_mov_b64_e32 v[106:107], 0
	v_mov_b64_e32 v[108:109], 0
	v_mov_b64_e32 v[110:111], 0
	v_mov_b64_e32 v[112:113], 0
	v_mov_b64_e32 v[114:115], 0
	v_mov_b64_e32 v[116:117], 0
	v_mov_b64_e32 v[118:119], 0
	v_mov_b64_e32 v[120:121], 0
	v_mov_b64_e32 v[122:123], 0
	v_mov_b64_e32 v[124:125], 0
	v_mov_b64_e32 v[126:127], 0
	v_mov_b64_e32 v[128:129], 0
	v_mov_b64_e32 v[130:131], 0
	v_mov_b64_e32 v[132:133], 0
	v_mov_b64_e32 v[134:135], 0
	v_mov_b64_e32 v[136:137], 0
	v_mov_b64_e32 v[138:139], 0
	v_mov_b64_e32 v[140:141], 0
	v_mov_b64_e32 v[142:143], 0
	v_mov_b64_e32 v[144:145], 0
	v_mov_b64_e32 v[146:147], 0
	v_mov_b64_e32 v[148:149], 0
	v_mov_b64_e32 v[150:151], 0
	v_mov_b64_e32 v[152:153], 0
	v_mov_b64_e32 v[154:155], 0
	v_mov_b64_e32 v[156:157], 0
	v_mov_b64_e32 v[158:159], 0
	s_barrier
	s_cmp_lt_u32 s91, 0x100
	s_cbranch_scc1 .Lyoung_9
	s_setprio 1
; #define PG8_STAGE(bufoff, gbase, o0, o1) do { \
;         __builtin_amdgcn_global_load_lds((const unsigned*)((const char*)(gbase) + (o0)), (LAS unsigned*)(lds + (bufoff) + ldsw), 16, 0, 0); \
;         __builtin_amdgcn_global_load_lds((const unsigned*)((const char*)(gbase) + (o1)), (LAS unsigned*)(lds + (bufoff) + ldsw + 8192), 16, 0, 0); } while (0)
; #define PG8_LDA(dst, b, h) do { _Pragma("unroll") for (int m = 0; m < 4; ++m) _Pragma("unroll") for (int k = 0; k < 2; ++k) dst[m][k] = *(const LAS bf16x8*)(lds + PG8_SA(b, h) + aoff + m * 2048 + k * 1024); } while (0)
; #define PG8_LDB(dst, b, h) do { _Pragma("unroll") for (int n = 0; n < 2; ++n) _Pragma("unroll") for (int k = 0; k < 2; ++k) dst[n][k] = *(const LAS bf16x8*)(lds + PG8_SB(b, h) + boff + n * 2048 + k * 1024); } while (0)
; #define PG8_WAIT_V(n) asm volatile("s_waitcnt vmcnt(" #n ")" ::: "memory")
; #define PG8_WAIT_L(n) asm volatile("s_waitcnt lgkmcnt(" #n ")" ::: "memory")
; #define PG8_BAR __builtin_amdgcn_s_barrier()
; #define PG8_SCHED __builtin_amdgcn_sched_barrier(0)
; template <class Epi, class Sched, class Prob>
; __device__ __forceinline__ void gemm_phase(LAS unsigned char* lds, LAS unsigned char* lds_epi, const Prob g, const Sched& S, const Epi& E, int wid) {
;     ...
;         for (int t = 0; t < nt; t += 2) {
;             const bool last = (t == nt - 2);
;             const char* a1 = cA + (size_t)(t + 1) * kstep;
;             const char* a2 = last ? nA : cA + (size_t)(t + 2) * kstep; const char* b2 = last ? nB : cB + (size_t)(t + 2) * kstep;
;             const char* a3 = a2 + kstep; const char* b3 = b2 + kstep;
;             PG8_LDB(B0, 0, 0); PG8_LDB(B1, 0, 1); PG8_SCHED; PG8_LDA(At, 0, 0); PG8_STAGE(PG8_SA(1, 1), a1, cA10, cA11);
;             PG8_WAIT_V(8); PG8_WAIT_L(0); PG8_BAR; PG8_MMA(0, 0, At, B0); PG8_MMA(0, 1, At, B1); PG8_BAR; PG8_SCHED;
;             PG8_LDA(At, 0, 1); PG8_STAGE(PG8_SB(0, 0), b2, vB0, vB1); PG8_STAGE(PG8_SB(0, 1), b2 + hstepB, vB0, vB1); PG8_STAGE(PG8_SA(0, 0), a2, cA00, cA01);
;             PG8_WAIT_V(8); PG8_WAIT_L(0); PG8_BAR; PG8_MMA(1, 0, At, B0); PG8_MMA(1, 1, At, B1); PG8_BAR; PG8_SCHED;
.Lyoung_9:
.LBB0_2191:
	ds_read_b128 v[24:27], v161
	ds_read_b128 v[28:31], v161 offset:1024
	ds_read_b128 v[16:19], v161 offset:2048
	ds_read_b128 v[20:23], v161 offset:3072
	ds_read_b128 v[8:11], v186
	ds_read_b128 v[12:15], v186 offset:1024
	ds_read_b128 v[0:3], v186 offset:2048
	ds_read_b128 v[4:7], v186 offset:3072
	s_add_u32 s18, s14, s16
	s_addc_u32 s19, s15, s17
	s_add_u32 s18, s18, 0x41000100
	s_addc_u32 s19, s19, 0
	s_add_u32 s47, s31, s16
	s_addc_u32 s48, s33, s17
	s_cmpk_eq_i32 s16, 0x600
	s_cselect_b32 s21, s5, s19
	s_cselect_b32 s20, s4, s18
	s_cselect_b32 s19, s11, s48
	s_cselect_b32 s18, s10, s47
	s_mov_b32 m0, s35
	v_lshl_add_u64 v[208:209], v[176:177], 0, s[16:17]
	ds_read_b128 v[178:181], v187
	ds_read_b128 v[182:185], v187 offset:1024
	ds_read_b128 v[190:193], v187 offset:2048
	ds_read_b128 v[194:197], v187 offset:3072
	ds_read_b128 v[200:203], v187 offset:4096
	ds_read_b128 v[204:207], v187 offset:5120
	ds_read_b128 v[216:219], v187 offset:6144
	ds_read_b128 v[220:223], v187 offset:7168
	global_load_lds_dwordx4 v[208:209], off
	v_lshl_add_u64 v[208:209], v[174:175], 0, s[16:17]
	s_mov_b32 m0, s36
	s_nop 0
	global_load_lds_dwordx4 v[208:209], off
	s_waitcnt vmcnt(8)
	s_waitcnt lgkmcnt(0)
	s_barrier
	s_waitcnt lgkmcnt(0)
	v_mfma_f32_16x16x128_f8f6f4 v[156:159], v[24:31], v[178:185], v[156:159]
	v_mfma_f32_16x16x128_f8f6f4 v[152:155], v[16:23], v[178:185], v[152:155]
	v_mfma_f32_16x16x128_f8f6f4 v[148:151], v[24:31], v[190:197], v[148:151]
	v_mfma_f32_16x16x128_f8f6f4 v[144:147], v[16:23], v[190:197], v[144:147]
	v_mfma_f32_16x16x128_f8f6f4 v[140:143], v[24:31], v[200:207], v[140:143]
	v_mfma_f32_16x16x128_f8f6f4 v[136:139], v[16:23], v[200:207], v[136:139]
	v_mfma_f32_16x16x128_f8f6f4 v[132:135], v[24:31], v[216:223], v[132:135]
	v_mfma_f32_16x16x128_f8f6f4 v[128:131], v[16:23], v[216:223], v[128:131]
	v_mfma_f32_16x16x128_f8f6f4 v[124:127], v[8:15], v[178:185], v[124:127]
	v_mfma_f32_16x16x128_f8f6f4 v[120:123], v[0:7], v[178:185], v[120:123]
	v_mfma_f32_16x16x128_f8f6f4 v[116:119], v[8:15], v[190:197], v[116:119]
	v_mfma_f32_16x16x128_f8f6f4 v[112:115], v[0:7], v[190:197], v[112:115]
	v_mfma_f32_16x16x128_f8f6f4 v[108:111], v[8:15], v[200:207], v[108:111]
	v_mfma_f32_16x16x128_f8f6f4 v[104:107], v[0:7], v[200:207], v[104:107]
	v_mfma_f32_16x16x128_f8f6f4 v[100:103], v[8:15], v[216:223], v[100:103]
	v_mfma_f32_16x16x128_f8f6f4 v[96:99], v[0:7], v[216:223], v[96:99]
	s_barrier
	s_mov_b32 m0, s37
	v_lshl_add_u64 v[178:179], s[18:19], 0, v[162:163]
	s_add_u32 s48, s18, 0xe0000
	ds_read_b128 v[190:193], v187 offset:16384
	ds_read_b128 v[194:197], v187 offset:17408
	ds_read_b128 v[200:203], v187 offset:18432
	ds_read_b128 v[204:207], v187 offset:19456
	ds_read_b128 v[216:219], v187 offset:20480
	ds_read_b128 v[220:223], v187 offset:21504
	ds_read_b128 v[224:227], v187 offset:22528
	ds_read_b128 v[228:231], v187 offset:23552
	global_load_lds_dwordx4 v[178:179], off
	v_lshl_add_u64 v[180:181], s[18:19], 0, v[164:165]
	s_mov_b32 m0, s40
	s_addc_u32 s49, s19, 0
	global_load_lds_dwordx4 v[180:181], off
	v_lshl_add_u64 v[182:183], s[48:49], 0, v[162:163]
	s_mov_b32 m0, s41
	v_lshl_add_u64 v[184:185], s[20:21], 0, v[168:169]
	global_load_lds_dwordx4 v[182:183], off
	v_lshl_add_u64 v[182:183], s[48:49], 0, v[164:165]
	s_mov_b32 m0, s42
	s_nop 0
	global_load_lds_dwordx4 v[182:183], off
	v_lshl_add_u64 v[182:183], s[20:21], 0, v[166:167]
	s_mov_b32 m0, s25
	s_nop 0
	global_load_lds_dwordx4 v[182:183], off
	s_mov_b32 m0, s26
	s_nop 0
	global_load_lds_dwordx4 v[184:185], off
	s_waitcnt vmcnt(8)
	s_waitcnt lgkmcnt(0)
	s_barrier
	s_waitcnt lgkmcnt(0)
	v_mfma_f32_16x16x128_f8f6f4 v[92:95], v[24:31], v[190:197], v[92:95]
	v_mfma_f32_16x16x128_f8f6f4 v[88:91], v[16:23], v[190:197], v[88:91]
	v_mfma_f32_16x16x128_f8f6f4 v[84:87], v[24:31], v[200:207], v[84:87]
	v_mfma_f32_16x16x128_f8f6f4 v[80:83], v[16:23], v[200:207], v[80:83]
	v_mfma_f32_16x16x128_f8f6f4 v[76:79], v[24:31], v[216:223], v[76:79]
	v_mfma_f32_16x16x128_f8f6f4 v[72:75], v[16:23], v[216:223], v[72:75]
	v_mfma_f32_16x16x128_f8f6f4 v[68:71], v[24:31], v[224:231], v[68:71]
	v_mfma_f32_16x16x128_f8f6f4 v[64:67], v[16:23], v[224:231], v[64:67]
	v_mfma_f32_16x16x128_f8f6f4 v[60:63], v[8:15], v[190:197], v[60:63]
	v_mfma_f32_16x16x128_f8f6f4 v[56:59], v[0:7], v[190:197], v[56:59]
	v_mfma_f32_16x16x128_f8f6f4 v[52:55], v[8:15], v[200:207], v[52:55]
	v_mfma_f32_16x16x128_f8f6f4 v[48:51], v[0:7], v[200:207], v[48:51]
	v_mfma_f32_16x16x128_f8f6f4 v[44:47], v[8:15], v[216:223], v[44:47]
	v_mfma_f32_16x16x128_f8f6f4 v[40:43], v[0:7], v[216:223], v[40:43]
	v_mfma_f32_16x16x128_f8f6f4 v[36:39], v[8:15], v[224:231], v[36:39]
	v_mfma_f32_16x16x128_f8f6f4 v[32:35], v[0:7], v[224:231], v[32:35]
	s_barrier
; #define PG8_STAGE(bufoff, gbase, o0, o1) do { \
;         __builtin_amdgcn_global_load_lds((const unsigned*)((const char*)(gbase) + (o0)), (LAS unsigned*)(lds + (bufoff) + ldsw), 16, 0, 0); \
;         __builtin_amdgcn_global_load_lds((const unsigned*)((const char*)(gbase) + (o1)), (LAS unsigned*)(lds + (bufoff) + ldsw + 8192), 16, 0, 0); } while (0)
; #define PG8_LDA(dst, b, h) do { _Pragma("unroll") for (int m = 0; m < 4; ++m) _Pragma("unroll") for (int k = 0; k < 2; ++k) dst[m][k] = *(const LAS bf16x8*)(lds + PG8_SA(b, h) + aoff + m * 2048 + k * 1024); } while (0)
; #define PG8_LDB(dst, b, h) do { _Pragma("unroll") for (int n = 0; n < 2; ++n) _Pragma("unroll") for (int k = 0; k < 2; ++k) dst[n][k] = *(const LAS bf16x8*)(lds + PG8_SB(b, h) + boff + n * 2048 + k * 1024); } while (0)
; #define PG8_WAIT_V(n) asm volatile("s_waitcnt vmcnt(" #n ")" ::: "memory")
; #define PG8_WAIT_L(n) asm volatile("s_waitcnt lgkmcnt(" #n ")" ::: "memory")
; #define PG8_BAR __builtin_amdgcn_s_barrier()
; #define PG8_SCHED __builtin_amdgcn_sched_barrier(0)
; template <class Epi, class Sched, class Prob>
; __device__ __forceinline__ void gemm_phase(LAS unsigned char* lds, LAS unsigned char* lds_epi, const Prob g, const Sched& S, const Epi& E, int wid) {
;     ...
;             PG8_LDB(B0, 1, 0); PG8_LDB(B1, 1, 1); PG8_SCHED; PG8_LDA(At, 1, 0); PG8_STAGE(PG8_SA(0, 1), a2, cA10, cA11);
;             PG8_WAIT_V(8); PG8_WAIT_L(0); PG8_BAR; PG8_MMA(0, 0, At, B0); PG8_MMA(0, 1, At, B1); PG8_BAR; PG8_SCHED;
;             PG8_LDA(At, 1, 1); PG8_STAGE(PG8_SB(1, 0), b3, vB0, vB1); PG8_STAGE(PG8_SB(1, 1), b3 + hstepB, vB0, vB1); PG8_STAGE(PG8_SA(1, 0), a3, cA00, cA01);
;             PG8_WAIT_V(8); PG8_WAIT_L(0); PG8_BAR; PG8_MMA(1, 0, At, B0); PG8_MMA(1, 1, At, B1); PG8_BAR; PG8_SCHED;
;         }
;         if constexpr (Prob::FP8) asm volatile("s_nop 7\n\ts_nop 7\n\ts_nop 7" ::: "memory");
;         if (wr == 0) PG8_BAR;
	ds_read_b128 v[0:3], v188
	ds_read_b128 v[4:7], v188 offset:1024
	ds_read_b128 v[8:11], v188 offset:2048
	ds_read_b128 v[12:15], v188 offset:3072
	ds_read_b128 v[16:19], v189
	ds_read_b128 v[20:23], v189 offset:1024
	ds_read_b128 v[24:27], v189 offset:2048
	ds_read_b128 v[28:31], v189 offset:3072
	s_mov_b32 m0, s27
	v_lshl_add_u64 v[208:209], s[20:21], 0, v[170:171]
	ds_read_b128 v[190:193], v187 offset:32768
	ds_read_b128 v[194:197], v187 offset:33792
	ds_read_b128 v[200:203], v187 offset:34816
	ds_read_b128 v[204:207], v187 offset:35840
	ds_read_b128 v[216:219], v187 offset:36864
	ds_read_b128 v[220:223], v187 offset:37888
	ds_read_b128 v[224:227], v187 offset:38912
	ds_read_b128 v[228:231], v187 offset:39936
	global_load_lds_dwordx4 v[208:209], off
	v_lshl_add_u64 v[208:209], s[20:21], 0, v[172:173]
	s_mov_b32 m0, s28
	s_nop 0
	global_load_lds_dwordx4 v[208:209], off
	s_waitcnt vmcnt(8)
	s_waitcnt lgkmcnt(0)
	s_barrier
	s_waitcnt lgkmcnt(0)
	v_mfma_f32_16x16x128_f8f6f4 v[156:159], v[0:7], v[190:197], v[156:159]
	v_mfma_f32_16x16x128_f8f6f4 v[152:155], v[8:15], v[190:197], v[152:155]
	v_mfma_f32_16x16x128_f8f6f4 v[148:151], v[0:7], v[200:207], v[148:151]
	v_mfma_f32_16x16x128_f8f6f4 v[144:147], v[8:15], v[200:207], v[144:147]
	v_mfma_f32_16x16x128_f8f6f4 v[140:143], v[0:7], v[216:223], v[140:143]
	v_mfma_f32_16x16x128_f8f6f4 v[136:139], v[8:15], v[216:223], v[136:139]
	v_mfma_f32_16x16x128_f8f6f4 v[132:135], v[0:7], v[224:231], v[132:135]
	v_mfma_f32_16x16x128_f8f6f4 v[128:131], v[8:15], v[224:231], v[128:131]
	v_mfma_f32_16x16x128_f8f6f4 v[124:127], v[16:23], v[190:197], v[124:127]
	v_mfma_f32_16x16x128_f8f6f4 v[120:123], v[24:31], v[190:197], v[120:123]
	v_mfma_f32_16x16x128_f8f6f4 v[116:119], v[16:23], v[200:207], v[116:119]
	v_mfma_f32_16x16x128_f8f6f4 v[112:115], v[24:31], v[200:207], v[112:115]
	v_mfma_f32_16x16x128_f8f6f4 v[108:111], v[16:23], v[216:223], v[108:111]
	v_mfma_f32_16x16x128_f8f6f4 v[104:107], v[24:31], v[216:223], v[104:107]
	v_mfma_f32_16x16x128_f8f6f4 v[100:103], v[16:23], v[224:231], v[100:103]
	v_mfma_f32_16x16x128_f8f6f4 v[96:99], v[24:31], v[224:231], v[96:99]
	s_barrier
	s_mov_b32 m0, s43
	v_lshl_add_u64 v[178:179], v[178:179], 0, s[12:13]
	s_add_u32 s18, s18, 0xe0080
	ds_read_b128 v[190:193], v187 offset:49152
	ds_read_b128 v[194:197], v187 offset:50176
	ds_read_b128 v[200:203], v187 offset:51200
	ds_read_b128 v[204:207], v187 offset:52224
	ds_read_b128 v[216:219], v187 offset:53248
	ds_read_b128 v[220:223], v187 offset:54272
	ds_read_b128 v[224:227], v187 offset:55296
	ds_read_b128 v[228:231], v187 offset:56320
	global_load_lds_dwordx4 v[178:179], off
	v_lshl_add_u64 v[178:179], v[180:181], 0, s[12:13]
	s_mov_b32 m0, s44
	s_addc_u32 s19, s19, 0
	global_load_lds_dwordx4 v[178:179], off
	v_lshl_add_u64 v[178:179], s[18:19], 0, v[162:163]
	s_mov_b32 m0, s45
	s_nop 0
	global_load_lds_dwordx4 v[178:179], off
	v_lshl_add_u64 v[178:179], s[18:19], 0, v[164:165]
	s_mov_b32 m0, s46
	s_nop 0
	global_load_lds_dwordx4 v[178:179], off
	v_lshl_add_u64 v[178:179], v[182:183], 0, s[12:13]
	s_mov_b32 m0, s29
	s_nop 0
	global_load_lds_dwordx4 v[178:179], off
	v_lshl_add_u64 v[178:179], v[184:185], 0, s[12:13]
	s_mov_b32 m0, s30
	s_nop 0
	global_load_lds_dwordx4 v[178:179], off
	s_waitcnt vmcnt(8)
	s_waitcnt lgkmcnt(0)
	s_barrier
	s_waitcnt lgkmcnt(0)
	v_mfma_f32_16x16x128_f8f6f4 v[92:95], v[0:7], v[190:197], v[92:95]
	v_mfma_f32_16x16x128_f8f6f4 v[88:91], v[8:15], v[190:197], v[88:91]
	v_mfma_f32_16x16x128_f8f6f4 v[84:87], v[0:7], v[200:207], v[84:87]
	v_mfma_f32_16x16x128_f8f6f4 v[80:83], v[8:15], v[200:207], v[80:83]
	v_mfma_f32_16x16x128_f8f6f4 v[76:79], v[0:7], v[216:223], v[76:79]
	v_mfma_f32_16x16x128_f8f6f4 v[72:75], v[8:15], v[216:223], v[72:75]
	v_mfma_f32_16x16x128_f8f6f4 v[68:71], v[0:7], v[224:231], v[68:71]
	v_mfma_f32_16x16x128_f8f6f4 v[64:67], v[8:15], v[224:231], v[64:67]
	v_mfma_f32_16x16x128_f8f6f4 v[60:63], v[16:23], v[190:197], v[60:63]
	v_mfma_f32_16x16x128_f8f6f4 v[56:59], v[24:31], v[190:197], v[56:59]
	v_mfma_f32_16x16x128_f8f6f4 v[52:55], v[16:23], v[200:207], v[52:55]
	v_mfma_f32_16x16x128_f8f6f4 v[48:51], v[24:31], v[200:207], v[48:51]
	v_mfma_f32_16x16x128_f8f6f4 v[44:47], v[16:23], v[216:223], v[44:47]
	v_mfma_f32_16x16x128_f8f6f4 v[40:43], v[24:31], v[216:223], v[40:43]
	v_mfma_f32_16x16x128_f8f6f4 v[36:39], v[16:23], v[224:231], v[36:39]
	v_mfma_f32_16x16x128_f8f6f4 v[32:35], v[24:31], v[224:231], v[32:35]
	s_barrier
	s_add_i32 s34, s34, 2
	s_add_u32 s16, s16, 0x100
	s_addc_u32 s17, s17, 0
	s_cmp_gt_u32 s34, 11
	s_cbranch_scc0 .LBB0_2191
	s_setprio 0
	s_nop 7
	s_nop 7
	s_nop 7
	v_readlane_b32 s4, v254, 27
	v_readlane_b32 s5, v254, 28
	s_and_b64 vcc, exec, s[4:5]
	s_cbranch_vccz .LBB0_2194
	s_barrier
